# cache policy: nt+sc1 on f32 weight conversion loads, sc1(+nt for w_gu) write-through on fp8 weight conversion stores
# speedup vs baseline: 1.0264x; 1.0264x over previous
.LBB0_51:
	s_cmpk_gt_i32 s1, 0xfff
	s_cbranch_scc1 .LBB0_56
	s_abs_i32 s3, s0
	s_waitcnt vmcnt(9)
	v_cvt_f32_u32_e32 v0, s3
	s_sub_i32 s9, 0, s3
	s_sub_i32 s6, 0xfff, s1
	s_abs_i32 s8, s6
	v_rcp_iflag_f32_e32 v0, v0
	s_xor_b32 s7, s6, s0
	s_ashr_i32 s7, s7, 31
	s_mov_b32 s2, 0
	v_mul_f32_e32 v0, 0x4f7ffffe, v0
	v_cvt_u32_f32_e32 v0, v0
	s_nop 0
	v_readfirstlane_b32 s10, v0
	s_mul_i32 s9, s9, s10
	s_mul_hi_u32 s9, s10, s9
	s_add_i32 s10, s10, s9
	s_mul_hi_u32 s9, s8, s10
	s_mul_i32 s10, s9, s3
	s_sub_i32 s8, s8, s10
	s_add_i32 s11, s9, 1
	s_sub_i32 s10, s8, s3
	s_cmp_ge_u32 s8, s3
	s_cselect_b32 s9, s11, s9
	s_cselect_b32 s8, s10, s8
	s_add_i32 s10, s9, 1
	s_cmp_ge_u32 s8, s3
	s_cselect_b32 s3, s10, s9
	s_xor_b32 s3, s3, s7
	s_sub_i32 s3, s3, s7
	s_cmp_lt_i32 s3, 0
	v_mbcnt_lo_u32_b32 v0, -1, 0
	v_mbcnt_hi_u32_b32 v0, -1, v0
	s_cbranch_scc1 .LBB0_55
	s_mul_i32 s7, s3, s0
	s_sub_i32 s7, s7, s6
	s_add_i32 s10, s6, s7
	s_ashr_i32 s6, s1, 31
	s_lshr_b32 s6, s6, 24
	s_add_i32 s6, s1, s6
	s_ashr_i32 s11, s6, 8
	s_lshl_b32 s6, s11, 7
	s_ashr_i32 s7, s6, 31
	s_add_i32 s10, s10, s1
	s_lshl_b64 s[8:9], s[6:7], 15
	s_add_u32 s14, s76, s8
	s_addc_u32 s15, s77, s9
	s_lshl_b32 s8, s1, 5
	s_lshl_b32 s9, s11, 13
	s_sub_i32 s8, s8, s9
	v_lshlrev_b32_e32 v1, 1, v0
	s_ashr_i32 s9, s8, 31
	v_and_b32_e32 v88, -16, v1
	s_lshl_b64 s[12:13], s[8:9], 2
	v_ashrrev_i32_e32 v89, 31, v88
	v_lshlrev_b32_e32 v0, 2, v0
	s_add_u32 s12, s14, s12
	v_and_b32_e32 v16, 28, v0
	s_addc_u32 s13, s15, s13
	v_lshlrev_b64 v[0:1], 15, v[88:89]
	v_mov_b32_e32 v91, 0
	v_lshl_add_u64 v[0:1], s[12:13], 0, v[0:1]
	v_lshlrev_b32_e32 v90, 2, v16
	v_lshl_add_u64 v[18:19], v[0:1], 0, v[90:91]
	s_mov_b32 s11, 0x78000
	v_add_co_u32_e32 v36, vcc, s11, v18
	s_mov_b32 s12, 0x70000
	s_nop 0
	v_addc_co_u32_e32 v37, vcc, 0, v19, vcc
	v_add_co_u32_e32 v0, vcc, s12, v18
	s_mov_b32 s13, 0x68000
	s_nop 0
	v_addc_co_u32_e32 v1, vcc, 0, v19, vcc
	v_add_co_u32_e32 v4, vcc, s13, v18
	s_mov_b32 s14, 0x60000
	s_nop 0
	v_addc_co_u32_e32 v5, vcc, 0, v19, vcc
	v_add_co_u32_e32 v8, vcc, s14, v18
	s_mov_b32 s15, 0x58000
	s_nop 0
	v_addc_co_u32_e32 v9, vcc, 0, v19, vcc
	v_add_co_u32_e32 v12, vcc, s15, v18
	s_mov_b32 s16, 0x50000
	s_nop 0
	v_addc_co_u32_e32 v13, vcc, 0, v19, vcc
	v_add_co_u32_e32 v20, vcc, s16, v18
	s_mov_b32 s17, 0x48000
	s_nop 0
	v_addc_co_u32_e32 v21, vcc, 0, v19, vcc
	v_add_co_u32_e32 v24, vcc, s17, v18
	s_mov_b32 s18, 0x40000
	s_nop 0
	v_addc_co_u32_e32 v25, vcc, 0, v19, vcc
	v_add_co_u32_e32 v28, vcc, s18, v18
	s_mov_b32 s19, 0x38000
	s_nop 0
	v_addc_co_u32_e32 v29, vcc, 0, v19, vcc
	v_add_co_u32_e32 v32, vcc, s19, v18
	s_mov_b32 s20, 0x30000
	s_nop 0
	v_addc_co_u32_e32 v33, vcc, 0, v19, vcc
	v_add_co_u32_e32 v38, vcc, s20, v18
	s_mov_b32 s21, 0x28000
	s_nop 0
	v_addc_co_u32_e32 v39, vcc, 0, v19, vcc
	v_add_co_u32_e32 v42, vcc, s21, v18
	s_mov_b32 s22, 0x20000
	s_nop 0
	v_addc_co_u32_e32 v43, vcc, 0, v19, vcc
	v_add_co_u32_e32 v46, vcc, s22, v18
	s_mov_b32 s23, 0x18000
	s_nop 0
	v_addc_co_u32_e32 v47, vcc, 0, v19, vcc
	v_add_co_u32_e32 v48, vcc, s23, v18
	s_mov_b32 s24, 0x10000
	s_nop 0
	v_addc_co_u32_e32 v49, vcc, 0, v19, vcc
	global_load_dwordx4 v[0:3], v[0:1], off sc1 nt
	s_nop 0
	global_load_dwordx4 v[4:7], v[4:5], off sc1 nt
	s_nop 0
	global_load_dwordx4 v[8:11], v[8:9], off sc1 nt
	s_nop 0
	global_load_dwordx4 v[12:15], v[12:13], off sc1 nt
	s_nop 0
	global_load_dwordx4 v[20:23], v[20:21], off sc1 nt
	s_nop 0
	global_load_dwordx4 v[24:27], v[24:25], off sc1 nt
	s_nop 0
	global_load_dwordx4 v[28:31], v[28:29], off sc1 nt
	s_nop 0
	global_load_dwordx4 v[32:35], v[32:33], off sc1 nt
	s_nop 0
	global_load_dwordx4 v[38:41], v[38:39], off sc1 nt
	s_nop 0
	global_load_dwordx4 v[42:45], v[42:43], off sc1 nt
	s_nop 0
	global_load_dwordx4 v[50:53], v[46:47], off sc1 nt
	global_load_dwordx4 v[54:57], v[48:49], off sc1 nt
	v_add_co_u32_e32 v46, vcc, s24, v18
	s_mov_b32 s25, 0x8000
	s_nop 0
	v_addc_co_u32_e32 v47, vcc, 0, v19, vcc
	v_add_co_u32_e32 v48, vcc, s25, v18
	s_add_u32 s26, s90, 0x2900000
	s_nop 0
	v_addc_co_u32_e32 v49, vcc, 0, v19, vcc
	global_load_dwordx4 v[62:65], v[46:47], off sc1 nt
	global_load_dwordx4 v[68:71], v[48:49], off sc1 nt
	global_load_dwordx4 v[58:61], v[36:37], off sc1 nt
	s_nop 0
	global_load_dwordx4 v[46:49], v[18:19], off sc1 nt
	s_addc_u32 s27, s91, 0
	s_lshl_b64 s[8:9], s[8:9], 11
	s_add_u32 s8, s26, s8
	s_addc_u32 s9, s27, s9
	v_lshlrev_b64 v[18:19], 13, v[88:89]
	s_add_u32 s6, s8, s6
	s_addc_u32 s7, s9, s7
	v_lshlrev_b32_e32 v92, 11, v16
	v_mov_b32_e32 v93, v91
	v_lshlrev_b64 v[94:95], 2, v[18:19]
	v_lshlrev_b32_e32 v90, 2, v16
	s_movk_i32 s8, 0x1000
.LBB0_54:
	s_add_i32 s1, s1, s0
	s_min_i32 s9, s1, s10
	v_lshl_add_u64 v[96:97], s[6:7], 0, v[92:93]
	s_ashr_i32 s6, s9, 31
	s_lshr_b32 s6, s6, 24
	s_add_i32 s6, s9, s6
	s_ashr_i32 s30, s6, 8
	s_lshl_b32 s6, s30, 7
	s_add_i32 s1, s1, s0
	s_ashr_i32 s7, s6, 31
	s_min_i32 s1, s1, s10
	s_lshl_b64 s[28:29], s[6:7], 15
	s_add_u32 s33, s76, s28
	s_addc_u32 s34, s77, s29
	s_lshl_b32 s28, s30, 13
	s_lshl_b32 s9, s9, 5
	s_sub_i32 s28, s9, s28
	s_ashr_i32 s29, s28, 31
	s_lshl_b64 s[30:31], s[28:29], 2
	s_add_u32 s30, s33, s30
	s_waitcnt vmcnt(9)
	v_mul_f32_e32 v28, 0x44000000, v28
	v_mul_f32_e32 v24, 0x44000000, v24
	v_mov_b32_e32 v18, v91
	s_waitcnt vmcnt(7)
	v_mul_f32_e32 v8, 0x44000000, v8
	s_waitcnt vmcnt(6)
	v_mul_f32_e32 v100, 0x44000000, v4
	v_mov_b32_e32 v19, v91
	s_waitcnt vmcnt(2)
	v_mul_f32_e32 v102, 0x44000000, v69
	v_mul_f32_e32 v103, 0x44000000, v39
	v_mul_f32_e32 v9, 0x44000000, v9
	v_mul_f32_e32 v104, 0x44000000, v5
	v_mov_b32_e32 v39, v91
	v_mul_f32_e32 v10, 0x44000000, v10
	v_mul_f32_e32 v6, 0x44000000, v6
	v_mov_b32_e32 v69, v91
	v_lshl_add_u64 v[4:5], v[96:97], 0, v[88:89]
	s_addc_u32 s31, s34, s31
	v_mul_f32_e32 v99, 0x44000000, v38
	v_mul_f32_e32 v29, 0x44000000, v29
	v_mul_f32_e32 v25, 0x44000000, v25
	v_mov_b32_e32 v38, v91
	v_mul_f32_e32 v11, 0x44000000, v11
	v_mul_f32_e32 v7, 0x44000000, v7
	v_mul_f32_e32 v107, 0x44000000, v3
	v_mov_b32_e32 v3, v91
	v_cvt_pk_fp8_f32 v18, v28, v24
	v_cvt_pk_fp8_f32 v19, v8, v100
	v_cvt_pk_fp8_f32 v39, v9, v104
	v_cvt_pk_fp8_f32 v69, v10, v6
	v_add_co_u32_e32 v6, vcc, s8, v4
	v_lshl_add_u64 v[8:9], s[30:31], 0, v[94:95]
	v_mul_f32_e32 v98, 0x44000000, v68
	v_mul_f32_e32 v30, 0x44000000, v30
	v_mul_f32_e32 v26, 0x44000000, v26
	v_mov_b32_e32 v68, v91
	v_cvt_pk_fp8_f32 v38, v29, v25
	v_cvt_pk_fp8_f32 v3, v11, v7
	v_addc_co_u32_e32 v7, vcc, 0, v5, vcc
	v_lshl_add_u64 v[8:9], v[8:9], 0, v[90:91]
	v_mul_f32_e32 v106, 0x44000000, v2
	v_mul_f32_e32 v31, 0x44000000, v31
	v_mul_f32_e32 v27, 0x44000000, v27
	v_mov_b32_e32 v2, v91
	v_cvt_pk_fp8_f32 v68, v30, v26
	v_add_co_u32_e32 v10, vcc, s25, v8
	v_mul_f32_e32 v20, 0x44000000, v20
	v_mul_f32_e32 v12, 0x44000000, v12
	v_cvt_pk_fp8_f32 v2, v31, v27
	v_addc_co_u32_e32 v11, vcc, 0, v9, vcc
	v_mul_f32_e32 v21, 0x44000000, v21
	v_mul_f32_e32 v13, 0x44000000, v13
	v_cvt_pk_fp8_f32 v18, v20, v12 op_sel:[0,0,1]
	v_add_co_u32_e32 v12, vcc, s24, v8
	v_mul_f32_e32 v22, 0x44000000, v22
	v_mul_f32_e32 v14, 0x44000000, v14
	v_cvt_pk_fp8_f32 v38, v21, v13 op_sel:[0,0,1]
	v_addc_co_u32_e32 v13, vcc, 0, v9, vcc
	v_mul_f32_e32 v23, 0x44000000, v23
	v_mul_f32_e32 v15, 0x44000000, v15
	v_cvt_pk_fp8_f32 v68, v22, v14 op_sel:[0,0,1]
	v_add_co_u32_e32 v14, vcc, s23, v8
	v_cvt_pk_fp8_f32 v2, v23, v15 op_sel:[0,0,1]
	s_nop 0
	v_addc_co_u32_e32 v15, vcc, 0, v9, vcc
	v_add_co_u32_e32 v20, vcc, s22, v8
	v_mul_f32_e32 v50, 0x44000000, v50
	s_nop 0
	v_addc_co_u32_e32 v21, vcc, 0, v9, vcc
	v_add_co_u32_e32 v22, vcc, s21, v8
	v_mul_f32_e32 v42, 0x44000000, v42
	s_nop 0
	v_addc_co_u32_e32 v23, vcc, 0, v9, vcc
	v_add_co_u32_e32 v24, vcc, s20, v8
	v_mov_b32_e32 v17, v91
	s_nop 0
	v_addc_co_u32_e32 v25, vcc, 0, v9, vcc
	v_add_co_u32_e32 v26, vcc, s19, v8
	v_mul_f32_e32 v51, 0x44000000, v51
	s_nop 0
	v_addc_co_u32_e32 v27, vcc, 0, v9, vcc
	v_mul_f32_e32 v43, 0x44000000, v43
	v_mov_b32_e32 v37, v91
	v_cvt_pk_fp8_f32 v17, v50, v42
	v_add_co_u32_e32 v28, vcc, s18, v8
	v_mul_f32_e32 v52, 0x44000000, v52
	v_mul_f32_e32 v44, 0x44000000, v44
	v_mov_b32_e32 v67, v91
	v_cvt_pk_fp8_f32 v37, v51, v43
	v_addc_co_u32_e32 v29, vcc, 0, v9, vcc
	v_mul_f32_e32 v105, 0x44000000, v1
	v_mul_f32_e32 v53, 0x44000000, v53
	v_mul_f32_e32 v45, 0x44000000, v45
	v_mov_b32_e32 v1, v91
	v_cvt_pk_fp8_f32 v67, v52, v44
	v_add_co_u32_e32 v30, vcc, s17, v8
	v_mul_f32_e32 v32, 0x44000000, v32
	v_cvt_pk_fp8_f32 v1, v53, v45
	v_addc_co_u32_e32 v31, vcc, 0, v9, vcc
	v_mul_f32_e32 v33, 0x44000000, v33
	v_cvt_pk_fp8_f32 v17, v99, v32 op_sel:[0,0,1]
	v_add_co_u32_e32 v32, vcc, s16, v8
	v_mul_f32_e32 v40, 0x44000000, v40
	v_mul_f32_e32 v34, 0x44000000, v34
	v_cvt_pk_fp8_f32 v37, v103, v33 op_sel:[0,0,1]
	v_addc_co_u32_e32 v33, vcc, 0, v9, vcc
	s_waitcnt vmcnt(0)
	v_mul_f32_e32 v46, 0x44000000, v46
	v_mov_b32_e32 v16, v91
	v_mul_f32_e32 v41, 0x44000000, v41
	v_mul_f32_e32 v35, 0x44000000, v35
	v_cvt_pk_fp8_f32 v67, v40, v34 op_sel:[0,0,1]
	v_add_co_u32_e32 v34, vcc, s15, v8
	v_mul_f32_e32 v47, 0x44000000, v47
	v_mov_b32_e32 v36, v91
	v_cvt_pk_fp8_f32 v16, v46, v98
	v_cvt_pk_fp8_f32 v1, v41, v35 op_sel:[0,0,1]
	v_addc_co_u32_e32 v35, vcc, 0, v9, vcc
	v_mul_f32_e32 v48, 0x44000000, v48
	v_mul_f32_e32 v70, 0x44000000, v70
	v_mov_b32_e32 v66, v91
	v_cvt_pk_fp8_f32 v36, v47, v102
	v_add_co_u32_e32 v40, vcc, s14, v8
	v_mul_f32_e32 v101, 0x44000000, v0
	v_mul_f32_e32 v49, 0x44000000, v49
	v_mul_f32_e32 v71, 0x44000000, v71
	v_mov_b32_e32 v0, v91
	v_cvt_pk_fp8_f32 v66, v48, v70
	s_lshl_b64 s[28:29], s[28:29], 11
	v_addc_co_u32_e32 v41, vcc, 0, v9, vcc
	v_mul_f32_e32 v62, 0x44000000, v62
	v_mul_f32_e32 v54, 0x44000000, v54
	v_mul_f32_e32 v58, 0x44000000, v58
	v_cvt_pk_fp8_f32 v0, v49, v71
	s_add_u32 s9, s26, s28
	v_add_co_u32_e32 v42, vcc, s13, v8
	v_mul_f32_e32 v63, 0x44000000, v63
	v_mul_f32_e32 v55, 0x44000000, v55
	v_mul_f32_e32 v59, 0x44000000, v59
	v_cvt_pk_fp8_f32 v16, v62, v54 op_sel:[0,0,1]
	v_cvt_pk_fp8_f32 v19, v101, v58 op_sel:[0,0,1]
	s_addc_u32 s28, s27, s29
	v_addc_co_u32_e32 v43, vcc, 0, v9, vcc
	v_mul_f32_e32 v64, 0x44000000, v64
	v_mul_f32_e32 v56, 0x44000000, v56
	v_mul_f32_e32 v60, 0x44000000, v60
	v_cvt_pk_fp8_f32 v36, v63, v55 op_sel:[0,0,1]
	v_cvt_pk_fp8_f32 v39, v105, v59 op_sel:[0,0,1]
	s_add_u32 s6, s9, s6
	v_add_co_u32_e32 v44, vcc, s12, v8
	v_mul_f32_e32 v65, 0x44000000, v65
	v_mul_f32_e32 v57, 0x44000000, v57
	v_mul_f32_e32 v61, 0x44000000, v61
	v_cvt_pk_fp8_f32 v66, v64, v56 op_sel:[0,0,1]
	v_cvt_pk_fp8_f32 v69, v106, v60 op_sel:[0,0,1]
	v_addc_co_u32_e32 v45, vcc, 0, v9, vcc
	s_addc_u32 s7, s28, s7
	s_ashr_i32 s9, s1, 31
	v_cvt_pk_fp8_f32 v0, v65, v57 op_sel:[0,0,1]
	v_cvt_pk_fp8_f32 v3, v107, v61 op_sel:[0,0,1]
	global_load_dwordx4 v[96:99], v[8:9], off sc1 nt
	v_add_co_u32_e32 v8, vcc, s11, v8
	s_lshr_b32 s9, s9, 24
	s_nop 0
	v_addc_co_u32_e32 v9, vcc, 0, v9, vcc
	global_load_dwordx4 v[100:103], v[10:11], off sc1 nt
	global_load_dwordx4 v[104:107], v[12:13], off sc1 nt
	global_load_dwordx4 v[108:111], v[14:15], off sc1 nt
	global_load_dwordx4 v[112:115], v[20:21], off sc1 nt
	global_load_dwordx4 v[116:119], v[22:23], off sc1 nt
	global_load_dwordx4 v[120:123], v[24:25], off sc1 nt
	global_load_dwordx4 v[124:127], v[26:27], off sc1 nt
	global_load_dwordx4 v[128:131], v[28:29], off sc1 nt
	global_load_dwordx4 v[132:135], v[30:31], off sc1 nt
	global_load_dwordx4 v[136:139], v[32:33], off sc1 nt
	global_load_dwordx4 v[140:143], v[34:35], off sc1 nt
	global_load_dwordx4 v[144:147], v[40:41], off sc1 nt
	global_load_dwordx4 v[148:151], v[42:43], off sc1 nt
	global_load_dwordx4 v[152:155], v[44:45], off sc1 nt
	global_load_dwordx4 v[156:159], v[8:9], off sc1 nt
	s_nop 0
	global_store_dwordx4 v[4:5], v[16:19], off sc1 nt
	global_store_dwordx4 v[4:5], v[36:39], off offset:2048 sc1 nt
	global_store_dwordx4 v[6:7], v[66:69], off sc1 nt
	global_store_dwordx4 v[6:7], v[0:3], off offset:2048 sc1 nt
	v_mov_b32_e32 v72, v91
	v_mov_b32_e32 v73, v91
	v_lshl_add_u64 v[0:1], s[6:7], 0, v[92:93]
	s_add_i32 s6, s1, s9
	s_ashr_i32 s9, s6, 8
	s_lshl_b32 s6, s9, 7
	s_ashr_i32 s7, s6, 31
	s_lshl_b64 s[28:29], s[6:7], 15
	s_add_u32 s33, s76, s28
	s_addc_u32 s34, s77, s29
	s_lshl_b32 s9, s9, 13
	s_lshl_b32 s28, s1, 5
	s_sub_i32 s28, s28, s9
	s_ashr_i32 s29, s28, 31
	s_lshl_b64 s[30:31], s[28:29], 2
	s_add_u32 s30, s33, s30
	v_lshl_add_u64 v[16:17], v[0:1], 0, v[88:89]
	s_addc_u32 s31, s34, s31
	v_add_co_u32_e32 v18, vcc, s8, v16
	v_lshl_add_u64 v[0:1], s[30:31], 0, v[94:95]
	s_nop 0
	v_addc_co_u32_e32 v19, vcc, 0, v17, vcc
	v_lshl_add_u64 v[0:1], v[0:1], 0, v[90:91]
	v_add_co_u32_e32 v2, vcc, s25, v0
	global_load_dwordx4 v[46:49], v[0:1], off sc1 nt
	s_nop 0
	v_addc_co_u32_e32 v3, vcc, 0, v1, vcc
	v_add_co_u32_e32 v4, vcc, s24, v0
	v_mov_b32_e32 v74, v91
	s_nop 0
	v_addc_co_u32_e32 v5, vcc, 0, v1, vcc
	v_add_co_u32_e32 v6, vcc, s23, v0
	v_mov_b32_e32 v75, v91
	s_nop 0
	v_addc_co_u32_e32 v7, vcc, 0, v1, vcc
	v_add_co_u32_e32 v8, vcc, s22, v0
	v_mov_b32_e32 v76, v91
	s_nop 0
	v_addc_co_u32_e32 v9, vcc, 0, v1, vcc
	v_add_co_u32_e32 v10, vcc, s21, v0
	v_mov_b32_e32 v77, v91
	s_nop 0
	v_addc_co_u32_e32 v11, vcc, 0, v1, vcc
	v_add_co_u32_e32 v12, vcc, s20, v0
	v_mov_b32_e32 v78, v91
	s_nop 0
	v_addc_co_u32_e32 v13, vcc, 0, v1, vcc
	v_add_co_u32_e32 v14, vcc, s19, v0
	v_mov_b32_e32 v79, v91
	s_nop 0
	v_addc_co_u32_e32 v15, vcc, 0, v1, vcc
	v_add_co_u32_e32 v20, vcc, s18, v0
	v_mov_b32_e32 v80, v91
	s_nop 0
	v_addc_co_u32_e32 v21, vcc, 0, v1, vcc
	v_add_co_u32_e32 v22, vcc, s17, v0
	s_waitcnt vmcnt(19)
	v_mul_f32_e32 v101, 0x44000000, v101
	v_addc_co_u32_e32 v23, vcc, 0, v1, vcc
	v_add_co_u32_e32 v36, vcc, s16, v0
	s_waitcnt vmcnt(16)
	v_mul_f32_e32 v113, 0x44000000, v113
	v_addc_co_u32_e32 v37, vcc, 0, v1, vcc
	v_add_co_u32_e32 v58, vcc, s15, v0
	s_waitcnt vmcnt(15)
	v_mul_f32_e32 v117, 0x44000000, v117
	v_addc_co_u32_e32 v59, vcc, 0, v1, vcc
	v_add_co_u32_e32 v60, vcc, s14, v0
	s_waitcnt vmcnt(12)
	v_mul_f32_e32 v129, 0x44000000, v129
	v_addc_co_u32_e32 v61, vcc, 0, v1, vcc
	v_add_co_u32_e32 v66, vcc, s13, v0
	s_waitcnt vmcnt(11)
	v_mul_f32_e32 v133, 0x44000000, v133
	v_addc_co_u32_e32 v67, vcc, 0, v1, vcc
	v_add_co_u32_e32 v160, vcc, s12, v0
	v_mov_b32_e32 v81, v91
	s_nop 0
	v_addc_co_u32_e32 v161, vcc, 0, v1, vcc
	v_add_co_u32_e32 v162, vcc, s11, v0
	v_mov_b32_e32 v82, v91
	s_nop 0
	v_addc_co_u32_e32 v163, vcc, 0, v1, vcc
	global_load_dwordx4 v[68:71], v[2:3], off sc1 nt
	global_load_dwordx4 v[62:65], v[4:5], off sc1 nt
	global_load_dwordx4 v[54:57], v[6:7], off sc1 nt
	global_load_dwordx4 v[50:53], v[8:9], off sc1 nt
	global_load_dwordx4 v[42:45], v[10:11], off sc1 nt
	global_load_dwordx4 v[38:41], v[12:13], off sc1 nt
	global_load_dwordx4 v[32:35], v[14:15], off sc1 nt
	global_load_dwordx4 v[28:31], v[20:21], off sc1 nt
	global_load_dwordx4 v[24:27], v[22:23], off sc1 nt
	s_nop 0
	global_load_dwordx4 v[20:23], v[36:37], off sc1 nt
	global_load_dwordx4 v[12:15], v[58:59], off sc1 nt
	global_load_dwordx4 v[8:11], v[60:61], off sc1 nt
	global_load_dwordx4 v[4:7], v[66:67], off sc1 nt
	global_load_dwordx4 v[0:3], v[160:161], off sc1 nt
	s_nop 0
	global_load_dwordx4 v[58:61], v[162:163], off sc1 nt
	v_mul_f32_e32 v36, 0x44000000, v96
	v_mul_f32_e32 v67, 0x44000000, v99
	v_mul_f32_e32 v96, 0x44000000, v100
	v_mul_f32_e32 v99, 0x44000000, v112
	v_mul_f32_e32 v100, 0x44000000, v116
	v_mul_f32_e32 v112, 0x44000000, v128
	v_mul_f32_e32 v116, 0x44000000, v132
	s_waitcnt vmcnt(23)
	v_mul_f32_e32 v128, 0x44000000, v144
	s_waitcnt vmcnt(22)
	v_mul_f32_e32 v132, 0x44000000, v148
	v_mul_f32_e32 v37, 0x44000000, v97
	v_mul_f32_e32 v144, 0x44000000, v145
	v_mul_f32_e32 v145, 0x44000000, v149
	v_cvt_pk_fp8_f32 v72, v36, v96
	v_cvt_pk_fp8_f32 v73, v99, v100
	v_cvt_pk_fp8_f32 v74, v112, v116
	v_cvt_pk_fp8_f32 v75, v128, v132
	v_mov_b32_e32 v83, v91
	v_mul_f32_e32 v66, 0x44000000, v98
	v_mul_f32_e32 v102, 0x44000000, v102
	v_mul_f32_e32 v114, 0x44000000, v114
	v_mul_f32_e32 v118, 0x44000000, v118
	v_mul_f32_e32 v130, 0x44000000, v130
	v_mul_f32_e32 v134, 0x44000000, v134
	v_mul_f32_e32 v146, 0x44000000, v146
	v_mul_f32_e32 v150, 0x44000000, v150
	v_cvt_pk_fp8_f32 v76, v37, v101
	v_cvt_pk_fp8_f32 v77, v113, v117
	v_cvt_pk_fp8_f32 v78, v129, v133
	v_cvt_pk_fp8_f32 v79, v144, v145
	v_mov_b32_e32 v84, v91
	v_mov_b32_e32 v85, v91
	v_mov_b32_e32 v86, v91
	v_mov_b32_e32 v87, v91
	s_lshl_b64 s[28:29], s[28:29], 11
	v_mul_f32_e32 v103, 0x44000000, v103
	v_mul_f32_e32 v115, 0x44000000, v115
	v_mul_f32_e32 v119, 0x44000000, v119
	v_mul_f32_e32 v131, 0x44000000, v131
	v_mul_f32_e32 v135, 0x44000000, v135
	v_mul_f32_e32 v147, 0x44000000, v147
	v_mul_f32_e32 v151, 0x44000000, v151
	v_cvt_pk_fp8_f32 v80, v66, v102
	v_cvt_pk_fp8_f32 v81, v114, v118
	v_cvt_pk_fp8_f32 v82, v130, v134
	v_cvt_pk_fp8_f32 v83, v146, v150
	s_add_u32 s9, s26, s28
	v_mul_f32_e32 v97, 0x44000000, v104
	v_mul_f32_e32 v98, 0x44000000, v108
	v_mul_f32_e32 v104, 0x44000000, v120
	v_mul_f32_e32 v108, 0x44000000, v124
	v_mul_f32_e32 v120, 0x44000000, v136
	v_mul_f32_e32 v124, 0x44000000, v140
	s_waitcnt vmcnt(21)
	v_mul_f32_e32 v136, 0x44000000, v152
	s_waitcnt vmcnt(20)
	v_mul_f32_e32 v140, 0x44000000, v156
	v_cvt_pk_fp8_f32 v84, v67, v103
	v_cvt_pk_fp8_f32 v85, v115, v119
	v_cvt_pk_fp8_f32 v86, v131, v135
	v_cvt_pk_fp8_f32 v87, v147, v151
	s_addc_u32 s28, s27, s29
	v_mul_f32_e32 v105, 0x44000000, v105
	v_mul_f32_e32 v109, 0x44000000, v109
	v_mul_f32_e32 v121, 0x44000000, v121
	v_mul_f32_e32 v125, 0x44000000, v125
	v_mul_f32_e32 v137, 0x44000000, v137
	v_mul_f32_e32 v141, 0x44000000, v141
	v_mul_f32_e32 v148, 0x44000000, v153
	v_mul_f32_e32 v149, 0x44000000, v157
	v_cvt_pk_fp8_f32 v72, v97, v98 op_sel:[0,0,1]
	v_cvt_pk_fp8_f32 v73, v104, v108 op_sel:[0,0,1]
	v_cvt_pk_fp8_f32 v74, v120, v124 op_sel:[0,0,1]
	v_cvt_pk_fp8_f32 v75, v136, v140 op_sel:[0,0,1]
	s_add_u32 s6, s9, s6
	v_mul_f32_e32 v106, 0x44000000, v106
	v_mul_f32_e32 v110, 0x44000000, v110
	v_mul_f32_e32 v122, 0x44000000, v122
	v_mul_f32_e32 v126, 0x44000000, v126
	v_mul_f32_e32 v138, 0x44000000, v138
	v_mul_f32_e32 v142, 0x44000000, v142
	v_mul_f32_e32 v152, 0x44000000, v154
	v_mul_f32_e32 v153, 0x44000000, v158
	v_cvt_pk_fp8_f32 v76, v105, v109 op_sel:[0,0,1]
	v_cvt_pk_fp8_f32 v77, v121, v125 op_sel:[0,0,1]
	v_cvt_pk_fp8_f32 v78, v137, v141 op_sel:[0,0,1]
	v_cvt_pk_fp8_f32 v79, v148, v149 op_sel:[0,0,1]
	s_addc_u32 s7, s28, s7
	s_add_i32 s2, s2, 2
	v_mul_f32_e32 v107, 0x44000000, v107
	v_mul_f32_e32 v111, 0x44000000, v111
	v_mul_f32_e32 v123, 0x44000000, v123
	v_mul_f32_e32 v127, 0x44000000, v127
	v_mul_f32_e32 v139, 0x44000000, v139
	v_mul_f32_e32 v143, 0x44000000, v143
	v_mul_f32_e32 v154, 0x44000000, v155
	v_mul_f32_e32 v155, 0x44000000, v159
	v_cvt_pk_fp8_f32 v80, v106, v110 op_sel:[0,0,1]
	v_cvt_pk_fp8_f32 v81, v122, v126 op_sel:[0,0,1]
	v_cvt_pk_fp8_f32 v82, v138, v142 op_sel:[0,0,1]
	v_cvt_pk_fp8_f32 v83, v152, v153 op_sel:[0,0,1]
	s_cmp_le_i32 s2, s3
	v_cvt_pk_fp8_f32 v84, v107, v111 op_sel:[0,0,1]
	v_cvt_pk_fp8_f32 v85, v123, v127 op_sel:[0,0,1]
	v_cvt_pk_fp8_f32 v86, v139, v143 op_sel:[0,0,1]
	v_cvt_pk_fp8_f32 v87, v154, v155 op_sel:[0,0,1]
	global_store_dwordx4 v[16:17], v[72:75], off sc1 nt
	global_store_dwordx4 v[16:17], v[76:79], off offset:2048 sc1 nt
	global_store_dwordx4 v[18:19], v[80:83], off sc1 nt
	global_store_dwordx4 v[18:19], v[84:87], off offset:2048 sc1 nt
	s_cbranch_scc1 .LBB0_54

.LBB0_68:
	v_lshlrev_b32_e32 v1, 1, v0
	v_and_b32_e32 v130, -16, v1
	v_lshlrev_b32_e32 v0, 2, v0
	v_and_b32_e32 v48, 28, v0
	v_mad_i64_i32 v[0:1], s[18:19], s16, v130, 0
	v_mov_b32_e32 v67, 0
	v_lshl_add_u64 v[0:1], v[0:1], 2, s[14:15]
	v_lshlrev_b32_e32 v66, 2, v48
	s_mov_b32 s3, 0
	v_lshl_add_u64 v[62:63], v[0:1], 0, v[66:67]
	s_mul_i32 s2, s16, 60
	v_lshl_add_u64 v[24:25], v[62:63], 0, s[2:3]
	s_lshl_b32 s2, s16, 2
	s_sub_u32 s2, 0, s2
	s_subb_u32 s3, 0, 0
	v_lshl_add_u64 v[0:1], v[24:25], 0, s[2:3]
	v_lshl_add_u64 v[8:9], v[0:1], 0, s[2:3]
	global_load_dwordx4 v[0:3], v[0:1], off sc1 nt
	s_nop 0
	global_load_dwordx4 v[4:7], v[8:9], off sc1 nt
	v_lshl_add_u64 v[8:9], v[8:9], 0, s[2:3]
	v_lshl_add_u64 v[16:17], v[8:9], 0, s[2:3]
	global_load_dwordx4 v[8:11], v[8:9], off sc1 nt
	s_nop 0
	global_load_dwordx4 v[12:15], v[16:17], off sc1 nt
	v_lshl_add_u64 v[16:17], v[16:17], 0, s[2:3]
	v_lshl_add_u64 v[26:27], v[16:17], 0, s[2:3]
	global_load_dwordx4 v[16:19], v[16:17], off sc1 nt
	s_nop 0
	global_load_dwordx4 v[20:23], v[26:27], off sc1 nt
	v_lshl_add_u64 v[26:27], v[26:27], 0, s[2:3]
	global_load_dwordx4 v[28:31], v[26:27], off sc1 nt
	v_lshl_add_u64 v[26:27], v[26:27], 0, s[2:3]
	global_load_dwordx4 v[32:35], v[26:27], off sc1 nt
	v_lshl_add_u64 v[26:27], v[26:27], 0, s[2:3]
	global_load_dwordx4 v[36:39], v[26:27], off sc1 nt
	v_lshl_add_u64 v[26:27], v[26:27], 0, s[2:3]
	global_load_dwordx4 v[40:43], v[26:27], off sc1 nt
	v_lshl_add_u64 v[26:27], v[26:27], 0, s[2:3]
	global_load_dwordx4 v[44:47], v[26:27], off sc1 nt
	v_lshl_add_u64 v[26:27], v[26:27], 0, s[2:3]
	global_load_dwordx4 v[50:53], v[26:27], off sc1 nt
	v_lshl_add_u64 v[26:27], v[26:27], 0, s[2:3]
	global_load_dwordx4 v[54:57], v[26:27], off sc1 nt
	v_lshl_add_u64 v[26:27], v[26:27], 0, s[2:3]
	global_load_dwordx4 v[58:61], v[26:27], off sc1 nt
	s_nop 0
	global_load_dwordx4 v[24:27], v[24:25], off sc1 nt
	s_nop 0
	global_load_dwordx4 v[62:65], v[62:63], off sc1 nt
	v_ashrrev_i32_e32 v131, 31, v130
	s_and_b64 vcc, exec, s[12:13]
	s_cbranch_vccz .LBB0_71
	s_cmp_lt_u32 s0, 0x18000
	s_cbranch_scc0 .LBB0_72
	s_addk_i32 s1, 0xf0ff
	s_lshr_b32 s14, s1, 10
	s_mov_b32 s15, 0
	s_lshl_b64 s[2:3], s[14:15], 22
	s_lshl_b64 s[12:13], s[14:15], 24
	s_add_u32 s1, s70, s12
	s_addc_u32 s16, s71, s13
	s_add_u32 s2, s90, s2
	s_addc_u32 s3, s91, s3
	s_add_u32 s12, s2, 0x3b100000
	s_addc_u32 s13, s3, 0
	s_lshl_b32 s2, s0, 1
	s_and_b32 s14, s2, 0x780
	s_lshl_b32 s2, s14, 13
	s_add_u32 s1, s1, s2
	s_addc_u32 s2, s16, 0
	s_lshl_b32 s3, s0, 5
	s_and_b32 s18, s3, 0x7e0
	s_lshl_b32 s3, s18, 2
	s_add_u32 s16, s1, s3
	s_mov_b32 s19, s15
	s_addc_u32 s17, s2, 0
	s_mov_b64 s[20:21], 0
	s_branch .LBB0_73

.LBB0_77:
	s_lshl_b64 s[0:1], s[10:11], 11
	s_add_u32 s0, s4, s0
	s_addc_u32 s1, s5, s1
	s_add_u32 s8, s0, s8
	s_addc_u32 s9, s1, s9
	s_lshl_b64 s[2:3], s[18:19], 11
	s_add_u32 s0, s12, s2
	s_addc_u32 s2, s13, s3
	s_add_u32 s4, s0, s14
	v_mov_b32_e32 v49, 0
	s_addc_u32 s5, s2, s15
	v_mad_i64_i32 v[68:69], s[2:3], s20, v130, 0
	v_lshl_add_u64 v[68:69], v[68:69], 2, s[16:17]
	v_mov_b32_e32 v67, v49
	s_mov_b32 s1, 0
	v_lshl_add_u64 v[66:67], v[68:69], 0, v[66:67]
	s_lshl_b32 s0, s20, 2
	v_lshl_add_u64 v[68:69], v[66:67], 0, s[0:1]
	global_load_dwordx4 v[82:85], v[66:67], off sc1 nt
	global_load_dwordx4 v[86:89], v[68:69], off sc1 nt
	v_lshl_add_u64 v[66:67], v[68:69], 0, s[0:1]
	v_lshl_add_u64 v[68:69], v[66:67], 0, s[0:1]
	global_load_dwordx4 v[122:125], v[66:67], off sc1 nt
	global_load_dwordx4 v[126:129], v[68:69], off sc1 nt
	v_lshl_add_u64 v[66:67], v[68:69], 0, s[0:1]
	v_lshl_add_u64 v[68:69], v[66:67], 0, s[0:1]
	global_load_dwordx4 v[110:113], v[66:67], off sc1 nt
	global_load_dwordx4 v[114:117], v[68:69], off sc1 nt
	v_lshl_add_u64 v[66:67], v[68:69], 0, s[0:1]
	v_lshl_add_u64 v[68:69], v[66:67], 0, s[0:1]
	global_load_dwordx4 v[90:93], v[66:67], off sc1 nt
	global_load_dwordx4 v[94:97], v[68:69], off sc1 nt
	v_lshl_add_u64 v[66:67], v[68:69], 0, s[0:1]
	global_load_dwordx4 v[74:77], v[66:67], off sc1 nt
	v_lshl_add_u64 v[66:67], v[66:67], 0, s[0:1]
	global_load_dwordx4 v[98:101], v[66:67], off sc1 nt
	v_lshl_add_u64 v[66:67], v[66:67], 0, s[0:1]
	global_load_dwordx4 v[106:109], v[66:67], off sc1 nt
	v_lshl_add_u64 v[66:67], v[66:67], 0, s[0:1]
	global_load_dwordx4 v[118:121], v[66:67], off sc1 nt
	v_lshl_add_u64 v[66:67], v[66:67], 0, s[0:1]
	global_load_dwordx4 v[78:81], v[66:67], off sc1 nt
	v_lshl_add_u64 v[66:67], v[66:67], 0, s[0:1]
	global_load_dwordx4 v[102:105], v[66:67], off sc1 nt
	v_lshl_add_u64 v[70:71], v[66:67], 0, s[0:1]
	global_load_dwordx4 v[66:69], v[70:71], off sc1 nt
	v_lshl_add_u64 v[70:71], v[70:71], 0, s[0:1]
	global_load_dwordx4 v[70:73], v[70:71], off sc1 nt
	s_waitcnt vmcnt(29)
	v_mul_f32_e32 v8, 0x44000000, v8
	v_mul_f32_e32 v4, 0x44000000, v4
	v_mov_b32_e32 v135, v49
	v_cvt_pk_fp8_f32 v135, v8, v4
	v_mul_f32_e32 v0, 0x44000000, v0
	s_waitcnt vmcnt(17)
	v_mul_f32_e32 v4, 0x44000000, v24
	v_mov_b32_e32 v136, v49
	v_cvt_pk_fp8_f32 v135, v0, v4 op_sel:[0,0,1]
	s_waitcnt vmcnt(16)
	v_mul_f32_e32 v0, 0x44000000, v63
	v_mul_f32_e32 v4, 0x44000000, v59
	v_cvt_pk_fp8_f32 v136, v0, v4
	v_mul_f32_e32 v0, 0x44000000, v45
	v_mul_f32_e32 v4, 0x44000000, v41
	v_mov_b32_e32 v137, v49
	v_cvt_pk_fp8_f32 v137, v0, v4
	v_mul_f32_e32 v28, 0x44000000, v28
	v_mul_f32_e32 v20, 0x44000000, v20
	v_mov_b32_e32 v134, v49
	v_mul_f32_e32 v0, 0x44000000, v37
	v_mul_f32_e32 v4, 0x44000000, v33
	v_mul_f32_e32 v62, 0x44000000, v62
	v_mul_f32_e32 v58, 0x44000000, v58
	v_mov_b32_e32 v132, v49
	v_mul_f32_e32 v44, 0x44000000, v44
	v_mul_f32_e32 v40, 0x44000000, v40
	v_mov_b32_e32 v133, v49
	v_cvt_pk_fp8_f32 v134, v28, v20
	v_cvt_pk_fp8_f32 v137, v0, v4 op_sel:[0,0,1]
	v_mul_f32_e32 v0, 0x44000000, v29
	v_mul_f32_e32 v4, 0x44000000, v21
	v_mov_b32_e32 v138, v49
	v_cvt_pk_fp8_f32 v132, v62, v58
	v_cvt_pk_fp8_f32 v133, v44, v40
	v_cvt_pk_fp8_f32 v138, v0, v4
	v_mul_f32_e32 v0, 0x44000000, v9
	v_mul_f32_e32 v4, 0x44000000, v5
	v_mov_b32_e32 v139, v49
	v_cvt_pk_fp8_f32 v139, v0, v4
	v_mul_f32_e32 v16, 0x44000000, v16
	v_mul_f32_e32 v12, 0x44000000, v12
	v_mul_f32_e32 v54, 0x44000000, v54
	v_mul_f32_e32 v50, 0x44000000, v50
	v_mul_f32_e32 v36, 0x44000000, v36
	v_mul_f32_e32 v32, 0x44000000, v32
	v_cvt_pk_fp8_f32 v134, v16, v12 op_sel:[0,0,1]
	v_mul_f32_e32 v8, 0x44000000, v55
	v_mul_f32_e32 v12, 0x44000000, v51
	v_cvt_pk_fp8_f32 v132, v54, v50 op_sel:[0,0,1]
	v_cvt_pk_fp8_f32 v133, v36, v32 op_sel:[0,0,1]
	v_cvt_pk_fp8_f32 v136, v8, v12 op_sel:[0,0,1]
	v_mul_f32_e32 v8, 0x44000000, v17
	v_mul_f32_e32 v12, 0x44000000, v13
	v_mul_f32_e32 v0, 0x44000000, v1
	v_mul_f32_e32 v1, 0x44000000, v25
	v_lshlrev_b32_e32 v48, 11, v48
	v_cvt_pk_fp8_f32 v138, v8, v12 op_sel:[0,0,1]
	v_cvt_pk_fp8_f32 v139, v0, v1 op_sel:[0,0,1]
	v_lshl_add_u64 v[0:1], s[8:9], 0, v[48:49]
	v_lshl_add_u64 v[0:1], v[0:1], 0, v[130:131]
	global_store_dwordx4 v[0:1], v[132:135], off sc1 nt
	global_store_dwordx4 v[0:1], v[136:139], off offset:2048 sc1 nt
	v_mul_f32_e32 v4, 0x44000000, v64
	v_mul_f32_e32 v5, 0x44000000, v60
	v_mov_b32_e32 v132, v49
	v_cvt_pk_fp8_f32 v132, v4, v5
	v_mul_f32_e32 v4, 0x44000000, v46
	v_mul_f32_e32 v5, 0x44000000, v42
	v_mov_b32_e32 v133, v49
	v_cvt_pk_fp8_f32 v133, v4, v5
	v_mul_f32_e32 v4, 0x44000000, v38
	v_mul_f32_e32 v5, 0x44000000, v34
	v_mov_b32_e32 v134, v49
	v_cvt_pk_fp8_f32 v133, v4, v5 op_sel:[0,0,1]
	v_mul_f32_e32 v4, 0x44000000, v30
	v_mul_f32_e32 v5, 0x44000000, v22
	v_cvt_pk_fp8_f32 v134, v4, v5
	v_mul_f32_e32 v4, 0x44000000, v10
	v_mul_f32_e32 v5, 0x44000000, v6
	v_mov_b32_e32 v135, v49
	v_cvt_pk_fp8_f32 v135, v4, v5
	v_mul_f32_e32 v8, 0x44000000, v56
	v_mul_f32_e32 v9, 0x44000000, v52
	v_mul_f32_e32 v2, 0x44000000, v2
	v_mul_f32_e32 v4, 0x44000000, v26
	v_cvt_pk_fp8_f32 v132, v8, v9 op_sel:[0,0,1]
	v_mul_f32_e32 v8, 0x44000000, v18
	v_mul_f32_e32 v9, 0x44000000, v14
	v_cvt_pk_fp8_f32 v135, v2, v4 op_sel:[0,0,1]
	v_mul_f32_e32 v2, 0x44000000, v65
	v_mul_f32_e32 v5, 0x44000000, v61
	v_mov_b32_e32 v4, v49
	v_cvt_pk_fp8_f32 v134, v8, v9 op_sel:[0,0,1]
	v_cvt_pk_fp8_f32 v4, v2, v5
	v_mul_f32_e32 v2, 0x44000000, v47
	v_mul_f32_e32 v9, 0x44000000, v43
	v_mov_b32_e32 v5, v49
	v_cvt_pk_fp8_f32 v5, v2, v9
	v_mul_f32_e32 v6, 0x44000000, v57
	v_mul_f32_e32 v8, 0x44000000, v53
	v_cvt_pk_fp8_f32 v4, v6, v8 op_sel:[0,0,1]
	v_mul_f32_e32 v2, 0x44000000, v39
	v_mul_f32_e32 v6, 0x44000000, v35
	v_cvt_pk_fp8_f32 v5, v2, v6 op_sel:[0,0,1]
	v_mul_f32_e32 v2, 0x44000000, v31
	v_mul_f32_e32 v8, 0x44000000, v23
	v_mov_b32_e32 v6, v49
	v_cvt_pk_fp8_f32 v6, v2, v8
	v_mul_f32_e32 v2, 0x44000000, v11
	v_mul_f32_e32 v8, 0x44000000, v7
	v_mov_b32_e32 v7, v49
	v_cvt_pk_fp8_f32 v7, v2, v8
	v_mul_f32_e32 v9, 0x44000000, v19
	v_mul_f32_e32 v10, 0x44000000, v15
	v_mul_f32_e32 v2, 0x44000000, v3
	v_mul_f32_e32 v3, 0x44000000, v27
	s_movk_i32 s0, 0x1000
	v_cvt_pk_fp8_f32 v6, v9, v10 op_sel:[0,0,1]
	v_cvt_pk_fp8_f32 v7, v2, v3 op_sel:[0,0,1]
	v_add_co_u32_e32 v0, vcc, s0, v0
	s_waitcnt vmcnt(16)
	v_mul_f32_e32 v2, 0x44000000, v86
	v_addc_co_u32_e32 v1, vcc, 0, v1, vcc
	global_store_dwordx4 v[0:1], v[132:135], off sc1 nt
	global_store_dwordx4 v[0:1], v[4:7], off offset:2048 sc1 nt
	v_mul_f32_e32 v1, 0x44000000, v82
	v_mov_b32_e32 v0, v49
	v_cvt_pk_fp8_f32 v0, v1, v2
	s_waitcnt vmcnt(15)
	v_mul_f32_e32 v2, 0x44000000, v110
	s_waitcnt vmcnt(14)
	v_mul_f32_e32 v5, 0x44000000, v114
	v_mov_b32_e32 v1, v49
	v_cvt_pk_fp8_f32 v1, v2, v5
	v_mul_f32_e32 v3, 0x44000000, v122
	v_mul_f32_e32 v4, 0x44000000, v126
	v_cvt_pk_fp8_f32 v0, v3, v4 op_sel:[0,0,1]
	s_waitcnt vmcnt(13)
	v_mul_f32_e32 v2, 0x44000000, v90
	s_waitcnt vmcnt(12)
	v_mul_f32_e32 v3, 0x44000000, v94
	v_cvt_pk_fp8_f32 v1, v2, v3 op_sel:[0,0,1]
	s_waitcnt vmcnt(11)
	v_mul_f32_e32 v3, 0x44000000, v74
	s_waitcnt vmcnt(10)
	v_mul_f32_e32 v4, 0x44000000, v98
	v_mov_b32_e32 v2, v49
	v_cvt_pk_fp8_f32 v2, v3, v4
	s_waitcnt vmcnt(7)
	v_mul_f32_e32 v4, 0x44000000, v78
	s_waitcnt vmcnt(6)
	v_mul_f32_e32 v7, 0x44000000, v102
	v_mov_b32_e32 v3, v49
	v_cvt_pk_fp8_f32 v3, v4, v7
	v_mul_f32_e32 v5, 0x44000000, v106
	v_mul_f32_e32 v6, 0x44000000, v118
	v_cvt_pk_fp8_f32 v2, v5, v6 op_sel:[0,0,1]
	s_waitcnt vmcnt(5)
	v_mul_f32_e32 v4, 0x44000000, v66
	s_waitcnt vmcnt(4)
	v_mul_f32_e32 v5, 0x44000000, v70
	v_cvt_pk_fp8_f32 v3, v4, v5 op_sel:[0,0,1]
	v_mul_f32_e32 v5, 0x44000000, v83
	v_mul_f32_e32 v6, 0x44000000, v87
	v_mov_b32_e32 v4, v49
	v_cvt_pk_fp8_f32 v4, v5, v6
	v_mul_f32_e32 v6, 0x44000000, v111
	v_mul_f32_e32 v9, 0x44000000, v115
	v_mov_b32_e32 v5, v49
	v_cvt_pk_fp8_f32 v5, v6, v9
	v_mul_f32_e32 v7, 0x44000000, v123
	v_mul_f32_e32 v8, 0x44000000, v127
	v_cvt_pk_fp8_f32 v4, v7, v8 op_sel:[0,0,1]
	v_mul_f32_e32 v6, 0x44000000, v91
	v_mul_f32_e32 v7, 0x44000000, v95
	v_cvt_pk_fp8_f32 v5, v6, v7 op_sel:[0,0,1]
	v_mul_f32_e32 v7, 0x44000000, v75
	v_mul_f32_e32 v8, 0x44000000, v99
	v_mov_b32_e32 v6, v49
	v_cvt_pk_fp8_f32 v6, v7, v8
	v_mul_f32_e32 v8, 0x44000000, v79
	v_mul_f32_e32 v11, 0x44000000, v103
	v_mov_b32_e32 v7, v49
	v_cvt_pk_fp8_f32 v7, v8, v11
	v_mul_f32_e32 v9, 0x44000000, v107
	v_mul_f32_e32 v10, 0x44000000, v119
	v_cvt_pk_fp8_f32 v6, v9, v10 op_sel:[0,0,1]
	v_mul_f32_e32 v8, 0x44000000, v67
	v_mul_f32_e32 v9, 0x44000000, v71
	v_cvt_pk_fp8_f32 v7, v8, v9 op_sel:[0,0,1]
	v_lshl_add_u64 v[8:9], s[4:5], 0, v[48:49]
	v_lshl_add_u64 v[8:9], v[8:9], 0, v[130:131]
	global_store_dwordx4 v[8:9], v[0:3], off sc1 nt
	global_store_dwordx4 v[8:9], v[4:7], off offset:2048 sc1 nt
	v_mov_b32_e32 v46, v49
	v_mul_f32_e32 v1, 0x44000000, v84
	v_mul_f32_e32 v2, 0x44000000, v88
	v_mov_b32_e32 v0, v49
	v_cvt_pk_fp8_f32 v0, v1, v2
	v_mul_f32_e32 v2, 0x44000000, v112
	v_mul_f32_e32 v5, 0x44000000, v116
	v_mov_b32_e32 v1, v49
	v_cvt_pk_fp8_f32 v1, v2, v5
	v_mul_f32_e32 v3, 0x44000000, v124
	v_mul_f32_e32 v4, 0x44000000, v128
	v_cvt_pk_fp8_f32 v0, v3, v4 op_sel:[0,0,1]
	v_mul_f32_e32 v2, 0x44000000, v92
	v_mul_f32_e32 v3, 0x44000000, v96
	v_cvt_pk_fp8_f32 v1, v2, v3 op_sel:[0,0,1]
	v_mul_f32_e32 v3, 0x44000000, v76
	v_mul_f32_e32 v4, 0x44000000, v100
	v_mov_b32_e32 v2, v49
	v_cvt_pk_fp8_f32 v2, v3, v4
	v_mul_f32_e32 v4, 0x44000000, v80
	v_mul_f32_e32 v7, 0x44000000, v104
	v_mov_b32_e32 v3, v49
	v_cvt_pk_fp8_f32 v3, v4, v7
	v_mul_f32_e32 v5, 0x44000000, v108
	v_mul_f32_e32 v6, 0x44000000, v120
	v_cvt_pk_fp8_f32 v2, v5, v6 op_sel:[0,0,1]
	v_mul_f32_e32 v4, 0x44000000, v68
	v_mul_f32_e32 v5, 0x44000000, v72
	v_cvt_pk_fp8_f32 v3, v4, v5 op_sel:[0,0,1]
	v_mul_f32_e32 v4, 0x44000000, v85
	v_mul_f32_e32 v5, 0x44000000, v89
	v_cvt_pk_fp8_f32 v46, v4, v5
	v_mul_f32_e32 v4, 0x44000000, v113
	v_mul_f32_e32 v5, 0x44000000, v117
	v_mov_b32_e32 v47, v49
	v_cvt_pk_fp8_f32 v47, v4, v5
	v_mul_f32_e32 v4, 0x44000000, v93
	v_mul_f32_e32 v5, 0x44000000, v97
	v_mov_b32_e32 v48, v49
	v_cvt_pk_fp8_f32 v47, v4, v5 op_sel:[0,0,1]
	v_mul_f32_e32 v4, 0x44000000, v77
	v_mul_f32_e32 v5, 0x44000000, v101
	v_cvt_pk_fp8_f32 v48, v4, v5
	v_mul_f32_e32 v4, 0x44000000, v81
	v_mul_f32_e32 v5, 0x44000000, v105
	v_cvt_pk_fp8_f32 v49, v4, v5
	v_mul_f32_e32 v6, 0x44000000, v125
	v_mul_f32_e32 v7, 0x44000000, v129
	v_cvt_pk_fp8_f32 v46, v6, v7 op_sel:[0,0,1]
	v_mul_f32_e32 v6, 0x44000000, v109
	v_mul_f32_e32 v7, 0x44000000, v121
	v_mul_f32_e32 v4, 0x44000000, v69
	v_mul_f32_e32 v5, 0x44000000, v73
	v_cvt_pk_fp8_f32 v48, v6, v7 op_sel:[0,0,1]
	v_cvt_pk_fp8_f32 v49, v4, v5 op_sel:[0,0,1]
	v_add_co_u32_e32 v4, vcc, s0, v8
	s_nop 1
	v_addc_co_u32_e32 v5, vcc, 0, v9, vcc
	global_store_dwordx4 v[4:5], v[0:3], off sc1 nt
	global_store_dwordx4 v[4:5], v[46:49], off offset:2048 sc1 nt
	s_waitcnt vmcnt(0)

.LBB0_152:
	s_not_b32 s1, s0
	s_add_i32 s1, s33, s1
	s_cmp_lt_i32 s1, -7
	s_cbranch_scc1 .LBB0_172
	s_ashr_i32 s2, s1, 31
	v_lshlrev_b32_e32 v1, 1, v0
	s_lshr_b32 s2, s2, 29
	v_and_b32_e32 v128, -16, v1
	v_lshlrev_b32_e32 v0, 2, v0
	s_add_i32 s2, s1, s2
	v_and_b32_e32 v64, 28, v0
	s_ashr_i32 s1, s2, 3
	s_and_b32 s2, s2, -8
	v_mad_i64_i32 v[0:1], s[6:7], s20, v128, 0
	v_mov_b32_e32 v131, 0
	s_add_i32 s2, s2, s0
	v_lshl_add_u64 v[0:1], v[0:1], 2, s[18:19]
	v_lshlrev_b32_e32 v130, 2, v64
	s_lshl_b32 s3, s20, 2
	s_mov_b32 s5, 0
	s_waitcnt vmcnt(4)
	v_lshl_add_u64 v[60:61], v[0:1], 0, v[130:131]
	s_mul_i32 s4, s20, 60
	s_sub_u32 s6, 0, s3
	v_lshl_add_u64 v[44:45], v[60:61], 0, s[4:5]
	s_subb_u32 s7, 0, 0
	v_lshl_add_u64 v[0:1], v[44:45], 0, s[6:7]
	v_lshl_add_u64 v[8:9], v[0:1], 0, s[6:7]
	global_load_dwordx4 v[0:3], v[0:1], off sc1 nt
	s_nop 0
	global_load_dwordx4 v[4:7], v[8:9], off sc1 nt
	v_lshl_add_u64 v[8:9], v[8:9], 0, s[6:7]
	v_lshl_add_u64 v[16:17], v[8:9], 0, s[6:7]
	global_load_dwordx4 v[8:11], v[8:9], off sc1 nt
	s_nop 0
	global_load_dwordx4 v[12:15], v[16:17], off sc1 nt
	v_lshl_add_u64 v[16:17], v[16:17], 0, s[6:7]
	v_lshl_add_u64 v[24:25], v[16:17], 0, s[6:7]
	v_lshl_add_u64 v[28:29], v[24:25], 0, s[6:7]
	v_lshl_add_u64 v[32:33], v[28:29], 0, s[6:7]
	v_lshl_add_u64 v[36:37], v[32:33], 0, s[6:7]
	v_lshl_add_u64 v[40:41], v[36:37], 0, s[6:7]
	v_lshl_add_u64 v[46:47], v[40:41], 0, s[6:7]
	global_load_dwordx4 v[16:19], v[16:17], off sc1 nt
	s_nop 0
	global_load_dwordx4 v[20:23], v[24:25], off sc1 nt
	s_mov_b64 s[34:35], s[24:25]
	global_load_dwordx4 v[24:27], v[28:29], off sc1 nt
	s_mov_b64 s[30:31], s[22:23]
	global_load_dwordx4 v[28:31], v[32:33], off sc1 nt
	v_ashrrev_i32_e32 v129, 31, v128
	global_load_dwordx4 v[32:35], v[36:37], off sc1 nt
	v_lshlrev_b32_e32 v132, 11, v64
	global_load_dwordx4 v[36:39], v[40:41], off sc1 nt
	v_mov_b32_e32 v133, v131
	global_load_dwordx4 v[40:43], v[46:47], off sc1 nt
	v_lshl_add_u64 v[46:47], v[46:47], 0, s[6:7]
	global_load_dwordx4 v[48:51], v[46:47], off sc1 nt
	v_lshl_add_u64 v[46:47], v[46:47], 0, s[6:7]
	global_load_dwordx4 v[56:59], v[46:47], off sc1 nt
	v_lshl_add_u64 v[46:47], v[46:47], 0, s[6:7]
	global_load_dwordx4 v[52:55], v[46:47], off sc1 nt
	s_nop 0
	global_load_dwordx4 v[44:47], v[44:45], off sc1 nt
	s_nop 0
	global_load_dwordx4 v[60:63], v[60:61], off sc1 nt
	s_lshl_b64 s[6:7], s[16:17], 11
	s_add_u32 s3, s12, s6
	s_addc_u32 s4, s13, s7
	s_add_u32 s14, s3, s14
	s_addc_u32 s15, s4, s15
	s_add_u32 s3, s90, 0x3b100000
	s_addc_u32 s6, s91, 0
	s_add_u32 s12, s90, 0x1900000
	s_addc_u32 s13, s91, 0
	s_add_u32 s7, s90, 0x4b100000
	s_addc_u32 s8, s91, 0
	v_lshlrev_b32_e32 v130, 2, v64
	s_movk_i32 s9, 0x1000
	s_mov_b32 s10, 0
	s_branch .LBB0_155
.LBB0_154:
	s_lshl_b64 s[18:19], s[18:19], 11
	s_add_u32 s4, s16, s18
	s_addc_u32 s11, s17, s19
	s_add_u32 s16, s4, s20
	s_addc_u32 s17, s11, s21
	s_lshl_b64 s[18:19], s[24:25], 11
	s_add_u32 s4, s14, s18
	s_addc_u32 s11, s15, s19
	v_mad_i64_i32 v[0:1], s[18:19], s28, v128, 0
	s_add_u32 s14, s4, s26
	v_lshl_add_u64 v[0:1], v[0:1], 2, s[22:23]
	s_addc_u32 s15, s11, s27
	v_lshl_add_u64 v[0:1], v[0:1], 0, v[130:131]
	s_lshl_b32 s4, s28, 2
	v_lshl_add_u64 v[2:3], v[0:1], 0, s[4:5]
	global_load_dwordx4 v[60:63], v[0:1], off sc1 nt
	global_load_dwordx4 v[52:55], v[2:3], off sc1 nt
	v_lshl_add_u64 v[0:1], v[2:3], 0, s[4:5]
	v_lshl_add_u64 v[2:3], v[0:1], 0, s[4:5]
	global_load_dwordx4 v[56:59], v[0:1], off sc1 nt
	global_load_dwordx4 v[48:51], v[2:3], off sc1 nt
	v_lshl_add_u64 v[0:1], v[2:3], 0, s[4:5]
	v_lshl_add_u64 v[2:3], v[0:1], 0, s[4:5]
	global_load_dwordx4 v[40:43], v[0:1], off sc1 nt
	global_load_dwordx4 v[36:39], v[2:3], off sc1 nt
	v_lshl_add_u64 v[0:1], v[2:3], 0, s[4:5]
	v_lshl_add_u64 v[2:3], v[0:1], 0, s[4:5]
	global_load_dwordx4 v[32:35], v[0:1], off sc1 nt
	global_load_dwordx4 v[28:31], v[2:3], off sc1 nt
	v_lshl_add_u64 v[0:1], v[2:3], 0, s[4:5]
	global_load_dwordx4 v[24:27], v[0:1], off sc1 nt
	v_lshl_add_u64 v[0:1], v[0:1], 0, s[4:5]
	global_load_dwordx4 v[20:23], v[0:1], off sc1 nt
	v_lshl_add_u64 v[0:1], v[0:1], 0, s[4:5]
	global_load_dwordx4 v[16:19], v[0:1], off sc1 nt
	v_lshl_add_u64 v[0:1], v[0:1], 0, s[4:5]
	global_load_dwordx4 v[12:15], v[0:1], off sc1 nt
	v_lshl_add_u64 v[0:1], v[0:1], 0, s[4:5]
	global_load_dwordx4 v[8:11], v[0:1], off sc1 nt
	v_lshl_add_u64 v[0:1], v[0:1], 0, s[4:5]
	v_lshl_add_u64 v[44:45], v[0:1], 0, s[4:5]
	global_load_dwordx4 v[4:7], v[0:1], off sc1 nt
	s_waitcnt vmcnt(33)
	v_mul_f32_e32 v80, 0x44000000, v80
	global_load_dwordx4 v[0:3], v[44:45], off sc1 nt
	v_lshl_add_u64 v[44:45], v[44:45], 0, s[4:5]
	global_load_dwordx4 v[44:47], v[44:45], off sc1 nt
	s_waitcnt vmcnt(34)
	v_mul_f32_e32 v84, 0x44000000, v84
	v_mov_b32_e32 v134, v131
	v_cvt_pk_fp8_f32 v134, v80, v84
	s_waitcnt vmcnt(31)
	v_mul_f32_e32 v80, 0x44000000, v108
	s_waitcnt vmcnt(30)
	v_mul_f32_e32 v84, 0x44000000, v112
	v_mov_b32_e32 v135, v131
	v_cvt_pk_fp8_f32 v135, v80, v84
	s_waitcnt vmcnt(29)
	v_mul_f32_e32 v80, 0x44000000, v88
	s_waitcnt vmcnt(28)
	v_mul_f32_e32 v84, 0x44000000, v92
	s_waitcnt vmcnt(27)
	v_mul_f32_e32 v72, 0x44000000, v72
	v_cvt_pk_fp8_f32 v135, v80, v84 op_sel:[0,0,1]
	s_waitcnt vmcnt(26)
	v_mul_f32_e32 v80, 0x44000000, v96
	v_mov_b32_e32 v136, v131
	v_cvt_pk_fp8_f32 v136, v72, v80
	s_waitcnt vmcnt(23)
	v_mul_f32_e32 v72, 0x44000000, v76
	s_waitcnt vmcnt(22)
	v_mul_f32_e32 v76, 0x44000000, v100
	v_mov_b32_e32 v137, v131
	v_cvt_pk_fp8_f32 v137, v72, v76
	s_waitcnt vmcnt(21)
	v_mul_f32_e32 v64, 0x44000000, v64
	s_waitcnt vmcnt(20)
	v_mul_f32_e32 v68, 0x44000000, v68
	v_mov_b32_e32 v138, v131
	v_cvt_pk_fp8_f32 v137, v64, v68 op_sel:[0,0,1]
	v_mul_f32_e32 v64, 0x44000000, v81
	v_mul_f32_e32 v68, 0x44000000, v85
	v_cvt_pk_fp8_f32 v138, v64, v68
	v_mul_f32_e32 v64, 0x44000000, v109
	v_mul_f32_e32 v68, 0x44000000, v113
	v_mov_b32_e32 v139, v131
	v_cvt_pk_fp8_f32 v139, v64, v68
	v_mul_f32_e32 v64, 0x44000000, v89
	v_mul_f32_e32 v68, 0x44000000, v93
	v_mov_b32_e32 v140, v131
	v_cvt_pk_fp8_f32 v139, v64, v68 op_sel:[0,0,1]
	v_mul_f32_e32 v64, 0x44000000, v73
	v_mul_f32_e32 v68, 0x44000000, v97
	v_cvt_pk_fp8_f32 v140, v64, v68
	v_mul_f32_e32 v64, 0x44000000, v77
	v_mul_f32_e32 v68, 0x44000000, v101
	v_mov_b32_e32 v141, v131
	v_cvt_pk_fp8_f32 v141, v64, v68
	v_mul_f32_e32 v120, 0x44000000, v120
	v_mul_f32_e32 v124, 0x44000000, v124
	v_mul_f32_e32 v84, 0x44000000, v104
	v_mul_f32_e32 v88, 0x44000000, v116
	v_mul_f32_e32 v72, 0x44000000, v121
	v_mul_f32_e32 v76, 0x44000000, v125
	v_cvt_pk_fp8_f32 v134, v120, v124 op_sel:[0,0,1]
	v_cvt_pk_fp8_f32 v136, v84, v88 op_sel:[0,0,1]
	v_cvt_pk_fp8_f32 v138, v72, v76 op_sel:[0,0,1]
	v_mul_f32_e32 v72, 0x44000000, v105
	v_mul_f32_e32 v73, 0x44000000, v117
	v_mul_f32_e32 v64, 0x44000000, v65
	v_mul_f32_e32 v65, 0x44000000, v69
	v_cvt_pk_fp8_f32 v140, v72, v73 op_sel:[0,0,1]
	v_cvt_pk_fp8_f32 v141, v64, v65 op_sel:[0,0,1]
	v_lshl_add_u64 v[64:65], s[16:17], 0, v[132:133]
	v_lshl_add_u64 v[64:65], v[64:65], 0, v[128:129]
	global_store_dwordx4 v[64:65], v[134:137], off sc1 nt
	global_store_dwordx4 v[64:65], v[138:141], off offset:2048 sc1 nt
	v_mul_f32_e32 v68, 0x44000000, v82
	v_mul_f32_e32 v69, 0x44000000, v86
	v_mov_b32_e32 v134, v131
	v_cvt_pk_fp8_f32 v134, v68, v69
	v_mul_f32_e32 v68, 0x44000000, v110
	v_mul_f32_e32 v69, 0x44000000, v114
	v_mov_b32_e32 v135, v131
	v_cvt_pk_fp8_f32 v135, v68, v69
	v_mul_f32_e32 v68, 0x44000000, v90
	v_mul_f32_e32 v69, 0x44000000, v94
	v_mov_b32_e32 v136, v131
	v_cvt_pk_fp8_f32 v135, v68, v69 op_sel:[0,0,1]
	v_mul_f32_e32 v68, 0x44000000, v74
	v_mul_f32_e32 v69, 0x44000000, v98
	v_cvt_pk_fp8_f32 v136, v68, v69
	v_mul_f32_e32 v68, 0x44000000, v78
	v_mul_f32_e32 v69, 0x44000000, v102
	v_mov_b32_e32 v137, v131
	v_cvt_pk_fp8_f32 v137, v68, v69
	v_mul_f32_e32 v72, 0x44000000, v122
	v_mul_f32_e32 v73, 0x44000000, v126
	v_cvt_pk_fp8_f32 v134, v72, v73 op_sel:[0,0,1]
	v_mul_f32_e32 v72, 0x44000000, v106
	v_mul_f32_e32 v73, 0x44000000, v118
	v_mul_f32_e32 v66, 0x44000000, v66
	v_mul_f32_e32 v68, 0x44000000, v70
	v_cvt_pk_fp8_f32 v136, v72, v73 op_sel:[0,0,1]
	v_cvt_pk_fp8_f32 v137, v66, v68 op_sel:[0,0,1]
	v_mul_f32_e32 v66, 0x44000000, v83
	v_mul_f32_e32 v68, 0x44000000, v87
	v_mov_b32_e32 v72, v131
	v_cvt_pk_fp8_f32 v72, v66, v68
	v_mul_f32_e32 v66, 0x44000000, v111
	v_mul_f32_e32 v68, 0x44000000, v115
	v_mov_b32_e32 v73, v131
	v_cvt_pk_fp8_f32 v73, v66, v68
	v_mul_f32_e32 v66, 0x44000000, v91
	v_mul_f32_e32 v68, 0x44000000, v95
	v_mov_b32_e32 v74, v131
	v_cvt_pk_fp8_f32 v73, v66, v68 op_sel:[0,0,1]
	v_mul_f32_e32 v66, 0x44000000, v75
	v_mul_f32_e32 v68, 0x44000000, v99
	v_cvt_pk_fp8_f32 v74, v66, v68
	v_mul_f32_e32 v66, 0x44000000, v79
	v_mul_f32_e32 v68, 0x44000000, v103
	v_mov_b32_e32 v75, v131
	v_cvt_pk_fp8_f32 v75, v66, v68
	v_mul_f32_e32 v69, 0x44000000, v123
	v_mul_f32_e32 v70, 0x44000000, v127
	v_cvt_pk_fp8_f32 v72, v69, v70 op_sel:[0,0,1]
	v_mul_f32_e32 v69, 0x44000000, v107
	v_mul_f32_e32 v70, 0x44000000, v119
	v_mul_f32_e32 v66, 0x44000000, v67
	v_mul_f32_e32 v67, 0x44000000, v71
	v_cvt_pk_fp8_f32 v74, v69, v70 op_sel:[0,0,1]
	v_cvt_pk_fp8_f32 v75, v66, v67 op_sel:[0,0,1]
	v_add_co_u32_e32 v64, vcc, s9, v64
	s_add_i32 s10, s10, 2
	s_nop 0
	v_addc_co_u32_e32 v65, vcc, 0, v65, vcc
	s_cmp_le_i32 s10, s1
	global_store_dwordx4 v[64:65], v[134:137], off sc1 nt
	global_store_dwordx4 v[64:65], v[72:75], off offset:2048 sc1 nt
	s_cbranch_scc0 .LBB0_171

.LBB0_163:
	v_mad_i64_i32 v[64:65], s[26:27], s24, v128, 0
	v_lshl_add_u64 v[64:65], v[64:65], 2, s[22:23]
	v_lshl_add_u64 v[64:65], v[64:65], 0, v[130:131]
	s_lshl_b32 s4, s24, 2
	v_lshl_add_u64 v[66:67], v[64:65], 0, s[4:5]
	global_load_dwordx4 v[80:83], v[64:65], off sc1 nt
	global_load_dwordx4 v[84:87], v[66:67], off sc1 nt
	v_lshl_add_u64 v[64:65], v[66:67], 0, s[4:5]
	v_lshl_add_u64 v[66:67], v[64:65], 0, s[4:5]
	global_load_dwordx4 v[120:123], v[64:65], off sc1 nt
	global_load_dwordx4 v[124:127], v[66:67], off sc1 nt
	v_lshl_add_u64 v[64:65], v[66:67], 0, s[4:5]
	v_lshl_add_u64 v[66:67], v[64:65], 0, s[4:5]
	global_load_dwordx4 v[108:111], v[64:65], off sc1 nt
	global_load_dwordx4 v[112:115], v[66:67], off sc1 nt
	v_lshl_add_u64 v[64:65], v[66:67], 0, s[4:5]
	v_lshl_add_u64 v[66:67], v[64:65], 0, s[4:5]
	global_load_dwordx4 v[88:91], v[64:65], off sc1 nt
	global_load_dwordx4 v[92:95], v[66:67], off sc1 nt
	v_lshl_add_u64 v[64:65], v[66:67], 0, s[4:5]
	global_load_dwordx4 v[72:75], v[64:65], off sc1 nt
	v_lshl_add_u64 v[64:65], v[64:65], 0, s[4:5]
	global_load_dwordx4 v[96:99], v[64:65], off sc1 nt
	v_lshl_add_u64 v[64:65], v[64:65], 0, s[4:5]
	global_load_dwordx4 v[104:107], v[64:65], off sc1 nt
	v_lshl_add_u64 v[64:65], v[64:65], 0, s[4:5]
	global_load_dwordx4 v[116:119], v[64:65], off sc1 nt
	v_lshl_add_u64 v[64:65], v[64:65], 0, s[4:5]
	global_load_dwordx4 v[76:79], v[64:65], off sc1 nt
	v_lshl_add_u64 v[64:65], v[64:65], 0, s[4:5]
	v_lshl_add_u64 v[68:69], v[64:65], 0, s[4:5]
	global_load_dwordx4 v[100:103], v[64:65], off sc1 nt
	s_waitcnt vmcnt(21)
	v_mul_f32_e32 v8, 0x44000000, v8
	global_load_dwordx4 v[64:67], v[68:69], off sc1 nt
	v_lshl_add_u64 v[68:69], v[68:69], 0, s[4:5]
	global_load_dwordx4 v[68:71], v[68:69], off sc1 nt
	s_waitcnt vmcnt(22)
	v_mul_f32_e32 v4, 0x44000000, v4
	v_mov_b32_e32 v137, v131
	v_cvt_pk_fp8_f32 v137, v8, v4
	s_waitcnt vmcnt(21)
	v_mul_f32_e32 v0, 0x44000000, v0
	s_waitcnt vmcnt(17)
	v_mul_f32_e32 v4, 0x44000000, v44
	v_mov_b32_e32 v138, v131
	v_cvt_pk_fp8_f32 v137, v0, v4 op_sel:[0,0,1]
	s_waitcnt vmcnt(16)
	v_mul_f32_e32 v0, 0x44000000, v61
	v_mul_f32_e32 v4, 0x44000000, v53
	v_cvt_pk_fp8_f32 v138, v0, v4
	v_mul_f32_e32 v0, 0x44000000, v41
	v_mul_f32_e32 v4, 0x44000000, v37
	v_mov_b32_e32 v139, v131
	v_cvt_pk_fp8_f32 v139, v0, v4
	v_mul_f32_e32 v24, 0x44000000, v24
	v_mul_f32_e32 v20, 0x44000000, v20
	v_mov_b32_e32 v136, v131
	v_mul_f32_e32 v0, 0x44000000, v33
	v_mul_f32_e32 v4, 0x44000000, v29
	v_mul_f32_e32 v60, 0x44000000, v60
	v_mul_f32_e32 v52, 0x44000000, v52
	v_mov_b32_e32 v134, v131
	v_mul_f32_e32 v40, 0x44000000, v40
	v_mul_f32_e32 v36, 0x44000000, v36
	v_mov_b32_e32 v135, v131
	v_cvt_pk_fp8_f32 v136, v24, v20
	v_cvt_pk_fp8_f32 v139, v0, v4 op_sel:[0,0,1]
	v_mul_f32_e32 v0, 0x44000000, v25
	v_mul_f32_e32 v4, 0x44000000, v21
	v_mov_b32_e32 v140, v131
	v_cvt_pk_fp8_f32 v134, v60, v52
	v_cvt_pk_fp8_f32 v135, v40, v36
	v_cvt_pk_fp8_f32 v140, v0, v4
	v_mul_f32_e32 v0, 0x44000000, v9
	v_mul_f32_e32 v4, 0x44000000, v5
	v_mov_b32_e32 v141, v131
	v_cvt_pk_fp8_f32 v141, v0, v4
	v_mul_f32_e32 v16, 0x44000000, v16
	v_mul_f32_e32 v12, 0x44000000, v12
	v_mul_f32_e32 v56, 0x44000000, v56
	v_mul_f32_e32 v48, 0x44000000, v48
	v_mul_f32_e32 v32, 0x44000000, v32
	v_mul_f32_e32 v28, 0x44000000, v28
	v_cvt_pk_fp8_f32 v136, v16, v12 op_sel:[0,0,1]
	v_mul_f32_e32 v8, 0x44000000, v57
	v_mul_f32_e32 v12, 0x44000000, v49
	v_cvt_pk_fp8_f32 v134, v56, v48 op_sel:[0,0,1]
	v_cvt_pk_fp8_f32 v135, v32, v28 op_sel:[0,0,1]
	v_cvt_pk_fp8_f32 v138, v8, v12 op_sel:[0,0,1]
	v_mul_f32_e32 v8, 0x44000000, v17
	v_mul_f32_e32 v12, 0x44000000, v13
	v_mul_f32_e32 v0, 0x44000000, v1
	v_mul_f32_e32 v1, 0x44000000, v45
	v_cvt_pk_fp8_f32 v140, v8, v12 op_sel:[0,0,1]
	v_cvt_pk_fp8_f32 v141, v0, v1 op_sel:[0,0,1]
	v_lshl_add_u64 v[0:1], s[14:15], 0, v[132:133]
	v_lshl_add_u64 v[0:1], v[0:1], 0, v[128:129]
	global_store_dwordx4 v[0:1], v[134:137], off sc1 nt
	global_store_dwordx4 v[0:1], v[138:141], off offset:2048 sc1 nt
	v_mul_f32_e32 v4, 0x44000000, v62
	v_mul_f32_e32 v5, 0x44000000, v54
	v_mov_b32_e32 v134, v131
	v_cvt_pk_fp8_f32 v134, v4, v5
	v_mul_f32_e32 v4, 0x44000000, v42
	v_mul_f32_e32 v5, 0x44000000, v38
	v_mov_b32_e32 v135, v131
	v_cvt_pk_fp8_f32 v135, v4, v5
	v_mul_f32_e32 v4, 0x44000000, v34
	v_mul_f32_e32 v5, 0x44000000, v30
	v_mov_b32_e32 v136, v131
	v_cvt_pk_fp8_f32 v135, v4, v5 op_sel:[0,0,1]
	v_mul_f32_e32 v4, 0x44000000, v26
	v_mul_f32_e32 v5, 0x44000000, v22
	v_cvt_pk_fp8_f32 v136, v4, v5
	v_mul_f32_e32 v4, 0x44000000, v10
	v_mul_f32_e32 v5, 0x44000000, v6
	v_mov_b32_e32 v137, v131
	v_cvt_pk_fp8_f32 v137, v4, v5
	v_mul_f32_e32 v8, 0x44000000, v58
	v_mul_f32_e32 v9, 0x44000000, v50
	v_mul_f32_e32 v2, 0x44000000, v2
	v_mul_f32_e32 v4, 0x44000000, v46
	v_cvt_pk_fp8_f32 v134, v8, v9 op_sel:[0,0,1]
	v_mul_f32_e32 v8, 0x44000000, v18
	v_mul_f32_e32 v9, 0x44000000, v14
	v_cvt_pk_fp8_f32 v137, v2, v4 op_sel:[0,0,1]
	v_mul_f32_e32 v2, 0x44000000, v63
	v_mul_f32_e32 v5, 0x44000000, v55
	v_mov_b32_e32 v4, v131
	v_cvt_pk_fp8_f32 v136, v8, v9 op_sel:[0,0,1]
	v_cvt_pk_fp8_f32 v4, v2, v5
	v_mul_f32_e32 v2, 0x44000000, v43
	v_mul_f32_e32 v9, 0x44000000, v39
	v_mov_b32_e32 v5, v131
	v_cvt_pk_fp8_f32 v5, v2, v9
	v_mul_f32_e32 v6, 0x44000000, v59
	v_mul_f32_e32 v8, 0x44000000, v51
	v_cvt_pk_fp8_f32 v4, v6, v8 op_sel:[0,0,1]
	v_mul_f32_e32 v2, 0x44000000, v35
	v_mul_f32_e32 v6, 0x44000000, v31
	v_cvt_pk_fp8_f32 v5, v2, v6 op_sel:[0,0,1]
	v_mul_f32_e32 v2, 0x44000000, v27
	v_mul_f32_e32 v8, 0x44000000, v23
	v_mov_b32_e32 v6, v131
	v_cvt_pk_fp8_f32 v6, v2, v8
	v_mul_f32_e32 v2, 0x44000000, v11
	v_mul_f32_e32 v8, 0x44000000, v7
	v_mov_b32_e32 v7, v131
	v_cvt_pk_fp8_f32 v7, v2, v8
	v_mul_f32_e32 v9, 0x44000000, v19
	v_mul_f32_e32 v10, 0x44000000, v15
	v_mul_f32_e32 v2, 0x44000000, v3
	v_mul_f32_e32 v3, 0x44000000, v47
	s_add_i32 s0, s0, 16
	v_cvt_pk_fp8_f32 v6, v9, v10 op_sel:[0,0,1]
	v_cvt_pk_fp8_f32 v7, v2, v3 op_sel:[0,0,1]
	s_min_i32 s0, s0, s2
	v_add_co_u32_e32 v0, vcc, s9, v0
	s_cmp_gt_i32 s0, 0xffff
	s_nop 0
	v_addc_co_u32_e32 v1, vcc, 0, v1, vcc
	s_mov_b64 s[28:29], -1
	global_store_dwordx4 v[0:1], v[134:137], off sc1 nt
	global_store_dwordx4 v[0:1], v[4:7], off offset:2048 sc1 nt
	s_cbranch_scc0 .LBB0_169
	s_cmp_lt_u32 s0, 0x18000
	s_cbranch_scc0 .LBB0_166
	s_add_i32 s4, s0, 0xffff0000
	s_lshr_b32 s4, s4, 10
	s_lshl_b64 s[14:15], s[4:5], 22
	s_lshl_b64 s[22:23], s[4:5], 24
	s_add_u32 s11, s70, s22
	s_addc_u32 s22, s71, s23
	s_add_u32 s14, s3, s14
	s_addc_u32 s15, s6, s15
	s_lshl_b32 s4, s0, 1
	s_and_b32 s4, s4, 0x780
	s_lshl_b32 s23, s4, 13
	s_add_u32 s11, s11, s23
	s_addc_u32 s23, s22, 0
	s_lshl_b32 s22, s0, 5
	s_and_b32 s24, s22, 0x7e0
	s_lshl_b32 s22, s24, 2
	s_add_u32 s22, s11, s22
	s_mov_b32 s25, s5
	s_addc_u32 s23, s23, 0
	s_mov_b64 s[28:29], 0
	s_mov_b64 s[26:27], s[4:5]

.LBB0_175:
	v_readlane_b32 s0, v255, 0
	s_cmpk_gt_u32 s0, 0xff
	s_cbranch_scc1 .LBB0_177
	v_readlane_b32 s3, v255, 4
	s_lshl_b32 s0, s3, 2
	v_readlane_b32 s1, v255, 28
	s_or_b32 s2, s0, s1
	s_bfe_i32 s0, s3, 0x1001d
	s_lshr_b32 s0, s0, 26
	s_add_i32 s0, s2, s0
	s_ashr_i32 s3, s0, 6
	s_lshl_b32 s4, s3, 7
	s_ashr_i32 s5, s4, 31
	s_lshl_b64 s[0:1], s[4:5], 13
	s_add_u32 s6, s56, s0
	s_addc_u32 s7, s57, s1
	s_lshl_b32 s0, s2, 5
	s_lshl_b32 s1, s3, 11
	s_sub_i32 s12, s0, s1
	s_waitcnt vmcnt(5)
	v_mbcnt_lo_u32_b32 v2, -1, 0
	v_mbcnt_hi_u32_b32 v2, -1, v2
	s_ashr_i32 s13, s12, 31
	v_lshlrev_b32_e32 v0, 1, v2
	v_and_b32_e32 v0, -16, v0
	s_lshl_b64 s[0:1], s[12:13], 2
	v_ashrrev_i32_e32 v1, 31, v0
	v_lshlrev_b32_e32 v2, 2, v2
	s_add_u32 s0, s6, s0
	v_and_b32_e32 v68, 28, v2
	s_addc_u32 s1, s7, s1
	v_lshlrev_b64 v[2:3], 13, v[0:1]
	v_lshl_add_u64 v[4:5], s[0:1], 0, v[2:3]
	v_lshlrev_b32_e32 v2, 2, v68
	v_mov_b32_e32 v3, 0
	v_lshl_add_u64 v[64:65], v[4:5], 0, v[2:3]
	s_mov_b32 s1, 0x1c000
	v_add_co_u32_e32 v56, vcc, s1, v64
	s_mov_b32 s2, 0x18000
	s_nop 0
	v_addc_co_u32_e32 v57, vcc, 0, v65, vcc
	v_add_co_u32_e32 v4, vcc, s2, v64
	s_mov_b32 s2, 0x16000
	s_nop 0
	v_addc_co_u32_e32 v5, vcc, 0, v65, vcc
	v_add_co_u32_e32 v8, vcc, s2, v64
	s_mov_b32 s2, 0x14000
	s_nop 0
	v_addc_co_u32_e32 v9, vcc, 0, v65, vcc
	v_add_co_u32_e32 v48, vcc, s2, v64
	s_mov_b32 s3, 0x10000
	s_nop 0
	v_addc_co_u32_e32 v49, vcc, 0, v65, vcc
	v_add_co_u32_e32 v40, vcc, s3, v64
	s_mov_b32 s3, 0xe000
	s_nop 0
	v_addc_co_u32_e32 v41, vcc, 0, v65, vcc
	s_waitcnt vmcnt(4)
	v_add_co_u32_e32 v44, vcc, s3, v64
	s_mov_b32 s3, 0xc000
	s_nop 0
	v_addc_co_u32_e32 v45, vcc, 0, v65, vcc
	v_add_co_u32_e32 v32, vcc, s3, v64
	s_mov_b32 s6, 0x8000
	s_nop 0
	v_addc_co_u32_e32 v33, vcc, 0, v65, vcc
	v_add_co_u32_e32 v12, vcc, s6, v64
	s_movk_i32 s6, 0x6000
	s_nop 0
	v_addc_co_u32_e32 v13, vcc, 0, v65, vcc
	v_add_co_u32_e32 v16, vcc, s6, v64
	s_movk_i32 s6, 0x4000
	s_nop 0
	v_addc_co_u32_e32 v17, vcc, 0, v65, vcc
	v_add_co_u32_e32 v24, vcc, s6, v64
	s_movk_i32 s6, 0x2000
	s_nop 0
	v_addc_co_u32_e32 v25, vcc, 0, v65, vcc
	v_add_co_u32_e32 v28, vcc, s6, v64
	global_load_dwordx4 v[4:7], v[4:5], off sc1 nt
	s_nop 0
	global_load_dwordx4 v[8:11], v[8:9], off sc1 nt
	v_addc_co_u32_e32 v29, vcc, 0, v65, vcc
	s_mov_b32 s3, 0xa000
	global_load_dwordx4 v[12:15], v[12:13], off sc1 nt
	s_nop 0
	global_load_dwordx4 v[16:19], v[16:17], off sc1 nt
	s_nop 0
	global_load_dwordx4 v[20:23], v[64:65], off sc1 nt
	s_nop 0
	global_load_dwordx4 v[24:27], v[24:25], off sc1 nt
	s_nop 0
	global_load_dwordx4 v[28:31], v[28:29], off sc1 nt
	v_add_co_u32_e32 v36, vcc, s3, v64
	s_mov_b32 s2, 0x12000
	s_nop 0
	v_addc_co_u32_e32 v37, vcc, 0, v65, vcc
	global_load_dwordx4 v[32:35], v[32:33], off sc1 nt
	s_nop 0
	global_load_dwordx4 v[36:39], v[36:37], off sc1 nt
	s_nop 0
	global_load_dwordx4 v[40:43], v[40:41], off sc1 nt
	s_nop 0
	global_load_dwordx4 v[44:47], v[44:45], off sc1 nt
	v_add_co_u32_e32 v52, vcc, s2, v64
	s_mov_b32 s1, 0x1a000
	s_nop 0
	v_addc_co_u32_e32 v53, vcc, 0, v65, vcc
	v_add_co_u32_e32 v60, vcc, s1, v64
	global_load_dwordx4 v[48:51], v[48:49], off sc1 nt
	s_nop 0
	global_load_dwordx4 v[52:55], v[52:53], off sc1 nt
	v_addc_co_u32_e32 v61, vcc, 0, v65, vcc
	global_load_dwordx4 v[56:59], v[56:57], off sc1 nt
	s_nop 0
	global_load_dwordx4 v[60:63], v[60:61], off sc1 nt
	s_mov_b32 s0, 0x1e000
	v_add_co_u32_e32 v64, vcc, s0, v64
	s_lshl_b64 s[0:1], s[12:13], 11
	s_nop 0
	v_addc_co_u32_e32 v65, vcc, 0, v65, vcc
	global_load_dwordx4 v[64:67], v[64:65], off sc1 nt
	s_add_u32 s0, s90, s0
	s_addc_u32 s1, s91, s1
	s_add_u32 s0, s0, s4
	s_addc_u32 s1, s1, s5
	v_lshlrev_b32_e32 v2, 11, v68
	v_lshl_add_u64 v[68:69], s[0:1], 0, v[2:3]
	v_lshl_add_u64 v[80:81], v[68:69], 0, v[0:1]
	v_mov_b32_e32 v68, v3
	v_mov_b32_e32 v69, v3
	v_mov_b32_e32 v70, v3
	v_mov_b32_e32 v71, v3
	v_mov_b32_e32 v72, v3
	v_mov_b32_e32 v73, v3
	v_mov_b32_e32 v74, v3
	v_mov_b32_e32 v75, v3
	v_mov_b32_e32 v76, v3
	v_mov_b32_e32 v77, v3
	v_mov_b32_e32 v78, v3
	v_mov_b32_e32 v79, v3
	s_mov_b64 s[0:1], 0x1100000
	v_lshl_add_u64 v[82:83], v[80:81], 0, s[0:1]
	s_mov_b32 s0, 0x1100000
	s_waitcnt vmcnt(14)
	v_mul_f32_e32 v8, 0x44000000, v8
	s_waitcnt vmcnt(11)
	v_mul_f32_e32 v0, 0x44000000, v20
	s_waitcnt vmcnt(10)
	v_mul_f32_e32 v2, 0x44000000, v24
	s_waitcnt vmcnt(9)
	v_mul_f32_e32 v1, 0x44000000, v28
	v_cvt_pk_fp8_f32 v68, v0, v1
	v_mul_f32_e32 v0, 0x44000000, v12
	v_mul_f32_e32 v16, 0x44000000, v16
	s_waitcnt vmcnt(7)
	v_mul_f32_e32 v1, 0x44000000, v36
	v_cvt_pk_fp8_f32 v69, v0, v1
	v_mul_f32_e32 v0, 0x44000000, v32
	s_waitcnt vmcnt(5)
	v_mul_f32_e32 v1, 0x44000000, v44
	v_cvt_pk_fp8_f32 v68, v2, v16 op_sel:[0,0,1]
	v_cvt_pk_fp8_f32 v69, v0, v1 op_sel:[0,0,1]
	v_mul_f32_e32 v0, 0x44000000, v40
	s_waitcnt vmcnt(4)
	v_mul_f32_e32 v2, 0x44000000, v48
	s_waitcnt vmcnt(3)
	v_mul_f32_e32 v1, 0x44000000, v52
	v_cvt_pk_fp8_f32 v70, v0, v1
	v_mul_f32_e32 v0, 0x44000000, v4
	s_waitcnt vmcnt(1)
	v_mul_f32_e32 v1, 0x44000000, v60
	v_cvt_pk_fp8_f32 v71, v0, v1
	v_mul_f32_e32 v0, 0x44000000, v56
	v_cvt_pk_fp8_f32 v70, v2, v8 op_sel:[0,0,1]
	v_mul_f32_e32 v2, 0x44000000, v25
	v_mul_f32_e32 v4, 0x44000000, v17
	v_mul_f32_e32 v8, 0x44000000, v11
	s_waitcnt vmcnt(0)
	v_mul_f32_e32 v1, 0x44000000, v64
	v_cvt_pk_fp8_f32 v71, v0, v1 op_sel:[0,0,1]
	v_mul_f32_e32 v0, 0x44000000, v21
	v_mul_f32_e32 v1, 0x44000000, v29
	v_cvt_pk_fp8_f32 v72, v0, v1
	v_mul_f32_e32 v0, 0x44000000, v13
	v_mul_f32_e32 v1, 0x44000000, v37
	v_cvt_pk_fp8_f32 v73, v0, v1
	v_mul_f32_e32 v0, 0x44000000, v33
	v_mul_f32_e32 v1, 0x44000000, v45
	v_cvt_pk_fp8_f32 v72, v2, v4 op_sel:[0,0,1]
	v_cvt_pk_fp8_f32 v73, v0, v1 op_sel:[0,0,1]
	v_mul_f32_e32 v0, 0x44000000, v41
	v_mul_f32_e32 v1, 0x44000000, v53
	v_cvt_pk_fp8_f32 v74, v0, v1
	v_mul_f32_e32 v0, 0x44000000, v5
	v_mul_f32_e32 v1, 0x44000000, v61
	v_cvt_pk_fp8_f32 v75, v0, v1
	v_mul_f32_e32 v0, 0x44000000, v57
	v_mul_f32_e32 v1, 0x44000000, v65
	v_mul_f32_e32 v2, 0x44000000, v49
	v_cvt_pk_fp8_f32 v75, v0, v1 op_sel:[0,0,1]
	v_mul_f32_e32 v0, 0x44000000, v22
	v_mul_f32_e32 v1, 0x44000000, v30
	v_cvt_pk_fp8_f32 v76, v0, v1
	v_mul_f32_e32 v0, 0x44000000, v14
	v_mul_f32_e32 v1, 0x44000000, v38
	v_cvt_pk_fp8_f32 v77, v0, v1
	v_mul_f32_e32 v0, 0x44000000, v34
	v_mul_f32_e32 v1, 0x44000000, v46
	v_mul_f32_e32 v4, 0x44000000, v9
	v_cvt_pk_fp8_f32 v77, v0, v1 op_sel:[0,0,1]
	v_mul_f32_e32 v0, 0x44000000, v42
	v_mul_f32_e32 v1, 0x44000000, v54
	v_cvt_pk_fp8_f32 v78, v0, v1
	v_mul_f32_e32 v0, 0x44000000, v6
	v_mul_f32_e32 v1, 0x44000000, v62
	v_cvt_pk_fp8_f32 v79, v0, v1
	v_cvt_pk_fp8_f32 v74, v2, v4 op_sel:[0,0,1]
	v_mul_f32_e32 v2, 0x44000000, v26
	v_mul_f32_e32 v4, 0x44000000, v18
	v_cvt_pk_fp8_f32 v76, v2, v4 op_sel:[0,0,1]
	v_mul_f32_e32 v2, 0x44000000, v50
	v_mul_f32_e32 v4, 0x44000000, v10
	v_mul_f32_e32 v0, 0x44000000, v58
	v_mul_f32_e32 v1, 0x44000000, v66
	v_cvt_pk_fp8_f32 v78, v2, v4 op_sel:[0,0,1]
	v_cvt_pk_fp8_f32 v79, v0, v1 op_sel:[0,0,1]
	v_mul_f32_e32 v1, 0x44000000, v23
	v_mul_f32_e32 v2, 0x44000000, v31
	v_mov_b32_e32 v0, v3
	v_cvt_pk_fp8_f32 v0, v1, v2
	v_mul_f32_e32 v2, 0x44000000, v15
	v_mul_f32_e32 v6, 0x44000000, v39
	v_mov_b32_e32 v1, v3
	v_cvt_pk_fp8_f32 v1, v2, v6
	v_mul_f32_e32 v4, 0x44000000, v27
	v_mul_f32_e32 v5, 0x44000000, v19
	v_cvt_pk_fp8_f32 v0, v4, v5 op_sel:[0,0,1]
	v_mul_f32_e32 v2, 0x44000000, v35
	v_mul_f32_e32 v4, 0x44000000, v47
	v_cvt_pk_fp8_f32 v1, v2, v4 op_sel:[0,0,1]
	v_mul_f32_e32 v4, 0x44000000, v43
	v_mul_f32_e32 v5, 0x44000000, v55
	v_mov_b32_e32 v2, v3
	v_cvt_pk_fp8_f32 v2, v4, v5
	v_mul_f32_e32 v4, 0x44000000, v7
	v_mul_f32_e32 v5, 0x44000000, v63
	v_cvt_pk_fp8_f32 v3, v4, v5
	v_mul_f32_e32 v4, 0x44000000, v59
	v_mul_f32_e32 v5, 0x44000000, v67
	v_mul_f32_e32 v6, 0x44000000, v51
	v_cvt_pk_fp8_f32 v3, v4, v5 op_sel:[0,0,1]
	v_add_co_u32_e32 v4, vcc, s0, v80
	v_cvt_pk_fp8_f32 v2, v6, v8 op_sel:[0,0,1]
	s_nop 0
	v_addc_co_u32_e32 v5, vcc, 0, v81, vcc
	global_store_dwordx4 v[4:5], v[68:71], off sc1 nt
	global_store_dwordx4 v[82:83], v[72:75], off offset:2048 sc1 nt
	v_add_co_u32_e32 v4, vcc, 0x1101000, v80
	s_nop 1
	v_addc_co_u32_e32 v5, vcc, 0, v81, vcc
	global_store_dwordx4 v[4:5], v[76:79], off sc1 nt
	global_store_dwordx4 v[4:5], v[0:3], off offset:2048 sc1 nt
	s_waitcnt vmcnt(0)

.LBB0_248:
	s_not_b32 s1, s0
	s_add_i32 s1, s33, s1
	s_cmp_lt_i32 s1, -7
	s_cbranch_scc1 .LBB0_268
	s_ashr_i32 s2, s1, 31
	v_lshlrev_b32_e32 v1, 1, v0
	s_lshr_b32 s2, s2, 29
	v_and_b32_e32 v128, -16, v1
	v_lshlrev_b32_e32 v0, 2, v0
	s_add_i32 s2, s1, s2
	v_and_b32_e32 v64, 28, v0
	s_ashr_i32 s1, s2, 3
	s_and_b32 s2, s2, -8
	v_mad_i64_i32 v[0:1], s[6:7], s18, v128, 0
	v_mov_b32_e32 v131, 0
	s_add_i32 s2, s2, s0
	v_lshl_add_u64 v[0:1], v[0:1], 2, s[16:17]
	v_lshlrev_b32_e32 v130, 2, v64
	s_lshl_b32 s3, s18, 2
	s_mov_b32 s5, 0
	s_waitcnt vmcnt(4)
	v_lshl_add_u64 v[60:61], v[0:1], 0, v[130:131]
	s_mul_i32 s4, s18, 60
	s_sub_u32 s6, 0, s3
	v_lshl_add_u64 v[44:45], v[60:61], 0, s[4:5]
	s_subb_u32 s7, 0, 0
	v_lshl_add_u64 v[0:1], v[44:45], 0, s[6:7]
	v_lshl_add_u64 v[8:9], v[0:1], 0, s[6:7]
	global_load_dwordx4 v[0:3], v[0:1], off sc1 nt
	s_nop 0
	global_load_dwordx4 v[4:7], v[8:9], off sc1 nt
	v_lshl_add_u64 v[8:9], v[8:9], 0, s[6:7]
	v_lshl_add_u64 v[16:17], v[8:9], 0, s[6:7]
	global_load_dwordx4 v[8:11], v[8:9], off sc1 nt
	s_nop 0
	global_load_dwordx4 v[12:15], v[16:17], off sc1 nt
	v_lshl_add_u64 v[16:17], v[16:17], 0, s[6:7]
	v_lshl_add_u64 v[24:25], v[16:17], 0, s[6:7]
	v_lshl_add_u64 v[28:29], v[24:25], 0, s[6:7]
	v_lshl_add_u64 v[32:33], v[28:29], 0, s[6:7]
	v_lshl_add_u64 v[36:37], v[32:33], 0, s[6:7]
	v_lshl_add_u64 v[40:41], v[36:37], 0, s[6:7]
	v_lshl_add_u64 v[46:47], v[40:41], 0, s[6:7]
	global_load_dwordx4 v[16:19], v[16:17], off sc1 nt
	s_nop 0
	global_load_dwordx4 v[20:23], v[24:25], off sc1 nt
	s_mov_b32 s33, s20
	global_load_dwordx4 v[24:27], v[28:29], off sc1 nt
	s_mov_b64 s[34:35], s[24:25]
	global_load_dwordx4 v[28:31], v[32:33], off sc1 nt
	s_mov_b64 s[30:31], s[22:23]
	global_load_dwordx4 v[32:35], v[36:37], off sc1 nt
	v_ashrrev_i32_e32 v129, 31, v128
	global_load_dwordx4 v[36:39], v[40:41], off sc1 nt
	v_lshlrev_b32_e32 v132, 11, v64
	global_load_dwordx4 v[40:43], v[46:47], off sc1 nt
	v_lshl_add_u64 v[46:47], v[46:47], 0, s[6:7]
	global_load_dwordx4 v[48:51], v[46:47], off sc1 nt
	v_lshl_add_u64 v[46:47], v[46:47], 0, s[6:7]
	global_load_dwordx4 v[56:59], v[46:47], off sc1 nt
	v_lshl_add_u64 v[46:47], v[46:47], 0, s[6:7]
	global_load_dwordx4 v[52:55], v[46:47], off sc1 nt
	s_nop 0
	global_load_dwordx4 v[44:47], v[44:45], off sc1 nt
	s_nop 0
	global_load_dwordx4 v[60:63], v[60:61], off sc1 nt
	s_lshl_b64 s[6:7], s[14:15], 11
	s_add_u32 s3, s10, s6
	s_addc_u32 s4, s11, s7
	s_add_u32 s12, s3, s12
	s_addc_u32 s13, s4, s13
	s_add_u32 s3, s90, 0x3b100000
	s_addc_u32 s6, s91, 0
	s_add_u32 s10, s90, 0x1900000
	s_addc_u32 s11, s91, 0
	s_add_u32 s7, s90, 0x4b100000
	v_mov_b32_e32 v133, v131
	s_addc_u32 s8, s91, 0
	v_lshlrev_b32_e32 v130, 2, v64
	s_movk_i32 s9, 0x1000
	s_mov_b32 s28, 0
	s_branch .LBB0_251
.LBB0_250:
	s_lshl_b64 s[16:17], s[16:17], 11
	s_add_u32 s4, s14, s16
	s_addc_u32 s15, s15, s17
	s_add_u32 s14, s4, s18
	s_addc_u32 s15, s15, s19
	s_lshl_b64 s[16:17], s[22:23], 11
	s_add_u32 s4, s12, s16
	s_addc_u32 s13, s13, s17
	v_mad_i64_i32 v[0:1], s[16:17], s26, v128, 0
	s_add_u32 s12, s4, s24
	v_lshl_add_u64 v[0:1], v[0:1], 2, s[20:21]
	s_addc_u32 s13, s13, s25
	v_lshl_add_u64 v[0:1], v[0:1], 0, v[130:131]
	s_lshl_b32 s4, s26, 2
	v_lshl_add_u64 v[2:3], v[0:1], 0, s[4:5]
	global_load_dwordx4 v[60:63], v[0:1], off sc1 nt
	global_load_dwordx4 v[52:55], v[2:3], off sc1 nt
	v_lshl_add_u64 v[0:1], v[2:3], 0, s[4:5]
	v_lshl_add_u64 v[2:3], v[0:1], 0, s[4:5]
	global_load_dwordx4 v[56:59], v[0:1], off sc1 nt
	global_load_dwordx4 v[48:51], v[2:3], off sc1 nt
	v_lshl_add_u64 v[0:1], v[2:3], 0, s[4:5]
	v_lshl_add_u64 v[2:3], v[0:1], 0, s[4:5]
	global_load_dwordx4 v[40:43], v[0:1], off sc1 nt
	global_load_dwordx4 v[36:39], v[2:3], off sc1 nt
	v_lshl_add_u64 v[0:1], v[2:3], 0, s[4:5]
	v_lshl_add_u64 v[2:3], v[0:1], 0, s[4:5]
	global_load_dwordx4 v[32:35], v[0:1], off sc1 nt
	global_load_dwordx4 v[28:31], v[2:3], off sc1 nt
	v_lshl_add_u64 v[0:1], v[2:3], 0, s[4:5]
	global_load_dwordx4 v[24:27], v[0:1], off sc1 nt
	v_lshl_add_u64 v[0:1], v[0:1], 0, s[4:5]
	global_load_dwordx4 v[20:23], v[0:1], off sc1 nt
	v_lshl_add_u64 v[0:1], v[0:1], 0, s[4:5]
	global_load_dwordx4 v[16:19], v[0:1], off sc1 nt
	v_lshl_add_u64 v[0:1], v[0:1], 0, s[4:5]
	global_load_dwordx4 v[12:15], v[0:1], off sc1 nt
	v_lshl_add_u64 v[0:1], v[0:1], 0, s[4:5]
	global_load_dwordx4 v[8:11], v[0:1], off sc1 nt
	v_lshl_add_u64 v[0:1], v[0:1], 0, s[4:5]
	v_lshl_add_u64 v[44:45], v[0:1], 0, s[4:5]
	global_load_dwordx4 v[4:7], v[0:1], off sc1 nt
	s_waitcnt vmcnt(33)
	v_mul_f32_e32 v80, 0x44000000, v80
	global_load_dwordx4 v[0:3], v[44:45], off sc1 nt
	v_lshl_add_u64 v[44:45], v[44:45], 0, s[4:5]
	global_load_dwordx4 v[44:47], v[44:45], off sc1 nt
	s_waitcnt vmcnt(34)
	v_mul_f32_e32 v84, 0x44000000, v84
	v_mov_b32_e32 v134, v131
	v_cvt_pk_fp8_f32 v134, v80, v84
	s_waitcnt vmcnt(31)
	v_mul_f32_e32 v80, 0x44000000, v108
	s_waitcnt vmcnt(30)
	v_mul_f32_e32 v84, 0x44000000, v112
	v_mov_b32_e32 v135, v131
	v_cvt_pk_fp8_f32 v135, v80, v84
	s_waitcnt vmcnt(29)
	v_mul_f32_e32 v80, 0x44000000, v88
	s_waitcnt vmcnt(28)
	v_mul_f32_e32 v84, 0x44000000, v92
	s_waitcnt vmcnt(27)
	v_mul_f32_e32 v72, 0x44000000, v72
	v_cvt_pk_fp8_f32 v135, v80, v84 op_sel:[0,0,1]
	s_waitcnt vmcnt(26)
	v_mul_f32_e32 v80, 0x44000000, v96
	v_mov_b32_e32 v136, v131
	v_cvt_pk_fp8_f32 v136, v72, v80
	s_waitcnt vmcnt(23)
	v_mul_f32_e32 v72, 0x44000000, v76
	s_waitcnt vmcnt(22)
	v_mul_f32_e32 v76, 0x44000000, v100
	v_mov_b32_e32 v137, v131
	v_cvt_pk_fp8_f32 v137, v72, v76
	s_waitcnt vmcnt(21)
	v_mul_f32_e32 v64, 0x44000000, v64
	s_waitcnt vmcnt(20)
	v_mul_f32_e32 v68, 0x44000000, v68
	v_mov_b32_e32 v138, v131
	v_cvt_pk_fp8_f32 v137, v64, v68 op_sel:[0,0,1]
	v_mul_f32_e32 v64, 0x44000000, v81
	v_mul_f32_e32 v68, 0x44000000, v85
	v_cvt_pk_fp8_f32 v138, v64, v68
	v_mul_f32_e32 v64, 0x44000000, v109
	v_mul_f32_e32 v68, 0x44000000, v113
	v_mov_b32_e32 v139, v131
	v_cvt_pk_fp8_f32 v139, v64, v68
	v_mul_f32_e32 v64, 0x44000000, v89
	v_mul_f32_e32 v68, 0x44000000, v93
	v_mov_b32_e32 v140, v131
	v_cvt_pk_fp8_f32 v139, v64, v68 op_sel:[0,0,1]
	v_mul_f32_e32 v64, 0x44000000, v73
	v_mul_f32_e32 v68, 0x44000000, v97
	v_cvt_pk_fp8_f32 v140, v64, v68
	v_mul_f32_e32 v64, 0x44000000, v77
	v_mul_f32_e32 v68, 0x44000000, v101
	v_mov_b32_e32 v141, v131
	v_cvt_pk_fp8_f32 v141, v64, v68
	v_mul_f32_e32 v120, 0x44000000, v120
	v_mul_f32_e32 v124, 0x44000000, v124
	v_mul_f32_e32 v84, 0x44000000, v104
	v_mul_f32_e32 v88, 0x44000000, v116
	v_mul_f32_e32 v72, 0x44000000, v121
	v_mul_f32_e32 v76, 0x44000000, v125
	v_cvt_pk_fp8_f32 v134, v120, v124 op_sel:[0,0,1]
	v_cvt_pk_fp8_f32 v136, v84, v88 op_sel:[0,0,1]
	v_cvt_pk_fp8_f32 v138, v72, v76 op_sel:[0,0,1]
	v_mul_f32_e32 v72, 0x44000000, v105
	v_mul_f32_e32 v73, 0x44000000, v117
	v_mul_f32_e32 v64, 0x44000000, v65
	v_mul_f32_e32 v65, 0x44000000, v69
	v_cvt_pk_fp8_f32 v140, v72, v73 op_sel:[0,0,1]
	v_cvt_pk_fp8_f32 v141, v64, v65 op_sel:[0,0,1]
	v_lshl_add_u64 v[64:65], s[14:15], 0, v[132:133]
	v_lshl_add_u64 v[64:65], v[64:65], 0, v[128:129]
	global_store_dwordx4 v[64:65], v[134:137], off sc1 nt
	global_store_dwordx4 v[64:65], v[138:141], off offset:2048 sc1 nt
	v_mul_f32_e32 v68, 0x44000000, v82
	v_mul_f32_e32 v69, 0x44000000, v86
	v_mov_b32_e32 v134, v131
	v_cvt_pk_fp8_f32 v134, v68, v69
	v_mul_f32_e32 v68, 0x44000000, v110
	v_mul_f32_e32 v69, 0x44000000, v114
	v_mov_b32_e32 v135, v131
	v_cvt_pk_fp8_f32 v135, v68, v69
	v_mul_f32_e32 v68, 0x44000000, v90
	v_mul_f32_e32 v69, 0x44000000, v94
	v_mov_b32_e32 v136, v131
	v_cvt_pk_fp8_f32 v135, v68, v69 op_sel:[0,0,1]
	v_mul_f32_e32 v68, 0x44000000, v74
	v_mul_f32_e32 v69, 0x44000000, v98
	v_cvt_pk_fp8_f32 v136, v68, v69
	v_mul_f32_e32 v68, 0x44000000, v78
	v_mul_f32_e32 v69, 0x44000000, v102
	v_mov_b32_e32 v137, v131
	v_cvt_pk_fp8_f32 v137, v68, v69
	v_mul_f32_e32 v72, 0x44000000, v122
	v_mul_f32_e32 v73, 0x44000000, v126
	v_cvt_pk_fp8_f32 v134, v72, v73 op_sel:[0,0,1]
	v_mul_f32_e32 v72, 0x44000000, v106
	v_mul_f32_e32 v73, 0x44000000, v118
	v_mul_f32_e32 v66, 0x44000000, v66
	v_mul_f32_e32 v68, 0x44000000, v70
	v_cvt_pk_fp8_f32 v136, v72, v73 op_sel:[0,0,1]
	v_cvt_pk_fp8_f32 v137, v66, v68 op_sel:[0,0,1]
	v_mul_f32_e32 v66, 0x44000000, v83
	v_mul_f32_e32 v68, 0x44000000, v87
	v_mov_b32_e32 v72, v131
	v_cvt_pk_fp8_f32 v72, v66, v68
	v_mul_f32_e32 v66, 0x44000000, v111
	v_mul_f32_e32 v68, 0x44000000, v115
	v_mov_b32_e32 v73, v131
	v_cvt_pk_fp8_f32 v73, v66, v68
	v_mul_f32_e32 v66, 0x44000000, v91
	v_mul_f32_e32 v68, 0x44000000, v95
	v_mov_b32_e32 v74, v131
	v_cvt_pk_fp8_f32 v73, v66, v68 op_sel:[0,0,1]
	v_mul_f32_e32 v66, 0x44000000, v75
	v_mul_f32_e32 v68, 0x44000000, v99
	v_cvt_pk_fp8_f32 v74, v66, v68
	v_mul_f32_e32 v66, 0x44000000, v79
	v_mul_f32_e32 v68, 0x44000000, v103
	v_mov_b32_e32 v75, v131
	v_cvt_pk_fp8_f32 v75, v66, v68
	v_mul_f32_e32 v69, 0x44000000, v123
	v_mul_f32_e32 v70, 0x44000000, v127
	v_cvt_pk_fp8_f32 v72, v69, v70 op_sel:[0,0,1]
	v_mul_f32_e32 v69, 0x44000000, v107
	v_mul_f32_e32 v70, 0x44000000, v119
	v_mul_f32_e32 v66, 0x44000000, v67
	v_mul_f32_e32 v67, 0x44000000, v71
	v_cvt_pk_fp8_f32 v74, v69, v70 op_sel:[0,0,1]
	v_cvt_pk_fp8_f32 v75, v66, v67 op_sel:[0,0,1]
	v_add_co_u32_e32 v64, vcc, s9, v64
	s_add_i32 s28, s28, 2
	s_nop 0
	v_addc_co_u32_e32 v65, vcc, 0, v65, vcc
	s_cmp_le_i32 s28, s1
	global_store_dwordx4 v[64:65], v[134:137], off sc1 nt
	global_store_dwordx4 v[64:65], v[72:75], off offset:2048 sc1 nt
	s_cbranch_scc0 .LBB0_267

.LBB0_259:
	v_mad_i64_i32 v[64:65], s[24:25], s22, v128, 0
	v_lshl_add_u64 v[64:65], v[64:65], 2, s[20:21]
	v_lshl_add_u64 v[64:65], v[64:65], 0, v[130:131]
	s_lshl_b32 s4, s22, 2
	v_lshl_add_u64 v[66:67], v[64:65], 0, s[4:5]
	global_load_dwordx4 v[80:83], v[64:65], off sc1 nt
	global_load_dwordx4 v[84:87], v[66:67], off sc1 nt
	v_lshl_add_u64 v[64:65], v[66:67], 0, s[4:5]
	v_lshl_add_u64 v[66:67], v[64:65], 0, s[4:5]
	global_load_dwordx4 v[120:123], v[64:65], off sc1 nt
	global_load_dwordx4 v[124:127], v[66:67], off sc1 nt
	v_lshl_add_u64 v[64:65], v[66:67], 0, s[4:5]
	v_lshl_add_u64 v[66:67], v[64:65], 0, s[4:5]
	global_load_dwordx4 v[108:111], v[64:65], off sc1 nt
	global_load_dwordx4 v[112:115], v[66:67], off sc1 nt
	v_lshl_add_u64 v[64:65], v[66:67], 0, s[4:5]
	v_lshl_add_u64 v[66:67], v[64:65], 0, s[4:5]
	global_load_dwordx4 v[88:91], v[64:65], off sc1 nt
	global_load_dwordx4 v[92:95], v[66:67], off sc1 nt
	v_lshl_add_u64 v[64:65], v[66:67], 0, s[4:5]
	global_load_dwordx4 v[72:75], v[64:65], off sc1 nt
	v_lshl_add_u64 v[64:65], v[64:65], 0, s[4:5]
	global_load_dwordx4 v[96:99], v[64:65], off sc1 nt
	v_lshl_add_u64 v[64:65], v[64:65], 0, s[4:5]
	global_load_dwordx4 v[104:107], v[64:65], off sc1 nt
	v_lshl_add_u64 v[64:65], v[64:65], 0, s[4:5]
	global_load_dwordx4 v[116:119], v[64:65], off sc1 nt
	v_lshl_add_u64 v[64:65], v[64:65], 0, s[4:5]
	global_load_dwordx4 v[76:79], v[64:65], off sc1 nt
	v_lshl_add_u64 v[64:65], v[64:65], 0, s[4:5]
	v_lshl_add_u64 v[68:69], v[64:65], 0, s[4:5]
	global_load_dwordx4 v[100:103], v[64:65], off sc1 nt
	s_waitcnt vmcnt(21)
	v_mul_f32_e32 v8, 0x44000000, v8
	global_load_dwordx4 v[64:67], v[68:69], off sc1 nt
	v_lshl_add_u64 v[68:69], v[68:69], 0, s[4:5]
	global_load_dwordx4 v[68:71], v[68:69], off sc1 nt
	s_waitcnt vmcnt(22)
	v_mul_f32_e32 v4, 0x44000000, v4
	v_mov_b32_e32 v137, v131
	v_cvt_pk_fp8_f32 v137, v8, v4
	s_waitcnt vmcnt(21)
	v_mul_f32_e32 v0, 0x44000000, v0
	s_waitcnt vmcnt(17)
	v_mul_f32_e32 v4, 0x44000000, v44
	v_mov_b32_e32 v138, v131
	v_cvt_pk_fp8_f32 v137, v0, v4 op_sel:[0,0,1]
	s_waitcnt vmcnt(16)
	v_mul_f32_e32 v0, 0x44000000, v61
	v_mul_f32_e32 v4, 0x44000000, v53
	v_cvt_pk_fp8_f32 v138, v0, v4
	v_mul_f32_e32 v0, 0x44000000, v41
	v_mul_f32_e32 v4, 0x44000000, v37
	v_mov_b32_e32 v139, v131
	v_cvt_pk_fp8_f32 v139, v0, v4
	v_mul_f32_e32 v24, 0x44000000, v24
	v_mul_f32_e32 v20, 0x44000000, v20
	v_mov_b32_e32 v136, v131
	v_mul_f32_e32 v0, 0x44000000, v33
	v_mul_f32_e32 v4, 0x44000000, v29
	v_mul_f32_e32 v60, 0x44000000, v60
	v_mul_f32_e32 v52, 0x44000000, v52
	v_mov_b32_e32 v134, v131
	v_mul_f32_e32 v40, 0x44000000, v40
	v_mul_f32_e32 v36, 0x44000000, v36
	v_mov_b32_e32 v135, v131
	v_cvt_pk_fp8_f32 v136, v24, v20
	v_cvt_pk_fp8_f32 v139, v0, v4 op_sel:[0,0,1]
	v_mul_f32_e32 v0, 0x44000000, v25
	v_mul_f32_e32 v4, 0x44000000, v21
	v_mov_b32_e32 v140, v131
	v_cvt_pk_fp8_f32 v134, v60, v52
	v_cvt_pk_fp8_f32 v135, v40, v36
	v_cvt_pk_fp8_f32 v140, v0, v4
	v_mul_f32_e32 v0, 0x44000000, v9
	v_mul_f32_e32 v4, 0x44000000, v5
	v_mov_b32_e32 v141, v131
	v_cvt_pk_fp8_f32 v141, v0, v4
	v_mul_f32_e32 v16, 0x44000000, v16
	v_mul_f32_e32 v12, 0x44000000, v12
	v_mul_f32_e32 v56, 0x44000000, v56
	v_mul_f32_e32 v48, 0x44000000, v48
	v_mul_f32_e32 v32, 0x44000000, v32
	v_mul_f32_e32 v28, 0x44000000, v28
	v_cvt_pk_fp8_f32 v136, v16, v12 op_sel:[0,0,1]
	v_mul_f32_e32 v8, 0x44000000, v57
	v_mul_f32_e32 v12, 0x44000000, v49
	v_cvt_pk_fp8_f32 v134, v56, v48 op_sel:[0,0,1]
	v_cvt_pk_fp8_f32 v135, v32, v28 op_sel:[0,0,1]
	v_cvt_pk_fp8_f32 v138, v8, v12 op_sel:[0,0,1]
	v_mul_f32_e32 v8, 0x44000000, v17
	v_mul_f32_e32 v12, 0x44000000, v13
	v_mul_f32_e32 v0, 0x44000000, v1
	v_mul_f32_e32 v1, 0x44000000, v45
	v_cvt_pk_fp8_f32 v140, v8, v12 op_sel:[0,0,1]
	v_cvt_pk_fp8_f32 v141, v0, v1 op_sel:[0,0,1]
	v_lshl_add_u64 v[0:1], s[12:13], 0, v[132:133]
	v_lshl_add_u64 v[0:1], v[0:1], 0, v[128:129]
	global_store_dwordx4 v[0:1], v[134:137], off sc1 nt
	global_store_dwordx4 v[0:1], v[138:141], off offset:2048 sc1 nt
	v_mul_f32_e32 v4, 0x44000000, v62
	v_mul_f32_e32 v5, 0x44000000, v54
	v_mov_b32_e32 v134, v131
	v_cvt_pk_fp8_f32 v134, v4, v5
	v_mul_f32_e32 v4, 0x44000000, v42
	v_mul_f32_e32 v5, 0x44000000, v38
	v_mov_b32_e32 v135, v131
	v_cvt_pk_fp8_f32 v135, v4, v5
	v_mul_f32_e32 v4, 0x44000000, v34
	v_mul_f32_e32 v5, 0x44000000, v30
	v_mov_b32_e32 v136, v131
	v_cvt_pk_fp8_f32 v135, v4, v5 op_sel:[0,0,1]
	v_mul_f32_e32 v4, 0x44000000, v26
	v_mul_f32_e32 v5, 0x44000000, v22
	v_cvt_pk_fp8_f32 v136, v4, v5
	v_mul_f32_e32 v4, 0x44000000, v10
	v_mul_f32_e32 v5, 0x44000000, v6
	v_mov_b32_e32 v137, v131
	v_cvt_pk_fp8_f32 v137, v4, v5
	v_mul_f32_e32 v8, 0x44000000, v58
	v_mul_f32_e32 v9, 0x44000000, v50
	v_mul_f32_e32 v2, 0x44000000, v2
	v_mul_f32_e32 v4, 0x44000000, v46
	v_cvt_pk_fp8_f32 v134, v8, v9 op_sel:[0,0,1]
	v_mul_f32_e32 v8, 0x44000000, v18
	v_mul_f32_e32 v9, 0x44000000, v14
	v_cvt_pk_fp8_f32 v137, v2, v4 op_sel:[0,0,1]
	v_mul_f32_e32 v2, 0x44000000, v63
	v_mul_f32_e32 v5, 0x44000000, v55
	v_mov_b32_e32 v4, v131
	v_cvt_pk_fp8_f32 v136, v8, v9 op_sel:[0,0,1]
	v_cvt_pk_fp8_f32 v4, v2, v5
	v_mul_f32_e32 v2, 0x44000000, v43
	v_mul_f32_e32 v9, 0x44000000, v39
	v_mov_b32_e32 v5, v131
	v_cvt_pk_fp8_f32 v5, v2, v9
	v_mul_f32_e32 v6, 0x44000000, v59
	v_mul_f32_e32 v8, 0x44000000, v51
	v_cvt_pk_fp8_f32 v4, v6, v8 op_sel:[0,0,1]
	v_mul_f32_e32 v2, 0x44000000, v35
	v_mul_f32_e32 v6, 0x44000000, v31
	v_cvt_pk_fp8_f32 v5, v2, v6 op_sel:[0,0,1]
	v_mul_f32_e32 v2, 0x44000000, v27
	v_mul_f32_e32 v8, 0x44000000, v23
	v_mov_b32_e32 v6, v131
	v_cvt_pk_fp8_f32 v6, v2, v8
	v_mul_f32_e32 v2, 0x44000000, v11
	v_mul_f32_e32 v8, 0x44000000, v7
	v_mov_b32_e32 v7, v131
	v_cvt_pk_fp8_f32 v7, v2, v8
	v_mul_f32_e32 v9, 0x44000000, v19
	v_mul_f32_e32 v10, 0x44000000, v15
	v_mul_f32_e32 v2, 0x44000000, v3
	v_mul_f32_e32 v3, 0x44000000, v47
	s_add_i32 s0, s0, 16
	v_cvt_pk_fp8_f32 v6, v9, v10 op_sel:[0,0,1]
	v_cvt_pk_fp8_f32 v7, v2, v3 op_sel:[0,0,1]
	s_min_i32 s0, s0, s2
	v_add_co_u32_e32 v0, vcc, s9, v0
	s_cmp_gt_i32 s0, 0xffff
	s_nop 0
	v_addc_co_u32_e32 v1, vcc, 0, v1, vcc
	s_mov_b64 s[26:27], -1
	global_store_dwordx4 v[0:1], v[134:137], off sc1 nt
	global_store_dwordx4 v[0:1], v[4:7], off offset:2048 sc1 nt
	s_cbranch_scc0 .LBB0_265
	s_cmp_lt_u32 s0, 0x18000
	s_cbranch_scc0 .LBB0_262
	s_add_i32 s4, s0, 0xffff0000
	s_lshr_b32 s4, s4, 10
	s_lshl_b64 s[12:13], s[4:5], 22
	s_lshl_b64 s[20:21], s[4:5], 24
	s_add_u32 s20, s70, s20
	s_addc_u32 s21, s71, s21
	s_add_u32 s12, s3, s12
	s_addc_u32 s13, s6, s13
	s_lshl_b32 s4, s0, 1
	s_and_b32 s4, s4, 0x780
	s_lshl_b32 s22, s4, 13
	s_add_u32 s20, s20, s22
	s_addc_u32 s21, s21, 0
	s_lshl_b32 s22, s0, 5
	s_and_b32 s22, s22, 0x7e0
	s_lshl_b32 s24, s22, 2
	s_add_u32 s20, s20, s24
	s_mov_b32 s23, s5
	s_addc_u32 s21, s21, 0
	s_mov_b64 s[26:27], 0
	s_mov_b64 s[24:25], s[4:5]

.LBB0_271:
	v_readlane_b32 s0, v255, 0
	s_cmpk_gt_u32 s0, 0xff
	s_cbranch_scc1 .LBB0_273
	v_readlane_b32 s3, v255, 4
	s_lshl_b32 s0, s3, 2
	v_readlane_b32 s1, v255, 28
	s_or_b32 s2, s0, s1
	s_bfe_i32 s0, s3, 0x1001d
	s_lshr_b32 s0, s0, 26
	s_add_i32 s0, s2, s0
	s_ashr_i32 s3, s0, 6
	s_lshl_b32 s4, s3, 7
	s_ashr_i32 s5, s4, 31
	s_lshl_b64 s[0:1], s[4:5], 13
	s_add_u32 s6, s56, s0
	s_addc_u32 s7, s57, s1
	s_lshl_b32 s0, s2, 5
	s_lshl_b32 s1, s3, 11
	s_sub_i32 s10, s0, s1
	s_waitcnt vmcnt(5)
	v_mbcnt_lo_u32_b32 v2, -1, 0
	v_mbcnt_hi_u32_b32 v2, -1, v2
	s_ashr_i32 s11, s10, 31
	v_lshlrev_b32_e32 v0, 1, v2
	v_and_b32_e32 v0, -16, v0
	s_lshl_b64 s[0:1], s[10:11], 2
	v_ashrrev_i32_e32 v1, 31, v0
	v_lshlrev_b32_e32 v2, 2, v2
	s_add_u32 s0, s6, s0
	v_and_b32_e32 v68, 28, v2
	s_addc_u32 s1, s7, s1
	v_lshlrev_b64 v[2:3], 13, v[0:1]
	v_lshl_add_u64 v[4:5], s[0:1], 0, v[2:3]
	v_lshlrev_b32_e32 v2, 2, v68
	v_mov_b32_e32 v3, 0
	v_lshl_add_u64 v[64:65], v[4:5], 0, v[2:3]
	s_mov_b32 s1, 0x1c000
	v_add_co_u32_e32 v56, vcc, s1, v64
	s_mov_b32 s2, 0x18000
	s_nop 0
	v_addc_co_u32_e32 v57, vcc, 0, v65, vcc
	v_add_co_u32_e32 v4, vcc, s2, v64
	s_mov_b32 s2, 0x16000
	s_nop 0
	v_addc_co_u32_e32 v5, vcc, 0, v65, vcc
	v_add_co_u32_e32 v8, vcc, s2, v64
	s_mov_b32 s2, 0x14000
	s_nop 0
	v_addc_co_u32_e32 v9, vcc, 0, v65, vcc
	v_add_co_u32_e32 v48, vcc, s2, v64
	s_mov_b32 s3, 0x10000
	s_nop 0
	v_addc_co_u32_e32 v49, vcc, 0, v65, vcc
	v_add_co_u32_e32 v40, vcc, s3, v64
	s_mov_b32 s3, 0xe000
	s_nop 0
	v_addc_co_u32_e32 v41, vcc, 0, v65, vcc
	s_waitcnt vmcnt(4)
	v_add_co_u32_e32 v44, vcc, s3, v64
	s_mov_b32 s3, 0xc000
	s_nop 0
	v_addc_co_u32_e32 v45, vcc, 0, v65, vcc
	v_add_co_u32_e32 v32, vcc, s3, v64
	s_mov_b32 s6, 0x8000
	s_nop 0
	v_addc_co_u32_e32 v33, vcc, 0, v65, vcc
	v_add_co_u32_e32 v12, vcc, s6, v64
	s_movk_i32 s6, 0x6000
	s_nop 0
	v_addc_co_u32_e32 v13, vcc, 0, v65, vcc
	v_add_co_u32_e32 v16, vcc, s6, v64
	s_movk_i32 s6, 0x4000
	s_nop 0
	v_addc_co_u32_e32 v17, vcc, 0, v65, vcc
	v_add_co_u32_e32 v24, vcc, s6, v64
	s_movk_i32 s6, 0x2000
	s_nop 0
	v_addc_co_u32_e32 v25, vcc, 0, v65, vcc
	v_add_co_u32_e32 v28, vcc, s6, v64
	global_load_dwordx4 v[4:7], v[4:5], off sc1 nt
	s_nop 0
	global_load_dwordx4 v[8:11], v[8:9], off sc1 nt
	v_addc_co_u32_e32 v29, vcc, 0, v65, vcc
	s_mov_b32 s3, 0xa000
	global_load_dwordx4 v[12:15], v[12:13], off sc1 nt
	s_nop 0
	global_load_dwordx4 v[16:19], v[16:17], off sc1 nt
	s_nop 0
	global_load_dwordx4 v[20:23], v[64:65], off sc1 nt
	s_nop 0
	global_load_dwordx4 v[24:27], v[24:25], off sc1 nt
	s_nop 0
	global_load_dwordx4 v[28:31], v[28:29], off sc1 nt
	v_add_co_u32_e32 v36, vcc, s3, v64
	s_mov_b32 s2, 0x12000
	s_nop 0
	v_addc_co_u32_e32 v37, vcc, 0, v65, vcc
	global_load_dwordx4 v[32:35], v[32:33], off sc1 nt
	s_nop 0
	global_load_dwordx4 v[36:39], v[36:37], off sc1 nt
	s_nop 0
	global_load_dwordx4 v[40:43], v[40:41], off sc1 nt
	s_nop 0
	global_load_dwordx4 v[44:47], v[44:45], off sc1 nt
	v_add_co_u32_e32 v52, vcc, s2, v64
	s_mov_b32 s1, 0x1a000
	s_nop 0
	v_addc_co_u32_e32 v53, vcc, 0, v65, vcc
	v_add_co_u32_e32 v60, vcc, s1, v64
	global_load_dwordx4 v[48:51], v[48:49], off sc1 nt
	s_nop 0
	global_load_dwordx4 v[52:55], v[52:53], off sc1 nt
	v_addc_co_u32_e32 v61, vcc, 0, v65, vcc
	global_load_dwordx4 v[56:59], v[56:57], off sc1 nt
	s_nop 0
	global_load_dwordx4 v[60:63], v[60:61], off sc1 nt
	s_mov_b32 s0, 0x1e000
	v_add_co_u32_e32 v64, vcc, s0, v64
	s_lshl_b64 s[0:1], s[10:11], 11
	s_nop 0
	v_addc_co_u32_e32 v65, vcc, 0, v65, vcc
	global_load_dwordx4 v[64:67], v[64:65], off sc1 nt
	s_add_u32 s0, s90, s0
	s_addc_u32 s1, s91, s1
	s_add_u32 s0, s0, s4
	s_addc_u32 s1, s1, s5
	v_lshlrev_b32_e32 v2, 11, v68
	v_lshl_add_u64 v[68:69], s[0:1], 0, v[2:3]
	v_lshl_add_u64 v[80:81], v[68:69], 0, v[0:1]
	v_mov_b32_e32 v68, v3
	v_mov_b32_e32 v69, v3
	v_mov_b32_e32 v70, v3
	v_mov_b32_e32 v71, v3
	v_mov_b32_e32 v72, v3
	v_mov_b32_e32 v73, v3
	v_mov_b32_e32 v74, v3
	v_mov_b32_e32 v75, v3
	v_mov_b32_e32 v76, v3
	v_mov_b32_e32 v77, v3
	v_mov_b32_e32 v78, v3
	v_mov_b32_e32 v79, v3
	s_mov_b64 s[0:1], 0x1100000
	v_lshl_add_u64 v[82:83], v[80:81], 0, s[0:1]
	s_mov_b32 s0, 0x1100000
	s_waitcnt vmcnt(14)
	v_mul_f32_e32 v8, 0x44000000, v8
	s_waitcnt vmcnt(11)
	v_mul_f32_e32 v0, 0x44000000, v20
	s_waitcnt vmcnt(10)
	v_mul_f32_e32 v2, 0x44000000, v24
	s_waitcnt vmcnt(9)
	v_mul_f32_e32 v1, 0x44000000, v28
	v_cvt_pk_fp8_f32 v68, v0, v1
	v_mul_f32_e32 v0, 0x44000000, v12
	v_mul_f32_e32 v16, 0x44000000, v16
	s_waitcnt vmcnt(7)
	v_mul_f32_e32 v1, 0x44000000, v36
	v_cvt_pk_fp8_f32 v69, v0, v1
	v_mul_f32_e32 v0, 0x44000000, v32
	s_waitcnt vmcnt(5)
	v_mul_f32_e32 v1, 0x44000000, v44
	v_cvt_pk_fp8_f32 v68, v2, v16 op_sel:[0,0,1]
	v_cvt_pk_fp8_f32 v69, v0, v1 op_sel:[0,0,1]
	v_mul_f32_e32 v0, 0x44000000, v40
	s_waitcnt vmcnt(4)
	v_mul_f32_e32 v2, 0x44000000, v48
	s_waitcnt vmcnt(3)
	v_mul_f32_e32 v1, 0x44000000, v52
	v_cvt_pk_fp8_f32 v70, v0, v1
	v_mul_f32_e32 v0, 0x44000000, v4
	s_waitcnt vmcnt(1)
	v_mul_f32_e32 v1, 0x44000000, v60
	v_cvt_pk_fp8_f32 v71, v0, v1
	v_mul_f32_e32 v0, 0x44000000, v56
	v_cvt_pk_fp8_f32 v70, v2, v8 op_sel:[0,0,1]
	v_mul_f32_e32 v2, 0x44000000, v25
	v_mul_f32_e32 v4, 0x44000000, v17
	v_mul_f32_e32 v8, 0x44000000, v11
	s_waitcnt vmcnt(0)
	v_mul_f32_e32 v1, 0x44000000, v64
	v_cvt_pk_fp8_f32 v71, v0, v1 op_sel:[0,0,1]
	v_mul_f32_e32 v0, 0x44000000, v21
	v_mul_f32_e32 v1, 0x44000000, v29
	v_cvt_pk_fp8_f32 v72, v0, v1
	v_mul_f32_e32 v0, 0x44000000, v13
	v_mul_f32_e32 v1, 0x44000000, v37
	v_cvt_pk_fp8_f32 v73, v0, v1
	v_mul_f32_e32 v0, 0x44000000, v33
	v_mul_f32_e32 v1, 0x44000000, v45
	v_cvt_pk_fp8_f32 v72, v2, v4 op_sel:[0,0,1]
	v_cvt_pk_fp8_f32 v73, v0, v1 op_sel:[0,0,1]
	v_mul_f32_e32 v0, 0x44000000, v41
	v_mul_f32_e32 v1, 0x44000000, v53
	v_cvt_pk_fp8_f32 v74, v0, v1
	v_mul_f32_e32 v0, 0x44000000, v5
	v_mul_f32_e32 v1, 0x44000000, v61
	v_cvt_pk_fp8_f32 v75, v0, v1
	v_mul_f32_e32 v0, 0x44000000, v57
	v_mul_f32_e32 v1, 0x44000000, v65
	v_mul_f32_e32 v2, 0x44000000, v49
	v_cvt_pk_fp8_f32 v75, v0, v1 op_sel:[0,0,1]
	v_mul_f32_e32 v0, 0x44000000, v22
	v_mul_f32_e32 v1, 0x44000000, v30
	v_cvt_pk_fp8_f32 v76, v0, v1
	v_mul_f32_e32 v0, 0x44000000, v14
	v_mul_f32_e32 v1, 0x44000000, v38
	v_cvt_pk_fp8_f32 v77, v0, v1
	v_mul_f32_e32 v0, 0x44000000, v34
	v_mul_f32_e32 v1, 0x44000000, v46
	v_mul_f32_e32 v4, 0x44000000, v9
	v_cvt_pk_fp8_f32 v77, v0, v1 op_sel:[0,0,1]
	v_mul_f32_e32 v0, 0x44000000, v42
	v_mul_f32_e32 v1, 0x44000000, v54
	v_cvt_pk_fp8_f32 v78, v0, v1
	v_mul_f32_e32 v0, 0x44000000, v6
	v_mul_f32_e32 v1, 0x44000000, v62
	v_cvt_pk_fp8_f32 v79, v0, v1
	v_cvt_pk_fp8_f32 v74, v2, v4 op_sel:[0,0,1]
	v_mul_f32_e32 v2, 0x44000000, v26
	v_mul_f32_e32 v4, 0x44000000, v18
	v_cvt_pk_fp8_f32 v76, v2, v4 op_sel:[0,0,1]
	v_mul_f32_e32 v2, 0x44000000, v50
	v_mul_f32_e32 v4, 0x44000000, v10
	v_mul_f32_e32 v0, 0x44000000, v58
	v_mul_f32_e32 v1, 0x44000000, v66
	v_cvt_pk_fp8_f32 v78, v2, v4 op_sel:[0,0,1]
	v_cvt_pk_fp8_f32 v79, v0, v1 op_sel:[0,0,1]
	v_mul_f32_e32 v1, 0x44000000, v23
	v_mul_f32_e32 v2, 0x44000000, v31
	v_mov_b32_e32 v0, v3
	v_cvt_pk_fp8_f32 v0, v1, v2
	v_mul_f32_e32 v2, 0x44000000, v15
	v_mul_f32_e32 v6, 0x44000000, v39
	v_mov_b32_e32 v1, v3
	v_cvt_pk_fp8_f32 v1, v2, v6
	v_mul_f32_e32 v4, 0x44000000, v27
	v_mul_f32_e32 v5, 0x44000000, v19
	v_cvt_pk_fp8_f32 v0, v4, v5 op_sel:[0,0,1]
	v_mul_f32_e32 v2, 0x44000000, v35
	v_mul_f32_e32 v4, 0x44000000, v47
	v_cvt_pk_fp8_f32 v1, v2, v4 op_sel:[0,0,1]
	v_mul_f32_e32 v4, 0x44000000, v43
	v_mul_f32_e32 v5, 0x44000000, v55
	v_mov_b32_e32 v2, v3
	v_cvt_pk_fp8_f32 v2, v4, v5
	v_mul_f32_e32 v4, 0x44000000, v7
	v_mul_f32_e32 v5, 0x44000000, v63
	v_cvt_pk_fp8_f32 v3, v4, v5
	v_mul_f32_e32 v4, 0x44000000, v59
	v_mul_f32_e32 v5, 0x44000000, v67
	v_mul_f32_e32 v6, 0x44000000, v51
	v_cvt_pk_fp8_f32 v3, v4, v5 op_sel:[0,0,1]
	v_add_co_u32_e32 v4, vcc, s0, v80
	v_cvt_pk_fp8_f32 v2, v6, v8 op_sel:[0,0,1]
	s_nop 0
	v_addc_co_u32_e32 v5, vcc, 0, v81, vcc
	global_store_dwordx4 v[4:5], v[68:71], off sc1 nt
	global_store_dwordx4 v[82:83], v[72:75], off offset:2048 sc1 nt
	v_add_co_u32_e32 v4, vcc, 0x1101000, v80
	s_nop 1
	v_addc_co_u32_e32 v5, vcc, 0, v81, vcc
	global_store_dwordx4 v[4:5], v[76:79], off sc1 nt
	global_store_dwordx4 v[4:5], v[0:3], off offset:2048 sc1 nt
	s_waitcnt vmcnt(0)

.LBB0_308:
	v_lshlrev_b32_e32 v1, 1, v0
	v_and_b32_e32 v130, -16, v1
	v_lshlrev_b32_e32 v0, 2, v0
	v_and_b32_e32 v48, 28, v0
	v_mad_i64_i32 v[0:1], s[18:19], s16, v130, 0
	v_mov_b32_e32 v67, 0
	v_lshl_add_u64 v[0:1], v[0:1], 2, s[14:15]
	v_lshlrev_b32_e32 v66, 2, v48
	s_mov_b32 s3, 0
	v_lshl_add_u64 v[62:63], v[0:1], 0, v[66:67]
	s_mul_i32 s2, s16, 60
	v_lshl_add_u64 v[24:25], v[62:63], 0, s[2:3]
	s_lshl_b32 s2, s16, 2
	s_sub_u32 s2, 0, s2
	s_subb_u32 s3, 0, 0
	v_lshl_add_u64 v[0:1], v[24:25], 0, s[2:3]
	v_lshl_add_u64 v[8:9], v[0:1], 0, s[2:3]
	global_load_dwordx4 v[0:3], v[0:1], off sc1 nt
	s_nop 0
	global_load_dwordx4 v[4:7], v[8:9], off sc1 nt
	v_lshl_add_u64 v[8:9], v[8:9], 0, s[2:3]
	v_lshl_add_u64 v[16:17], v[8:9], 0, s[2:3]
	global_load_dwordx4 v[8:11], v[8:9], off sc1 nt
	s_nop 0
	global_load_dwordx4 v[12:15], v[16:17], off sc1 nt
	v_lshl_add_u64 v[16:17], v[16:17], 0, s[2:3]
	v_lshl_add_u64 v[26:27], v[16:17], 0, s[2:3]
	global_load_dwordx4 v[16:19], v[16:17], off sc1 nt
	s_nop 0
	global_load_dwordx4 v[20:23], v[26:27], off sc1 nt
	v_lshl_add_u64 v[26:27], v[26:27], 0, s[2:3]
	global_load_dwordx4 v[28:31], v[26:27], off sc1 nt
	v_lshl_add_u64 v[26:27], v[26:27], 0, s[2:3]
	global_load_dwordx4 v[32:35], v[26:27], off sc1 nt
	v_lshl_add_u64 v[26:27], v[26:27], 0, s[2:3]
	global_load_dwordx4 v[36:39], v[26:27], off sc1 nt
	v_lshl_add_u64 v[26:27], v[26:27], 0, s[2:3]
	global_load_dwordx4 v[40:43], v[26:27], off sc1 nt
	v_lshl_add_u64 v[26:27], v[26:27], 0, s[2:3]
	global_load_dwordx4 v[44:47], v[26:27], off sc1 nt
	v_lshl_add_u64 v[26:27], v[26:27], 0, s[2:3]
	global_load_dwordx4 v[50:53], v[26:27], off sc1 nt
	v_lshl_add_u64 v[26:27], v[26:27], 0, s[2:3]
	global_load_dwordx4 v[54:57], v[26:27], off sc1 nt
	v_lshl_add_u64 v[26:27], v[26:27], 0, s[2:3]
	global_load_dwordx4 v[58:61], v[26:27], off sc1 nt
	s_nop 0
	global_load_dwordx4 v[24:27], v[24:25], off sc1 nt
	s_nop 0
	global_load_dwordx4 v[62:65], v[62:63], off sc1 nt
	v_ashrrev_i32_e32 v131, 31, v130
	s_and_b64 vcc, exec, s[12:13]
	s_cbranch_vccz .LBB0_311
	s_cmp_lt_u32 s0, 0x18000
	s_cbranch_scc0 .LBB0_312
	s_addk_i32 s1, 0xf3ff
	s_lshr_b32 s14, s1, 10
	s_mov_b32 s15, 0
	s_lshl_b64 s[2:3], s[14:15], 22
	s_lshl_b64 s[12:13], s[14:15], 24
	s_add_u32 s1, s70, s12
	s_addc_u32 s16, s71, s13
	s_add_u32 s2, s90, s2
	s_addc_u32 s3, s91, s3
	s_add_u32 s12, s2, 0x3b100000
	s_addc_u32 s13, s3, 0
	s_lshl_b32 s2, s0, 1
	s_and_b32 s14, s2, 0x780
	s_lshl_b32 s2, s14, 13
	s_add_u32 s1, s1, s2
	s_addc_u32 s2, s16, 0
	s_lshl_b32 s3, s0, 5
	s_and_b32 s18, s3, 0x7e0
	s_lshl_b32 s3, s18, 2
	s_add_u32 s16, s1, s3
	s_mov_b32 s19, s15
	s_addc_u32 s17, s2, 0
	s_mov_b64 s[20:21], 0
	s_branch .LBB0_313

.LBB0_317:
	s_lshl_b64 s[0:1], s[10:11], 11
	s_add_u32 s0, s6, s0
	s_addc_u32 s1, s7, s1
	s_add_u32 s8, s0, s8
	s_addc_u32 s9, s1, s9
	s_lshl_b64 s[2:3], s[18:19], 11
	s_add_u32 s0, s12, s2
	s_addc_u32 s2, s13, s3
	s_add_u32 s6, s0, s14
	v_mov_b32_e32 v49, 0
	s_addc_u32 s7, s2, s15
	v_mad_i64_i32 v[68:69], s[2:3], s20, v130, 0
	v_lshl_add_u64 v[68:69], v[68:69], 2, s[16:17]
	v_mov_b32_e32 v67, v49
	s_mov_b32 s1, 0
	v_lshl_add_u64 v[66:67], v[68:69], 0, v[66:67]
	s_lshl_b32 s0, s20, 2
	v_lshl_add_u64 v[68:69], v[66:67], 0, s[0:1]
	global_load_dwordx4 v[82:85], v[66:67], off sc1 nt
	global_load_dwordx4 v[86:89], v[68:69], off sc1 nt
	v_lshl_add_u64 v[66:67], v[68:69], 0, s[0:1]
	v_lshl_add_u64 v[68:69], v[66:67], 0, s[0:1]
	global_load_dwordx4 v[122:125], v[66:67], off sc1 nt
	global_load_dwordx4 v[126:129], v[68:69], off sc1 nt
	v_lshl_add_u64 v[66:67], v[68:69], 0, s[0:1]
	v_lshl_add_u64 v[68:69], v[66:67], 0, s[0:1]
	global_load_dwordx4 v[110:113], v[66:67], off sc1 nt
	global_load_dwordx4 v[114:117], v[68:69], off sc1 nt
	v_lshl_add_u64 v[66:67], v[68:69], 0, s[0:1]
	v_lshl_add_u64 v[68:69], v[66:67], 0, s[0:1]
	global_load_dwordx4 v[90:93], v[66:67], off sc1 nt
	global_load_dwordx4 v[94:97], v[68:69], off sc1 nt
	v_lshl_add_u64 v[66:67], v[68:69], 0, s[0:1]
	global_load_dwordx4 v[74:77], v[66:67], off sc1 nt
	v_lshl_add_u64 v[66:67], v[66:67], 0, s[0:1]
	global_load_dwordx4 v[98:101], v[66:67], off sc1 nt
	v_lshl_add_u64 v[66:67], v[66:67], 0, s[0:1]
	global_load_dwordx4 v[106:109], v[66:67], off sc1 nt
	v_lshl_add_u64 v[66:67], v[66:67], 0, s[0:1]
	global_load_dwordx4 v[118:121], v[66:67], off sc1 nt
	v_lshl_add_u64 v[66:67], v[66:67], 0, s[0:1]
	global_load_dwordx4 v[78:81], v[66:67], off sc1 nt
	v_lshl_add_u64 v[66:67], v[66:67], 0, s[0:1]
	global_load_dwordx4 v[102:105], v[66:67], off sc1 nt
	v_lshl_add_u64 v[70:71], v[66:67], 0, s[0:1]
	global_load_dwordx4 v[66:69], v[70:71], off sc1 nt
	v_lshl_add_u64 v[70:71], v[70:71], 0, s[0:1]
	global_load_dwordx4 v[70:73], v[70:71], off sc1 nt
	s_waitcnt vmcnt(29)
	v_mul_f32_e32 v8, 0x44000000, v8
	v_mul_f32_e32 v4, 0x44000000, v4
	v_mov_b32_e32 v135, v49
	v_cvt_pk_fp8_f32 v135, v8, v4
	v_mul_f32_e32 v0, 0x44000000, v0
	s_waitcnt vmcnt(17)
	v_mul_f32_e32 v4, 0x44000000, v24
	v_mov_b32_e32 v136, v49
	v_cvt_pk_fp8_f32 v135, v0, v4 op_sel:[0,0,1]
	s_waitcnt vmcnt(16)
	v_mul_f32_e32 v0, 0x44000000, v63
	v_mul_f32_e32 v4, 0x44000000, v59
	v_cvt_pk_fp8_f32 v136, v0, v4
	v_mul_f32_e32 v0, 0x44000000, v45
	v_mul_f32_e32 v4, 0x44000000, v41
	v_mov_b32_e32 v137, v49
	v_cvt_pk_fp8_f32 v137, v0, v4
	v_mul_f32_e32 v28, 0x44000000, v28
	v_mul_f32_e32 v20, 0x44000000, v20
	v_mov_b32_e32 v134, v49
	v_mul_f32_e32 v0, 0x44000000, v37
	v_mul_f32_e32 v4, 0x44000000, v33
	v_mul_f32_e32 v62, 0x44000000, v62
	v_mul_f32_e32 v58, 0x44000000, v58
	v_mov_b32_e32 v132, v49
	v_mul_f32_e32 v44, 0x44000000, v44
	v_mul_f32_e32 v40, 0x44000000, v40
	v_mov_b32_e32 v133, v49
	v_cvt_pk_fp8_f32 v134, v28, v20
	v_cvt_pk_fp8_f32 v137, v0, v4 op_sel:[0,0,1]
	v_mul_f32_e32 v0, 0x44000000, v29
	v_mul_f32_e32 v4, 0x44000000, v21
	v_mov_b32_e32 v138, v49
	v_cvt_pk_fp8_f32 v132, v62, v58
	v_cvt_pk_fp8_f32 v133, v44, v40
	v_cvt_pk_fp8_f32 v138, v0, v4
	v_mul_f32_e32 v0, 0x44000000, v9
	v_mul_f32_e32 v4, 0x44000000, v5
	v_mov_b32_e32 v139, v49
	v_cvt_pk_fp8_f32 v139, v0, v4
	v_mul_f32_e32 v16, 0x44000000, v16
	v_mul_f32_e32 v12, 0x44000000, v12
	v_mul_f32_e32 v54, 0x44000000, v54
	v_mul_f32_e32 v50, 0x44000000, v50
	v_mul_f32_e32 v36, 0x44000000, v36
	v_mul_f32_e32 v32, 0x44000000, v32
	v_cvt_pk_fp8_f32 v134, v16, v12 op_sel:[0,0,1]
	v_mul_f32_e32 v8, 0x44000000, v55
	v_mul_f32_e32 v12, 0x44000000, v51
	v_cvt_pk_fp8_f32 v132, v54, v50 op_sel:[0,0,1]
	v_cvt_pk_fp8_f32 v133, v36, v32 op_sel:[0,0,1]
	v_cvt_pk_fp8_f32 v136, v8, v12 op_sel:[0,0,1]
	v_mul_f32_e32 v8, 0x44000000, v17
	v_mul_f32_e32 v12, 0x44000000, v13
	v_mul_f32_e32 v0, 0x44000000, v1
	v_mul_f32_e32 v1, 0x44000000, v25
	v_lshlrev_b32_e32 v48, 11, v48
	v_cvt_pk_fp8_f32 v138, v8, v12 op_sel:[0,0,1]
	v_cvt_pk_fp8_f32 v139, v0, v1 op_sel:[0,0,1]
	v_lshl_add_u64 v[0:1], s[8:9], 0, v[48:49]
	v_lshl_add_u64 v[0:1], v[0:1], 0, v[130:131]
	global_store_dwordx4 v[0:1], v[132:135], off sc1 nt
	global_store_dwordx4 v[0:1], v[136:139], off offset:2048 sc1 nt
	v_mul_f32_e32 v4, 0x44000000, v64
	v_mul_f32_e32 v5, 0x44000000, v60
	v_mov_b32_e32 v132, v49
	v_cvt_pk_fp8_f32 v132, v4, v5
	v_mul_f32_e32 v4, 0x44000000, v46
	v_mul_f32_e32 v5, 0x44000000, v42
	v_mov_b32_e32 v133, v49
	v_cvt_pk_fp8_f32 v133, v4, v5
	v_mul_f32_e32 v4, 0x44000000, v38
	v_mul_f32_e32 v5, 0x44000000, v34
	v_mov_b32_e32 v134, v49
	v_cvt_pk_fp8_f32 v133, v4, v5 op_sel:[0,0,1]
	v_mul_f32_e32 v4, 0x44000000, v30
	v_mul_f32_e32 v5, 0x44000000, v22
	v_cvt_pk_fp8_f32 v134, v4, v5
	v_mul_f32_e32 v4, 0x44000000, v10
	v_mul_f32_e32 v5, 0x44000000, v6
	v_mov_b32_e32 v135, v49
	v_cvt_pk_fp8_f32 v135, v4, v5
	v_mul_f32_e32 v8, 0x44000000, v56
	v_mul_f32_e32 v9, 0x44000000, v52
	v_mul_f32_e32 v2, 0x44000000, v2
	v_mul_f32_e32 v4, 0x44000000, v26
	v_cvt_pk_fp8_f32 v132, v8, v9 op_sel:[0,0,1]
	v_mul_f32_e32 v8, 0x44000000, v18
	v_mul_f32_e32 v9, 0x44000000, v14
	v_cvt_pk_fp8_f32 v135, v2, v4 op_sel:[0,0,1]
	v_mul_f32_e32 v2, 0x44000000, v65
	v_mul_f32_e32 v5, 0x44000000, v61
	v_mov_b32_e32 v4, v49
	v_cvt_pk_fp8_f32 v134, v8, v9 op_sel:[0,0,1]
	v_cvt_pk_fp8_f32 v4, v2, v5
	v_mul_f32_e32 v2, 0x44000000, v47
	v_mul_f32_e32 v9, 0x44000000, v43
	v_mov_b32_e32 v5, v49
	v_cvt_pk_fp8_f32 v5, v2, v9
	v_mul_f32_e32 v6, 0x44000000, v57
	v_mul_f32_e32 v8, 0x44000000, v53
	v_cvt_pk_fp8_f32 v4, v6, v8 op_sel:[0,0,1]
	v_mul_f32_e32 v2, 0x44000000, v39
	v_mul_f32_e32 v6, 0x44000000, v35
	v_cvt_pk_fp8_f32 v5, v2, v6 op_sel:[0,0,1]
	v_mul_f32_e32 v2, 0x44000000, v31
	v_mul_f32_e32 v8, 0x44000000, v23
	v_mov_b32_e32 v6, v49
	v_cvt_pk_fp8_f32 v6, v2, v8
	v_mul_f32_e32 v2, 0x44000000, v11
	v_mul_f32_e32 v8, 0x44000000, v7
	v_mov_b32_e32 v7, v49
	v_cvt_pk_fp8_f32 v7, v2, v8
	v_mul_f32_e32 v9, 0x44000000, v19
	v_mul_f32_e32 v10, 0x44000000, v15
	v_mul_f32_e32 v2, 0x44000000, v3
	v_mul_f32_e32 v3, 0x44000000, v27
	s_movk_i32 s0, 0x1000
	v_cvt_pk_fp8_f32 v6, v9, v10 op_sel:[0,0,1]
	v_cvt_pk_fp8_f32 v7, v2, v3 op_sel:[0,0,1]
	v_add_co_u32_e32 v0, vcc, s0, v0
	s_waitcnt vmcnt(16)
	v_mul_f32_e32 v2, 0x44000000, v86
	v_addc_co_u32_e32 v1, vcc, 0, v1, vcc
	global_store_dwordx4 v[0:1], v[132:135], off sc1 nt
	global_store_dwordx4 v[0:1], v[4:7], off offset:2048 sc1 nt
	v_mul_f32_e32 v1, 0x44000000, v82
	v_mov_b32_e32 v0, v49
	v_cvt_pk_fp8_f32 v0, v1, v2
	s_waitcnt vmcnt(15)
	v_mul_f32_e32 v2, 0x44000000, v110
	s_waitcnt vmcnt(14)
	v_mul_f32_e32 v5, 0x44000000, v114
	v_mov_b32_e32 v1, v49
	v_cvt_pk_fp8_f32 v1, v2, v5
	v_mul_f32_e32 v3, 0x44000000, v122
	v_mul_f32_e32 v4, 0x44000000, v126
	v_cvt_pk_fp8_f32 v0, v3, v4 op_sel:[0,0,1]
	s_waitcnt vmcnt(13)
	v_mul_f32_e32 v2, 0x44000000, v90
	s_waitcnt vmcnt(12)
	v_mul_f32_e32 v3, 0x44000000, v94
	v_cvt_pk_fp8_f32 v1, v2, v3 op_sel:[0,0,1]
	s_waitcnt vmcnt(11)
	v_mul_f32_e32 v3, 0x44000000, v74
	s_waitcnt vmcnt(10)
	v_mul_f32_e32 v4, 0x44000000, v98
	v_mov_b32_e32 v2, v49
	v_cvt_pk_fp8_f32 v2, v3, v4
	s_waitcnt vmcnt(7)
	v_mul_f32_e32 v4, 0x44000000, v78
	s_waitcnt vmcnt(6)
	v_mul_f32_e32 v7, 0x44000000, v102
	v_mov_b32_e32 v3, v49
	v_cvt_pk_fp8_f32 v3, v4, v7
	v_mul_f32_e32 v5, 0x44000000, v106
	v_mul_f32_e32 v6, 0x44000000, v118
	v_cvt_pk_fp8_f32 v2, v5, v6 op_sel:[0,0,1]
	s_waitcnt vmcnt(5)
	v_mul_f32_e32 v4, 0x44000000, v66
	s_waitcnt vmcnt(4)
	v_mul_f32_e32 v5, 0x44000000, v70
	v_cvt_pk_fp8_f32 v3, v4, v5 op_sel:[0,0,1]
	v_mul_f32_e32 v5, 0x44000000, v83
	v_mul_f32_e32 v6, 0x44000000, v87
	v_mov_b32_e32 v4, v49
	v_cvt_pk_fp8_f32 v4, v5, v6
	v_mul_f32_e32 v6, 0x44000000, v111
	v_mul_f32_e32 v9, 0x44000000, v115
	v_mov_b32_e32 v5, v49
	v_cvt_pk_fp8_f32 v5, v6, v9
	v_mul_f32_e32 v7, 0x44000000, v123
	v_mul_f32_e32 v8, 0x44000000, v127
	v_cvt_pk_fp8_f32 v4, v7, v8 op_sel:[0,0,1]
	v_mul_f32_e32 v6, 0x44000000, v91
	v_mul_f32_e32 v7, 0x44000000, v95
	v_cvt_pk_fp8_f32 v5, v6, v7 op_sel:[0,0,1]
	v_mul_f32_e32 v7, 0x44000000, v75
	v_mul_f32_e32 v8, 0x44000000, v99
	v_mov_b32_e32 v6, v49
	v_cvt_pk_fp8_f32 v6, v7, v8
	v_mul_f32_e32 v8, 0x44000000, v79
	v_mul_f32_e32 v11, 0x44000000, v103
	v_mov_b32_e32 v7, v49
	v_cvt_pk_fp8_f32 v7, v8, v11
	v_mul_f32_e32 v9, 0x44000000, v107
	v_mul_f32_e32 v10, 0x44000000, v119
	v_cvt_pk_fp8_f32 v6, v9, v10 op_sel:[0,0,1]
	v_mul_f32_e32 v8, 0x44000000, v67
	v_mul_f32_e32 v9, 0x44000000, v71
	v_cvt_pk_fp8_f32 v7, v8, v9 op_sel:[0,0,1]
	v_lshl_add_u64 v[8:9], s[6:7], 0, v[48:49]
	v_lshl_add_u64 v[8:9], v[8:9], 0, v[130:131]
	global_store_dwordx4 v[8:9], v[0:3], off sc1 nt
	global_store_dwordx4 v[8:9], v[4:7], off offset:2048 sc1 nt
	v_mov_b32_e32 v46, v49
	v_mul_f32_e32 v1, 0x44000000, v84
	v_mul_f32_e32 v2, 0x44000000, v88
	v_mov_b32_e32 v0, v49
	v_cvt_pk_fp8_f32 v0, v1, v2
	v_mul_f32_e32 v2, 0x44000000, v112
	v_mul_f32_e32 v5, 0x44000000, v116
	v_mov_b32_e32 v1, v49
	v_cvt_pk_fp8_f32 v1, v2, v5
	v_mul_f32_e32 v3, 0x44000000, v124
	v_mul_f32_e32 v4, 0x44000000, v128
	v_cvt_pk_fp8_f32 v0, v3, v4 op_sel:[0,0,1]
	v_mul_f32_e32 v2, 0x44000000, v92
	v_mul_f32_e32 v3, 0x44000000, v96
	v_cvt_pk_fp8_f32 v1, v2, v3 op_sel:[0,0,1]
	v_mul_f32_e32 v3, 0x44000000, v76
	v_mul_f32_e32 v4, 0x44000000, v100
	v_mov_b32_e32 v2, v49
	v_cvt_pk_fp8_f32 v2, v3, v4
	v_mul_f32_e32 v4, 0x44000000, v80
	v_mul_f32_e32 v7, 0x44000000, v104
	v_mov_b32_e32 v3, v49
	v_cvt_pk_fp8_f32 v3, v4, v7
	v_mul_f32_e32 v5, 0x44000000, v108
	v_mul_f32_e32 v6, 0x44000000, v120
	v_cvt_pk_fp8_f32 v2, v5, v6 op_sel:[0,0,1]
	v_mul_f32_e32 v4, 0x44000000, v68
	v_mul_f32_e32 v5, 0x44000000, v72
	v_cvt_pk_fp8_f32 v3, v4, v5 op_sel:[0,0,1]
	v_mul_f32_e32 v4, 0x44000000, v85
	v_mul_f32_e32 v5, 0x44000000, v89
	v_cvt_pk_fp8_f32 v46, v4, v5
	v_mul_f32_e32 v4, 0x44000000, v113
	v_mul_f32_e32 v5, 0x44000000, v117
	v_mov_b32_e32 v47, v49
	v_cvt_pk_fp8_f32 v47, v4, v5
	v_mul_f32_e32 v4, 0x44000000, v93
	v_mul_f32_e32 v5, 0x44000000, v97
	v_mov_b32_e32 v48, v49
	v_cvt_pk_fp8_f32 v47, v4, v5 op_sel:[0,0,1]
	v_mul_f32_e32 v4, 0x44000000, v77
	v_mul_f32_e32 v5, 0x44000000, v101
	v_cvt_pk_fp8_f32 v48, v4, v5
	v_mul_f32_e32 v4, 0x44000000, v81
	v_mul_f32_e32 v5, 0x44000000, v105
	v_cvt_pk_fp8_f32 v49, v4, v5
	v_mul_f32_e32 v6, 0x44000000, v125
	v_mul_f32_e32 v7, 0x44000000, v129
	v_cvt_pk_fp8_f32 v46, v6, v7 op_sel:[0,0,1]
	v_mul_f32_e32 v6, 0x44000000, v109
	v_mul_f32_e32 v7, 0x44000000, v121
	v_mul_f32_e32 v4, 0x44000000, v69
	v_mul_f32_e32 v5, 0x44000000, v73
	v_cvt_pk_fp8_f32 v48, v6, v7 op_sel:[0,0,1]
	v_cvt_pk_fp8_f32 v49, v4, v5 op_sel:[0,0,1]
	v_add_co_u32_e32 v4, vcc, s0, v8
	s_nop 1
	v_addc_co_u32_e32 v5, vcc, 0, v9, vcc
	global_store_dwordx4 v[4:5], v[0:3], off sc1 nt
	global_store_dwordx4 v[4:5], v[46:49], off offset:2048 sc1 nt
	s_waitcnt vmcnt(0)

.LBB0_399:
	v_lshlrev_b32_e32 v1, 1, v0
	v_and_b32_e32 v130, -16, v1
	v_lshlrev_b32_e32 v0, 2, v0
	v_and_b32_e32 v48, 28, v0
	v_mad_i64_i32 v[0:1], s[16:17], s14, v130, 0
	v_mov_b32_e32 v67, 0
	v_lshl_add_u64 v[0:1], v[0:1], 2, s[12:13]
	v_lshlrev_b32_e32 v66, 2, v48
	s_mov_b32 s3, 0
	v_lshl_add_u64 v[62:63], v[0:1], 0, v[66:67]
	s_mul_i32 s2, s14, 60
	v_lshl_add_u64 v[24:25], v[62:63], 0, s[2:3]
	s_lshl_b32 s2, s14, 2
	s_sub_u32 s2, 0, s2
	s_subb_u32 s3, 0, 0
	v_lshl_add_u64 v[0:1], v[24:25], 0, s[2:3]
	v_lshl_add_u64 v[8:9], v[0:1], 0, s[2:3]
	global_load_dwordx4 v[0:3], v[0:1], off sc1 nt
	s_nop 0
	global_load_dwordx4 v[4:7], v[8:9], off sc1 nt
	v_lshl_add_u64 v[8:9], v[8:9], 0, s[2:3]
	v_lshl_add_u64 v[16:17], v[8:9], 0, s[2:3]
	global_load_dwordx4 v[8:11], v[8:9], off sc1 nt
	s_nop 0
	global_load_dwordx4 v[12:15], v[16:17], off sc1 nt
	v_lshl_add_u64 v[16:17], v[16:17], 0, s[2:3]
	v_lshl_add_u64 v[26:27], v[16:17], 0, s[2:3]
	global_load_dwordx4 v[16:19], v[16:17], off sc1 nt
	s_nop 0
	global_load_dwordx4 v[20:23], v[26:27], off sc1 nt
	v_lshl_add_u64 v[26:27], v[26:27], 0, s[2:3]
	global_load_dwordx4 v[28:31], v[26:27], off sc1 nt
	v_lshl_add_u64 v[26:27], v[26:27], 0, s[2:3]
	global_load_dwordx4 v[32:35], v[26:27], off sc1 nt
	v_lshl_add_u64 v[26:27], v[26:27], 0, s[2:3]
	global_load_dwordx4 v[36:39], v[26:27], off sc1 nt
	v_lshl_add_u64 v[26:27], v[26:27], 0, s[2:3]
	global_load_dwordx4 v[40:43], v[26:27], off sc1 nt
	v_lshl_add_u64 v[26:27], v[26:27], 0, s[2:3]
	global_load_dwordx4 v[44:47], v[26:27], off sc1 nt
	v_lshl_add_u64 v[26:27], v[26:27], 0, s[2:3]
	global_load_dwordx4 v[50:53], v[26:27], off sc1 nt
	v_lshl_add_u64 v[26:27], v[26:27], 0, s[2:3]
	global_load_dwordx4 v[54:57], v[26:27], off sc1 nt
	v_lshl_add_u64 v[26:27], v[26:27], 0, s[2:3]
	global_load_dwordx4 v[58:61], v[26:27], off sc1 nt
	s_nop 0
	global_load_dwordx4 v[24:27], v[24:25], off sc1 nt
	s_nop 0
	global_load_dwordx4 v[62:65], v[62:63], off sc1 nt
	v_ashrrev_i32_e32 v131, 31, v130
	s_and_b64 vcc, exec, s[10:11]
	s_cbranch_vccz .LBB0_402
	s_cmp_lt_u32 s0, 0x18000
	s_cbranch_scc0 .LBB0_403
	s_addk_i32 s1, 0xf6ff
	s_lshr_b32 s12, s1, 10
	s_mov_b32 s13, 0
	s_lshl_b64 s[2:3], s[12:13], 22
	s_lshl_b64 s[10:11], s[12:13], 24
	s_add_u32 s1, s70, s10
	s_addc_u32 s14, s71, s11
	s_add_u32 s2, s90, s2
	s_addc_u32 s3, s91, s3
	s_add_u32 s10, s2, 0x3b100000
	s_addc_u32 s11, s3, 0
	s_lshl_b32 s2, s0, 1
	s_and_b32 s12, s2, 0x780
	s_lshl_b32 s2, s12, 13
	s_add_u32 s1, s1, s2
	s_addc_u32 s2, s14, 0
	s_lshl_b32 s3, s0, 5
	s_and_b32 s16, s3, 0x7e0
	s_lshl_b32 s3, s16, 2
	s_add_u32 s14, s1, s3
	s_mov_b32 s17, s13
	s_addc_u32 s15, s2, 0
	s_mov_b64 s[18:19], 0
	s_branch .LBB0_404

.LBB0_408:
	s_lshl_b64 s[0:1], s[8:9], 11
	s_add_u32 s0, s4, s0
	s_addc_u32 s1, s5, s1
	s_add_u32 s6, s0, s6
	s_addc_u32 s7, s1, s7
	s_lshl_b64 s[2:3], s[16:17], 11
	s_add_u32 s0, s10, s2
	s_addc_u32 s2, s11, s3
	s_add_u32 s4, s0, s12
	v_mov_b32_e32 v49, 0
	s_addc_u32 s5, s2, s13
	v_mad_i64_i32 v[68:69], s[2:3], s18, v130, 0
	v_lshl_add_u64 v[68:69], v[68:69], 2, s[14:15]
	v_mov_b32_e32 v67, v49
	s_mov_b32 s1, 0
	v_lshl_add_u64 v[66:67], v[68:69], 0, v[66:67]
	s_lshl_b32 s0, s18, 2
	v_lshl_add_u64 v[68:69], v[66:67], 0, s[0:1]
	global_load_dwordx4 v[82:85], v[66:67], off sc1 nt
	global_load_dwordx4 v[86:89], v[68:69], off sc1 nt
	v_lshl_add_u64 v[66:67], v[68:69], 0, s[0:1]
	v_lshl_add_u64 v[68:69], v[66:67], 0, s[0:1]
	global_load_dwordx4 v[122:125], v[66:67], off sc1 nt
	global_load_dwordx4 v[126:129], v[68:69], off sc1 nt
	v_lshl_add_u64 v[66:67], v[68:69], 0, s[0:1]
	v_lshl_add_u64 v[68:69], v[66:67], 0, s[0:1]
	global_load_dwordx4 v[110:113], v[66:67], off sc1 nt
	global_load_dwordx4 v[114:117], v[68:69], off sc1 nt
	v_lshl_add_u64 v[66:67], v[68:69], 0, s[0:1]
	v_lshl_add_u64 v[68:69], v[66:67], 0, s[0:1]
	global_load_dwordx4 v[90:93], v[66:67], off sc1 nt
	global_load_dwordx4 v[94:97], v[68:69], off sc1 nt
	v_lshl_add_u64 v[66:67], v[68:69], 0, s[0:1]
	global_load_dwordx4 v[74:77], v[66:67], off sc1 nt
	v_lshl_add_u64 v[66:67], v[66:67], 0, s[0:1]
	global_load_dwordx4 v[98:101], v[66:67], off sc1 nt
	v_lshl_add_u64 v[66:67], v[66:67], 0, s[0:1]
	global_load_dwordx4 v[106:109], v[66:67], off sc1 nt
	v_lshl_add_u64 v[66:67], v[66:67], 0, s[0:1]
	global_load_dwordx4 v[118:121], v[66:67], off sc1 nt
	v_lshl_add_u64 v[66:67], v[66:67], 0, s[0:1]
	global_load_dwordx4 v[78:81], v[66:67], off sc1 nt
	v_lshl_add_u64 v[66:67], v[66:67], 0, s[0:1]
	global_load_dwordx4 v[102:105], v[66:67], off sc1 nt
	v_lshl_add_u64 v[70:71], v[66:67], 0, s[0:1]
	global_load_dwordx4 v[66:69], v[70:71], off sc1 nt
	v_lshl_add_u64 v[70:71], v[70:71], 0, s[0:1]
	global_load_dwordx4 v[70:73], v[70:71], off sc1 nt
	s_waitcnt vmcnt(29)
	v_mul_f32_e32 v8, 0x44000000, v8
	v_mul_f32_e32 v4, 0x44000000, v4
	v_mov_b32_e32 v135, v49
	v_cvt_pk_fp8_f32 v135, v8, v4
	v_mul_f32_e32 v0, 0x44000000, v0
	s_waitcnt vmcnt(17)
	v_mul_f32_e32 v4, 0x44000000, v24
	v_mov_b32_e32 v136, v49
	v_cvt_pk_fp8_f32 v135, v0, v4 op_sel:[0,0,1]
	s_waitcnt vmcnt(16)
	v_mul_f32_e32 v0, 0x44000000, v63
	v_mul_f32_e32 v4, 0x44000000, v59
	v_cvt_pk_fp8_f32 v136, v0, v4
	v_mul_f32_e32 v0, 0x44000000, v45
	v_mul_f32_e32 v4, 0x44000000, v41
	v_mov_b32_e32 v137, v49
	v_cvt_pk_fp8_f32 v137, v0, v4
	v_mul_f32_e32 v28, 0x44000000, v28
	v_mul_f32_e32 v20, 0x44000000, v20
	v_mov_b32_e32 v134, v49
	v_mul_f32_e32 v0, 0x44000000, v37
	v_mul_f32_e32 v4, 0x44000000, v33
	v_mul_f32_e32 v62, 0x44000000, v62
	v_mul_f32_e32 v58, 0x44000000, v58
	v_mov_b32_e32 v132, v49
	v_mul_f32_e32 v44, 0x44000000, v44
	v_mul_f32_e32 v40, 0x44000000, v40
	v_mov_b32_e32 v133, v49
	v_cvt_pk_fp8_f32 v134, v28, v20
	v_cvt_pk_fp8_f32 v137, v0, v4 op_sel:[0,0,1]
	v_mul_f32_e32 v0, 0x44000000, v29
	v_mul_f32_e32 v4, 0x44000000, v21
	v_mov_b32_e32 v138, v49
	v_cvt_pk_fp8_f32 v132, v62, v58
	v_cvt_pk_fp8_f32 v133, v44, v40
	v_cvt_pk_fp8_f32 v138, v0, v4
	v_mul_f32_e32 v0, 0x44000000, v9
	v_mul_f32_e32 v4, 0x44000000, v5
	v_mov_b32_e32 v139, v49
	v_cvt_pk_fp8_f32 v139, v0, v4
	v_mul_f32_e32 v16, 0x44000000, v16
	v_mul_f32_e32 v12, 0x44000000, v12
	v_mul_f32_e32 v54, 0x44000000, v54
	v_mul_f32_e32 v50, 0x44000000, v50
	v_mul_f32_e32 v36, 0x44000000, v36
	v_mul_f32_e32 v32, 0x44000000, v32
	v_cvt_pk_fp8_f32 v134, v16, v12 op_sel:[0,0,1]
	v_mul_f32_e32 v8, 0x44000000, v55
	v_mul_f32_e32 v12, 0x44000000, v51
	v_cvt_pk_fp8_f32 v132, v54, v50 op_sel:[0,0,1]
	v_cvt_pk_fp8_f32 v133, v36, v32 op_sel:[0,0,1]
	v_cvt_pk_fp8_f32 v136, v8, v12 op_sel:[0,0,1]
	v_mul_f32_e32 v8, 0x44000000, v17
	v_mul_f32_e32 v12, 0x44000000, v13
	v_mul_f32_e32 v0, 0x44000000, v1
	v_mul_f32_e32 v1, 0x44000000, v25
	v_lshlrev_b32_e32 v48, 11, v48
	v_cvt_pk_fp8_f32 v138, v8, v12 op_sel:[0,0,1]
	v_cvt_pk_fp8_f32 v139, v0, v1 op_sel:[0,0,1]
	v_lshl_add_u64 v[0:1], s[6:7], 0, v[48:49]
	v_lshl_add_u64 v[0:1], v[0:1], 0, v[130:131]
	global_store_dwordx4 v[0:1], v[132:135], off sc1 nt
	global_store_dwordx4 v[0:1], v[136:139], off offset:2048 sc1 nt
	v_mul_f32_e32 v4, 0x44000000, v64
	v_mul_f32_e32 v5, 0x44000000, v60
	v_mov_b32_e32 v132, v49
	v_cvt_pk_fp8_f32 v132, v4, v5
	v_mul_f32_e32 v4, 0x44000000, v46
	v_mul_f32_e32 v5, 0x44000000, v42
	v_mov_b32_e32 v133, v49
	v_cvt_pk_fp8_f32 v133, v4, v5
	v_mul_f32_e32 v4, 0x44000000, v38
	v_mul_f32_e32 v5, 0x44000000, v34
	v_mov_b32_e32 v134, v49
	v_cvt_pk_fp8_f32 v133, v4, v5 op_sel:[0,0,1]
	v_mul_f32_e32 v4, 0x44000000, v30
	v_mul_f32_e32 v5, 0x44000000, v22
	v_cvt_pk_fp8_f32 v134, v4, v5
	v_mul_f32_e32 v4, 0x44000000, v10
	v_mul_f32_e32 v5, 0x44000000, v6
	v_mov_b32_e32 v135, v49
	v_cvt_pk_fp8_f32 v135, v4, v5
	v_mul_f32_e32 v8, 0x44000000, v56
	v_mul_f32_e32 v9, 0x44000000, v52
	v_mul_f32_e32 v2, 0x44000000, v2
	v_mul_f32_e32 v4, 0x44000000, v26
	v_cvt_pk_fp8_f32 v132, v8, v9 op_sel:[0,0,1]
	v_mul_f32_e32 v8, 0x44000000, v18
	v_mul_f32_e32 v9, 0x44000000, v14
	v_cvt_pk_fp8_f32 v135, v2, v4 op_sel:[0,0,1]
	v_mul_f32_e32 v2, 0x44000000, v65
	v_mul_f32_e32 v5, 0x44000000, v61
	v_mov_b32_e32 v4, v49
	v_cvt_pk_fp8_f32 v134, v8, v9 op_sel:[0,0,1]
	v_cvt_pk_fp8_f32 v4, v2, v5
	v_mul_f32_e32 v2, 0x44000000, v47
	v_mul_f32_e32 v9, 0x44000000, v43
	v_mov_b32_e32 v5, v49
	v_cvt_pk_fp8_f32 v5, v2, v9
	v_mul_f32_e32 v6, 0x44000000, v57
	v_mul_f32_e32 v8, 0x44000000, v53
	v_cvt_pk_fp8_f32 v4, v6, v8 op_sel:[0,0,1]
	v_mul_f32_e32 v2, 0x44000000, v39
	v_mul_f32_e32 v6, 0x44000000, v35
	v_cvt_pk_fp8_f32 v5, v2, v6 op_sel:[0,0,1]
	v_mul_f32_e32 v2, 0x44000000, v31
	v_mul_f32_e32 v8, 0x44000000, v23
	v_mov_b32_e32 v6, v49
	v_cvt_pk_fp8_f32 v6, v2, v8
	v_mul_f32_e32 v2, 0x44000000, v11
	v_mul_f32_e32 v8, 0x44000000, v7
	v_mov_b32_e32 v7, v49
	v_cvt_pk_fp8_f32 v7, v2, v8
	v_mul_f32_e32 v9, 0x44000000, v19
	v_mul_f32_e32 v10, 0x44000000, v15
	v_mul_f32_e32 v2, 0x44000000, v3
	v_mul_f32_e32 v3, 0x44000000, v27
	s_movk_i32 s0, 0x1000
	v_cvt_pk_fp8_f32 v6, v9, v10 op_sel:[0,0,1]
	v_cvt_pk_fp8_f32 v7, v2, v3 op_sel:[0,0,1]
	v_add_co_u32_e32 v0, vcc, s0, v0
	s_waitcnt vmcnt(16)
	v_mul_f32_e32 v2, 0x44000000, v86
	v_addc_co_u32_e32 v1, vcc, 0, v1, vcc
	global_store_dwordx4 v[0:1], v[132:135], off sc1 nt
	global_store_dwordx4 v[0:1], v[4:7], off offset:2048 sc1 nt
	v_mul_f32_e32 v1, 0x44000000, v82
	v_mov_b32_e32 v0, v49
	v_cvt_pk_fp8_f32 v0, v1, v2
	s_waitcnt vmcnt(15)
	v_mul_f32_e32 v2, 0x44000000, v110
	s_waitcnt vmcnt(14)
	v_mul_f32_e32 v5, 0x44000000, v114
	v_mov_b32_e32 v1, v49
	v_cvt_pk_fp8_f32 v1, v2, v5
	v_mul_f32_e32 v3, 0x44000000, v122
	v_mul_f32_e32 v4, 0x44000000, v126
	v_cvt_pk_fp8_f32 v0, v3, v4 op_sel:[0,0,1]
	s_waitcnt vmcnt(13)
	v_mul_f32_e32 v2, 0x44000000, v90
	s_waitcnt vmcnt(12)
	v_mul_f32_e32 v3, 0x44000000, v94
	v_cvt_pk_fp8_f32 v1, v2, v3 op_sel:[0,0,1]
	s_waitcnt vmcnt(11)
	v_mul_f32_e32 v3, 0x44000000, v74
	s_waitcnt vmcnt(10)
	v_mul_f32_e32 v4, 0x44000000, v98
	v_mov_b32_e32 v2, v49
	v_cvt_pk_fp8_f32 v2, v3, v4
	s_waitcnt vmcnt(7)
	v_mul_f32_e32 v4, 0x44000000, v78
	s_waitcnt vmcnt(6)
	v_mul_f32_e32 v7, 0x44000000, v102
	v_mov_b32_e32 v3, v49
	v_cvt_pk_fp8_f32 v3, v4, v7
	v_mul_f32_e32 v5, 0x44000000, v106
	v_mul_f32_e32 v6, 0x44000000, v118
	v_cvt_pk_fp8_f32 v2, v5, v6 op_sel:[0,0,1]
	s_waitcnt vmcnt(5)
	v_mul_f32_e32 v4, 0x44000000, v66
	s_waitcnt vmcnt(4)
	v_mul_f32_e32 v5, 0x44000000, v70
	v_cvt_pk_fp8_f32 v3, v4, v5 op_sel:[0,0,1]
	v_mul_f32_e32 v5, 0x44000000, v83
	v_mul_f32_e32 v6, 0x44000000, v87
	v_mov_b32_e32 v4, v49
	v_cvt_pk_fp8_f32 v4, v5, v6
	v_mul_f32_e32 v6, 0x44000000, v111
	v_mul_f32_e32 v9, 0x44000000, v115
	v_mov_b32_e32 v5, v49
	v_cvt_pk_fp8_f32 v5, v6, v9
	v_mul_f32_e32 v7, 0x44000000, v123
	v_mul_f32_e32 v8, 0x44000000, v127
	v_cvt_pk_fp8_f32 v4, v7, v8 op_sel:[0,0,1]
	v_mul_f32_e32 v6, 0x44000000, v91
	v_mul_f32_e32 v7, 0x44000000, v95
	v_cvt_pk_fp8_f32 v5, v6, v7 op_sel:[0,0,1]
	v_mul_f32_e32 v7, 0x44000000, v75
	v_mul_f32_e32 v8, 0x44000000, v99
	v_mov_b32_e32 v6, v49
	v_cvt_pk_fp8_f32 v6, v7, v8
	v_mul_f32_e32 v8, 0x44000000, v79
	v_mul_f32_e32 v11, 0x44000000, v103
	v_mov_b32_e32 v7, v49
	v_cvt_pk_fp8_f32 v7, v8, v11
	v_mul_f32_e32 v9, 0x44000000, v107
	v_mul_f32_e32 v10, 0x44000000, v119
	v_cvt_pk_fp8_f32 v6, v9, v10 op_sel:[0,0,1]
	v_mul_f32_e32 v8, 0x44000000, v67
	v_mul_f32_e32 v9, 0x44000000, v71
	v_cvt_pk_fp8_f32 v7, v8, v9 op_sel:[0,0,1]
	v_lshl_add_u64 v[8:9], s[4:5], 0, v[48:49]
	v_lshl_add_u64 v[8:9], v[8:9], 0, v[130:131]
	global_store_dwordx4 v[8:9], v[0:3], off sc1 nt
	global_store_dwordx4 v[8:9], v[4:7], off offset:2048 sc1 nt
	v_mov_b32_e32 v46, v49
	v_mul_f32_e32 v1, 0x44000000, v84
	v_mul_f32_e32 v2, 0x44000000, v88
	v_mov_b32_e32 v0, v49
	v_cvt_pk_fp8_f32 v0, v1, v2
	v_mul_f32_e32 v2, 0x44000000, v112
	v_mul_f32_e32 v5, 0x44000000, v116
	v_mov_b32_e32 v1, v49
	v_cvt_pk_fp8_f32 v1, v2, v5
	v_mul_f32_e32 v3, 0x44000000, v124
	v_mul_f32_e32 v4, 0x44000000, v128
	v_cvt_pk_fp8_f32 v0, v3, v4 op_sel:[0,0,1]
	v_mul_f32_e32 v2, 0x44000000, v92
	v_mul_f32_e32 v3, 0x44000000, v96
	v_cvt_pk_fp8_f32 v1, v2, v3 op_sel:[0,0,1]
	v_mul_f32_e32 v3, 0x44000000, v76
	v_mul_f32_e32 v4, 0x44000000, v100
	v_mov_b32_e32 v2, v49
	v_cvt_pk_fp8_f32 v2, v3, v4
	v_mul_f32_e32 v4, 0x44000000, v80
	v_mul_f32_e32 v7, 0x44000000, v104
	v_mov_b32_e32 v3, v49
	v_cvt_pk_fp8_f32 v3, v4, v7
	v_mul_f32_e32 v5, 0x44000000, v108
	v_mul_f32_e32 v6, 0x44000000, v120
	v_cvt_pk_fp8_f32 v2, v5, v6 op_sel:[0,0,1]
	v_mul_f32_e32 v4, 0x44000000, v68
	v_mul_f32_e32 v5, 0x44000000, v72
	v_cvt_pk_fp8_f32 v3, v4, v5 op_sel:[0,0,1]
	v_mul_f32_e32 v4, 0x44000000, v85
	v_mul_f32_e32 v5, 0x44000000, v89
	v_cvt_pk_fp8_f32 v46, v4, v5
	v_mul_f32_e32 v4, 0x44000000, v113
	v_mul_f32_e32 v5, 0x44000000, v117
	v_mov_b32_e32 v47, v49
	v_cvt_pk_fp8_f32 v47, v4, v5
	v_mul_f32_e32 v4, 0x44000000, v93
	v_mul_f32_e32 v5, 0x44000000, v97
	v_mov_b32_e32 v48, v49
	v_cvt_pk_fp8_f32 v47, v4, v5 op_sel:[0,0,1]
	v_mul_f32_e32 v4, 0x44000000, v77
	v_mul_f32_e32 v5, 0x44000000, v101
	v_cvt_pk_fp8_f32 v48, v4, v5
	v_mul_f32_e32 v4, 0x44000000, v81
	v_mul_f32_e32 v5, 0x44000000, v105
	v_cvt_pk_fp8_f32 v49, v4, v5
	v_mul_f32_e32 v6, 0x44000000, v125
	v_mul_f32_e32 v7, 0x44000000, v129
	v_cvt_pk_fp8_f32 v46, v6, v7 op_sel:[0,0,1]
	v_mul_f32_e32 v6, 0x44000000, v109
	v_mul_f32_e32 v7, 0x44000000, v121
	v_mul_f32_e32 v4, 0x44000000, v69
	v_mul_f32_e32 v5, 0x44000000, v73
	v_cvt_pk_fp8_f32 v48, v6, v7 op_sel:[0,0,1]
	v_cvt_pk_fp8_f32 v49, v4, v5 op_sel:[0,0,1]
	v_add_co_u32_e32 v4, vcc, s0, v8
	s_nop 1
	v_addc_co_u32_e32 v5, vcc, 0, v9, vcc
	global_store_dwordx4 v[4:5], v[0:3], off sc1 nt
	global_store_dwordx4 v[4:5], v[46:49], off offset:2048 sc1 nt
	s_waitcnt vmcnt(0)

.LBB0_479:
	s_not_b32 s2, s0
	s_add_i32 s1, s1, s2
	s_cmp_lt_i32 s1, -7
	s_cbranch_scc1 .LBB0_498
	s_ashr_i32 s2, s1, 31
	v_lshlrev_b32_e32 v1, 1, v0
	s_lshr_b32 s2, s2, 29
	v_and_b32_e32 v128, -16, v1
	v_lshlrev_b32_e32 v0, 2, v0
	s_add_i32 s2, s1, s2
	v_and_b32_e32 v64, 28, v0
	s_ashr_i32 s1, s2, 3
	s_and_b32 s2, s2, -8
	v_mad_i64_i32 v[0:1], s[4:5], s18, v128, 0
	v_mov_b32_e32 v131, 0
	s_add_i32 s2, s2, s0
	v_lshl_add_u64 v[0:1], v[0:1], 2, s[16:17]
	v_lshlrev_b32_e32 v130, 2, v64
	s_lshl_b32 s3, s18, 2
	s_mov_b32 s9, 0
	s_waitcnt vmcnt(4)
	v_lshl_add_u64 v[60:61], v[0:1], 0, v[130:131]
	s_mul_i32 s8, s18, 60
	s_sub_u32 s4, 0, s3
	v_lshl_add_u64 v[44:45], v[60:61], 0, s[8:9]
	s_subb_u32 s5, 0, 0
	v_lshl_add_u64 v[0:1], v[44:45], 0, s[4:5]
	v_lshl_add_u64 v[8:9], v[0:1], 0, s[4:5]
	global_load_dwordx4 v[0:3], v[0:1], off sc1 nt
	s_nop 0
	global_load_dwordx4 v[4:7], v[8:9], off sc1 nt
	v_lshl_add_u64 v[8:9], v[8:9], 0, s[4:5]
	v_lshl_add_u64 v[16:17], v[8:9], 0, s[4:5]
	global_load_dwordx4 v[8:11], v[8:9], off sc1 nt
	s_nop 0
	global_load_dwordx4 v[12:15], v[16:17], off sc1 nt
	v_lshl_add_u64 v[16:17], v[16:17], 0, s[4:5]
	v_lshl_add_u64 v[24:25], v[16:17], 0, s[4:5]
	v_lshl_add_u64 v[28:29], v[24:25], 0, s[4:5]
	v_lshl_add_u64 v[32:33], v[28:29], 0, s[4:5]
	v_lshl_add_u64 v[36:37], v[32:33], 0, s[4:5]
	v_lshl_add_u64 v[40:41], v[36:37], 0, s[4:5]
	v_lshl_add_u64 v[46:47], v[40:41], 0, s[4:5]
	global_load_dwordx4 v[16:19], v[16:17], off sc1 nt
	s_nop 0
	global_load_dwordx4 v[20:23], v[24:25], off sc1 nt
	v_ashrrev_i32_e32 v129, 31, v128
	global_load_dwordx4 v[24:27], v[28:29], off sc1 nt
	v_lshlrev_b32_e32 v132, 11, v64
	global_load_dwordx4 v[28:31], v[32:33], off sc1 nt
	v_mov_b32_e32 v133, v131
	global_load_dwordx4 v[32:35], v[36:37], off sc1 nt
	v_lshlrev_b32_e32 v130, 2, v64
	global_load_dwordx4 v[36:39], v[40:41], off sc1 nt
	s_movk_i32 s7, 0x1000
	global_load_dwordx4 v[40:43], v[46:47], off sc1 nt
	v_lshl_add_u64 v[46:47], v[46:47], 0, s[4:5]
	global_load_dwordx4 v[48:51], v[46:47], off sc1 nt
	v_lshl_add_u64 v[46:47], v[46:47], 0, s[4:5]
	global_load_dwordx4 v[56:59], v[46:47], off sc1 nt
	v_lshl_add_u64 v[46:47], v[46:47], 0, s[4:5]
	global_load_dwordx4 v[52:55], v[46:47], off sc1 nt
	s_nop 0
	global_load_dwordx4 v[44:47], v[44:45], off sc1 nt
	s_nop 0
	global_load_dwordx4 v[60:63], v[60:61], off sc1 nt
	s_lshl_b64 s[4:5], s[14:15], 11
	s_add_u32 s3, s10, s4
	s_addc_u32 s4, s11, s5
	s_add_u32 s12, s3, s12
	s_addc_u32 s13, s4, s13
	s_add_u32 s3, s90, 0x3b100000
	s_addc_u32 s4, s91, 0
	s_add_u32 s10, s90, 0x1900000
	s_addc_u32 s11, s91, 0
	s_add_u32 s5, s90, 0x4b100000
	s_addc_u32 s6, s91, 0
	s_mov_b32 s28, 0
	s_branch .LBB0_482
.LBB0_481:
	s_lshl_b64 s[16:17], s[16:17], 11
	s_add_u32 s8, s14, s16
	s_addc_u32 s15, s15, s17
	s_add_u32 s14, s8, s18
	s_addc_u32 s15, s15, s19
	s_lshl_b64 s[16:17], s[22:23], 11
	s_add_u32 s8, s12, s16
	s_addc_u32 s13, s13, s17
	v_mad_i64_i32 v[0:1], s[16:17], s26, v128, 0
	s_add_u32 s12, s8, s24
	v_lshl_add_u64 v[0:1], v[0:1], 2, s[20:21]
	s_addc_u32 s13, s13, s25
	v_lshl_add_u64 v[0:1], v[0:1], 0, v[130:131]
	s_lshl_b32 s8, s26, 2
	v_lshl_add_u64 v[2:3], v[0:1], 0, s[8:9]
	global_load_dwordx4 v[60:63], v[0:1], off sc1 nt
	global_load_dwordx4 v[52:55], v[2:3], off sc1 nt
	v_lshl_add_u64 v[0:1], v[2:3], 0, s[8:9]
	v_lshl_add_u64 v[2:3], v[0:1], 0, s[8:9]
	global_load_dwordx4 v[56:59], v[0:1], off sc1 nt
	global_load_dwordx4 v[48:51], v[2:3], off sc1 nt
	v_lshl_add_u64 v[0:1], v[2:3], 0, s[8:9]
	v_lshl_add_u64 v[2:3], v[0:1], 0, s[8:9]
	global_load_dwordx4 v[40:43], v[0:1], off sc1 nt
	global_load_dwordx4 v[36:39], v[2:3], off sc1 nt
	v_lshl_add_u64 v[0:1], v[2:3], 0, s[8:9]
	v_lshl_add_u64 v[2:3], v[0:1], 0, s[8:9]
	global_load_dwordx4 v[32:35], v[0:1], off sc1 nt
	global_load_dwordx4 v[28:31], v[2:3], off sc1 nt
	v_lshl_add_u64 v[0:1], v[2:3], 0, s[8:9]
	global_load_dwordx4 v[24:27], v[0:1], off sc1 nt
	v_lshl_add_u64 v[0:1], v[0:1], 0, s[8:9]
	global_load_dwordx4 v[20:23], v[0:1], off sc1 nt
	v_lshl_add_u64 v[0:1], v[0:1], 0, s[8:9]
	global_load_dwordx4 v[16:19], v[0:1], off sc1 nt
	v_lshl_add_u64 v[0:1], v[0:1], 0, s[8:9]
	global_load_dwordx4 v[12:15], v[0:1], off sc1 nt
	v_lshl_add_u64 v[0:1], v[0:1], 0, s[8:9]
	global_load_dwordx4 v[8:11], v[0:1], off sc1 nt
	v_lshl_add_u64 v[0:1], v[0:1], 0, s[8:9]
	v_lshl_add_u64 v[44:45], v[0:1], 0, s[8:9]
	global_load_dwordx4 v[4:7], v[0:1], off sc1 nt
	s_waitcnt vmcnt(33)
	v_mul_f32_e32 v80, 0x44000000, v80
	global_load_dwordx4 v[0:3], v[44:45], off sc1 nt
	v_lshl_add_u64 v[44:45], v[44:45], 0, s[8:9]
	global_load_dwordx4 v[44:47], v[44:45], off sc1 nt
	s_waitcnt vmcnt(34)
	v_mul_f32_e32 v84, 0x44000000, v84
	v_mov_b32_e32 v134, v131
	v_cvt_pk_fp8_f32 v134, v80, v84
	s_waitcnt vmcnt(31)
	v_mul_f32_e32 v80, 0x44000000, v108
	s_waitcnt vmcnt(30)
	v_mul_f32_e32 v84, 0x44000000, v112
	v_mov_b32_e32 v135, v131
	v_cvt_pk_fp8_f32 v135, v80, v84
	s_waitcnt vmcnt(29)
	v_mul_f32_e32 v80, 0x44000000, v88
	s_waitcnt vmcnt(28)
	v_mul_f32_e32 v84, 0x44000000, v92
	s_waitcnt vmcnt(27)
	v_mul_f32_e32 v72, 0x44000000, v72
	v_cvt_pk_fp8_f32 v135, v80, v84 op_sel:[0,0,1]
	s_waitcnt vmcnt(26)
	v_mul_f32_e32 v80, 0x44000000, v96
	v_mov_b32_e32 v136, v131
	v_cvt_pk_fp8_f32 v136, v72, v80
	s_waitcnt vmcnt(23)
	v_mul_f32_e32 v72, 0x44000000, v76
	s_waitcnt vmcnt(22)
	v_mul_f32_e32 v76, 0x44000000, v100
	v_mov_b32_e32 v137, v131
	v_cvt_pk_fp8_f32 v137, v72, v76
	s_waitcnt vmcnt(21)
	v_mul_f32_e32 v64, 0x44000000, v64
	s_waitcnt vmcnt(20)
	v_mul_f32_e32 v68, 0x44000000, v68
	v_mov_b32_e32 v138, v131
	v_cvt_pk_fp8_f32 v137, v64, v68 op_sel:[0,0,1]
	v_mul_f32_e32 v64, 0x44000000, v81
	v_mul_f32_e32 v68, 0x44000000, v85
	v_cvt_pk_fp8_f32 v138, v64, v68
	v_mul_f32_e32 v64, 0x44000000, v109
	v_mul_f32_e32 v68, 0x44000000, v113
	v_mov_b32_e32 v139, v131
	v_cvt_pk_fp8_f32 v139, v64, v68
	v_mul_f32_e32 v64, 0x44000000, v89
	v_mul_f32_e32 v68, 0x44000000, v93
	v_mov_b32_e32 v140, v131
	v_cvt_pk_fp8_f32 v139, v64, v68 op_sel:[0,0,1]
	v_mul_f32_e32 v64, 0x44000000, v73
	v_mul_f32_e32 v68, 0x44000000, v97
	v_cvt_pk_fp8_f32 v140, v64, v68
	v_mul_f32_e32 v64, 0x44000000, v77
	v_mul_f32_e32 v68, 0x44000000, v101
	v_mov_b32_e32 v141, v131
	v_cvt_pk_fp8_f32 v141, v64, v68
	v_mul_f32_e32 v120, 0x44000000, v120
	v_mul_f32_e32 v124, 0x44000000, v124
	v_mul_f32_e32 v84, 0x44000000, v104
	v_mul_f32_e32 v88, 0x44000000, v116
	v_mul_f32_e32 v72, 0x44000000, v121
	v_mul_f32_e32 v76, 0x44000000, v125
	v_cvt_pk_fp8_f32 v134, v120, v124 op_sel:[0,0,1]
	v_cvt_pk_fp8_f32 v136, v84, v88 op_sel:[0,0,1]
	v_cvt_pk_fp8_f32 v138, v72, v76 op_sel:[0,0,1]
	v_mul_f32_e32 v72, 0x44000000, v105
	v_mul_f32_e32 v73, 0x44000000, v117
	v_mul_f32_e32 v64, 0x44000000, v65
	v_mul_f32_e32 v65, 0x44000000, v69
	v_cvt_pk_fp8_f32 v140, v72, v73 op_sel:[0,0,1]
	v_cvt_pk_fp8_f32 v141, v64, v65 op_sel:[0,0,1]
	v_lshl_add_u64 v[64:65], s[14:15], 0, v[132:133]
	v_lshl_add_u64 v[64:65], v[64:65], 0, v[128:129]
	global_store_dwordx4 v[64:65], v[134:137], off sc1 nt
	global_store_dwordx4 v[64:65], v[138:141], off offset:2048 sc1 nt
	v_mul_f32_e32 v68, 0x44000000, v82
	v_mul_f32_e32 v69, 0x44000000, v86
	v_mov_b32_e32 v134, v131
	v_cvt_pk_fp8_f32 v134, v68, v69
	v_mul_f32_e32 v68, 0x44000000, v110
	v_mul_f32_e32 v69, 0x44000000, v114
	v_mov_b32_e32 v135, v131
	v_cvt_pk_fp8_f32 v135, v68, v69
	v_mul_f32_e32 v68, 0x44000000, v90
	v_mul_f32_e32 v69, 0x44000000, v94
	v_mov_b32_e32 v136, v131
	v_cvt_pk_fp8_f32 v135, v68, v69 op_sel:[0,0,1]
	v_mul_f32_e32 v68, 0x44000000, v74
	v_mul_f32_e32 v69, 0x44000000, v98
	v_cvt_pk_fp8_f32 v136, v68, v69
	v_mul_f32_e32 v68, 0x44000000, v78
	v_mul_f32_e32 v69, 0x44000000, v102
	v_mov_b32_e32 v137, v131
	v_cvt_pk_fp8_f32 v137, v68, v69
	v_mul_f32_e32 v72, 0x44000000, v122
	v_mul_f32_e32 v73, 0x44000000, v126
	v_cvt_pk_fp8_f32 v134, v72, v73 op_sel:[0,0,1]
	v_mul_f32_e32 v72, 0x44000000, v106
	v_mul_f32_e32 v73, 0x44000000, v118
	v_mul_f32_e32 v66, 0x44000000, v66
	v_mul_f32_e32 v68, 0x44000000, v70
	v_cvt_pk_fp8_f32 v136, v72, v73 op_sel:[0,0,1]
	v_cvt_pk_fp8_f32 v137, v66, v68 op_sel:[0,0,1]
	v_mul_f32_e32 v66, 0x44000000, v83
	v_mul_f32_e32 v68, 0x44000000, v87
	v_mov_b32_e32 v72, v131
	v_cvt_pk_fp8_f32 v72, v66, v68
	v_mul_f32_e32 v66, 0x44000000, v111
	v_mul_f32_e32 v68, 0x44000000, v115
	v_mov_b32_e32 v73, v131
	v_cvt_pk_fp8_f32 v73, v66, v68
	v_mul_f32_e32 v66, 0x44000000, v91
	v_mul_f32_e32 v68, 0x44000000, v95
	v_mov_b32_e32 v74, v131
	v_cvt_pk_fp8_f32 v73, v66, v68 op_sel:[0,0,1]
	v_mul_f32_e32 v66, 0x44000000, v75
	v_mul_f32_e32 v68, 0x44000000, v99
	v_cvt_pk_fp8_f32 v74, v66, v68
	v_mul_f32_e32 v66, 0x44000000, v79
	v_mul_f32_e32 v68, 0x44000000, v103
	v_mov_b32_e32 v75, v131
	v_cvt_pk_fp8_f32 v75, v66, v68
	v_mul_f32_e32 v69, 0x44000000, v123
	v_mul_f32_e32 v70, 0x44000000, v127
	v_cvt_pk_fp8_f32 v72, v69, v70 op_sel:[0,0,1]
	v_mul_f32_e32 v69, 0x44000000, v107
	v_mul_f32_e32 v70, 0x44000000, v119
	v_mul_f32_e32 v66, 0x44000000, v67
	v_mul_f32_e32 v67, 0x44000000, v71
	v_cvt_pk_fp8_f32 v74, v69, v70 op_sel:[0,0,1]
	v_cvt_pk_fp8_f32 v75, v66, v67 op_sel:[0,0,1]
	v_add_co_u32_e32 v64, vcc, s7, v64
	s_add_i32 s28, s28, 2
	s_nop 0
	v_addc_co_u32_e32 v65, vcc, 0, v65, vcc
	s_cmp_le_i32 s28, s1
	global_store_dwordx4 v[64:65], v[134:137], off sc1 nt
	global_store_dwordx4 v[64:65], v[72:75], off offset:2048 sc1 nt
	s_cbranch_scc0 .LBB0_498

.LBB0_490:
	v_mad_i64_i32 v[64:65], s[24:25], s22, v128, 0
	v_lshl_add_u64 v[64:65], v[64:65], 2, s[20:21]
	v_lshl_add_u64 v[64:65], v[64:65], 0, v[130:131]
	s_lshl_b32 s8, s22, 2
	v_lshl_add_u64 v[66:67], v[64:65], 0, s[8:9]
	global_load_dwordx4 v[80:83], v[64:65], off sc1 nt
	global_load_dwordx4 v[84:87], v[66:67], off sc1 nt
	v_lshl_add_u64 v[64:65], v[66:67], 0, s[8:9]
	v_lshl_add_u64 v[66:67], v[64:65], 0, s[8:9]
	global_load_dwordx4 v[120:123], v[64:65], off sc1 nt
	global_load_dwordx4 v[124:127], v[66:67], off sc1 nt
	v_lshl_add_u64 v[64:65], v[66:67], 0, s[8:9]
	v_lshl_add_u64 v[66:67], v[64:65], 0, s[8:9]
	global_load_dwordx4 v[108:111], v[64:65], off sc1 nt
	global_load_dwordx4 v[112:115], v[66:67], off sc1 nt
	v_lshl_add_u64 v[64:65], v[66:67], 0, s[8:9]
	v_lshl_add_u64 v[66:67], v[64:65], 0, s[8:9]
	global_load_dwordx4 v[88:91], v[64:65], off sc1 nt
	global_load_dwordx4 v[92:95], v[66:67], off sc1 nt
	v_lshl_add_u64 v[64:65], v[66:67], 0, s[8:9]
	global_load_dwordx4 v[72:75], v[64:65], off sc1 nt
	v_lshl_add_u64 v[64:65], v[64:65], 0, s[8:9]
	global_load_dwordx4 v[96:99], v[64:65], off sc1 nt
	v_lshl_add_u64 v[64:65], v[64:65], 0, s[8:9]
	global_load_dwordx4 v[104:107], v[64:65], off sc1 nt
	v_lshl_add_u64 v[64:65], v[64:65], 0, s[8:9]
	global_load_dwordx4 v[116:119], v[64:65], off sc1 nt
	v_lshl_add_u64 v[64:65], v[64:65], 0, s[8:9]
	global_load_dwordx4 v[76:79], v[64:65], off sc1 nt
	v_lshl_add_u64 v[64:65], v[64:65], 0, s[8:9]
	v_lshl_add_u64 v[68:69], v[64:65], 0, s[8:9]
	global_load_dwordx4 v[100:103], v[64:65], off sc1 nt
	s_waitcnt vmcnt(21)
	v_mul_f32_e32 v8, 0x44000000, v8
	global_load_dwordx4 v[64:67], v[68:69], off sc1 nt
	v_lshl_add_u64 v[68:69], v[68:69], 0, s[8:9]
	global_load_dwordx4 v[68:71], v[68:69], off sc1 nt
	s_waitcnt vmcnt(22)
	v_mul_f32_e32 v4, 0x44000000, v4
	v_mov_b32_e32 v137, v131
	v_cvt_pk_fp8_f32 v137, v8, v4
	s_waitcnt vmcnt(21)
	v_mul_f32_e32 v0, 0x44000000, v0
	s_waitcnt vmcnt(17)
	v_mul_f32_e32 v4, 0x44000000, v44
	v_mov_b32_e32 v138, v131
	v_cvt_pk_fp8_f32 v137, v0, v4 op_sel:[0,0,1]
	s_waitcnt vmcnt(16)
	v_mul_f32_e32 v0, 0x44000000, v61
	v_mul_f32_e32 v4, 0x44000000, v53
	v_cvt_pk_fp8_f32 v138, v0, v4
	v_mul_f32_e32 v0, 0x44000000, v41
	v_mul_f32_e32 v4, 0x44000000, v37
	v_mov_b32_e32 v139, v131
	v_cvt_pk_fp8_f32 v139, v0, v4
	v_mul_f32_e32 v24, 0x44000000, v24
	v_mul_f32_e32 v20, 0x44000000, v20
	v_mov_b32_e32 v136, v131
	v_mul_f32_e32 v0, 0x44000000, v33
	v_mul_f32_e32 v4, 0x44000000, v29
	v_mul_f32_e32 v60, 0x44000000, v60
	v_mul_f32_e32 v52, 0x44000000, v52
	v_mov_b32_e32 v134, v131
	v_mul_f32_e32 v40, 0x44000000, v40
	v_mul_f32_e32 v36, 0x44000000, v36
	v_mov_b32_e32 v135, v131
	v_cvt_pk_fp8_f32 v136, v24, v20
	v_cvt_pk_fp8_f32 v139, v0, v4 op_sel:[0,0,1]
	v_mul_f32_e32 v0, 0x44000000, v25
	v_mul_f32_e32 v4, 0x44000000, v21
	v_mov_b32_e32 v140, v131
	v_cvt_pk_fp8_f32 v134, v60, v52
	v_cvt_pk_fp8_f32 v135, v40, v36
	v_cvt_pk_fp8_f32 v140, v0, v4
	v_mul_f32_e32 v0, 0x44000000, v9
	v_mul_f32_e32 v4, 0x44000000, v5
	v_mov_b32_e32 v141, v131
	v_cvt_pk_fp8_f32 v141, v0, v4
	v_mul_f32_e32 v16, 0x44000000, v16
	v_mul_f32_e32 v12, 0x44000000, v12
	v_mul_f32_e32 v56, 0x44000000, v56
	v_mul_f32_e32 v48, 0x44000000, v48
	v_mul_f32_e32 v32, 0x44000000, v32
	v_mul_f32_e32 v28, 0x44000000, v28
	v_cvt_pk_fp8_f32 v136, v16, v12 op_sel:[0,0,1]
	v_mul_f32_e32 v8, 0x44000000, v57
	v_mul_f32_e32 v12, 0x44000000, v49
	v_cvt_pk_fp8_f32 v134, v56, v48 op_sel:[0,0,1]
	v_cvt_pk_fp8_f32 v135, v32, v28 op_sel:[0,0,1]
	v_cvt_pk_fp8_f32 v138, v8, v12 op_sel:[0,0,1]
	v_mul_f32_e32 v8, 0x44000000, v17
	v_mul_f32_e32 v12, 0x44000000, v13
	v_mul_f32_e32 v0, 0x44000000, v1
	v_mul_f32_e32 v1, 0x44000000, v45
	v_cvt_pk_fp8_f32 v140, v8, v12 op_sel:[0,0,1]
	v_cvt_pk_fp8_f32 v141, v0, v1 op_sel:[0,0,1]
	v_lshl_add_u64 v[0:1], s[12:13], 0, v[132:133]
	v_lshl_add_u64 v[0:1], v[0:1], 0, v[128:129]
	global_store_dwordx4 v[0:1], v[134:137], off sc1 nt
	global_store_dwordx4 v[0:1], v[138:141], off offset:2048 sc1 nt
	v_mul_f32_e32 v4, 0x44000000, v62
	v_mul_f32_e32 v5, 0x44000000, v54
	v_mov_b32_e32 v134, v131
	v_cvt_pk_fp8_f32 v134, v4, v5
	v_mul_f32_e32 v4, 0x44000000, v42
	v_mul_f32_e32 v5, 0x44000000, v38
	v_mov_b32_e32 v135, v131
	v_cvt_pk_fp8_f32 v135, v4, v5
	v_mul_f32_e32 v4, 0x44000000, v34
	v_mul_f32_e32 v5, 0x44000000, v30
	v_mov_b32_e32 v136, v131
	v_cvt_pk_fp8_f32 v135, v4, v5 op_sel:[0,0,1]
	v_mul_f32_e32 v4, 0x44000000, v26
	v_mul_f32_e32 v5, 0x44000000, v22
	v_cvt_pk_fp8_f32 v136, v4, v5
	v_mul_f32_e32 v4, 0x44000000, v10
	v_mul_f32_e32 v5, 0x44000000, v6
	v_mov_b32_e32 v137, v131
	v_cvt_pk_fp8_f32 v137, v4, v5
	v_mul_f32_e32 v8, 0x44000000, v58
	v_mul_f32_e32 v9, 0x44000000, v50
	v_mul_f32_e32 v2, 0x44000000, v2
	v_mul_f32_e32 v4, 0x44000000, v46
	v_cvt_pk_fp8_f32 v134, v8, v9 op_sel:[0,0,1]
	v_mul_f32_e32 v8, 0x44000000, v18
	v_mul_f32_e32 v9, 0x44000000, v14
	v_cvt_pk_fp8_f32 v137, v2, v4 op_sel:[0,0,1]
	v_mul_f32_e32 v2, 0x44000000, v63
	v_mul_f32_e32 v5, 0x44000000, v55
	v_mov_b32_e32 v4, v131
	v_cvt_pk_fp8_f32 v136, v8, v9 op_sel:[0,0,1]
	v_cvt_pk_fp8_f32 v4, v2, v5
	v_mul_f32_e32 v2, 0x44000000, v43
	v_mul_f32_e32 v9, 0x44000000, v39
	v_mov_b32_e32 v5, v131
	v_cvt_pk_fp8_f32 v5, v2, v9
	v_mul_f32_e32 v6, 0x44000000, v59
	v_mul_f32_e32 v8, 0x44000000, v51
	v_cvt_pk_fp8_f32 v4, v6, v8 op_sel:[0,0,1]
	v_mul_f32_e32 v2, 0x44000000, v35
	v_mul_f32_e32 v6, 0x44000000, v31
	v_cvt_pk_fp8_f32 v5, v2, v6 op_sel:[0,0,1]
	v_mul_f32_e32 v2, 0x44000000, v27
	v_mul_f32_e32 v8, 0x44000000, v23
	v_mov_b32_e32 v6, v131
	v_cvt_pk_fp8_f32 v6, v2, v8
	v_mul_f32_e32 v2, 0x44000000, v11
	v_mul_f32_e32 v8, 0x44000000, v7
	v_mov_b32_e32 v7, v131
	v_cvt_pk_fp8_f32 v7, v2, v8
	v_mul_f32_e32 v9, 0x44000000, v19
	v_mul_f32_e32 v10, 0x44000000, v15
	v_mul_f32_e32 v2, 0x44000000, v3
	v_mul_f32_e32 v3, 0x44000000, v47
	s_add_i32 s0, s0, 16
	v_cvt_pk_fp8_f32 v6, v9, v10 op_sel:[0,0,1]
	v_cvt_pk_fp8_f32 v7, v2, v3 op_sel:[0,0,1]
	s_min_i32 s0, s0, s2
	v_add_co_u32_e32 v0, vcc, s7, v0
	s_cmp_gt_i32 s0, 0xffff
	s_nop 0
	v_addc_co_u32_e32 v1, vcc, 0, v1, vcc
	s_mov_b64 s[26:27], -1
	global_store_dwordx4 v[0:1], v[134:137], off sc1 nt
	global_store_dwordx4 v[0:1], v[4:7], off offset:2048 sc1 nt
	s_cbranch_scc0 .LBB0_496
	s_cmp_lt_u32 s0, 0x18000
	s_cbranch_scc0 .LBB0_493
	s_add_i32 s8, s0, 0xffff0000
	s_lshr_b32 s8, s8, 10
	s_lshl_b64 s[12:13], s[8:9], 22
	s_lshl_b64 s[20:21], s[8:9], 24
	s_add_u32 s20, s70, s20
	s_addc_u32 s21, s71, s21
	s_add_u32 s12, s3, s12
	s_addc_u32 s13, s4, s13
	s_lshl_b32 s8, s0, 1
	s_and_b32 s8, s8, 0x780
	s_lshl_b32 s22, s8, 13
	s_add_u32 s20, s20, s22
	s_addc_u32 s21, s21, 0
	s_lshl_b32 s22, s0, 5
	s_and_b32 s22, s22, 0x7e0
	s_lshl_b32 s24, s22, 2
	s_add_u32 s20, s20, s24
	s_mov_b32 s23, s9
	s_addc_u32 s21, s21, 0
	s_mov_b64 s[26:27], 0
	s_mov_b64 s[24:25], s[8:9]

.LBB0_538:
	s_not_b32 s2, s0
	s_add_i32 s1, s1, s2
	s_cmp_lt_i32 s1, -7
	s_cbranch_scc1 .LBB0_557
	s_ashr_i32 s2, s1, 31
	v_lshlrev_b32_e32 v1, 1, v0
	s_lshr_b32 s2, s2, 29
	v_and_b32_e32 v128, -16, v1
	v_lshlrev_b32_e32 v0, 2, v0
	s_add_i32 s2, s1, s2
	v_and_b32_e32 v64, 28, v0
	s_ashr_i32 s1, s2, 3
	s_and_b32 s2, s2, -8
	v_mad_i64_i32 v[0:1], s[4:5], s16, v128, 0
	v_mov_b32_e32 v131, 0
	s_add_i32 s2, s2, s0
	v_lshl_add_u64 v[0:1], v[0:1], 2, s[14:15]
	v_lshlrev_b32_e32 v130, 2, v64
	s_lshl_b32 s3, s16, 2
	s_mov_b32 s7, 0
	s_waitcnt vmcnt(4)
	v_lshl_add_u64 v[60:61], v[0:1], 0, v[130:131]
	s_mul_i32 s6, s16, 60
	s_sub_u32 s4, 0, s3
	v_lshl_add_u64 v[44:45], v[60:61], 0, s[6:7]
	s_subb_u32 s5, 0, 0
	v_lshl_add_u64 v[0:1], v[44:45], 0, s[4:5]
	v_lshl_add_u64 v[8:9], v[0:1], 0, s[4:5]
	global_load_dwordx4 v[0:3], v[0:1], off sc1 nt
	s_nop 0
	global_load_dwordx4 v[4:7], v[8:9], off sc1 nt
	v_lshl_add_u64 v[8:9], v[8:9], 0, s[4:5]
	v_lshl_add_u64 v[16:17], v[8:9], 0, s[4:5]
	global_load_dwordx4 v[8:11], v[8:9], off sc1 nt
	s_nop 0
	global_load_dwordx4 v[12:15], v[16:17], off sc1 nt
	v_lshl_add_u64 v[16:17], v[16:17], 0, s[4:5]
	v_lshl_add_u64 v[24:25], v[16:17], 0, s[4:5]
	v_lshl_add_u64 v[28:29], v[24:25], 0, s[4:5]
	v_lshl_add_u64 v[32:33], v[28:29], 0, s[4:5]
	v_lshl_add_u64 v[36:37], v[32:33], 0, s[4:5]
	v_lshl_add_u64 v[40:41], v[36:37], 0, s[4:5]
	v_lshl_add_u64 v[46:47], v[40:41], 0, s[4:5]
	global_load_dwordx4 v[16:19], v[16:17], off sc1 nt
	s_nop 0
	global_load_dwordx4 v[20:23], v[24:25], off sc1 nt
	v_ashrrev_i32_e32 v129, 31, v128
	global_load_dwordx4 v[24:27], v[28:29], off sc1 nt
	v_lshlrev_b32_e32 v132, 11, v64
	global_load_dwordx4 v[28:31], v[32:33], off sc1 nt
	v_mov_b32_e32 v133, v131
	global_load_dwordx4 v[32:35], v[36:37], off sc1 nt
	v_lshlrev_b32_e32 v130, 2, v64
	global_load_dwordx4 v[36:39], v[40:41], off sc1 nt
	s_movk_i32 s27, 0x1000
	global_load_dwordx4 v[40:43], v[46:47], off sc1 nt
	v_lshl_add_u64 v[46:47], v[46:47], 0, s[4:5]
	global_load_dwordx4 v[48:51], v[46:47], off sc1 nt
	v_lshl_add_u64 v[46:47], v[46:47], 0, s[4:5]
	global_load_dwordx4 v[56:59], v[46:47], off sc1 nt
	v_lshl_add_u64 v[46:47], v[46:47], 0, s[4:5]
	global_load_dwordx4 v[52:55], v[46:47], off sc1 nt
	s_nop 0
	global_load_dwordx4 v[44:47], v[44:45], off sc1 nt
	s_nop 0
	global_load_dwordx4 v[60:63], v[60:61], off sc1 nt
	s_lshl_b64 s[4:5], s[12:13], 11
	s_add_u32 s3, s8, s4
	s_addc_u32 s4, s9, s5
	s_add_u32 s10, s3, s10
	s_addc_u32 s11, s4, s11
	s_add_u32 s3, s90, 0x3b100000
	s_addc_u32 s4, s91, 0
	s_add_u32 s8, s90, 0x1900000
	s_addc_u32 s9, s91, 0
	s_add_u32 s5, s90, 0x4b100000
	s_addc_u32 s26, s91, 0
	s_mov_b32 s28, 0
	s_branch .LBB0_541
.LBB0_540:
	s_lshl_b64 s[14:15], s[14:15], 11
	s_add_u32 s6, s12, s14
	s_addc_u32 s13, s13, s15
	s_add_u32 s12, s6, s16
	s_addc_u32 s13, s13, s17
	s_lshl_b64 s[14:15], s[20:21], 11
	s_add_u32 s6, s10, s14
	s_addc_u32 s11, s11, s15
	v_mad_i64_i32 v[0:1], s[14:15], s24, v128, 0
	s_add_u32 s10, s6, s22
	v_lshl_add_u64 v[0:1], v[0:1], 2, s[18:19]
	s_addc_u32 s11, s11, s23
	v_lshl_add_u64 v[0:1], v[0:1], 0, v[130:131]
	s_lshl_b32 s6, s24, 2
	v_lshl_add_u64 v[2:3], v[0:1], 0, s[6:7]
	global_load_dwordx4 v[60:63], v[0:1], off sc1 nt
	global_load_dwordx4 v[52:55], v[2:3], off sc1 nt
	v_lshl_add_u64 v[0:1], v[2:3], 0, s[6:7]
	v_lshl_add_u64 v[2:3], v[0:1], 0, s[6:7]
	global_load_dwordx4 v[56:59], v[0:1], off sc1 nt
	global_load_dwordx4 v[48:51], v[2:3], off sc1 nt
	v_lshl_add_u64 v[0:1], v[2:3], 0, s[6:7]
	v_lshl_add_u64 v[2:3], v[0:1], 0, s[6:7]
	global_load_dwordx4 v[40:43], v[0:1], off sc1 nt
	global_load_dwordx4 v[36:39], v[2:3], off sc1 nt
	v_lshl_add_u64 v[0:1], v[2:3], 0, s[6:7]
	v_lshl_add_u64 v[2:3], v[0:1], 0, s[6:7]
	global_load_dwordx4 v[32:35], v[0:1], off sc1 nt
	global_load_dwordx4 v[28:31], v[2:3], off sc1 nt
	v_lshl_add_u64 v[0:1], v[2:3], 0, s[6:7]
	global_load_dwordx4 v[24:27], v[0:1], off sc1 nt
	v_lshl_add_u64 v[0:1], v[0:1], 0, s[6:7]
	global_load_dwordx4 v[20:23], v[0:1], off sc1 nt
	v_lshl_add_u64 v[0:1], v[0:1], 0, s[6:7]
	global_load_dwordx4 v[16:19], v[0:1], off sc1 nt
	v_lshl_add_u64 v[0:1], v[0:1], 0, s[6:7]
	global_load_dwordx4 v[12:15], v[0:1], off sc1 nt
	v_lshl_add_u64 v[0:1], v[0:1], 0, s[6:7]
	global_load_dwordx4 v[8:11], v[0:1], off sc1 nt
	v_lshl_add_u64 v[0:1], v[0:1], 0, s[6:7]
	v_lshl_add_u64 v[44:45], v[0:1], 0, s[6:7]
	global_load_dwordx4 v[4:7], v[0:1], off sc1 nt
	s_waitcnt vmcnt(33)
	v_mul_f32_e32 v80, 0x44000000, v80
	global_load_dwordx4 v[0:3], v[44:45], off sc1 nt
	v_lshl_add_u64 v[44:45], v[44:45], 0, s[6:7]
	global_load_dwordx4 v[44:47], v[44:45], off sc1 nt
	s_waitcnt vmcnt(34)
	v_mul_f32_e32 v84, 0x44000000, v84
	v_mov_b32_e32 v134, v131
	v_cvt_pk_fp8_f32 v134, v80, v84
	s_waitcnt vmcnt(31)
	v_mul_f32_e32 v80, 0x44000000, v108
	s_waitcnt vmcnt(30)
	v_mul_f32_e32 v84, 0x44000000, v112
	v_mov_b32_e32 v135, v131
	v_cvt_pk_fp8_f32 v135, v80, v84
	s_waitcnt vmcnt(29)
	v_mul_f32_e32 v80, 0x44000000, v88
	s_waitcnt vmcnt(28)
	v_mul_f32_e32 v84, 0x44000000, v92
	s_waitcnt vmcnt(27)
	v_mul_f32_e32 v72, 0x44000000, v72
	v_cvt_pk_fp8_f32 v135, v80, v84 op_sel:[0,0,1]
	s_waitcnt vmcnt(26)
	v_mul_f32_e32 v80, 0x44000000, v96
	v_mov_b32_e32 v136, v131
	v_cvt_pk_fp8_f32 v136, v72, v80
	s_waitcnt vmcnt(23)
	v_mul_f32_e32 v72, 0x44000000, v76
	s_waitcnt vmcnt(22)
	v_mul_f32_e32 v76, 0x44000000, v100
	v_mov_b32_e32 v137, v131
	v_cvt_pk_fp8_f32 v137, v72, v76
	s_waitcnt vmcnt(21)
	v_mul_f32_e32 v64, 0x44000000, v64
	s_waitcnt vmcnt(20)
	v_mul_f32_e32 v68, 0x44000000, v68
	v_mov_b32_e32 v138, v131
	v_cvt_pk_fp8_f32 v137, v64, v68 op_sel:[0,0,1]
	v_mul_f32_e32 v64, 0x44000000, v81
	v_mul_f32_e32 v68, 0x44000000, v85
	v_cvt_pk_fp8_f32 v138, v64, v68
	v_mul_f32_e32 v64, 0x44000000, v109
	v_mul_f32_e32 v68, 0x44000000, v113
	v_mov_b32_e32 v139, v131
	v_cvt_pk_fp8_f32 v139, v64, v68
	v_mul_f32_e32 v64, 0x44000000, v89
	v_mul_f32_e32 v68, 0x44000000, v93
	v_mov_b32_e32 v140, v131
	v_cvt_pk_fp8_f32 v139, v64, v68 op_sel:[0,0,1]
	v_mul_f32_e32 v64, 0x44000000, v73
	v_mul_f32_e32 v68, 0x44000000, v97
	v_cvt_pk_fp8_f32 v140, v64, v68
	v_mul_f32_e32 v64, 0x44000000, v77
	v_mul_f32_e32 v68, 0x44000000, v101
	v_mov_b32_e32 v141, v131
	v_cvt_pk_fp8_f32 v141, v64, v68
	v_mul_f32_e32 v120, 0x44000000, v120
	v_mul_f32_e32 v124, 0x44000000, v124
	v_mul_f32_e32 v84, 0x44000000, v104
	v_mul_f32_e32 v88, 0x44000000, v116
	v_mul_f32_e32 v72, 0x44000000, v121
	v_mul_f32_e32 v76, 0x44000000, v125
	v_cvt_pk_fp8_f32 v134, v120, v124 op_sel:[0,0,1]
	v_cvt_pk_fp8_f32 v136, v84, v88 op_sel:[0,0,1]
	v_cvt_pk_fp8_f32 v138, v72, v76 op_sel:[0,0,1]
	v_mul_f32_e32 v72, 0x44000000, v105
	v_mul_f32_e32 v73, 0x44000000, v117
	v_mul_f32_e32 v64, 0x44000000, v65
	v_mul_f32_e32 v65, 0x44000000, v69
	v_cvt_pk_fp8_f32 v140, v72, v73 op_sel:[0,0,1]
	v_cvt_pk_fp8_f32 v141, v64, v65 op_sel:[0,0,1]
	v_lshl_add_u64 v[64:65], s[12:13], 0, v[132:133]
	v_lshl_add_u64 v[64:65], v[64:65], 0, v[128:129]
	global_store_dwordx4 v[64:65], v[134:137], off sc1 nt
	global_store_dwordx4 v[64:65], v[138:141], off offset:2048 sc1 nt
	v_mul_f32_e32 v68, 0x44000000, v82
	v_mul_f32_e32 v69, 0x44000000, v86
	v_mov_b32_e32 v134, v131
	v_cvt_pk_fp8_f32 v134, v68, v69
	v_mul_f32_e32 v68, 0x44000000, v110
	v_mul_f32_e32 v69, 0x44000000, v114
	v_mov_b32_e32 v135, v131
	v_cvt_pk_fp8_f32 v135, v68, v69
	v_mul_f32_e32 v68, 0x44000000, v90
	v_mul_f32_e32 v69, 0x44000000, v94
	v_mov_b32_e32 v136, v131
	v_cvt_pk_fp8_f32 v135, v68, v69 op_sel:[0,0,1]
	v_mul_f32_e32 v68, 0x44000000, v74
	v_mul_f32_e32 v69, 0x44000000, v98
	v_cvt_pk_fp8_f32 v136, v68, v69
	v_mul_f32_e32 v68, 0x44000000, v78
	v_mul_f32_e32 v69, 0x44000000, v102
	v_mov_b32_e32 v137, v131
	v_cvt_pk_fp8_f32 v137, v68, v69
	v_mul_f32_e32 v72, 0x44000000, v122
	v_mul_f32_e32 v73, 0x44000000, v126
	v_cvt_pk_fp8_f32 v134, v72, v73 op_sel:[0,0,1]
	v_mul_f32_e32 v72, 0x44000000, v106
	v_mul_f32_e32 v73, 0x44000000, v118
	v_mul_f32_e32 v66, 0x44000000, v66
	v_mul_f32_e32 v68, 0x44000000, v70
	v_cvt_pk_fp8_f32 v136, v72, v73 op_sel:[0,0,1]
	v_cvt_pk_fp8_f32 v137, v66, v68 op_sel:[0,0,1]
	v_mul_f32_e32 v66, 0x44000000, v83
	v_mul_f32_e32 v68, 0x44000000, v87
	v_mov_b32_e32 v72, v131
	v_cvt_pk_fp8_f32 v72, v66, v68
	v_mul_f32_e32 v66, 0x44000000, v111
	v_mul_f32_e32 v68, 0x44000000, v115
	v_mov_b32_e32 v73, v131
	v_cvt_pk_fp8_f32 v73, v66, v68
	v_mul_f32_e32 v66, 0x44000000, v91
	v_mul_f32_e32 v68, 0x44000000, v95
	v_mov_b32_e32 v74, v131
	v_cvt_pk_fp8_f32 v73, v66, v68 op_sel:[0,0,1]
	v_mul_f32_e32 v66, 0x44000000, v75
	v_mul_f32_e32 v68, 0x44000000, v99
	v_cvt_pk_fp8_f32 v74, v66, v68
	v_mul_f32_e32 v66, 0x44000000, v79
	v_mul_f32_e32 v68, 0x44000000, v103
	v_mov_b32_e32 v75, v131
	v_cvt_pk_fp8_f32 v75, v66, v68
	v_mul_f32_e32 v69, 0x44000000, v123
	v_mul_f32_e32 v70, 0x44000000, v127
	v_cvt_pk_fp8_f32 v72, v69, v70 op_sel:[0,0,1]
	v_mul_f32_e32 v69, 0x44000000, v107
	v_mul_f32_e32 v70, 0x44000000, v119
	v_mul_f32_e32 v66, 0x44000000, v67
	v_mul_f32_e32 v67, 0x44000000, v71
	v_cvt_pk_fp8_f32 v74, v69, v70 op_sel:[0,0,1]
	v_cvt_pk_fp8_f32 v75, v66, v67 op_sel:[0,0,1]
	v_add_co_u32_e32 v64, vcc, s27, v64
	s_add_i32 s28, s28, 2
	s_nop 0
	v_addc_co_u32_e32 v65, vcc, 0, v65, vcc
	s_cmp_le_i32 s28, s1
	global_store_dwordx4 v[64:65], v[134:137], off sc1 nt
	global_store_dwordx4 v[64:65], v[72:75], off offset:2048 sc1 nt
	s_cbranch_scc0 .LBB0_557

.LBB0_549:
	v_mad_i64_i32 v[64:65], s[22:23], s20, v128, 0
	v_lshl_add_u64 v[64:65], v[64:65], 2, s[18:19]
	v_lshl_add_u64 v[64:65], v[64:65], 0, v[130:131]
	s_lshl_b32 s6, s20, 2
	v_lshl_add_u64 v[66:67], v[64:65], 0, s[6:7]
	global_load_dwordx4 v[80:83], v[64:65], off sc1 nt
	global_load_dwordx4 v[84:87], v[66:67], off sc1 nt
	v_lshl_add_u64 v[64:65], v[66:67], 0, s[6:7]
	v_lshl_add_u64 v[66:67], v[64:65], 0, s[6:7]
	global_load_dwordx4 v[120:123], v[64:65], off sc1 nt
	global_load_dwordx4 v[124:127], v[66:67], off sc1 nt
	v_lshl_add_u64 v[64:65], v[66:67], 0, s[6:7]
	v_lshl_add_u64 v[66:67], v[64:65], 0, s[6:7]
	global_load_dwordx4 v[108:111], v[64:65], off sc1 nt
	global_load_dwordx4 v[112:115], v[66:67], off sc1 nt
	v_lshl_add_u64 v[64:65], v[66:67], 0, s[6:7]
	v_lshl_add_u64 v[66:67], v[64:65], 0, s[6:7]
	global_load_dwordx4 v[88:91], v[64:65], off sc1 nt
	global_load_dwordx4 v[92:95], v[66:67], off sc1 nt
	v_lshl_add_u64 v[64:65], v[66:67], 0, s[6:7]
	global_load_dwordx4 v[72:75], v[64:65], off sc1 nt
	v_lshl_add_u64 v[64:65], v[64:65], 0, s[6:7]
	global_load_dwordx4 v[96:99], v[64:65], off sc1 nt
	v_lshl_add_u64 v[64:65], v[64:65], 0, s[6:7]
	global_load_dwordx4 v[104:107], v[64:65], off sc1 nt
	v_lshl_add_u64 v[64:65], v[64:65], 0, s[6:7]
	global_load_dwordx4 v[116:119], v[64:65], off sc1 nt
	v_lshl_add_u64 v[64:65], v[64:65], 0, s[6:7]
	global_load_dwordx4 v[76:79], v[64:65], off sc1 nt
	v_lshl_add_u64 v[64:65], v[64:65], 0, s[6:7]
	v_lshl_add_u64 v[68:69], v[64:65], 0, s[6:7]
	global_load_dwordx4 v[100:103], v[64:65], off sc1 nt
	s_waitcnt vmcnt(21)
	v_mul_f32_e32 v8, 0x44000000, v8
	global_load_dwordx4 v[64:67], v[68:69], off sc1 nt
	v_lshl_add_u64 v[68:69], v[68:69], 0, s[6:7]
	global_load_dwordx4 v[68:71], v[68:69], off sc1 nt
	s_waitcnt vmcnt(22)
	v_mul_f32_e32 v4, 0x44000000, v4
	v_mov_b32_e32 v137, v131
	v_cvt_pk_fp8_f32 v137, v8, v4
	s_waitcnt vmcnt(21)
	v_mul_f32_e32 v0, 0x44000000, v0
	s_waitcnt vmcnt(17)
	v_mul_f32_e32 v4, 0x44000000, v44
	v_mov_b32_e32 v138, v131
	v_cvt_pk_fp8_f32 v137, v0, v4 op_sel:[0,0,1]
	s_waitcnt vmcnt(16)
	v_mul_f32_e32 v0, 0x44000000, v61
	v_mul_f32_e32 v4, 0x44000000, v53
	v_cvt_pk_fp8_f32 v138, v0, v4
	v_mul_f32_e32 v0, 0x44000000, v41
	v_mul_f32_e32 v4, 0x44000000, v37
	v_mov_b32_e32 v139, v131
	v_cvt_pk_fp8_f32 v139, v0, v4
	v_mul_f32_e32 v24, 0x44000000, v24
	v_mul_f32_e32 v20, 0x44000000, v20
	v_mov_b32_e32 v136, v131
	v_mul_f32_e32 v0, 0x44000000, v33
	v_mul_f32_e32 v4, 0x44000000, v29
	v_mul_f32_e32 v60, 0x44000000, v60
	v_mul_f32_e32 v52, 0x44000000, v52
	v_mov_b32_e32 v134, v131
	v_mul_f32_e32 v40, 0x44000000, v40
	v_mul_f32_e32 v36, 0x44000000, v36
	v_mov_b32_e32 v135, v131
	v_cvt_pk_fp8_f32 v136, v24, v20
	v_cvt_pk_fp8_f32 v139, v0, v4 op_sel:[0,0,1]
	v_mul_f32_e32 v0, 0x44000000, v25
	v_mul_f32_e32 v4, 0x44000000, v21
	v_mov_b32_e32 v140, v131
	v_cvt_pk_fp8_f32 v134, v60, v52
	v_cvt_pk_fp8_f32 v135, v40, v36
	v_cvt_pk_fp8_f32 v140, v0, v4
	v_mul_f32_e32 v0, 0x44000000, v9
	v_mul_f32_e32 v4, 0x44000000, v5
	v_mov_b32_e32 v141, v131
	v_cvt_pk_fp8_f32 v141, v0, v4
	v_mul_f32_e32 v16, 0x44000000, v16
	v_mul_f32_e32 v12, 0x44000000, v12
	v_mul_f32_e32 v56, 0x44000000, v56
	v_mul_f32_e32 v48, 0x44000000, v48
	v_mul_f32_e32 v32, 0x44000000, v32
	v_mul_f32_e32 v28, 0x44000000, v28
	v_cvt_pk_fp8_f32 v136, v16, v12 op_sel:[0,0,1]
	v_mul_f32_e32 v8, 0x44000000, v57
	v_mul_f32_e32 v12, 0x44000000, v49
	v_cvt_pk_fp8_f32 v134, v56, v48 op_sel:[0,0,1]
	v_cvt_pk_fp8_f32 v135, v32, v28 op_sel:[0,0,1]
	v_cvt_pk_fp8_f32 v138, v8, v12 op_sel:[0,0,1]
	v_mul_f32_e32 v8, 0x44000000, v17
	v_mul_f32_e32 v12, 0x44000000, v13
	v_mul_f32_e32 v0, 0x44000000, v1
	v_mul_f32_e32 v1, 0x44000000, v45
	v_cvt_pk_fp8_f32 v140, v8, v12 op_sel:[0,0,1]
	v_cvt_pk_fp8_f32 v141, v0, v1 op_sel:[0,0,1]
	v_lshl_add_u64 v[0:1], s[10:11], 0, v[132:133]
	v_lshl_add_u64 v[0:1], v[0:1], 0, v[128:129]
	global_store_dwordx4 v[0:1], v[134:137], off sc1 nt
	global_store_dwordx4 v[0:1], v[138:141], off offset:2048 sc1 nt
	v_mul_f32_e32 v4, 0x44000000, v62
	v_mul_f32_e32 v5, 0x44000000, v54
	v_mov_b32_e32 v134, v131
	v_cvt_pk_fp8_f32 v134, v4, v5
	v_mul_f32_e32 v4, 0x44000000, v42
	v_mul_f32_e32 v5, 0x44000000, v38
	v_mov_b32_e32 v135, v131
	v_cvt_pk_fp8_f32 v135, v4, v5
	v_mul_f32_e32 v4, 0x44000000, v34
	v_mul_f32_e32 v5, 0x44000000, v30
	v_mov_b32_e32 v136, v131
	v_cvt_pk_fp8_f32 v135, v4, v5 op_sel:[0,0,1]
	v_mul_f32_e32 v4, 0x44000000, v26
	v_mul_f32_e32 v5, 0x44000000, v22
	v_cvt_pk_fp8_f32 v136, v4, v5
	v_mul_f32_e32 v4, 0x44000000, v10
	v_mul_f32_e32 v5, 0x44000000, v6
	v_mov_b32_e32 v137, v131
	v_cvt_pk_fp8_f32 v137, v4, v5
	v_mul_f32_e32 v8, 0x44000000, v58
	v_mul_f32_e32 v9, 0x44000000, v50
	v_mul_f32_e32 v2, 0x44000000, v2
	v_mul_f32_e32 v4, 0x44000000, v46
	v_cvt_pk_fp8_f32 v134, v8, v9 op_sel:[0,0,1]
	v_mul_f32_e32 v8, 0x44000000, v18
	v_mul_f32_e32 v9, 0x44000000, v14
	v_cvt_pk_fp8_f32 v137, v2, v4 op_sel:[0,0,1]
	v_mul_f32_e32 v2, 0x44000000, v63
	v_mul_f32_e32 v5, 0x44000000, v55
	v_mov_b32_e32 v4, v131
	v_cvt_pk_fp8_f32 v136, v8, v9 op_sel:[0,0,1]
	v_cvt_pk_fp8_f32 v4, v2, v5
	v_mul_f32_e32 v2, 0x44000000, v43
	v_mul_f32_e32 v9, 0x44000000, v39
	v_mov_b32_e32 v5, v131
	v_cvt_pk_fp8_f32 v5, v2, v9
	v_mul_f32_e32 v6, 0x44000000, v59
	v_mul_f32_e32 v8, 0x44000000, v51
	v_cvt_pk_fp8_f32 v4, v6, v8 op_sel:[0,0,1]
	v_mul_f32_e32 v2, 0x44000000, v35
	v_mul_f32_e32 v6, 0x44000000, v31
	v_cvt_pk_fp8_f32 v5, v2, v6 op_sel:[0,0,1]
	v_mul_f32_e32 v2, 0x44000000, v27
	v_mul_f32_e32 v8, 0x44000000, v23
	v_mov_b32_e32 v6, v131
	v_cvt_pk_fp8_f32 v6, v2, v8
	v_mul_f32_e32 v2, 0x44000000, v11
	v_mul_f32_e32 v8, 0x44000000, v7
	v_mov_b32_e32 v7, v131
	v_cvt_pk_fp8_f32 v7, v2, v8
	v_mul_f32_e32 v9, 0x44000000, v19
	v_mul_f32_e32 v10, 0x44000000, v15
	v_mul_f32_e32 v2, 0x44000000, v3
	v_mul_f32_e32 v3, 0x44000000, v47
	s_add_i32 s0, s0, 16
	v_cvt_pk_fp8_f32 v6, v9, v10 op_sel:[0,0,1]
	v_cvt_pk_fp8_f32 v7, v2, v3 op_sel:[0,0,1]
	s_min_i32 s0, s0, s2
	v_add_co_u32_e32 v0, vcc, s27, v0
	s_cmp_gt_i32 s0, 0xffff
	s_nop 0
	v_addc_co_u32_e32 v1, vcc, 0, v1, vcc
	s_mov_b64 s[24:25], -1
	global_store_dwordx4 v[0:1], v[134:137], off sc1 nt
	global_store_dwordx4 v[0:1], v[4:7], off offset:2048 sc1 nt
	s_cbranch_scc0 .LBB0_555
	s_cmp_lt_u32 s0, 0x18000
	s_cbranch_scc0 .LBB0_552
	s_add_i32 s6, s0, 0xffff0000
	s_lshr_b32 s6, s6, 10
	s_lshl_b64 s[10:11], s[6:7], 22
	s_lshl_b64 s[18:19], s[6:7], 24
	s_add_u32 s18, s70, s18
	s_addc_u32 s19, s71, s19
	s_add_u32 s10, s3, s10
	s_addc_u32 s11, s4, s11
	s_lshl_b32 s6, s0, 1
	s_and_b32 s6, s6, 0x780
	s_lshl_b32 s20, s6, 13
	s_add_u32 s18, s18, s20
	s_addc_u32 s19, s19, 0
	s_lshl_b32 s20, s0, 5
	s_and_b32 s20, s20, 0x7e0
	s_lshl_b32 s22, s20, 2
	s_add_u32 s18, s18, s22
	s_mov_b32 s21, s7
	s_addc_u32 s19, s19, 0
	s_mov_b64 s[24:25], 0
	s_mov_b64 s[22:23], s[6:7]

.LBB0_570:
	v_lshlrev_b32_e32 v1, 1, v0
	v_and_b32_e32 v130, -16, v1
	v_lshlrev_b32_e32 v0, 2, v0
	v_and_b32_e32 v48, 28, v0
	v_mad_i64_i32 v[0:1], s[18:19], s16, v130, 0
	v_mov_b32_e32 v67, 0
	v_lshl_add_u64 v[0:1], v[0:1], 2, s[14:15]
	v_lshlrev_b32_e32 v66, 2, v48
	s_mov_b32 s3, 0
	v_lshl_add_u64 v[62:63], v[0:1], 0, v[66:67]
	s_mul_i32 s2, s16, 60
	v_lshl_add_u64 v[24:25], v[62:63], 0, s[2:3]
	s_lshl_b32 s2, s16, 2
	s_sub_u32 s2, 0, s2
	s_subb_u32 s3, 0, 0
	v_lshl_add_u64 v[0:1], v[24:25], 0, s[2:3]
	v_lshl_add_u64 v[8:9], v[0:1], 0, s[2:3]
	global_load_dwordx4 v[0:3], v[0:1], off sc1 nt
	s_nop 0
	global_load_dwordx4 v[4:7], v[8:9], off sc1 nt
	v_lshl_add_u64 v[8:9], v[8:9], 0, s[2:3]
	v_lshl_add_u64 v[16:17], v[8:9], 0, s[2:3]
	global_load_dwordx4 v[8:11], v[8:9], off sc1 nt
	s_nop 0
	global_load_dwordx4 v[12:15], v[16:17], off sc1 nt
	v_lshl_add_u64 v[16:17], v[16:17], 0, s[2:3]
	v_lshl_add_u64 v[26:27], v[16:17], 0, s[2:3]
	global_load_dwordx4 v[16:19], v[16:17], off sc1 nt
	s_nop 0
	global_load_dwordx4 v[20:23], v[26:27], off sc1 nt
	v_lshl_add_u64 v[26:27], v[26:27], 0, s[2:3]
	global_load_dwordx4 v[28:31], v[26:27], off sc1 nt
	v_lshl_add_u64 v[26:27], v[26:27], 0, s[2:3]
	global_load_dwordx4 v[32:35], v[26:27], off sc1 nt
	v_lshl_add_u64 v[26:27], v[26:27], 0, s[2:3]
	global_load_dwordx4 v[36:39], v[26:27], off sc1 nt
	v_lshl_add_u64 v[26:27], v[26:27], 0, s[2:3]
	global_load_dwordx4 v[40:43], v[26:27], off sc1 nt
	v_lshl_add_u64 v[26:27], v[26:27], 0, s[2:3]
	global_load_dwordx4 v[44:47], v[26:27], off sc1 nt
	v_lshl_add_u64 v[26:27], v[26:27], 0, s[2:3]
	global_load_dwordx4 v[50:53], v[26:27], off sc1 nt
	v_lshl_add_u64 v[26:27], v[26:27], 0, s[2:3]
	global_load_dwordx4 v[54:57], v[26:27], off sc1 nt
	v_lshl_add_u64 v[26:27], v[26:27], 0, s[2:3]
	global_load_dwordx4 v[58:61], v[26:27], off sc1 nt
	s_nop 0
	global_load_dwordx4 v[24:27], v[24:25], off sc1 nt
	s_nop 0
	global_load_dwordx4 v[62:65], v[62:63], off sc1 nt
	v_ashrrev_i32_e32 v131, 31, v130
	s_and_b64 vcc, exec, s[12:13]
	s_cbranch_vccz .LBB0_573
	s_cmp_lt_u32 s0, 0x18000
	s_cbranch_scc0 .LBB0_574
	s_addk_i32 s1, 0xf9ff
	s_lshr_b32 s14, s1, 10
	s_mov_b32 s15, 0
	s_lshl_b64 s[2:3], s[14:15], 22
	s_lshl_b64 s[12:13], s[14:15], 24
	s_add_u32 s1, s70, s12
	s_addc_u32 s16, s71, s13
	s_add_u32 s2, s90, s2
	s_addc_u32 s3, s91, s3
	s_add_u32 s12, s2, 0x3b100000
	s_addc_u32 s13, s3, 0
	s_lshl_b32 s2, s0, 1
	s_and_b32 s14, s2, 0x780
	s_lshl_b32 s2, s14, 13
	s_add_u32 s1, s1, s2
	s_addc_u32 s2, s16, 0
	s_lshl_b32 s3, s0, 5
	s_and_b32 s18, s3, 0x7e0
	s_lshl_b32 s3, s18, 2
	s_add_u32 s16, s1, s3
	s_mov_b32 s19, s15
	s_addc_u32 s17, s2, 0
	s_mov_b64 s[20:21], 0
	s_branch .LBB0_575

.LBB0_656:
	s_not_b32 s2, s0
	s_add_i32 s1, s1, s2
	s_cmp_lt_i32 s1, -7
	s_cbranch_scc1 .LBB0_675
	s_ashr_i32 s2, s1, 31
	v_lshlrev_b32_e32 v1, 1, v0
	s_lshr_b32 s2, s2, 29
	v_and_b32_e32 v128, -16, v1
	v_lshlrev_b32_e32 v0, 2, v0
	s_add_i32 s2, s1, s2
	v_and_b32_e32 v64, 28, v0
	s_ashr_i32 s1, s2, 3
	s_and_b32 s2, s2, -8
	v_mad_i64_i32 v[0:1], s[22:23], s20, v128, 0
	v_mov_b32_e32 v131, 0
	s_add_i32 s2, s2, s0
	v_lshl_add_u64 v[0:1], v[0:1], 2, s[18:19]
	v_lshlrev_b32_e32 v130, 2, v64
	s_lshl_b32 s3, s20, 2
	s_mov_b32 s7, 0
	s_waitcnt vmcnt(4)
	v_lshl_add_u64 v[60:61], v[0:1], 0, v[130:131]
	s_mul_i32 s6, s20, 60
	s_sub_u32 s18, 0, s3
	v_lshl_add_u64 v[44:45], v[60:61], 0, s[6:7]
	s_subb_u32 s19, 0, 0
	v_lshl_add_u64 v[0:1], v[44:45], 0, s[18:19]
	v_lshl_add_u64 v[8:9], v[0:1], 0, s[18:19]
	global_load_dwordx4 v[0:3], v[0:1], off sc1 nt
	s_nop 0
	global_load_dwordx4 v[4:7], v[8:9], off sc1 nt
	v_lshl_add_u64 v[8:9], v[8:9], 0, s[18:19]
	v_lshl_add_u64 v[16:17], v[8:9], 0, s[18:19]
	global_load_dwordx4 v[8:11], v[8:9], off sc1 nt
	s_nop 0
	global_load_dwordx4 v[12:15], v[16:17], off sc1 nt
	v_lshl_add_u64 v[16:17], v[16:17], 0, s[18:19]
	v_lshl_add_u64 v[24:25], v[16:17], 0, s[18:19]
	v_lshl_add_u64 v[28:29], v[24:25], 0, s[18:19]
	v_lshl_add_u64 v[32:33], v[28:29], 0, s[18:19]
	v_lshl_add_u64 v[36:37], v[32:33], 0, s[18:19]
	v_lshl_add_u64 v[40:41], v[36:37], 0, s[18:19]
	v_lshl_add_u64 v[46:47], v[40:41], 0, s[18:19]
	global_load_dwordx4 v[16:19], v[16:17], off sc1 nt
	s_nop 0
	global_load_dwordx4 v[20:23], v[24:25], off sc1 nt
	s_lshl_b64 s[16:17], s[16:17], 11
	global_load_dwordx4 v[24:27], v[28:29], off sc1 nt
	s_add_u32 s3, s12, s16
	global_load_dwordx4 v[28:31], v[32:33], off sc1 nt
	s_addc_u32 s6, s13, s17
	global_load_dwordx4 v[32:35], v[36:37], off sc1 nt
	s_add_u32 s14, s3, s14
	global_load_dwordx4 v[36:39], v[40:41], off sc1 nt
	s_addc_u32 s15, s6, s15
	global_load_dwordx4 v[40:43], v[46:47], off sc1 nt
	v_lshl_add_u64 v[46:47], v[46:47], 0, s[18:19]
	global_load_dwordx4 v[48:51], v[46:47], off sc1 nt
	v_lshl_add_u64 v[46:47], v[46:47], 0, s[18:19]
	global_load_dwordx4 v[56:59], v[46:47], off sc1 nt
	v_lshl_add_u64 v[46:47], v[46:47], 0, s[18:19]
	global_load_dwordx4 v[52:55], v[46:47], off sc1 nt
	s_nop 0
	global_load_dwordx4 v[44:47], v[44:45], off sc1 nt
	s_nop 0
	global_load_dwordx4 v[60:63], v[60:61], off sc1 nt
	s_add_u32 s3, s90, 0x3b100000
	s_addc_u32 s30, s91, 0
	s_add_u32 s12, s90, 0x1900000
	s_addc_u32 s13, s91, 0
	s_add_u32 s31, s90, 0x4b100000
	v_ashrrev_i32_e32 v129, 31, v128
	v_lshlrev_b32_e32 v132, 11, v64
	v_mov_b32_e32 v133, v131
	s_addc_u32 s33, s91, 0
	v_lshlrev_b32_e32 v130, 2, v64
	s_movk_i32 s34, 0x1000
	s_mov_b32 s35, 0
	s_branch .LBB0_659
.LBB0_658:
	s_lshl_b64 s[18:19], s[18:19], 11
	s_add_u32 s6, s16, s18
	s_addc_u32 s10, s17, s19
	s_add_u32 s16, s6, s20
	s_addc_u32 s17, s10, s21
	s_lshl_b64 s[18:19], s[24:25], 11
	s_add_u32 s6, s14, s18
	s_addc_u32 s10, s15, s19
	v_mad_i64_i32 v[0:1], s[18:19], s28, v128, 0
	s_add_u32 s14, s6, s26
	v_lshl_add_u64 v[0:1], v[0:1], 2, s[22:23]
	s_addc_u32 s15, s10, s27
	v_lshl_add_u64 v[0:1], v[0:1], 0, v[130:131]
	s_lshl_b32 s6, s28, 2
	v_lshl_add_u64 v[2:3], v[0:1], 0, s[6:7]
	global_load_dwordx4 v[60:63], v[0:1], off sc1 nt
	global_load_dwordx4 v[52:55], v[2:3], off sc1 nt
	v_lshl_add_u64 v[0:1], v[2:3], 0, s[6:7]
	v_lshl_add_u64 v[2:3], v[0:1], 0, s[6:7]
	global_load_dwordx4 v[56:59], v[0:1], off sc1 nt
	global_load_dwordx4 v[48:51], v[2:3], off sc1 nt
	v_lshl_add_u64 v[0:1], v[2:3], 0, s[6:7]
	v_lshl_add_u64 v[2:3], v[0:1], 0, s[6:7]
	global_load_dwordx4 v[40:43], v[0:1], off sc1 nt
	global_load_dwordx4 v[36:39], v[2:3], off sc1 nt
	v_lshl_add_u64 v[0:1], v[2:3], 0, s[6:7]
	v_lshl_add_u64 v[2:3], v[0:1], 0, s[6:7]
	global_load_dwordx4 v[32:35], v[0:1], off sc1 nt
	global_load_dwordx4 v[28:31], v[2:3], off sc1 nt
	v_lshl_add_u64 v[0:1], v[2:3], 0, s[6:7]
	global_load_dwordx4 v[24:27], v[0:1], off sc1 nt
	v_lshl_add_u64 v[0:1], v[0:1], 0, s[6:7]
	global_load_dwordx4 v[20:23], v[0:1], off sc1 nt
	v_lshl_add_u64 v[0:1], v[0:1], 0, s[6:7]
	global_load_dwordx4 v[16:19], v[0:1], off sc1 nt
	v_lshl_add_u64 v[0:1], v[0:1], 0, s[6:7]
	global_load_dwordx4 v[12:15], v[0:1], off sc1 nt
	v_lshl_add_u64 v[0:1], v[0:1], 0, s[6:7]
	global_load_dwordx4 v[8:11], v[0:1], off sc1 nt
	v_lshl_add_u64 v[0:1], v[0:1], 0, s[6:7]
	v_lshl_add_u64 v[44:45], v[0:1], 0, s[6:7]
	global_load_dwordx4 v[4:7], v[0:1], off sc1 nt
	s_waitcnt vmcnt(33)
	v_mul_f32_e32 v80, 0x44000000, v80
	global_load_dwordx4 v[0:3], v[44:45], off sc1 nt
	v_lshl_add_u64 v[44:45], v[44:45], 0, s[6:7]
	global_load_dwordx4 v[44:47], v[44:45], off sc1 nt
	s_waitcnt vmcnt(34)
	v_mul_f32_e32 v84, 0x44000000, v84
	v_mov_b32_e32 v134, v131
	v_cvt_pk_fp8_f32 v134, v80, v84
	s_waitcnt vmcnt(31)
	v_mul_f32_e32 v80, 0x44000000, v108
	s_waitcnt vmcnt(30)
	v_mul_f32_e32 v84, 0x44000000, v112
	v_mov_b32_e32 v135, v131
	v_cvt_pk_fp8_f32 v135, v80, v84
	s_waitcnt vmcnt(29)
	v_mul_f32_e32 v80, 0x44000000, v88
	s_waitcnt vmcnt(28)
	v_mul_f32_e32 v84, 0x44000000, v92
	s_waitcnt vmcnt(27)
	v_mul_f32_e32 v72, 0x44000000, v72
	v_cvt_pk_fp8_f32 v135, v80, v84 op_sel:[0,0,1]
	s_waitcnt vmcnt(26)
	v_mul_f32_e32 v80, 0x44000000, v96
	v_mov_b32_e32 v136, v131
	v_cvt_pk_fp8_f32 v136, v72, v80
	s_waitcnt vmcnt(23)
	v_mul_f32_e32 v72, 0x44000000, v76
	s_waitcnt vmcnt(22)
	v_mul_f32_e32 v76, 0x44000000, v100
	v_mov_b32_e32 v137, v131
	v_cvt_pk_fp8_f32 v137, v72, v76
	s_waitcnt vmcnt(21)
	v_mul_f32_e32 v64, 0x44000000, v64
	s_waitcnt vmcnt(20)
	v_mul_f32_e32 v68, 0x44000000, v68
	v_mov_b32_e32 v138, v131
	v_cvt_pk_fp8_f32 v137, v64, v68 op_sel:[0,0,1]
	v_mul_f32_e32 v64, 0x44000000, v81
	v_mul_f32_e32 v68, 0x44000000, v85
	v_cvt_pk_fp8_f32 v138, v64, v68
	v_mul_f32_e32 v64, 0x44000000, v109
	v_mul_f32_e32 v68, 0x44000000, v113
	v_mov_b32_e32 v139, v131
	v_cvt_pk_fp8_f32 v139, v64, v68
	v_mul_f32_e32 v64, 0x44000000, v89
	v_mul_f32_e32 v68, 0x44000000, v93
	v_mov_b32_e32 v140, v131
	v_cvt_pk_fp8_f32 v139, v64, v68 op_sel:[0,0,1]
	v_mul_f32_e32 v64, 0x44000000, v73
	v_mul_f32_e32 v68, 0x44000000, v97
	v_cvt_pk_fp8_f32 v140, v64, v68
	v_mul_f32_e32 v64, 0x44000000, v77
	v_mul_f32_e32 v68, 0x44000000, v101
	v_mov_b32_e32 v141, v131
	v_cvt_pk_fp8_f32 v141, v64, v68
	v_mul_f32_e32 v120, 0x44000000, v120
	v_mul_f32_e32 v124, 0x44000000, v124
	v_mul_f32_e32 v84, 0x44000000, v104
	v_mul_f32_e32 v88, 0x44000000, v116
	v_mul_f32_e32 v72, 0x44000000, v121
	v_mul_f32_e32 v76, 0x44000000, v125
	v_cvt_pk_fp8_f32 v134, v120, v124 op_sel:[0,0,1]
	v_cvt_pk_fp8_f32 v136, v84, v88 op_sel:[0,0,1]
	v_cvt_pk_fp8_f32 v138, v72, v76 op_sel:[0,0,1]
	v_mul_f32_e32 v72, 0x44000000, v105
	v_mul_f32_e32 v73, 0x44000000, v117
	v_mul_f32_e32 v64, 0x44000000, v65
	v_mul_f32_e32 v65, 0x44000000, v69
	v_cvt_pk_fp8_f32 v140, v72, v73 op_sel:[0,0,1]
	v_cvt_pk_fp8_f32 v141, v64, v65 op_sel:[0,0,1]
	v_lshl_add_u64 v[64:65], s[16:17], 0, v[132:133]
	v_lshl_add_u64 v[64:65], v[64:65], 0, v[128:129]
	global_store_dwordx4 v[64:65], v[134:137], off sc1 nt
	global_store_dwordx4 v[64:65], v[138:141], off offset:2048 sc1 nt
	v_mul_f32_e32 v68, 0x44000000, v82
	v_mul_f32_e32 v69, 0x44000000, v86
	v_mov_b32_e32 v134, v131
	v_cvt_pk_fp8_f32 v134, v68, v69
	v_mul_f32_e32 v68, 0x44000000, v110
	v_mul_f32_e32 v69, 0x44000000, v114
	v_mov_b32_e32 v135, v131
	v_cvt_pk_fp8_f32 v135, v68, v69
	v_mul_f32_e32 v68, 0x44000000, v90
	v_mul_f32_e32 v69, 0x44000000, v94
	v_mov_b32_e32 v136, v131
	v_cvt_pk_fp8_f32 v135, v68, v69 op_sel:[0,0,1]
	v_mul_f32_e32 v68, 0x44000000, v74
	v_mul_f32_e32 v69, 0x44000000, v98
	v_cvt_pk_fp8_f32 v136, v68, v69
	v_mul_f32_e32 v68, 0x44000000, v78
	v_mul_f32_e32 v69, 0x44000000, v102
	v_mov_b32_e32 v137, v131
	v_cvt_pk_fp8_f32 v137, v68, v69
	v_mul_f32_e32 v72, 0x44000000, v122
	v_mul_f32_e32 v73, 0x44000000, v126
	v_cvt_pk_fp8_f32 v134, v72, v73 op_sel:[0,0,1]
	v_mul_f32_e32 v72, 0x44000000, v106
	v_mul_f32_e32 v73, 0x44000000, v118
	v_mul_f32_e32 v66, 0x44000000, v66
	v_mul_f32_e32 v68, 0x44000000, v70
	v_cvt_pk_fp8_f32 v136, v72, v73 op_sel:[0,0,1]
	v_cvt_pk_fp8_f32 v137, v66, v68 op_sel:[0,0,1]
	v_mul_f32_e32 v66, 0x44000000, v83
	v_mul_f32_e32 v68, 0x44000000, v87
	v_mov_b32_e32 v72, v131
	v_cvt_pk_fp8_f32 v72, v66, v68
	v_mul_f32_e32 v66, 0x44000000, v111
	v_mul_f32_e32 v68, 0x44000000, v115
	v_mov_b32_e32 v73, v131
	v_cvt_pk_fp8_f32 v73, v66, v68
	v_mul_f32_e32 v66, 0x44000000, v91
	v_mul_f32_e32 v68, 0x44000000, v95
	v_mov_b32_e32 v74, v131
	v_cvt_pk_fp8_f32 v73, v66, v68 op_sel:[0,0,1]
	v_mul_f32_e32 v66, 0x44000000, v75
	v_mul_f32_e32 v68, 0x44000000, v99
	v_cvt_pk_fp8_f32 v74, v66, v68
	v_mul_f32_e32 v66, 0x44000000, v79
	v_mul_f32_e32 v68, 0x44000000, v103
	v_mov_b32_e32 v75, v131
	v_cvt_pk_fp8_f32 v75, v66, v68
	v_mul_f32_e32 v69, 0x44000000, v123
	v_mul_f32_e32 v70, 0x44000000, v127
	v_cvt_pk_fp8_f32 v72, v69, v70 op_sel:[0,0,1]
	v_mul_f32_e32 v69, 0x44000000, v107
	v_mul_f32_e32 v70, 0x44000000, v119
	v_mul_f32_e32 v66, 0x44000000, v67
	v_mul_f32_e32 v67, 0x44000000, v71
	v_cvt_pk_fp8_f32 v74, v69, v70 op_sel:[0,0,1]
	v_cvt_pk_fp8_f32 v75, v66, v67 op_sel:[0,0,1]
	v_add_co_u32_e32 v64, vcc, s34, v64
	s_add_i32 s35, s35, 2
	s_nop 0
	v_addc_co_u32_e32 v65, vcc, 0, v65, vcc
	s_cmp_le_i32 s35, s1
	global_store_dwordx4 v[64:65], v[134:137], off sc1 nt
	global_store_dwordx4 v[64:65], v[72:75], off offset:2048 sc1 nt
	s_cbranch_scc0 .LBB0_675

.LBB0_667:
	v_mad_i64_i32 v[64:65], s[26:27], s24, v128, 0
	v_lshl_add_u64 v[64:65], v[64:65], 2, s[22:23]
	v_lshl_add_u64 v[64:65], v[64:65], 0, v[130:131]
	s_lshl_b32 s6, s24, 2
	v_lshl_add_u64 v[66:67], v[64:65], 0, s[6:7]
	global_load_dwordx4 v[80:83], v[64:65], off sc1 nt
	global_load_dwordx4 v[84:87], v[66:67], off sc1 nt
	v_lshl_add_u64 v[64:65], v[66:67], 0, s[6:7]
	v_lshl_add_u64 v[66:67], v[64:65], 0, s[6:7]
	global_load_dwordx4 v[120:123], v[64:65], off sc1 nt
	global_load_dwordx4 v[124:127], v[66:67], off sc1 nt
	v_lshl_add_u64 v[64:65], v[66:67], 0, s[6:7]
	v_lshl_add_u64 v[66:67], v[64:65], 0, s[6:7]
	global_load_dwordx4 v[108:111], v[64:65], off sc1 nt
	global_load_dwordx4 v[112:115], v[66:67], off sc1 nt
	v_lshl_add_u64 v[64:65], v[66:67], 0, s[6:7]
	v_lshl_add_u64 v[66:67], v[64:65], 0, s[6:7]
	global_load_dwordx4 v[88:91], v[64:65], off sc1 nt
	global_load_dwordx4 v[92:95], v[66:67], off sc1 nt
	v_lshl_add_u64 v[64:65], v[66:67], 0, s[6:7]
	global_load_dwordx4 v[72:75], v[64:65], off sc1 nt
	v_lshl_add_u64 v[64:65], v[64:65], 0, s[6:7]
	global_load_dwordx4 v[96:99], v[64:65], off sc1 nt
	v_lshl_add_u64 v[64:65], v[64:65], 0, s[6:7]
	global_load_dwordx4 v[104:107], v[64:65], off sc1 nt
	v_lshl_add_u64 v[64:65], v[64:65], 0, s[6:7]
	global_load_dwordx4 v[116:119], v[64:65], off sc1 nt
	v_lshl_add_u64 v[64:65], v[64:65], 0, s[6:7]
	global_load_dwordx4 v[76:79], v[64:65], off sc1 nt
	v_lshl_add_u64 v[64:65], v[64:65], 0, s[6:7]
	v_lshl_add_u64 v[68:69], v[64:65], 0, s[6:7]
	global_load_dwordx4 v[100:103], v[64:65], off sc1 nt
	s_waitcnt vmcnt(21)
	v_mul_f32_e32 v8, 0x44000000, v8
	global_load_dwordx4 v[64:67], v[68:69], off sc1 nt
	v_lshl_add_u64 v[68:69], v[68:69], 0, s[6:7]
	global_load_dwordx4 v[68:71], v[68:69], off sc1 nt
	s_waitcnt vmcnt(22)
	v_mul_f32_e32 v4, 0x44000000, v4
	v_mov_b32_e32 v137, v131
	v_cvt_pk_fp8_f32 v137, v8, v4
	s_waitcnt vmcnt(21)
	v_mul_f32_e32 v0, 0x44000000, v0
	s_waitcnt vmcnt(17)
	v_mul_f32_e32 v4, 0x44000000, v44
	v_mov_b32_e32 v138, v131
	v_cvt_pk_fp8_f32 v137, v0, v4 op_sel:[0,0,1]
	s_waitcnt vmcnt(16)
	v_mul_f32_e32 v0, 0x44000000, v61
	v_mul_f32_e32 v4, 0x44000000, v53
	v_cvt_pk_fp8_f32 v138, v0, v4
	v_mul_f32_e32 v0, 0x44000000, v41
	v_mul_f32_e32 v4, 0x44000000, v37
	v_mov_b32_e32 v139, v131
	v_cvt_pk_fp8_f32 v139, v0, v4
	v_mul_f32_e32 v24, 0x44000000, v24
	v_mul_f32_e32 v20, 0x44000000, v20
	v_mov_b32_e32 v136, v131
	v_mul_f32_e32 v0, 0x44000000, v33
	v_mul_f32_e32 v4, 0x44000000, v29
	v_mul_f32_e32 v60, 0x44000000, v60
	v_mul_f32_e32 v52, 0x44000000, v52
	v_mov_b32_e32 v134, v131
	v_mul_f32_e32 v40, 0x44000000, v40
	v_mul_f32_e32 v36, 0x44000000, v36
	v_mov_b32_e32 v135, v131
	v_cvt_pk_fp8_f32 v136, v24, v20
	v_cvt_pk_fp8_f32 v139, v0, v4 op_sel:[0,0,1]
	v_mul_f32_e32 v0, 0x44000000, v25
	v_mul_f32_e32 v4, 0x44000000, v21
	v_mov_b32_e32 v140, v131
	v_cvt_pk_fp8_f32 v134, v60, v52
	v_cvt_pk_fp8_f32 v135, v40, v36
	v_cvt_pk_fp8_f32 v140, v0, v4
	v_mul_f32_e32 v0, 0x44000000, v9
	v_mul_f32_e32 v4, 0x44000000, v5
	v_mov_b32_e32 v141, v131
	v_cvt_pk_fp8_f32 v141, v0, v4
	v_mul_f32_e32 v16, 0x44000000, v16
	v_mul_f32_e32 v12, 0x44000000, v12
	v_mul_f32_e32 v56, 0x44000000, v56
	v_mul_f32_e32 v48, 0x44000000, v48
	v_mul_f32_e32 v32, 0x44000000, v32
	v_mul_f32_e32 v28, 0x44000000, v28
	v_cvt_pk_fp8_f32 v136, v16, v12 op_sel:[0,0,1]
	v_mul_f32_e32 v8, 0x44000000, v57
	v_mul_f32_e32 v12, 0x44000000, v49
	v_cvt_pk_fp8_f32 v134, v56, v48 op_sel:[0,0,1]
	v_cvt_pk_fp8_f32 v135, v32, v28 op_sel:[0,0,1]
	v_cvt_pk_fp8_f32 v138, v8, v12 op_sel:[0,0,1]
	v_mul_f32_e32 v8, 0x44000000, v17
	v_mul_f32_e32 v12, 0x44000000, v13
	v_mul_f32_e32 v0, 0x44000000, v1
	v_mul_f32_e32 v1, 0x44000000, v45
	v_cvt_pk_fp8_f32 v140, v8, v12 op_sel:[0,0,1]
	v_cvt_pk_fp8_f32 v141, v0, v1 op_sel:[0,0,1]
	v_lshl_add_u64 v[0:1], s[14:15], 0, v[132:133]
	v_lshl_add_u64 v[0:1], v[0:1], 0, v[128:129]
	global_store_dwordx4 v[0:1], v[134:137], off sc1 nt
	global_store_dwordx4 v[0:1], v[138:141], off offset:2048 sc1 nt
	v_mul_f32_e32 v4, 0x44000000, v62
	v_mul_f32_e32 v5, 0x44000000, v54
	v_mov_b32_e32 v134, v131
	v_cvt_pk_fp8_f32 v134, v4, v5
	v_mul_f32_e32 v4, 0x44000000, v42
	v_mul_f32_e32 v5, 0x44000000, v38
	v_mov_b32_e32 v135, v131
	v_cvt_pk_fp8_f32 v135, v4, v5
	v_mul_f32_e32 v4, 0x44000000, v34
	v_mul_f32_e32 v5, 0x44000000, v30
	v_mov_b32_e32 v136, v131
	v_cvt_pk_fp8_f32 v135, v4, v5 op_sel:[0,0,1]
	v_mul_f32_e32 v4, 0x44000000, v26
	v_mul_f32_e32 v5, 0x44000000, v22
	v_cvt_pk_fp8_f32 v136, v4, v5
	v_mul_f32_e32 v4, 0x44000000, v10
	v_mul_f32_e32 v5, 0x44000000, v6
	v_mov_b32_e32 v137, v131
	v_cvt_pk_fp8_f32 v137, v4, v5
	v_mul_f32_e32 v8, 0x44000000, v58
	v_mul_f32_e32 v9, 0x44000000, v50
	v_mul_f32_e32 v2, 0x44000000, v2
	v_mul_f32_e32 v4, 0x44000000, v46
	v_cvt_pk_fp8_f32 v134, v8, v9 op_sel:[0,0,1]
	v_mul_f32_e32 v8, 0x44000000, v18
	v_mul_f32_e32 v9, 0x44000000, v14
	v_cvt_pk_fp8_f32 v137, v2, v4 op_sel:[0,0,1]
	v_mul_f32_e32 v2, 0x44000000, v63
	v_mul_f32_e32 v5, 0x44000000, v55
	v_mov_b32_e32 v4, v131
	v_cvt_pk_fp8_f32 v136, v8, v9 op_sel:[0,0,1]
	v_cvt_pk_fp8_f32 v4, v2, v5
	v_mul_f32_e32 v2, 0x44000000, v43
	v_mul_f32_e32 v9, 0x44000000, v39
	v_mov_b32_e32 v5, v131
	v_cvt_pk_fp8_f32 v5, v2, v9
	v_mul_f32_e32 v6, 0x44000000, v59
	v_mul_f32_e32 v8, 0x44000000, v51
	v_cvt_pk_fp8_f32 v4, v6, v8 op_sel:[0,0,1]
	v_mul_f32_e32 v2, 0x44000000, v35
	v_mul_f32_e32 v6, 0x44000000, v31
	v_cvt_pk_fp8_f32 v5, v2, v6 op_sel:[0,0,1]
	v_mul_f32_e32 v2, 0x44000000, v27
	v_mul_f32_e32 v8, 0x44000000, v23
	v_mov_b32_e32 v6, v131
	v_cvt_pk_fp8_f32 v6, v2, v8
	v_mul_f32_e32 v2, 0x44000000, v11
	v_mul_f32_e32 v8, 0x44000000, v7
	v_mov_b32_e32 v7, v131
	v_cvt_pk_fp8_f32 v7, v2, v8
	v_mul_f32_e32 v9, 0x44000000, v19
	v_mul_f32_e32 v10, 0x44000000, v15
	v_mul_f32_e32 v2, 0x44000000, v3
	v_mul_f32_e32 v3, 0x44000000, v47
	s_add_i32 s0, s0, 16
	v_cvt_pk_fp8_f32 v6, v9, v10 op_sel:[0,0,1]
	v_cvt_pk_fp8_f32 v7, v2, v3 op_sel:[0,0,1]
	s_min_i32 s0, s0, s2
	v_add_co_u32_e32 v0, vcc, s34, v0
	s_cmp_gt_i32 s0, 0xffff
	s_nop 0
	v_addc_co_u32_e32 v1, vcc, 0, v1, vcc
	s_mov_b64 s[28:29], -1
	global_store_dwordx4 v[0:1], v[134:137], off sc1 nt
	global_store_dwordx4 v[0:1], v[4:7], off offset:2048 sc1 nt
	s_cbranch_scc0 .LBB0_673
	s_cmp_lt_u32 s0, 0x18000
	s_cbranch_scc0 .LBB0_670
	s_add_i32 s6, s0, 0xffff0000
	s_lshr_b32 s6, s6, 10
	s_lshl_b64 s[14:15], s[6:7], 22
	s_lshl_b64 s[22:23], s[6:7], 24
	s_add_u32 s10, s70, s22
	s_addc_u32 s11, s71, s23
	s_add_u32 s14, s3, s14
	s_addc_u32 s15, s30, s15
	s_lshl_b32 s6, s0, 1
	s_and_b32 s6, s6, 0x780
	s_lshl_b32 s22, s6, 13
	s_add_u32 s10, s10, s22
	s_addc_u32 s11, s11, 0
	s_lshl_b32 s22, s0, 5
	s_and_b32 s24, s22, 0x7e0
	s_lshl_b32 s22, s24, 2
	s_add_u32 s22, s10, s22
	s_mov_b32 s25, s7
	s_addc_u32 s23, s11, 0
	s_mov_b64 s[28:29], 0
	s_mov_b64 s[26:27], s[6:7]

.LBB0_748:
	s_not_b32 s2, s0
	s_add_i32 s1, s1, s2
	s_cmp_lt_i32 s1, -7
	s_cbranch_scc1 .LBB0_767
	s_ashr_i32 s2, s1, 31
	v_lshlrev_b32_e32 v1, 1, v0
	s_lshr_b32 s2, s2, 29
	v_and_b32_e32 v128, -16, v1
	v_lshlrev_b32_e32 v0, 2, v0
	s_add_i32 s2, s1, s2
	v_and_b32_e32 v64, 28, v0
	s_ashr_i32 s1, s2, 3
	s_and_b32 s2, s2, -8
	v_mad_i64_i32 v[0:1], s[18:19], s16, v128, 0
	v_mov_b32_e32 v131, 0
	s_add_i32 s2, s2, s0
	v_lshl_add_u64 v[0:1], v[0:1], 2, s[14:15]
	v_lshlrev_b32_e32 v130, 2, v64
	s_lshl_b32 s3, s16, 2
	s_mov_b32 s5, 0
	s_waitcnt vmcnt(4)
	v_lshl_add_u64 v[60:61], v[0:1], 0, v[130:131]
	s_mul_i32 s4, s16, 60
	s_sub_u32 s14, 0, s3
	v_lshl_add_u64 v[44:45], v[60:61], 0, s[4:5]
	s_subb_u32 s15, 0, 0
	v_lshl_add_u64 v[0:1], v[44:45], 0, s[14:15]
	v_lshl_add_u64 v[8:9], v[0:1], 0, s[14:15]
	global_load_dwordx4 v[0:3], v[0:1], off sc1 nt
	s_nop 0
	global_load_dwordx4 v[4:7], v[8:9], off sc1 nt
	v_lshl_add_u64 v[8:9], v[8:9], 0, s[14:15]
	v_lshl_add_u64 v[16:17], v[8:9], 0, s[14:15]
	global_load_dwordx4 v[8:11], v[8:9], off sc1 nt
	s_nop 0
	global_load_dwordx4 v[12:15], v[16:17], off sc1 nt
	v_lshl_add_u64 v[16:17], v[16:17], 0, s[14:15]
	v_lshl_add_u64 v[24:25], v[16:17], 0, s[14:15]
	v_lshl_add_u64 v[28:29], v[24:25], 0, s[14:15]
	v_lshl_add_u64 v[32:33], v[28:29], 0, s[14:15]
	v_lshl_add_u64 v[36:37], v[32:33], 0, s[14:15]
	v_lshl_add_u64 v[40:41], v[36:37], 0, s[14:15]
	v_lshl_add_u64 v[46:47], v[40:41], 0, s[14:15]
	global_load_dwordx4 v[16:19], v[16:17], off sc1 nt
	s_nop 0
	global_load_dwordx4 v[20:23], v[24:25], off sc1 nt
	s_lshl_b64 s[12:13], s[12:13], 11
	global_load_dwordx4 v[24:27], v[28:29], off sc1 nt
	s_add_u32 s3, s6, s12
	global_load_dwordx4 v[28:31], v[32:33], off sc1 nt
	s_addc_u32 s4, s7, s13
	global_load_dwordx4 v[32:35], v[36:37], off sc1 nt
	s_add_u32 s10, s3, s10
	global_load_dwordx4 v[36:39], v[40:41], off sc1 nt
	s_addc_u32 s11, s4, s11
	global_load_dwordx4 v[40:43], v[46:47], off sc1 nt
	v_lshl_add_u64 v[46:47], v[46:47], 0, s[14:15]
	global_load_dwordx4 v[48:51], v[46:47], off sc1 nt
	v_lshl_add_u64 v[46:47], v[46:47], 0, s[14:15]
	global_load_dwordx4 v[56:59], v[46:47], off sc1 nt
	v_lshl_add_u64 v[46:47], v[46:47], 0, s[14:15]
	global_load_dwordx4 v[52:55], v[46:47], off sc1 nt
	s_nop 0
	global_load_dwordx4 v[44:47], v[44:45], off sc1 nt
	s_nop 0
	global_load_dwordx4 v[60:63], v[60:61], off sc1 nt
	s_add_u32 s3, s90, 0x3b100000
	s_addc_u32 s26, s91, 0
	s_add_u32 s6, s90, 0x1900000
	s_addc_u32 s7, s91, 0
	s_add_u32 s27, s90, 0x4b100000
	v_ashrrev_i32_e32 v129, 31, v128
	v_lshlrev_b32_e32 v132, 11, v64
	v_mov_b32_e32 v133, v131
	s_addc_u32 s28, s91, 0
	v_lshlrev_b32_e32 v130, 2, v64
	s_movk_i32 s29, 0x1000
	s_mov_b32 s30, 0
	s_branch .LBB0_751
.LBB0_750:
	s_lshl_b64 s[14:15], s[14:15], 11
	s_add_u32 s4, s12, s14
	s_addc_u32 s13, s13, s15
	s_add_u32 s12, s4, s16
	s_addc_u32 s13, s13, s17
	s_lshl_b64 s[14:15], s[20:21], 11
	s_add_u32 s4, s10, s14
	s_addc_u32 s11, s11, s15
	v_mad_i64_i32 v[0:1], s[14:15], s24, v128, 0
	s_add_u32 s10, s4, s22
	v_lshl_add_u64 v[0:1], v[0:1], 2, s[18:19]
	s_addc_u32 s11, s11, s23
	v_lshl_add_u64 v[0:1], v[0:1], 0, v[130:131]
	s_lshl_b32 s4, s24, 2
	v_lshl_add_u64 v[2:3], v[0:1], 0, s[4:5]
	global_load_dwordx4 v[60:63], v[0:1], off sc1 nt
	global_load_dwordx4 v[52:55], v[2:3], off sc1 nt
	v_lshl_add_u64 v[0:1], v[2:3], 0, s[4:5]
	v_lshl_add_u64 v[2:3], v[0:1], 0, s[4:5]
	global_load_dwordx4 v[56:59], v[0:1], off sc1 nt
	global_load_dwordx4 v[48:51], v[2:3], off sc1 nt
	v_lshl_add_u64 v[0:1], v[2:3], 0, s[4:5]
	v_lshl_add_u64 v[2:3], v[0:1], 0, s[4:5]
	global_load_dwordx4 v[40:43], v[0:1], off sc1 nt
	global_load_dwordx4 v[36:39], v[2:3], off sc1 nt
	v_lshl_add_u64 v[0:1], v[2:3], 0, s[4:5]
	v_lshl_add_u64 v[2:3], v[0:1], 0, s[4:5]
	global_load_dwordx4 v[32:35], v[0:1], off sc1 nt
	global_load_dwordx4 v[28:31], v[2:3], off sc1 nt
	v_lshl_add_u64 v[0:1], v[2:3], 0, s[4:5]
	global_load_dwordx4 v[24:27], v[0:1], off sc1 nt
	v_lshl_add_u64 v[0:1], v[0:1], 0, s[4:5]
	global_load_dwordx4 v[20:23], v[0:1], off sc1 nt
	v_lshl_add_u64 v[0:1], v[0:1], 0, s[4:5]
	global_load_dwordx4 v[16:19], v[0:1], off sc1 nt
	v_lshl_add_u64 v[0:1], v[0:1], 0, s[4:5]
	global_load_dwordx4 v[12:15], v[0:1], off sc1 nt
	v_lshl_add_u64 v[0:1], v[0:1], 0, s[4:5]
	global_load_dwordx4 v[8:11], v[0:1], off sc1 nt
	v_lshl_add_u64 v[0:1], v[0:1], 0, s[4:5]
	v_lshl_add_u64 v[44:45], v[0:1], 0, s[4:5]
	global_load_dwordx4 v[4:7], v[0:1], off sc1 nt
	s_waitcnt vmcnt(33)
	v_mul_f32_e32 v80, 0x44000000, v80
	global_load_dwordx4 v[0:3], v[44:45], off sc1 nt
	v_lshl_add_u64 v[44:45], v[44:45], 0, s[4:5]
	global_load_dwordx4 v[44:47], v[44:45], off sc1 nt
	s_waitcnt vmcnt(34)
	v_mul_f32_e32 v84, 0x44000000, v84
	v_mov_b32_e32 v134, v131
	v_cvt_pk_fp8_f32 v134, v80, v84
	s_waitcnt vmcnt(31)
	v_mul_f32_e32 v80, 0x44000000, v108
	s_waitcnt vmcnt(30)
	v_mul_f32_e32 v84, 0x44000000, v112
	v_mov_b32_e32 v135, v131
	v_cvt_pk_fp8_f32 v135, v80, v84
	s_waitcnt vmcnt(29)
	v_mul_f32_e32 v80, 0x44000000, v88
	s_waitcnt vmcnt(28)
	v_mul_f32_e32 v84, 0x44000000, v92
	s_waitcnt vmcnt(27)
	v_mul_f32_e32 v72, 0x44000000, v72
	v_cvt_pk_fp8_f32 v135, v80, v84 op_sel:[0,0,1]
	s_waitcnt vmcnt(26)
	v_mul_f32_e32 v80, 0x44000000, v96
	v_mov_b32_e32 v136, v131
	v_cvt_pk_fp8_f32 v136, v72, v80
	s_waitcnt vmcnt(23)
	v_mul_f32_e32 v72, 0x44000000, v76
	s_waitcnt vmcnt(22)
	v_mul_f32_e32 v76, 0x44000000, v100
	v_mov_b32_e32 v137, v131
	v_cvt_pk_fp8_f32 v137, v72, v76
	s_waitcnt vmcnt(21)
	v_mul_f32_e32 v64, 0x44000000, v64
	s_waitcnt vmcnt(20)
	v_mul_f32_e32 v68, 0x44000000, v68
	v_mov_b32_e32 v138, v131
	v_cvt_pk_fp8_f32 v137, v64, v68 op_sel:[0,0,1]
	v_mul_f32_e32 v64, 0x44000000, v81
	v_mul_f32_e32 v68, 0x44000000, v85
	v_cvt_pk_fp8_f32 v138, v64, v68
	v_mul_f32_e32 v64, 0x44000000, v109
	v_mul_f32_e32 v68, 0x44000000, v113
	v_mov_b32_e32 v139, v131
	v_cvt_pk_fp8_f32 v139, v64, v68
	v_mul_f32_e32 v64, 0x44000000, v89
	v_mul_f32_e32 v68, 0x44000000, v93
	v_mov_b32_e32 v140, v131
	v_cvt_pk_fp8_f32 v139, v64, v68 op_sel:[0,0,1]
	v_mul_f32_e32 v64, 0x44000000, v73
	v_mul_f32_e32 v68, 0x44000000, v97
	v_cvt_pk_fp8_f32 v140, v64, v68
	v_mul_f32_e32 v64, 0x44000000, v77
	v_mul_f32_e32 v68, 0x44000000, v101
	v_mov_b32_e32 v141, v131
	v_cvt_pk_fp8_f32 v141, v64, v68
	v_mul_f32_e32 v120, 0x44000000, v120
	v_mul_f32_e32 v124, 0x44000000, v124
	v_mul_f32_e32 v84, 0x44000000, v104
	v_mul_f32_e32 v88, 0x44000000, v116
	v_mul_f32_e32 v72, 0x44000000, v121
	v_mul_f32_e32 v76, 0x44000000, v125
	v_cvt_pk_fp8_f32 v134, v120, v124 op_sel:[0,0,1]
	v_cvt_pk_fp8_f32 v136, v84, v88 op_sel:[0,0,1]
	v_cvt_pk_fp8_f32 v138, v72, v76 op_sel:[0,0,1]
	v_mul_f32_e32 v72, 0x44000000, v105
	v_mul_f32_e32 v73, 0x44000000, v117
	v_mul_f32_e32 v64, 0x44000000, v65
	v_mul_f32_e32 v65, 0x44000000, v69
	v_cvt_pk_fp8_f32 v140, v72, v73 op_sel:[0,0,1]
	v_cvt_pk_fp8_f32 v141, v64, v65 op_sel:[0,0,1]
	v_lshl_add_u64 v[64:65], s[12:13], 0, v[132:133]
	v_lshl_add_u64 v[64:65], v[64:65], 0, v[128:129]
	global_store_dwordx4 v[64:65], v[134:137], off sc1 nt
	global_store_dwordx4 v[64:65], v[138:141], off offset:2048 sc1 nt
	v_mul_f32_e32 v68, 0x44000000, v82
	v_mul_f32_e32 v69, 0x44000000, v86
	v_mov_b32_e32 v134, v131
	v_cvt_pk_fp8_f32 v134, v68, v69
	v_mul_f32_e32 v68, 0x44000000, v110
	v_mul_f32_e32 v69, 0x44000000, v114
	v_mov_b32_e32 v135, v131
	v_cvt_pk_fp8_f32 v135, v68, v69
	v_mul_f32_e32 v68, 0x44000000, v90
	v_mul_f32_e32 v69, 0x44000000, v94
	v_mov_b32_e32 v136, v131
	v_cvt_pk_fp8_f32 v135, v68, v69 op_sel:[0,0,1]
	v_mul_f32_e32 v68, 0x44000000, v74
	v_mul_f32_e32 v69, 0x44000000, v98
	v_cvt_pk_fp8_f32 v136, v68, v69
	v_mul_f32_e32 v68, 0x44000000, v78
	v_mul_f32_e32 v69, 0x44000000, v102
	v_mov_b32_e32 v137, v131
	v_cvt_pk_fp8_f32 v137, v68, v69
	v_mul_f32_e32 v72, 0x44000000, v122
	v_mul_f32_e32 v73, 0x44000000, v126
	v_cvt_pk_fp8_f32 v134, v72, v73 op_sel:[0,0,1]
	v_mul_f32_e32 v72, 0x44000000, v106
	v_mul_f32_e32 v73, 0x44000000, v118
	v_mul_f32_e32 v66, 0x44000000, v66
	v_mul_f32_e32 v68, 0x44000000, v70
	v_cvt_pk_fp8_f32 v136, v72, v73 op_sel:[0,0,1]
	v_cvt_pk_fp8_f32 v137, v66, v68 op_sel:[0,0,1]
	v_mul_f32_e32 v66, 0x44000000, v83
	v_mul_f32_e32 v68, 0x44000000, v87
	v_mov_b32_e32 v72, v131
	v_cvt_pk_fp8_f32 v72, v66, v68
	v_mul_f32_e32 v66, 0x44000000, v111
	v_mul_f32_e32 v68, 0x44000000, v115
	v_mov_b32_e32 v73, v131
	v_cvt_pk_fp8_f32 v73, v66, v68
	v_mul_f32_e32 v66, 0x44000000, v91
	v_mul_f32_e32 v68, 0x44000000, v95
	v_mov_b32_e32 v74, v131
	v_cvt_pk_fp8_f32 v73, v66, v68 op_sel:[0,0,1]
	v_mul_f32_e32 v66, 0x44000000, v75
	v_mul_f32_e32 v68, 0x44000000, v99
	v_cvt_pk_fp8_f32 v74, v66, v68
	v_mul_f32_e32 v66, 0x44000000, v79
	v_mul_f32_e32 v68, 0x44000000, v103
	v_mov_b32_e32 v75, v131
	v_cvt_pk_fp8_f32 v75, v66, v68
	v_mul_f32_e32 v69, 0x44000000, v123
	v_mul_f32_e32 v70, 0x44000000, v127
	v_cvt_pk_fp8_f32 v72, v69, v70 op_sel:[0,0,1]
	v_mul_f32_e32 v69, 0x44000000, v107
	v_mul_f32_e32 v70, 0x44000000, v119
	v_mul_f32_e32 v66, 0x44000000, v67
	v_mul_f32_e32 v67, 0x44000000, v71
	v_cvt_pk_fp8_f32 v74, v69, v70 op_sel:[0,0,1]
	v_cvt_pk_fp8_f32 v75, v66, v67 op_sel:[0,0,1]
	v_add_co_u32_e32 v64, vcc, s29, v64
	s_add_i32 s30, s30, 2
	s_nop 0
	v_addc_co_u32_e32 v65, vcc, 0, v65, vcc
	s_cmp_le_i32 s30, s1
	global_store_dwordx4 v[64:65], v[134:137], off sc1 nt
	global_store_dwordx4 v[64:65], v[72:75], off offset:2048 sc1 nt
	s_cbranch_scc0 .LBB0_767

.LBB0_759:
	v_mad_i64_i32 v[64:65], s[22:23], s20, v128, 0
	v_lshl_add_u64 v[64:65], v[64:65], 2, s[18:19]
	v_lshl_add_u64 v[64:65], v[64:65], 0, v[130:131]
	s_lshl_b32 s4, s20, 2
	v_lshl_add_u64 v[66:67], v[64:65], 0, s[4:5]
	global_load_dwordx4 v[80:83], v[64:65], off sc1 nt
	global_load_dwordx4 v[84:87], v[66:67], off sc1 nt
	v_lshl_add_u64 v[64:65], v[66:67], 0, s[4:5]
	v_lshl_add_u64 v[66:67], v[64:65], 0, s[4:5]
	global_load_dwordx4 v[120:123], v[64:65], off sc1 nt
	global_load_dwordx4 v[124:127], v[66:67], off sc1 nt
	v_lshl_add_u64 v[64:65], v[66:67], 0, s[4:5]
	v_lshl_add_u64 v[66:67], v[64:65], 0, s[4:5]
	global_load_dwordx4 v[108:111], v[64:65], off sc1 nt
	global_load_dwordx4 v[112:115], v[66:67], off sc1 nt
	v_lshl_add_u64 v[64:65], v[66:67], 0, s[4:5]
	v_lshl_add_u64 v[66:67], v[64:65], 0, s[4:5]
	global_load_dwordx4 v[88:91], v[64:65], off sc1 nt
	global_load_dwordx4 v[92:95], v[66:67], off sc1 nt
	v_lshl_add_u64 v[64:65], v[66:67], 0, s[4:5]
	global_load_dwordx4 v[72:75], v[64:65], off sc1 nt
	v_lshl_add_u64 v[64:65], v[64:65], 0, s[4:5]
	global_load_dwordx4 v[96:99], v[64:65], off sc1 nt
	v_lshl_add_u64 v[64:65], v[64:65], 0, s[4:5]
	global_load_dwordx4 v[104:107], v[64:65], off sc1 nt
	v_lshl_add_u64 v[64:65], v[64:65], 0, s[4:5]
	global_load_dwordx4 v[116:119], v[64:65], off sc1 nt
	v_lshl_add_u64 v[64:65], v[64:65], 0, s[4:5]
	global_load_dwordx4 v[76:79], v[64:65], off sc1 nt
	v_lshl_add_u64 v[64:65], v[64:65], 0, s[4:5]
	v_lshl_add_u64 v[68:69], v[64:65], 0, s[4:5]
	global_load_dwordx4 v[100:103], v[64:65], off sc1 nt
	s_waitcnt vmcnt(21)
	v_mul_f32_e32 v8, 0x44000000, v8
	global_load_dwordx4 v[64:67], v[68:69], off sc1 nt
	v_lshl_add_u64 v[68:69], v[68:69], 0, s[4:5]
	global_load_dwordx4 v[68:71], v[68:69], off sc1 nt
	s_waitcnt vmcnt(22)
	v_mul_f32_e32 v4, 0x44000000, v4
	v_mov_b32_e32 v137, v131
	v_cvt_pk_fp8_f32 v137, v8, v4
	s_waitcnt vmcnt(21)
	v_mul_f32_e32 v0, 0x44000000, v0
	s_waitcnt vmcnt(17)
	v_mul_f32_e32 v4, 0x44000000, v44
	v_mov_b32_e32 v138, v131
	v_cvt_pk_fp8_f32 v137, v0, v4 op_sel:[0,0,1]
	s_waitcnt vmcnt(16)
	v_mul_f32_e32 v0, 0x44000000, v61
	v_mul_f32_e32 v4, 0x44000000, v53
	v_cvt_pk_fp8_f32 v138, v0, v4
	v_mul_f32_e32 v0, 0x44000000, v41
	v_mul_f32_e32 v4, 0x44000000, v37
	v_mov_b32_e32 v139, v131
	v_cvt_pk_fp8_f32 v139, v0, v4
	v_mul_f32_e32 v24, 0x44000000, v24
	v_mul_f32_e32 v20, 0x44000000, v20
	v_mov_b32_e32 v136, v131
	v_mul_f32_e32 v0, 0x44000000, v33
	v_mul_f32_e32 v4, 0x44000000, v29
	v_mul_f32_e32 v60, 0x44000000, v60
	v_mul_f32_e32 v52, 0x44000000, v52
	v_mov_b32_e32 v134, v131
	v_mul_f32_e32 v40, 0x44000000, v40
	v_mul_f32_e32 v36, 0x44000000, v36
	v_mov_b32_e32 v135, v131
	v_cvt_pk_fp8_f32 v136, v24, v20
	v_cvt_pk_fp8_f32 v139, v0, v4 op_sel:[0,0,1]
	v_mul_f32_e32 v0, 0x44000000, v25
	v_mul_f32_e32 v4, 0x44000000, v21
	v_mov_b32_e32 v140, v131
	v_cvt_pk_fp8_f32 v134, v60, v52
	v_cvt_pk_fp8_f32 v135, v40, v36
	v_cvt_pk_fp8_f32 v140, v0, v4
	v_mul_f32_e32 v0, 0x44000000, v9
	v_mul_f32_e32 v4, 0x44000000, v5
	v_mov_b32_e32 v141, v131
	v_cvt_pk_fp8_f32 v141, v0, v4
	v_mul_f32_e32 v16, 0x44000000, v16
	v_mul_f32_e32 v12, 0x44000000, v12
	v_mul_f32_e32 v56, 0x44000000, v56
	v_mul_f32_e32 v48, 0x44000000, v48
	v_mul_f32_e32 v32, 0x44000000, v32
	v_mul_f32_e32 v28, 0x44000000, v28
	v_cvt_pk_fp8_f32 v136, v16, v12 op_sel:[0,0,1]
	v_mul_f32_e32 v8, 0x44000000, v57
	v_mul_f32_e32 v12, 0x44000000, v49
	v_cvt_pk_fp8_f32 v134, v56, v48 op_sel:[0,0,1]
	v_cvt_pk_fp8_f32 v135, v32, v28 op_sel:[0,0,1]
	v_cvt_pk_fp8_f32 v138, v8, v12 op_sel:[0,0,1]
	v_mul_f32_e32 v8, 0x44000000, v17
	v_mul_f32_e32 v12, 0x44000000, v13
	v_mul_f32_e32 v0, 0x44000000, v1
	v_mul_f32_e32 v1, 0x44000000, v45
	v_cvt_pk_fp8_f32 v140, v8, v12 op_sel:[0,0,1]
	v_cvt_pk_fp8_f32 v141, v0, v1 op_sel:[0,0,1]
	v_lshl_add_u64 v[0:1], s[10:11], 0, v[132:133]
	v_lshl_add_u64 v[0:1], v[0:1], 0, v[128:129]
	global_store_dwordx4 v[0:1], v[134:137], off sc1 nt
	global_store_dwordx4 v[0:1], v[138:141], off offset:2048 sc1 nt
	v_mul_f32_e32 v4, 0x44000000, v62
	v_mul_f32_e32 v5, 0x44000000, v54
	v_mov_b32_e32 v134, v131
	v_cvt_pk_fp8_f32 v134, v4, v5
	v_mul_f32_e32 v4, 0x44000000, v42
	v_mul_f32_e32 v5, 0x44000000, v38
	v_mov_b32_e32 v135, v131
	v_cvt_pk_fp8_f32 v135, v4, v5
	v_mul_f32_e32 v4, 0x44000000, v34
	v_mul_f32_e32 v5, 0x44000000, v30
	v_mov_b32_e32 v136, v131
	v_cvt_pk_fp8_f32 v135, v4, v5 op_sel:[0,0,1]
	v_mul_f32_e32 v4, 0x44000000, v26
	v_mul_f32_e32 v5, 0x44000000, v22
	v_cvt_pk_fp8_f32 v136, v4, v5
	v_mul_f32_e32 v4, 0x44000000, v10
	v_mul_f32_e32 v5, 0x44000000, v6
	v_mov_b32_e32 v137, v131
	v_cvt_pk_fp8_f32 v137, v4, v5
	v_mul_f32_e32 v8, 0x44000000, v58
	v_mul_f32_e32 v9, 0x44000000, v50
	v_mul_f32_e32 v2, 0x44000000, v2
	v_mul_f32_e32 v4, 0x44000000, v46
	v_cvt_pk_fp8_f32 v134, v8, v9 op_sel:[0,0,1]
	v_mul_f32_e32 v8, 0x44000000, v18
	v_mul_f32_e32 v9, 0x44000000, v14
	v_cvt_pk_fp8_f32 v137, v2, v4 op_sel:[0,0,1]
	v_mul_f32_e32 v2, 0x44000000, v63
	v_mul_f32_e32 v5, 0x44000000, v55
	v_mov_b32_e32 v4, v131
	v_cvt_pk_fp8_f32 v136, v8, v9 op_sel:[0,0,1]
	v_cvt_pk_fp8_f32 v4, v2, v5
	v_mul_f32_e32 v2, 0x44000000, v43
	v_mul_f32_e32 v9, 0x44000000, v39
	v_mov_b32_e32 v5, v131
	v_cvt_pk_fp8_f32 v5, v2, v9
	v_mul_f32_e32 v6, 0x44000000, v59
	v_mul_f32_e32 v8, 0x44000000, v51
	v_cvt_pk_fp8_f32 v4, v6, v8 op_sel:[0,0,1]
	v_mul_f32_e32 v2, 0x44000000, v35
	v_mul_f32_e32 v6, 0x44000000, v31
	v_cvt_pk_fp8_f32 v5, v2, v6 op_sel:[0,0,1]
	v_mul_f32_e32 v2, 0x44000000, v27
	v_mul_f32_e32 v8, 0x44000000, v23
	v_mov_b32_e32 v6, v131
	v_cvt_pk_fp8_f32 v6, v2, v8
	v_mul_f32_e32 v2, 0x44000000, v11
	v_mul_f32_e32 v8, 0x44000000, v7
	v_mov_b32_e32 v7, v131
	v_cvt_pk_fp8_f32 v7, v2, v8
	v_mul_f32_e32 v9, 0x44000000, v19
	v_mul_f32_e32 v10, 0x44000000, v15
	v_mul_f32_e32 v2, 0x44000000, v3
	v_mul_f32_e32 v3, 0x44000000, v47
	s_add_i32 s0, s0, 16
	v_cvt_pk_fp8_f32 v6, v9, v10 op_sel:[0,0,1]
	v_cvt_pk_fp8_f32 v7, v2, v3 op_sel:[0,0,1]
	s_min_i32 s0, s0, s2
	v_add_co_u32_e32 v0, vcc, s29, v0
	s_cmp_gt_i32 s0, 0xffff
	s_nop 0
	v_addc_co_u32_e32 v1, vcc, 0, v1, vcc
	s_mov_b64 s[24:25], -1
	global_store_dwordx4 v[0:1], v[134:137], off sc1 nt
	global_store_dwordx4 v[0:1], v[4:7], off offset:2048 sc1 nt
	s_cbranch_scc0 .LBB0_765
	s_cmp_lt_u32 s0, 0x18000
	s_cbranch_scc0 .LBB0_762
	s_add_i32 s4, s0, 0xffff0000
	s_lshr_b32 s4, s4, 10
	s_lshl_b64 s[10:11], s[4:5], 22
	s_lshl_b64 s[18:19], s[4:5], 24
	s_add_u32 s18, s70, s18
	s_addc_u32 s19, s71, s19
	s_add_u32 s10, s3, s10
	s_addc_u32 s11, s26, s11
	s_lshl_b32 s4, s0, 1
	s_and_b32 s4, s4, 0x780
	s_lshl_b32 s20, s4, 13
	s_add_u32 s18, s18, s20
	s_addc_u32 s19, s19, 0
	s_lshl_b32 s20, s0, 5
	s_and_b32 s20, s20, 0x7e0
	s_lshl_b32 s22, s20, 2
	s_add_u32 s18, s18, s22
	s_mov_b32 s21, s5
	s_addc_u32 s19, s19, 0
	s_mov_b64 s[24:25], 0
	s_mov_b64 s[22:23], s[4:5]

.LBB0_780:
	v_lshlrev_b32_e32 v1, 1, v0
	v_and_b32_e32 v130, -16, v1
	v_lshlrev_b32_e32 v0, 2, v0
	v_and_b32_e32 v48, 28, v0
	v_mad_i64_i32 v[0:1], s[18:19], s16, v130, 0
	v_mov_b32_e32 v67, 0
	v_lshl_add_u64 v[0:1], v[0:1], 2, s[14:15]
	v_lshlrev_b32_e32 v66, 2, v48
	s_mov_b32 s3, 0
	v_lshl_add_u64 v[62:63], v[0:1], 0, v[66:67]
	s_mul_i32 s2, s16, 60
	v_lshl_add_u64 v[24:25], v[62:63], 0, s[2:3]
	s_lshl_b32 s2, s16, 2
	s_sub_u32 s2, 0, s2
	s_subb_u32 s3, 0, 0
	v_lshl_add_u64 v[0:1], v[24:25], 0, s[2:3]
	v_lshl_add_u64 v[8:9], v[0:1], 0, s[2:3]
	global_load_dwordx4 v[0:3], v[0:1], off sc1 nt
	s_nop 0
	global_load_dwordx4 v[4:7], v[8:9], off sc1 nt
	v_lshl_add_u64 v[8:9], v[8:9], 0, s[2:3]
	v_lshl_add_u64 v[16:17], v[8:9], 0, s[2:3]
	global_load_dwordx4 v[8:11], v[8:9], off sc1 nt
	s_nop 0
	global_load_dwordx4 v[12:15], v[16:17], off sc1 nt
	v_lshl_add_u64 v[16:17], v[16:17], 0, s[2:3]
	v_lshl_add_u64 v[26:27], v[16:17], 0, s[2:3]
	global_load_dwordx4 v[16:19], v[16:17], off sc1 nt
	s_nop 0
	global_load_dwordx4 v[20:23], v[26:27], off sc1 nt
	v_lshl_add_u64 v[26:27], v[26:27], 0, s[2:3]
	global_load_dwordx4 v[28:31], v[26:27], off sc1 nt
	v_lshl_add_u64 v[26:27], v[26:27], 0, s[2:3]
	global_load_dwordx4 v[32:35], v[26:27], off sc1 nt
	v_lshl_add_u64 v[26:27], v[26:27], 0, s[2:3]
	global_load_dwordx4 v[36:39], v[26:27], off sc1 nt
	v_lshl_add_u64 v[26:27], v[26:27], 0, s[2:3]
	global_load_dwordx4 v[40:43], v[26:27], off sc1 nt
	v_lshl_add_u64 v[26:27], v[26:27], 0, s[2:3]
	global_load_dwordx4 v[44:47], v[26:27], off sc1 nt
	v_lshl_add_u64 v[26:27], v[26:27], 0, s[2:3]
	global_load_dwordx4 v[50:53], v[26:27], off sc1 nt
	v_lshl_add_u64 v[26:27], v[26:27], 0, s[2:3]
	global_load_dwordx4 v[54:57], v[26:27], off sc1 nt
	v_lshl_add_u64 v[26:27], v[26:27], 0, s[2:3]
	global_load_dwordx4 v[58:61], v[26:27], off sc1 nt
	s_nop 0
	global_load_dwordx4 v[24:27], v[24:25], off sc1 nt
	s_nop 0
	global_load_dwordx4 v[62:65], v[62:63], off sc1 nt
	v_ashrrev_i32_e32 v131, 31, v130
	s_and_b64 vcc, exec, s[12:13]
	s_cbranch_vccz .LBB0_783
	s_cmp_lt_u32 s0, 0x18000
	s_cbranch_scc0 .LBB0_784
	s_addk_i32 s1, 0xfcff
	s_lshr_b32 s14, s1, 10
	s_mov_b32 s15, 0
	s_lshl_b64 s[2:3], s[14:15], 22
	s_lshl_b64 s[12:13], s[14:15], 24
	s_add_u32 s1, s70, s12
	s_addc_u32 s16, s71, s13
	s_add_u32 s2, s90, s2
	s_addc_u32 s3, s91, s3
	s_add_u32 s12, s2, 0x3b100000
	s_addc_u32 s13, s3, 0
	s_lshl_b32 s2, s0, 1
	s_and_b32 s14, s2, 0x780
	s_lshl_b32 s2, s14, 13
	s_add_u32 s1, s1, s2
	s_addc_u32 s2, s16, 0
	s_lshl_b32 s3, s0, 5
	s_and_b32 s18, s3, 0x7e0
	s_lshl_b32 s3, s18, 2
	s_add_u32 s16, s1, s3
	s_mov_b32 s19, s15
	s_addc_u32 s17, s2, 0
	s_mov_b64 s[20:21], 0
	s_branch .LBB0_785

.LBB0_861:
	s_andn2_b64 vcc, exec, s[8:9]
	s_cbranch_vccnz .LBB0_863
	v_readlane_b32 s2, v255, 4
	s_lshl_b32 s2, s2, 2
	s_or_b32 s1, s2, s1
	s_ashr_i32 s2, s1, 31
	s_lshr_b32 s2, s2, 26
	s_add_i32 s2, s1, s2
	s_ashr_i32 s10, s2, 6
	s_lshl_b32 s8, s10, 7
	s_ashr_i32 s9, s8, 31
	v_readlane_b32 s12, v255, 5
	s_lshl_b64 s[2:3], s[8:9], 13
	v_readlane_b32 s18, v255, 11
	v_readlane_b32 s13, v255, 6
	v_readlane_b32 s19, v255, 12
	s_add_u32 s12, s18, s2
	s_addc_u32 s13, s19, s3
	s_lshl_b32 s1, s1, 5
	s_lshl_b32 s2, s10, 11
	s_sub_i32 s10, s1, s2
	v_mbcnt_lo_u32_b32 v2, -1, 0
	v_mbcnt_hi_u32_b32 v2, -1, v2
	s_ashr_i32 s11, s10, 31
	v_lshlrev_b32_e32 v0, 1, v2
	v_and_b32_e32 v0, -16, v0
	s_lshl_b64 s[2:3], s[10:11], 2
	v_ashrrev_i32_e32 v1, 31, v0
	v_lshlrev_b32_e32 v2, 2, v2
	s_add_u32 s2, s12, s2
	v_and_b32_e32 v68, 28, v2
	s_addc_u32 s3, s13, s3
	v_lshlrev_b64 v[2:3], 13, v[0:1]
	v_lshl_add_u64 v[4:5], s[2:3], 0, v[2:3]
	v_lshlrev_b32_e32 v2, 2, v68
	v_mov_b32_e32 v3, 0
	v_lshl_add_u64 v[64:65], v[4:5], 0, v[2:3]
	s_mov_b32 s2, 0x1c000
	v_add_co_u32_e32 v56, vcc, s2, v64
	s_mov_b32 s3, 0x18000
	s_nop 0
	v_addc_co_u32_e32 v57, vcc, 0, v65, vcc
	v_add_co_u32_e32 v4, vcc, s3, v64
	s_mov_b32 s3, 0x16000
	s_nop 0
	v_addc_co_u32_e32 v5, vcc, 0, v65, vcc
	v_add_co_u32_e32 v8, vcc, s3, v64
	s_mov_b32 s3, 0x14000
	s_nop 0
	v_addc_co_u32_e32 v9, vcc, 0, v65, vcc
	v_add_co_u32_e32 v48, vcc, s3, v64
	s_mov_b32 s12, 0x10000
	s_nop 0
	v_addc_co_u32_e32 v49, vcc, 0, v65, vcc
	v_add_co_u32_e32 v40, vcc, s12, v64
	s_mov_b32 s12, 0xe000
	s_nop 0
	v_addc_co_u32_e32 v41, vcc, 0, v65, vcc
	v_add_co_u32_e32 v44, vcc, s12, v64
	s_mov_b32 s12, 0xc000
	s_nop 0
	v_addc_co_u32_e32 v45, vcc, 0, v65, vcc
	v_add_co_u32_e32 v32, vcc, s12, v64
	s_mov_b32 s13, 0x8000
	s_nop 0
	v_addc_co_u32_e32 v33, vcc, 0, v65, vcc
	v_add_co_u32_e32 v12, vcc, s13, v64
	s_movk_i32 s13, 0x6000
	s_nop 0
	v_addc_co_u32_e32 v13, vcc, 0, v65, vcc
	v_add_co_u32_e32 v16, vcc, s13, v64
	s_movk_i32 s13, 0x4000
	s_nop 0
	v_addc_co_u32_e32 v17, vcc, 0, v65, vcc
	v_add_co_u32_e32 v24, vcc, s13, v64
	s_movk_i32 s13, 0x2000
	s_nop 0
	v_addc_co_u32_e32 v25, vcc, 0, v65, vcc
	v_add_co_u32_e32 v28, vcc, s13, v64
	global_load_dwordx4 v[4:7], v[4:5], off sc1 nt
	s_nop 0
	global_load_dwordx4 v[8:11], v[8:9], off sc1 nt
	v_addc_co_u32_e32 v29, vcc, 0, v65, vcc
	s_mov_b32 s12, 0xa000
	global_load_dwordx4 v[12:15], v[12:13], off sc1 nt
	s_nop 0
	global_load_dwordx4 v[16:19], v[16:17], off sc1 nt
	s_nop 0
	global_load_dwordx4 v[20:23], v[64:65], off sc1 nt
	s_nop 0
	global_load_dwordx4 v[24:27], v[24:25], off sc1 nt
	s_nop 0
	global_load_dwordx4 v[28:31], v[28:29], off sc1 nt
	v_add_co_u32_e32 v36, vcc, s12, v64
	s_mov_b32 s3, 0x12000
	s_nop 0
	v_addc_co_u32_e32 v37, vcc, 0, v65, vcc
	global_load_dwordx4 v[32:35], v[32:33], off sc1 nt
	s_nop 0
	global_load_dwordx4 v[36:39], v[36:37], off sc1 nt
	s_nop 0
	global_load_dwordx4 v[40:43], v[40:41], off sc1 nt
	s_nop 0
	global_load_dwordx4 v[44:47], v[44:45], off sc1 nt
	v_add_co_u32_e32 v52, vcc, s3, v64
	s_mov_b32 s2, 0x1a000
	s_nop 0
	v_addc_co_u32_e32 v53, vcc, 0, v65, vcc
	v_add_co_u32_e32 v60, vcc, s2, v64
	global_load_dwordx4 v[48:51], v[48:49], off sc1 nt
	s_nop 0
	global_load_dwordx4 v[52:55], v[52:53], off sc1 nt
	v_addc_co_u32_e32 v61, vcc, 0, v65, vcc
	global_load_dwordx4 v[56:59], v[56:57], off sc1 nt
	s_nop 0
	global_load_dwordx4 v[60:63], v[60:61], off sc1 nt
	s_mov_b32 s1, 0x1e000
	v_add_co_u32_e32 v64, vcc, s1, v64
	s_lshl_b64 s[2:3], s[10:11], 11
	s_nop 0
	v_addc_co_u32_e32 v65, vcc, 0, v65, vcc
	global_load_dwordx4 v[64:67], v[64:65], off sc1 nt
	s_add_u32 s1, s90, s2
	s_addc_u32 s3, s91, s3
	s_add_u32 s2, s1, s8
	s_addc_u32 s3, s3, s9
	v_lshlrev_b32_e32 v2, 11, v68
	v_lshl_add_u64 v[68:69], s[2:3], 0, v[2:3]
	v_lshl_add_u64 v[80:81], v[68:69], 0, v[0:1]
	v_mov_b32_e32 v68, v3
	v_mov_b32_e32 v69, v3
	v_mov_b32_e32 v70, v3
	v_mov_b32_e32 v71, v3
	v_mov_b32_e32 v72, v3
	v_mov_b32_e32 v73, v3
	v_mov_b32_e32 v74, v3
	v_mov_b32_e32 v75, v3
	v_mov_b32_e32 v76, v3
	v_mov_b32_e32 v77, v3
	v_mov_b32_e32 v78, v3
	v_mov_b32_e32 v79, v3
	s_mov_b32 s1, 0x1900000
	s_mov_b64 s[2:3], 0x1900000
	v_lshl_add_u64 v[82:83], v[80:81], 0, s[2:3]
	v_readlane_b32 s14, v255, 7
	v_readlane_b32 s15, v255, 8
	v_readlane_b32 s16, v255, 9
	v_readlane_b32 s17, v255, 10
	v_readlane_b32 s20, v255, 13
	v_readlane_b32 s21, v255, 14
	v_readlane_b32 s22, v255, 15
	v_readlane_b32 s23, v255, 16
	v_readlane_b32 s24, v255, 17
	v_readlane_b32 s25, v255, 18
	v_readlane_b32 s26, v255, 19
	v_readlane_b32 s27, v255, 20
	s_waitcnt vmcnt(14)
	v_mul_f32_e32 v8, 0x44000000, v8
	s_waitcnt vmcnt(11)
	v_mul_f32_e32 v0, 0x44000000, v20
	s_waitcnt vmcnt(10)
	v_mul_f32_e32 v2, 0x44000000, v24
	s_waitcnt vmcnt(9)
	v_mul_f32_e32 v1, 0x44000000, v28
	v_cvt_pk_fp8_f32 v68, v0, v1
	v_mul_f32_e32 v0, 0x44000000, v12
	v_mul_f32_e32 v16, 0x44000000, v16
	s_waitcnt vmcnt(7)
	v_mul_f32_e32 v1, 0x44000000, v36
	v_cvt_pk_fp8_f32 v69, v0, v1
	v_mul_f32_e32 v0, 0x44000000, v32
	s_waitcnt vmcnt(5)
	v_mul_f32_e32 v1, 0x44000000, v44
	v_cvt_pk_fp8_f32 v68, v2, v16 op_sel:[0,0,1]
	v_cvt_pk_fp8_f32 v69, v0, v1 op_sel:[0,0,1]
	v_mul_f32_e32 v0, 0x44000000, v40
	s_waitcnt vmcnt(4)
	v_mul_f32_e32 v2, 0x44000000, v48
	s_waitcnt vmcnt(3)
	v_mul_f32_e32 v1, 0x44000000, v52
	v_cvt_pk_fp8_f32 v70, v0, v1
	v_mul_f32_e32 v0, 0x44000000, v4
	s_waitcnt vmcnt(1)
	v_mul_f32_e32 v1, 0x44000000, v60
	v_cvt_pk_fp8_f32 v71, v0, v1
	v_mul_f32_e32 v0, 0x44000000, v56
	v_cvt_pk_fp8_f32 v70, v2, v8 op_sel:[0,0,1]
	v_mul_f32_e32 v2, 0x44000000, v25
	v_mul_f32_e32 v4, 0x44000000, v17
	v_mul_f32_e32 v8, 0x44000000, v11
	s_waitcnt vmcnt(0)
	v_mul_f32_e32 v1, 0x44000000, v64
	v_cvt_pk_fp8_f32 v71, v0, v1 op_sel:[0,0,1]
	v_mul_f32_e32 v0, 0x44000000, v21
	v_mul_f32_e32 v1, 0x44000000, v29
	v_cvt_pk_fp8_f32 v72, v0, v1
	v_mul_f32_e32 v0, 0x44000000, v13
	v_mul_f32_e32 v1, 0x44000000, v37
	v_cvt_pk_fp8_f32 v73, v0, v1
	v_mul_f32_e32 v0, 0x44000000, v33
	v_mul_f32_e32 v1, 0x44000000, v45
	v_cvt_pk_fp8_f32 v72, v2, v4 op_sel:[0,0,1]
	v_cvt_pk_fp8_f32 v73, v0, v1 op_sel:[0,0,1]
	v_mul_f32_e32 v0, 0x44000000, v41
	v_mul_f32_e32 v1, 0x44000000, v53
	v_cvt_pk_fp8_f32 v74, v0, v1
	v_mul_f32_e32 v0, 0x44000000, v5
	v_mul_f32_e32 v1, 0x44000000, v61
	v_cvt_pk_fp8_f32 v75, v0, v1
	v_mul_f32_e32 v0, 0x44000000, v57
	v_mul_f32_e32 v1, 0x44000000, v65
	v_mul_f32_e32 v2, 0x44000000, v49
	v_cvt_pk_fp8_f32 v75, v0, v1 op_sel:[0,0,1]
	v_mul_f32_e32 v0, 0x44000000, v22
	v_mul_f32_e32 v1, 0x44000000, v30
	v_cvt_pk_fp8_f32 v76, v0, v1
	v_mul_f32_e32 v0, 0x44000000, v14
	v_mul_f32_e32 v1, 0x44000000, v38
	v_cvt_pk_fp8_f32 v77, v0, v1
	v_mul_f32_e32 v0, 0x44000000, v34
	v_mul_f32_e32 v1, 0x44000000, v46
	v_mul_f32_e32 v4, 0x44000000, v9
	v_cvt_pk_fp8_f32 v77, v0, v1 op_sel:[0,0,1]
	v_mul_f32_e32 v0, 0x44000000, v42
	v_mul_f32_e32 v1, 0x44000000, v54
	v_cvt_pk_fp8_f32 v78, v0, v1
	v_mul_f32_e32 v0, 0x44000000, v6
	v_mul_f32_e32 v1, 0x44000000, v62
	v_cvt_pk_fp8_f32 v79, v0, v1
	v_cvt_pk_fp8_f32 v74, v2, v4 op_sel:[0,0,1]
	v_mul_f32_e32 v2, 0x44000000, v26
	v_mul_f32_e32 v4, 0x44000000, v18
	v_cvt_pk_fp8_f32 v76, v2, v4 op_sel:[0,0,1]
	v_mul_f32_e32 v2, 0x44000000, v50
	v_mul_f32_e32 v4, 0x44000000, v10
	v_mul_f32_e32 v0, 0x44000000, v58
	v_mul_f32_e32 v1, 0x44000000, v66
	v_cvt_pk_fp8_f32 v78, v2, v4 op_sel:[0,0,1]
	v_cvt_pk_fp8_f32 v79, v0, v1 op_sel:[0,0,1]
	v_mul_f32_e32 v1, 0x44000000, v23
	v_mul_f32_e32 v2, 0x44000000, v31
	v_mov_b32_e32 v0, v3
	v_cvt_pk_fp8_f32 v0, v1, v2
	v_mul_f32_e32 v2, 0x44000000, v15
	v_mul_f32_e32 v6, 0x44000000, v39
	v_mov_b32_e32 v1, v3
	v_cvt_pk_fp8_f32 v1, v2, v6
	v_mul_f32_e32 v4, 0x44000000, v27
	v_mul_f32_e32 v5, 0x44000000, v19
	v_cvt_pk_fp8_f32 v0, v4, v5 op_sel:[0,0,1]
	v_mul_f32_e32 v2, 0x44000000, v35
	v_mul_f32_e32 v4, 0x44000000, v47
	v_cvt_pk_fp8_f32 v1, v2, v4 op_sel:[0,0,1]
	v_mul_f32_e32 v4, 0x44000000, v43
	v_mul_f32_e32 v5, 0x44000000, v55
	v_mov_b32_e32 v2, v3
	v_cvt_pk_fp8_f32 v2, v4, v5
	v_mul_f32_e32 v4, 0x44000000, v7
	v_mul_f32_e32 v5, 0x44000000, v63
	v_cvt_pk_fp8_f32 v3, v4, v5
	v_mul_f32_e32 v4, 0x44000000, v59
	v_mul_f32_e32 v5, 0x44000000, v67
	v_mul_f32_e32 v6, 0x44000000, v51
	v_cvt_pk_fp8_f32 v3, v4, v5 op_sel:[0,0,1]
	v_add_co_u32_e32 v4, vcc, s1, v80
	v_cvt_pk_fp8_f32 v2, v6, v8 op_sel:[0,0,1]
	s_nop 0
	v_addc_co_u32_e32 v5, vcc, 0, v81, vcc
	global_store_dwordx4 v[4:5], v[68:71], off sc1 nt
	global_store_dwordx4 v[82:83], v[72:75], off offset:2048 sc1 nt
	v_add_co_u32_e32 v4, vcc, 0x1901000, v80
	s_nop 1
	v_addc_co_u32_e32 v5, vcc, 0, v81, vcc
	global_store_dwordx4 v[4:5], v[76:79], off sc1 nt
	global_store_dwordx4 v[4:5], v[0:3], off offset:2048 sc1 nt
	s_waitcnt vmcnt(0)

.LBB0_912:
	v_lshlrev_b32_e32 v1, 1, v0
	v_and_b32_e32 v130, -16, v1
	v_lshlrev_b32_e32 v0, 2, v0
	v_and_b32_e32 v48, 28, v0
	v_mad_i64_i32 v[0:1], s[18:19], s16, v130, 0
	v_mov_b32_e32 v67, 0
	v_lshl_add_u64 v[0:1], v[0:1], 2, s[14:15]
	v_lshlrev_b32_e32 v66, 2, v48
	s_mov_b32 s3, 0
	v_lshl_add_u64 v[62:63], v[0:1], 0, v[66:67]
	s_mul_i32 s2, s16, 60
	v_lshl_add_u64 v[24:25], v[62:63], 0, s[2:3]
	s_lshl_b32 s2, s16, 2
	s_sub_u32 s2, 0, s2
	s_subb_u32 s3, 0, 0
	v_lshl_add_u64 v[0:1], v[24:25], 0, s[2:3]
	v_lshl_add_u64 v[8:9], v[0:1], 0, s[2:3]
	global_load_dwordx4 v[0:3], v[0:1], off sc1 nt
	s_nop 0
	global_load_dwordx4 v[4:7], v[8:9], off sc1 nt
	v_lshl_add_u64 v[8:9], v[8:9], 0, s[2:3]
	v_lshl_add_u64 v[16:17], v[8:9], 0, s[2:3]
	global_load_dwordx4 v[8:11], v[8:9], off sc1 nt
	s_nop 0
	global_load_dwordx4 v[12:15], v[16:17], off sc1 nt
	v_lshl_add_u64 v[16:17], v[16:17], 0, s[2:3]
	v_lshl_add_u64 v[26:27], v[16:17], 0, s[2:3]
	global_load_dwordx4 v[16:19], v[16:17], off sc1 nt
	s_nop 0
	global_load_dwordx4 v[20:23], v[26:27], off sc1 nt
	v_lshl_add_u64 v[26:27], v[26:27], 0, s[2:3]
	global_load_dwordx4 v[28:31], v[26:27], off sc1 nt
	v_lshl_add_u64 v[26:27], v[26:27], 0, s[2:3]
	global_load_dwordx4 v[32:35], v[26:27], off sc1 nt
	v_lshl_add_u64 v[26:27], v[26:27], 0, s[2:3]
	global_load_dwordx4 v[36:39], v[26:27], off sc1 nt
	v_lshl_add_u64 v[26:27], v[26:27], 0, s[2:3]
	global_load_dwordx4 v[40:43], v[26:27], off sc1 nt
	v_lshl_add_u64 v[26:27], v[26:27], 0, s[2:3]
	global_load_dwordx4 v[44:47], v[26:27], off sc1 nt
	v_lshl_add_u64 v[26:27], v[26:27], 0, s[2:3]
	global_load_dwordx4 v[50:53], v[26:27], off sc1 nt
	v_lshl_add_u64 v[26:27], v[26:27], 0, s[2:3]
	global_load_dwordx4 v[54:57], v[26:27], off sc1 nt
	v_lshl_add_u64 v[26:27], v[26:27], 0, s[2:3]
	global_load_dwordx4 v[58:61], v[26:27], off sc1 nt
	s_nop 0
	global_load_dwordx4 v[24:27], v[24:25], off sc1 nt
	s_nop 0
	global_load_dwordx4 v[62:65], v[62:63], off sc1 nt
	v_ashrrev_i32_e32 v131, 31, v130
	s_and_b64 vcc, exec, s[12:13]
	s_cbranch_vccz .LBB0_915
	s_cmp_lt_u32 s0, 0x18000
	s_cbranch_scc0 .LBB0_916
	s_addk_i32 s1, 0x7cff
	s_lshr_b32 s14, s1, 10
	s_mov_b32 s15, 0
	s_lshl_b64 s[2:3], s[14:15], 22
	s_lshl_b64 s[12:13], s[14:15], 24
	s_add_u32 s1, s70, s12
	s_addc_u32 s16, s71, s13
	s_add_u32 s2, s90, s2
	s_addc_u32 s3, s91, s3
	s_add_u32 s12, s2, 0x3b100000
	s_addc_u32 s13, s3, 0
	s_lshl_b32 s2, s0, 1
	s_and_b32 s14, s2, 0x780
	s_lshl_b32 s2, s14, 13
	s_add_u32 s1, s1, s2
	s_addc_u32 s2, s16, 0
	s_lshl_b32 s3, s0, 5
	s_and_b32 s18, s3, 0x7e0
	s_lshl_b32 s3, s18, 2
	s_add_u32 s16, s1, s3
	s_mov_b32 s19, s15
	s_addc_u32 s17, s2, 0
	s_mov_b64 s[20:21], 0
	s_branch .LBB0_917

.LBB0_921:
	s_lshl_b64 s[0:1], s[10:11], 11
	s_add_u32 s0, s4, s0
	s_addc_u32 s1, s5, s1
	s_add_u32 s8, s0, s8
	s_addc_u32 s9, s1, s9
	s_lshl_b64 s[2:3], s[18:19], 11
	s_add_u32 s0, s12, s2
	s_addc_u32 s2, s13, s3
	s_add_u32 s4, s0, s14
	v_mov_b32_e32 v49, 0
	s_addc_u32 s5, s2, s15
	v_mad_i64_i32 v[68:69], s[2:3], s20, v130, 0
	v_lshl_add_u64 v[68:69], v[68:69], 2, s[16:17]
	v_mov_b32_e32 v67, v49
	s_mov_b32 s1, 0
	v_lshl_add_u64 v[66:67], v[68:69], 0, v[66:67]
	s_lshl_b32 s0, s20, 2
	v_lshl_add_u64 v[68:69], v[66:67], 0, s[0:1]
	global_load_dwordx4 v[82:85], v[66:67], off sc1 nt
	global_load_dwordx4 v[86:89], v[68:69], off sc1 nt
	v_lshl_add_u64 v[66:67], v[68:69], 0, s[0:1]
	v_lshl_add_u64 v[68:69], v[66:67], 0, s[0:1]
	global_load_dwordx4 v[122:125], v[66:67], off sc1 nt
	global_load_dwordx4 v[126:129], v[68:69], off sc1 nt
	v_lshl_add_u64 v[66:67], v[68:69], 0, s[0:1]
	v_lshl_add_u64 v[68:69], v[66:67], 0, s[0:1]
	global_load_dwordx4 v[110:113], v[66:67], off sc1 nt
	global_load_dwordx4 v[114:117], v[68:69], off sc1 nt
	v_lshl_add_u64 v[66:67], v[68:69], 0, s[0:1]
	v_lshl_add_u64 v[68:69], v[66:67], 0, s[0:1]
	global_load_dwordx4 v[90:93], v[66:67], off sc1 nt
	global_load_dwordx4 v[94:97], v[68:69], off sc1 nt
	v_lshl_add_u64 v[66:67], v[68:69], 0, s[0:1]
	global_load_dwordx4 v[74:77], v[66:67], off sc1 nt
	v_lshl_add_u64 v[66:67], v[66:67], 0, s[0:1]
	global_load_dwordx4 v[98:101], v[66:67], off sc1 nt
	v_lshl_add_u64 v[66:67], v[66:67], 0, s[0:1]
	global_load_dwordx4 v[106:109], v[66:67], off sc1 nt
	v_lshl_add_u64 v[66:67], v[66:67], 0, s[0:1]
	global_load_dwordx4 v[118:121], v[66:67], off sc1 nt
	v_lshl_add_u64 v[66:67], v[66:67], 0, s[0:1]
	global_load_dwordx4 v[78:81], v[66:67], off sc1 nt
	v_lshl_add_u64 v[66:67], v[66:67], 0, s[0:1]
	global_load_dwordx4 v[102:105], v[66:67], off sc1 nt
	v_lshl_add_u64 v[70:71], v[66:67], 0, s[0:1]
	global_load_dwordx4 v[66:69], v[70:71], off sc1 nt
	v_lshl_add_u64 v[70:71], v[70:71], 0, s[0:1]
	global_load_dwordx4 v[70:73], v[70:71], off sc1 nt
	s_waitcnt vmcnt(29)
	v_mul_f32_e32 v8, 0x44000000, v8
	v_mul_f32_e32 v4, 0x44000000, v4
	v_mov_b32_e32 v135, v49
	v_cvt_pk_fp8_f32 v135, v8, v4
	v_mul_f32_e32 v0, 0x44000000, v0
	s_waitcnt vmcnt(17)
	v_mul_f32_e32 v4, 0x44000000, v24
	v_mov_b32_e32 v136, v49
	v_cvt_pk_fp8_f32 v135, v0, v4 op_sel:[0,0,1]
	s_waitcnt vmcnt(16)
	v_mul_f32_e32 v0, 0x44000000, v63
	v_mul_f32_e32 v4, 0x44000000, v59
	v_cvt_pk_fp8_f32 v136, v0, v4
	v_mul_f32_e32 v0, 0x44000000, v45
	v_mul_f32_e32 v4, 0x44000000, v41
	v_mov_b32_e32 v137, v49
	v_cvt_pk_fp8_f32 v137, v0, v4
	v_mul_f32_e32 v28, 0x44000000, v28
	v_mul_f32_e32 v20, 0x44000000, v20
	v_mov_b32_e32 v134, v49
	v_mul_f32_e32 v0, 0x44000000, v37
	v_mul_f32_e32 v4, 0x44000000, v33
	v_mul_f32_e32 v62, 0x44000000, v62
	v_mul_f32_e32 v58, 0x44000000, v58
	v_mov_b32_e32 v132, v49
	v_mul_f32_e32 v44, 0x44000000, v44
	v_mul_f32_e32 v40, 0x44000000, v40
	v_mov_b32_e32 v133, v49
	v_cvt_pk_fp8_f32 v134, v28, v20
	v_cvt_pk_fp8_f32 v137, v0, v4 op_sel:[0,0,1]
	v_mul_f32_e32 v0, 0x44000000, v29
	v_mul_f32_e32 v4, 0x44000000, v21
	v_mov_b32_e32 v138, v49
	v_cvt_pk_fp8_f32 v132, v62, v58
	v_cvt_pk_fp8_f32 v133, v44, v40
	v_cvt_pk_fp8_f32 v138, v0, v4
	v_mul_f32_e32 v0, 0x44000000, v9
	v_mul_f32_e32 v4, 0x44000000, v5
	v_mov_b32_e32 v139, v49
	v_cvt_pk_fp8_f32 v139, v0, v4
	v_mul_f32_e32 v16, 0x44000000, v16
	v_mul_f32_e32 v12, 0x44000000, v12
	v_mul_f32_e32 v54, 0x44000000, v54
	v_mul_f32_e32 v50, 0x44000000, v50
	v_mul_f32_e32 v36, 0x44000000, v36
	v_mul_f32_e32 v32, 0x44000000, v32
	v_cvt_pk_fp8_f32 v134, v16, v12 op_sel:[0,0,1]
	v_mul_f32_e32 v8, 0x44000000, v55
	v_mul_f32_e32 v12, 0x44000000, v51
	v_cvt_pk_fp8_f32 v132, v54, v50 op_sel:[0,0,1]
	v_cvt_pk_fp8_f32 v133, v36, v32 op_sel:[0,0,1]
	v_cvt_pk_fp8_f32 v136, v8, v12 op_sel:[0,0,1]
	v_mul_f32_e32 v8, 0x44000000, v17
	v_mul_f32_e32 v12, 0x44000000, v13
	v_mul_f32_e32 v0, 0x44000000, v1
	v_mul_f32_e32 v1, 0x44000000, v25
	v_lshlrev_b32_e32 v48, 11, v48
	v_cvt_pk_fp8_f32 v138, v8, v12 op_sel:[0,0,1]
	v_cvt_pk_fp8_f32 v139, v0, v1 op_sel:[0,0,1]
	v_lshl_add_u64 v[0:1], s[8:9], 0, v[48:49]
	v_lshl_add_u64 v[0:1], v[0:1], 0, v[130:131]
	global_store_dwordx4 v[0:1], v[132:135], off sc1
	global_store_dwordx4 v[0:1], v[136:139], off offset:2048 sc1
	v_mul_f32_e32 v4, 0x44000000, v64
	v_mul_f32_e32 v5, 0x44000000, v60
	v_mov_b32_e32 v132, v49
	v_cvt_pk_fp8_f32 v132, v4, v5
	v_mul_f32_e32 v4, 0x44000000, v46
	v_mul_f32_e32 v5, 0x44000000, v42
	v_mov_b32_e32 v133, v49
	v_cvt_pk_fp8_f32 v133, v4, v5
	v_mul_f32_e32 v4, 0x44000000, v38
	v_mul_f32_e32 v5, 0x44000000, v34
	v_mov_b32_e32 v134, v49
	v_cvt_pk_fp8_f32 v133, v4, v5 op_sel:[0,0,1]
	v_mul_f32_e32 v4, 0x44000000, v30
	v_mul_f32_e32 v5, 0x44000000, v22
	v_cvt_pk_fp8_f32 v134, v4, v5
	v_mul_f32_e32 v4, 0x44000000, v10
	v_mul_f32_e32 v5, 0x44000000, v6
	v_mov_b32_e32 v135, v49
	v_cvt_pk_fp8_f32 v135, v4, v5
	v_mul_f32_e32 v8, 0x44000000, v56
	v_mul_f32_e32 v9, 0x44000000, v52
	v_mul_f32_e32 v2, 0x44000000, v2
	v_mul_f32_e32 v4, 0x44000000, v26
	v_cvt_pk_fp8_f32 v132, v8, v9 op_sel:[0,0,1]
	v_mul_f32_e32 v8, 0x44000000, v18
	v_mul_f32_e32 v9, 0x44000000, v14
	v_cvt_pk_fp8_f32 v135, v2, v4 op_sel:[0,0,1]
	v_mul_f32_e32 v2, 0x44000000, v65
	v_mul_f32_e32 v5, 0x44000000, v61
	v_mov_b32_e32 v4, v49
	v_cvt_pk_fp8_f32 v134, v8, v9 op_sel:[0,0,1]
	v_cvt_pk_fp8_f32 v4, v2, v5
	v_mul_f32_e32 v2, 0x44000000, v47
	v_mul_f32_e32 v9, 0x44000000, v43
	v_mov_b32_e32 v5, v49
	v_cvt_pk_fp8_f32 v5, v2, v9
	v_mul_f32_e32 v6, 0x44000000, v57
	v_mul_f32_e32 v8, 0x44000000, v53
	v_cvt_pk_fp8_f32 v4, v6, v8 op_sel:[0,0,1]
	v_mul_f32_e32 v2, 0x44000000, v39
	v_mul_f32_e32 v6, 0x44000000, v35
	v_cvt_pk_fp8_f32 v5, v2, v6 op_sel:[0,0,1]
	v_mul_f32_e32 v2, 0x44000000, v31
	v_mul_f32_e32 v8, 0x44000000, v23
	v_mov_b32_e32 v6, v49
	v_cvt_pk_fp8_f32 v6, v2, v8
	v_mul_f32_e32 v2, 0x44000000, v11
	v_mul_f32_e32 v8, 0x44000000, v7
	v_mov_b32_e32 v7, v49
	v_cvt_pk_fp8_f32 v7, v2, v8
	v_mul_f32_e32 v9, 0x44000000, v19
	v_mul_f32_e32 v10, 0x44000000, v15
	v_mul_f32_e32 v2, 0x44000000, v3
	v_mul_f32_e32 v3, 0x44000000, v27
	s_movk_i32 s0, 0x1000
	v_cvt_pk_fp8_f32 v6, v9, v10 op_sel:[0,0,1]
	v_cvt_pk_fp8_f32 v7, v2, v3 op_sel:[0,0,1]
	v_add_co_u32_e32 v0, vcc, s0, v0
	s_waitcnt vmcnt(16)
	v_mul_f32_e32 v2, 0x44000000, v86
	v_addc_co_u32_e32 v1, vcc, 0, v1, vcc
	global_store_dwordx4 v[0:1], v[132:135], off sc1
	global_store_dwordx4 v[0:1], v[4:7], off offset:2048 sc1
	v_mul_f32_e32 v1, 0x44000000, v82
	v_mov_b32_e32 v0, v49
	v_cvt_pk_fp8_f32 v0, v1, v2
	s_waitcnt vmcnt(15)
	v_mul_f32_e32 v2, 0x44000000, v110
	s_waitcnt vmcnt(14)
	v_mul_f32_e32 v5, 0x44000000, v114
	v_mov_b32_e32 v1, v49
	v_cvt_pk_fp8_f32 v1, v2, v5
	v_mul_f32_e32 v3, 0x44000000, v122
	v_mul_f32_e32 v4, 0x44000000, v126
	v_cvt_pk_fp8_f32 v0, v3, v4 op_sel:[0,0,1]
	s_waitcnt vmcnt(13)
	v_mul_f32_e32 v2, 0x44000000, v90
	s_waitcnt vmcnt(12)
	v_mul_f32_e32 v3, 0x44000000, v94
	v_cvt_pk_fp8_f32 v1, v2, v3 op_sel:[0,0,1]
	s_waitcnt vmcnt(11)
	v_mul_f32_e32 v3, 0x44000000, v74
	s_waitcnt vmcnt(10)
	v_mul_f32_e32 v4, 0x44000000, v98
	v_mov_b32_e32 v2, v49
	v_cvt_pk_fp8_f32 v2, v3, v4
	s_waitcnt vmcnt(7)
	v_mul_f32_e32 v4, 0x44000000, v78
	s_waitcnt vmcnt(6)
	v_mul_f32_e32 v7, 0x44000000, v102
	v_mov_b32_e32 v3, v49
	v_cvt_pk_fp8_f32 v3, v4, v7
	v_mul_f32_e32 v5, 0x44000000, v106
	v_mul_f32_e32 v6, 0x44000000, v118
	v_cvt_pk_fp8_f32 v2, v5, v6 op_sel:[0,0,1]
	s_waitcnt vmcnt(5)
	v_mul_f32_e32 v4, 0x44000000, v66
	s_waitcnt vmcnt(4)
	v_mul_f32_e32 v5, 0x44000000, v70
	v_cvt_pk_fp8_f32 v3, v4, v5 op_sel:[0,0,1]
	v_mul_f32_e32 v5, 0x44000000, v83
	v_mul_f32_e32 v6, 0x44000000, v87
	v_mov_b32_e32 v4, v49
	v_cvt_pk_fp8_f32 v4, v5, v6
	v_mul_f32_e32 v6, 0x44000000, v111
	v_mul_f32_e32 v9, 0x44000000, v115
	v_mov_b32_e32 v5, v49
	v_cvt_pk_fp8_f32 v5, v6, v9
	v_mul_f32_e32 v7, 0x44000000, v123
	v_mul_f32_e32 v8, 0x44000000, v127
	v_cvt_pk_fp8_f32 v4, v7, v8 op_sel:[0,0,1]
	v_mul_f32_e32 v6, 0x44000000, v91
	v_mul_f32_e32 v7, 0x44000000, v95
	v_cvt_pk_fp8_f32 v5, v6, v7 op_sel:[0,0,1]
	v_mul_f32_e32 v7, 0x44000000, v75
	v_mul_f32_e32 v8, 0x44000000, v99
	v_mov_b32_e32 v6, v49
	v_cvt_pk_fp8_f32 v6, v7, v8
	v_mul_f32_e32 v8, 0x44000000, v79
	v_mul_f32_e32 v11, 0x44000000, v103
	v_mov_b32_e32 v7, v49
	v_cvt_pk_fp8_f32 v7, v8, v11
	v_mul_f32_e32 v9, 0x44000000, v107
	v_mul_f32_e32 v10, 0x44000000, v119
	v_cvt_pk_fp8_f32 v6, v9, v10 op_sel:[0,0,1]
	v_mul_f32_e32 v8, 0x44000000, v67
	v_mul_f32_e32 v9, 0x44000000, v71
	v_cvt_pk_fp8_f32 v7, v8, v9 op_sel:[0,0,1]
	v_lshl_add_u64 v[8:9], s[4:5], 0, v[48:49]
	v_lshl_add_u64 v[8:9], v[8:9], 0, v[130:131]
	global_store_dwordx4 v[8:9], v[0:3], off sc1
	global_store_dwordx4 v[8:9], v[4:7], off offset:2048 sc1
	v_mov_b32_e32 v46, v49
	v_mul_f32_e32 v1, 0x44000000, v84
	v_mul_f32_e32 v2, 0x44000000, v88
	v_mov_b32_e32 v0, v49
	v_cvt_pk_fp8_f32 v0, v1, v2
	v_mul_f32_e32 v2, 0x44000000, v112
	v_mul_f32_e32 v5, 0x44000000, v116
	v_mov_b32_e32 v1, v49
	v_cvt_pk_fp8_f32 v1, v2, v5
	v_mul_f32_e32 v3, 0x44000000, v124
	v_mul_f32_e32 v4, 0x44000000, v128
	v_cvt_pk_fp8_f32 v0, v3, v4 op_sel:[0,0,1]
	v_mul_f32_e32 v2, 0x44000000, v92
	v_mul_f32_e32 v3, 0x44000000, v96
	v_cvt_pk_fp8_f32 v1, v2, v3 op_sel:[0,0,1]
	v_mul_f32_e32 v3, 0x44000000, v76
	v_mul_f32_e32 v4, 0x44000000, v100
	v_mov_b32_e32 v2, v49
	v_cvt_pk_fp8_f32 v2, v3, v4
	v_mul_f32_e32 v4, 0x44000000, v80
	v_mul_f32_e32 v7, 0x44000000, v104
	v_mov_b32_e32 v3, v49
	v_cvt_pk_fp8_f32 v3, v4, v7
	v_mul_f32_e32 v5, 0x44000000, v108
	v_mul_f32_e32 v6, 0x44000000, v120
	v_cvt_pk_fp8_f32 v2, v5, v6 op_sel:[0,0,1]
	v_mul_f32_e32 v4, 0x44000000, v68
	v_mul_f32_e32 v5, 0x44000000, v72
	v_cvt_pk_fp8_f32 v3, v4, v5 op_sel:[0,0,1]
	v_mul_f32_e32 v4, 0x44000000, v85
	v_mul_f32_e32 v5, 0x44000000, v89
	v_cvt_pk_fp8_f32 v46, v4, v5
	v_mul_f32_e32 v4, 0x44000000, v113
	v_mul_f32_e32 v5, 0x44000000, v117
	v_mov_b32_e32 v47, v49
	v_cvt_pk_fp8_f32 v47, v4, v5
	v_mul_f32_e32 v4, 0x44000000, v93
	v_mul_f32_e32 v5, 0x44000000, v97
	v_mov_b32_e32 v48, v49
	v_cvt_pk_fp8_f32 v47, v4, v5 op_sel:[0,0,1]
	v_mul_f32_e32 v4, 0x44000000, v77
	v_mul_f32_e32 v5, 0x44000000, v101
	v_cvt_pk_fp8_f32 v48, v4, v5
	v_mul_f32_e32 v4, 0x44000000, v81
	v_mul_f32_e32 v5, 0x44000000, v105
	v_cvt_pk_fp8_f32 v49, v4, v5
	v_mul_f32_e32 v6, 0x44000000, v125
	v_mul_f32_e32 v7, 0x44000000, v129
	v_cvt_pk_fp8_f32 v46, v6, v7 op_sel:[0,0,1]
	v_mul_f32_e32 v6, 0x44000000, v109
	v_mul_f32_e32 v7, 0x44000000, v121
	v_mul_f32_e32 v4, 0x44000000, v69
	v_mul_f32_e32 v5, 0x44000000, v73
	v_cvt_pk_fp8_f32 v48, v6, v7 op_sel:[0,0,1]
	v_cvt_pk_fp8_f32 v49, v4, v5 op_sel:[0,0,1]
	v_add_co_u32_e32 v4, vcc, s0, v8
	s_nop 1
	v_addc_co_u32_e32 v5, vcc, 0, v9, vcc
	global_store_dwordx4 v[4:5], v[0:3], off sc1
	global_store_dwordx4 v[4:5], v[46:49], off offset:2048 sc1
	s_waitcnt vmcnt(0)

.LBB0_1004:
	s_not_b32 s2, s0
	s_add_i32 s1, s1, s2
	s_cmp_lt_i32 s1, -7
	s_cbranch_scc1 .LBB0_1023
	s_ashr_i32 s2, s1, 31
	v_lshlrev_b32_e32 v1, 1, v0
	s_lshr_b32 s2, s2, 29
	v_and_b32_e32 v128, -16, v1
	v_lshlrev_b32_e32 v0, 2, v0
	s_add_i32 s2, s1, s2
	v_and_b32_e32 v64, 28, v0
	s_ashr_i32 s1, s2, 3
	s_and_b32 s2, s2, -8
	v_mad_i64_i32 v[0:1], s[18:19], s16, v128, 0
	v_mov_b32_e32 v131, 0
	s_add_i32 s2, s2, s0
	v_lshl_add_u64 v[0:1], v[0:1], 2, s[14:15]
	v_lshlrev_b32_e32 v130, 2, v64
	s_lshl_b32 s3, s16, 2
	s_mov_b32 s5, 0
	s_waitcnt vmcnt(4)
	v_lshl_add_u64 v[60:61], v[0:1], 0, v[130:131]
	s_mul_i32 s4, s16, 60
	s_sub_u32 s14, 0, s3
	v_lshl_add_u64 v[44:45], v[60:61], 0, s[4:5]
	s_subb_u32 s15, 0, 0
	v_lshl_add_u64 v[0:1], v[44:45], 0, s[14:15]
	v_lshl_add_u64 v[8:9], v[0:1], 0, s[14:15]
	global_load_dwordx4 v[0:3], v[0:1], off sc1 nt
	s_nop 0
	global_load_dwordx4 v[4:7], v[8:9], off sc1 nt
	v_lshl_add_u64 v[8:9], v[8:9], 0, s[14:15]
	v_lshl_add_u64 v[16:17], v[8:9], 0, s[14:15]
	global_load_dwordx4 v[8:11], v[8:9], off sc1 nt
	s_nop 0
	global_load_dwordx4 v[12:15], v[16:17], off sc1 nt
	v_lshl_add_u64 v[16:17], v[16:17], 0, s[14:15]
	v_lshl_add_u64 v[24:25], v[16:17], 0, s[14:15]
	v_lshl_add_u64 v[28:29], v[24:25], 0, s[14:15]
	v_lshl_add_u64 v[32:33], v[28:29], 0, s[14:15]
	v_lshl_add_u64 v[36:37], v[32:33], 0, s[14:15]
	v_lshl_add_u64 v[40:41], v[36:37], 0, s[14:15]
	v_lshl_add_u64 v[46:47], v[40:41], 0, s[14:15]
	global_load_dwordx4 v[16:19], v[16:17], off sc1 nt
	s_nop 0
	global_load_dwordx4 v[20:23], v[24:25], off sc1 nt
	s_lshl_b64 s[12:13], s[12:13], 11
	global_load_dwordx4 v[24:27], v[28:29], off sc1 nt
	s_add_u32 s3, s8, s12
	global_load_dwordx4 v[28:31], v[32:33], off sc1 nt
	s_addc_u32 s4, s9, s13
	global_load_dwordx4 v[32:35], v[36:37], off sc1 nt
	s_add_u32 s10, s3, s10
	global_load_dwordx4 v[36:39], v[40:41], off sc1 nt
	s_addc_u32 s11, s4, s11
	global_load_dwordx4 v[40:43], v[46:47], off sc1 nt
	v_lshl_add_u64 v[46:47], v[46:47], 0, s[14:15]
	global_load_dwordx4 v[48:51], v[46:47], off sc1 nt
	v_lshl_add_u64 v[46:47], v[46:47], 0, s[14:15]
	global_load_dwordx4 v[56:59], v[46:47], off sc1 nt
	v_lshl_add_u64 v[46:47], v[46:47], 0, s[14:15]
	global_load_dwordx4 v[52:55], v[46:47], off sc1 nt
	s_nop 0
	global_load_dwordx4 v[44:47], v[44:45], off sc1 nt
	s_nop 0
	global_load_dwordx4 v[60:63], v[60:61], off sc1 nt
	s_add_u32 s3, s90, 0x3b100000
	s_addc_u32 s26, s91, 0
	s_add_u32 s8, s90, 0x1900000
	v_ashrrev_i32_e32 v129, 31, v128
	v_lshlrev_b32_e32 v132, 11, v64
	v_mov_b32_e32 v133, v131
	s_addc_u32 s9, s91, 0
	v_lshlrev_b32_e32 v130, 2, v64
	s_movk_i32 s27, 0x1000
	s_mov_b32 s28, 0
	s_branch .LBB0_1007
.LBB0_1006:
	s_lshl_b64 s[14:15], s[14:15], 11
	s_add_u32 s4, s12, s14
	s_addc_u32 s13, s13, s15
	s_add_u32 s12, s4, s16
	s_addc_u32 s13, s13, s17
	s_lshl_b64 s[14:15], s[20:21], 11
	s_add_u32 s4, s10, s14
	s_addc_u32 s11, s11, s15
	v_mad_i64_i32 v[0:1], s[14:15], s24, v128, 0
	s_add_u32 s10, s4, s22
	v_lshl_add_u64 v[0:1], v[0:1], 2, s[18:19]
	s_addc_u32 s11, s11, s23
	v_lshl_add_u64 v[0:1], v[0:1], 0, v[130:131]
	s_lshl_b32 s4, s24, 2
	v_lshl_add_u64 v[2:3], v[0:1], 0, s[4:5]
	global_load_dwordx4 v[60:63], v[0:1], off sc1 nt
	global_load_dwordx4 v[52:55], v[2:3], off sc1 nt
	v_lshl_add_u64 v[0:1], v[2:3], 0, s[4:5]
	v_lshl_add_u64 v[2:3], v[0:1], 0, s[4:5]
	global_load_dwordx4 v[56:59], v[0:1], off sc1 nt
	global_load_dwordx4 v[48:51], v[2:3], off sc1 nt
	v_lshl_add_u64 v[0:1], v[2:3], 0, s[4:5]
	v_lshl_add_u64 v[2:3], v[0:1], 0, s[4:5]
	global_load_dwordx4 v[40:43], v[0:1], off sc1 nt
	global_load_dwordx4 v[36:39], v[2:3], off sc1 nt
	v_lshl_add_u64 v[0:1], v[2:3], 0, s[4:5]
	v_lshl_add_u64 v[2:3], v[0:1], 0, s[4:5]
	global_load_dwordx4 v[32:35], v[0:1], off sc1 nt
	global_load_dwordx4 v[28:31], v[2:3], off sc1 nt
	v_lshl_add_u64 v[0:1], v[2:3], 0, s[4:5]
	global_load_dwordx4 v[24:27], v[0:1], off sc1 nt
	v_lshl_add_u64 v[0:1], v[0:1], 0, s[4:5]
	global_load_dwordx4 v[20:23], v[0:1], off sc1 nt
	v_lshl_add_u64 v[0:1], v[0:1], 0, s[4:5]
	global_load_dwordx4 v[16:19], v[0:1], off sc1 nt
	v_lshl_add_u64 v[0:1], v[0:1], 0, s[4:5]
	global_load_dwordx4 v[12:15], v[0:1], off sc1 nt
	v_lshl_add_u64 v[0:1], v[0:1], 0, s[4:5]
	global_load_dwordx4 v[8:11], v[0:1], off sc1 nt
	v_lshl_add_u64 v[0:1], v[0:1], 0, s[4:5]
	v_lshl_add_u64 v[44:45], v[0:1], 0, s[4:5]
	global_load_dwordx4 v[4:7], v[0:1], off sc1 nt
	s_waitcnt vmcnt(33)
	v_mul_f32_e32 v80, 0x44000000, v80
	global_load_dwordx4 v[0:3], v[44:45], off sc1 nt
	v_lshl_add_u64 v[44:45], v[44:45], 0, s[4:5]
	global_load_dwordx4 v[44:47], v[44:45], off sc1 nt
	s_waitcnt vmcnt(34)
	v_mul_f32_e32 v84, 0x44000000, v84
	v_mov_b32_e32 v134, v131
	v_cvt_pk_fp8_f32 v134, v80, v84
	s_waitcnt vmcnt(31)
	v_mul_f32_e32 v80, 0x44000000, v108
	s_waitcnt vmcnt(30)
	v_mul_f32_e32 v84, 0x44000000, v112
	v_mov_b32_e32 v135, v131
	v_cvt_pk_fp8_f32 v135, v80, v84
	s_waitcnt vmcnt(29)
	v_mul_f32_e32 v80, 0x44000000, v88
	s_waitcnt vmcnt(28)
	v_mul_f32_e32 v84, 0x44000000, v92
	s_waitcnt vmcnt(27)
	v_mul_f32_e32 v72, 0x44000000, v72
	v_cvt_pk_fp8_f32 v135, v80, v84 op_sel:[0,0,1]
	s_waitcnt vmcnt(26)
	v_mul_f32_e32 v80, 0x44000000, v96
	v_mov_b32_e32 v136, v131
	v_cvt_pk_fp8_f32 v136, v72, v80
	s_waitcnt vmcnt(23)
	v_mul_f32_e32 v72, 0x44000000, v76
	s_waitcnt vmcnt(22)
	v_mul_f32_e32 v76, 0x44000000, v100
	v_mov_b32_e32 v137, v131
	v_cvt_pk_fp8_f32 v137, v72, v76
	s_waitcnt vmcnt(21)
	v_mul_f32_e32 v64, 0x44000000, v64
	s_waitcnt vmcnt(20)
	v_mul_f32_e32 v68, 0x44000000, v68
	v_mov_b32_e32 v138, v131
	v_cvt_pk_fp8_f32 v137, v64, v68 op_sel:[0,0,1]
	v_mul_f32_e32 v64, 0x44000000, v81
	v_mul_f32_e32 v68, 0x44000000, v85
	v_cvt_pk_fp8_f32 v138, v64, v68
	v_mul_f32_e32 v64, 0x44000000, v109
	v_mul_f32_e32 v68, 0x44000000, v113
	v_mov_b32_e32 v139, v131
	v_cvt_pk_fp8_f32 v139, v64, v68
	v_mul_f32_e32 v64, 0x44000000, v89
	v_mul_f32_e32 v68, 0x44000000, v93
	v_mov_b32_e32 v140, v131
	v_cvt_pk_fp8_f32 v139, v64, v68 op_sel:[0,0,1]
	v_mul_f32_e32 v64, 0x44000000, v73
	v_mul_f32_e32 v68, 0x44000000, v97
	v_cvt_pk_fp8_f32 v140, v64, v68
	v_mul_f32_e32 v64, 0x44000000, v77
	v_mul_f32_e32 v68, 0x44000000, v101
	v_mov_b32_e32 v141, v131
	v_cvt_pk_fp8_f32 v141, v64, v68
	v_mul_f32_e32 v120, 0x44000000, v120
	v_mul_f32_e32 v124, 0x44000000, v124
	v_mul_f32_e32 v84, 0x44000000, v104
	v_mul_f32_e32 v88, 0x44000000, v116
	v_mul_f32_e32 v72, 0x44000000, v121
	v_mul_f32_e32 v76, 0x44000000, v125
	v_cvt_pk_fp8_f32 v134, v120, v124 op_sel:[0,0,1]
	v_cvt_pk_fp8_f32 v136, v84, v88 op_sel:[0,0,1]
	v_cvt_pk_fp8_f32 v138, v72, v76 op_sel:[0,0,1]
	v_mul_f32_e32 v72, 0x44000000, v105
	v_mul_f32_e32 v73, 0x44000000, v117
	v_mul_f32_e32 v64, 0x44000000, v65
	v_mul_f32_e32 v65, 0x44000000, v69
	v_cvt_pk_fp8_f32 v140, v72, v73 op_sel:[0,0,1]
	v_cvt_pk_fp8_f32 v141, v64, v65 op_sel:[0,0,1]
	v_lshl_add_u64 v[64:65], s[12:13], 0, v[132:133]
	v_lshl_add_u64 v[64:65], v[64:65], 0, v[128:129]
	global_store_dwordx4 v[64:65], v[134:137], off sc1
	global_store_dwordx4 v[64:65], v[138:141], off offset:2048 sc1
	v_mul_f32_e32 v68, 0x44000000, v82
	v_mul_f32_e32 v69, 0x44000000, v86
	v_mov_b32_e32 v134, v131
	v_cvt_pk_fp8_f32 v134, v68, v69
	v_mul_f32_e32 v68, 0x44000000, v110
	v_mul_f32_e32 v69, 0x44000000, v114
	v_mov_b32_e32 v135, v131
	v_cvt_pk_fp8_f32 v135, v68, v69
	v_mul_f32_e32 v68, 0x44000000, v90
	v_mul_f32_e32 v69, 0x44000000, v94
	v_mov_b32_e32 v136, v131
	v_cvt_pk_fp8_f32 v135, v68, v69 op_sel:[0,0,1]
	v_mul_f32_e32 v68, 0x44000000, v74
	v_mul_f32_e32 v69, 0x44000000, v98
	v_cvt_pk_fp8_f32 v136, v68, v69
	v_mul_f32_e32 v68, 0x44000000, v78
	v_mul_f32_e32 v69, 0x44000000, v102
	v_mov_b32_e32 v137, v131
	v_cvt_pk_fp8_f32 v137, v68, v69
	v_mul_f32_e32 v72, 0x44000000, v122
	v_mul_f32_e32 v73, 0x44000000, v126
	v_cvt_pk_fp8_f32 v134, v72, v73 op_sel:[0,0,1]
	v_mul_f32_e32 v72, 0x44000000, v106
	v_mul_f32_e32 v73, 0x44000000, v118
	v_mul_f32_e32 v66, 0x44000000, v66
	v_mul_f32_e32 v68, 0x44000000, v70
	v_cvt_pk_fp8_f32 v136, v72, v73 op_sel:[0,0,1]
	v_cvt_pk_fp8_f32 v137, v66, v68 op_sel:[0,0,1]
	v_mul_f32_e32 v66, 0x44000000, v83
	v_mul_f32_e32 v68, 0x44000000, v87
	v_mov_b32_e32 v72, v131
	v_cvt_pk_fp8_f32 v72, v66, v68
	v_mul_f32_e32 v66, 0x44000000, v111
	v_mul_f32_e32 v68, 0x44000000, v115
	v_mov_b32_e32 v73, v131
	v_cvt_pk_fp8_f32 v73, v66, v68
	v_mul_f32_e32 v66, 0x44000000, v91
	v_mul_f32_e32 v68, 0x44000000, v95
	v_mov_b32_e32 v74, v131
	v_cvt_pk_fp8_f32 v73, v66, v68 op_sel:[0,0,1]
	v_mul_f32_e32 v66, 0x44000000, v75
	v_mul_f32_e32 v68, 0x44000000, v99
	v_cvt_pk_fp8_f32 v74, v66, v68
	v_mul_f32_e32 v66, 0x44000000, v79
	v_mul_f32_e32 v68, 0x44000000, v103
	v_mov_b32_e32 v75, v131
	v_cvt_pk_fp8_f32 v75, v66, v68
	v_mul_f32_e32 v69, 0x44000000, v123
	v_mul_f32_e32 v70, 0x44000000, v127
	v_cvt_pk_fp8_f32 v72, v69, v70 op_sel:[0,0,1]
	v_mul_f32_e32 v69, 0x44000000, v107
	v_mul_f32_e32 v70, 0x44000000, v119
	v_mul_f32_e32 v66, 0x44000000, v67
	v_mul_f32_e32 v67, 0x44000000, v71
	v_cvt_pk_fp8_f32 v74, v69, v70 op_sel:[0,0,1]
	v_cvt_pk_fp8_f32 v75, v66, v67 op_sel:[0,0,1]
	v_add_co_u32_e32 v64, vcc, s27, v64
	s_add_i32 s28, s28, 2
	s_nop 0
	v_addc_co_u32_e32 v65, vcc, 0, v65, vcc
	s_cmp_le_i32 s28, s1
	global_store_dwordx4 v[64:65], v[134:137], off sc1
	global_store_dwordx4 v[64:65], v[72:75], off offset:2048 sc1
	s_cbranch_scc0 .LBB0_1023

.LBB0_1015:
	v_mad_i64_i32 v[64:65], s[22:23], s20, v128, 0
	v_lshl_add_u64 v[64:65], v[64:65], 2, s[18:19]
	v_lshl_add_u64 v[64:65], v[64:65], 0, v[130:131]
	s_lshl_b32 s4, s20, 2
	v_lshl_add_u64 v[66:67], v[64:65], 0, s[4:5]
	global_load_dwordx4 v[80:83], v[64:65], off sc1 nt
	global_load_dwordx4 v[84:87], v[66:67], off sc1 nt
	v_lshl_add_u64 v[64:65], v[66:67], 0, s[4:5]
	v_lshl_add_u64 v[66:67], v[64:65], 0, s[4:5]
	global_load_dwordx4 v[120:123], v[64:65], off sc1 nt
	global_load_dwordx4 v[124:127], v[66:67], off sc1 nt
	v_lshl_add_u64 v[64:65], v[66:67], 0, s[4:5]
	v_lshl_add_u64 v[66:67], v[64:65], 0, s[4:5]
	global_load_dwordx4 v[108:111], v[64:65], off sc1 nt
	global_load_dwordx4 v[112:115], v[66:67], off sc1 nt
	v_lshl_add_u64 v[64:65], v[66:67], 0, s[4:5]
	v_lshl_add_u64 v[66:67], v[64:65], 0, s[4:5]
	global_load_dwordx4 v[88:91], v[64:65], off sc1 nt
	global_load_dwordx4 v[92:95], v[66:67], off sc1 nt
	v_lshl_add_u64 v[64:65], v[66:67], 0, s[4:5]
	global_load_dwordx4 v[72:75], v[64:65], off sc1 nt
	v_lshl_add_u64 v[64:65], v[64:65], 0, s[4:5]
	global_load_dwordx4 v[96:99], v[64:65], off sc1 nt
	v_lshl_add_u64 v[64:65], v[64:65], 0, s[4:5]
	global_load_dwordx4 v[104:107], v[64:65], off sc1 nt
	v_lshl_add_u64 v[64:65], v[64:65], 0, s[4:5]
	global_load_dwordx4 v[116:119], v[64:65], off sc1 nt
	v_lshl_add_u64 v[64:65], v[64:65], 0, s[4:5]
	global_load_dwordx4 v[76:79], v[64:65], off sc1 nt
	v_lshl_add_u64 v[64:65], v[64:65], 0, s[4:5]
	v_lshl_add_u64 v[68:69], v[64:65], 0, s[4:5]
	global_load_dwordx4 v[100:103], v[64:65], off sc1 nt
	s_waitcnt vmcnt(21)
	v_mul_f32_e32 v8, 0x44000000, v8
	global_load_dwordx4 v[64:67], v[68:69], off sc1 nt
	v_lshl_add_u64 v[68:69], v[68:69], 0, s[4:5]
	global_load_dwordx4 v[68:71], v[68:69], off sc1 nt
	s_waitcnt vmcnt(22)
	v_mul_f32_e32 v4, 0x44000000, v4
	v_mov_b32_e32 v137, v131
	v_cvt_pk_fp8_f32 v137, v8, v4
	s_waitcnt vmcnt(21)
	v_mul_f32_e32 v0, 0x44000000, v0
	s_waitcnt vmcnt(17)
	v_mul_f32_e32 v4, 0x44000000, v44
	v_mov_b32_e32 v138, v131
	v_cvt_pk_fp8_f32 v137, v0, v4 op_sel:[0,0,1]
	s_waitcnt vmcnt(16)
	v_mul_f32_e32 v0, 0x44000000, v61
	v_mul_f32_e32 v4, 0x44000000, v53
	v_cvt_pk_fp8_f32 v138, v0, v4
	v_mul_f32_e32 v0, 0x44000000, v41
	v_mul_f32_e32 v4, 0x44000000, v37
	v_mov_b32_e32 v139, v131
	v_cvt_pk_fp8_f32 v139, v0, v4
	v_mul_f32_e32 v24, 0x44000000, v24
	v_mul_f32_e32 v20, 0x44000000, v20
	v_mov_b32_e32 v136, v131
	v_mul_f32_e32 v0, 0x44000000, v33
	v_mul_f32_e32 v4, 0x44000000, v29
	v_mul_f32_e32 v60, 0x44000000, v60
	v_mul_f32_e32 v52, 0x44000000, v52
	v_mov_b32_e32 v134, v131
	v_mul_f32_e32 v40, 0x44000000, v40
	v_mul_f32_e32 v36, 0x44000000, v36
	v_mov_b32_e32 v135, v131
	v_cvt_pk_fp8_f32 v136, v24, v20
	v_cvt_pk_fp8_f32 v139, v0, v4 op_sel:[0,0,1]
	v_mul_f32_e32 v0, 0x44000000, v25
	v_mul_f32_e32 v4, 0x44000000, v21
	v_mov_b32_e32 v140, v131
	v_cvt_pk_fp8_f32 v134, v60, v52
	v_cvt_pk_fp8_f32 v135, v40, v36
	v_cvt_pk_fp8_f32 v140, v0, v4
	v_mul_f32_e32 v0, 0x44000000, v9
	v_mul_f32_e32 v4, 0x44000000, v5
	v_mov_b32_e32 v141, v131
	v_cvt_pk_fp8_f32 v141, v0, v4
	v_mul_f32_e32 v16, 0x44000000, v16
	v_mul_f32_e32 v12, 0x44000000, v12
	v_mul_f32_e32 v56, 0x44000000, v56
	v_mul_f32_e32 v48, 0x44000000, v48
	v_mul_f32_e32 v32, 0x44000000, v32
	v_mul_f32_e32 v28, 0x44000000, v28
	v_cvt_pk_fp8_f32 v136, v16, v12 op_sel:[0,0,1]
	v_mul_f32_e32 v8, 0x44000000, v57
	v_mul_f32_e32 v12, 0x44000000, v49
	v_cvt_pk_fp8_f32 v134, v56, v48 op_sel:[0,0,1]
	v_cvt_pk_fp8_f32 v135, v32, v28 op_sel:[0,0,1]
	v_cvt_pk_fp8_f32 v138, v8, v12 op_sel:[0,0,1]
	v_mul_f32_e32 v8, 0x44000000, v17
	v_mul_f32_e32 v12, 0x44000000, v13
	v_mul_f32_e32 v0, 0x44000000, v1
	v_mul_f32_e32 v1, 0x44000000, v45
	v_cvt_pk_fp8_f32 v140, v8, v12 op_sel:[0,0,1]
	v_cvt_pk_fp8_f32 v141, v0, v1 op_sel:[0,0,1]
	v_lshl_add_u64 v[0:1], s[10:11], 0, v[132:133]
	v_lshl_add_u64 v[0:1], v[0:1], 0, v[128:129]
	global_store_dwordx4 v[0:1], v[134:137], off sc1
	global_store_dwordx4 v[0:1], v[138:141], off offset:2048 sc1
	v_mul_f32_e32 v4, 0x44000000, v62
	v_mul_f32_e32 v5, 0x44000000, v54
	v_mov_b32_e32 v134, v131
	v_cvt_pk_fp8_f32 v134, v4, v5
	v_mul_f32_e32 v4, 0x44000000, v42
	v_mul_f32_e32 v5, 0x44000000, v38
	v_mov_b32_e32 v135, v131
	v_cvt_pk_fp8_f32 v135, v4, v5
	v_mul_f32_e32 v4, 0x44000000, v34
	v_mul_f32_e32 v5, 0x44000000, v30
	v_mov_b32_e32 v136, v131
	v_cvt_pk_fp8_f32 v135, v4, v5 op_sel:[0,0,1]
	v_mul_f32_e32 v4, 0x44000000, v26
	v_mul_f32_e32 v5, 0x44000000, v22
	v_cvt_pk_fp8_f32 v136, v4, v5
	v_mul_f32_e32 v4, 0x44000000, v10
	v_mul_f32_e32 v5, 0x44000000, v6
	v_mov_b32_e32 v137, v131
	v_cvt_pk_fp8_f32 v137, v4, v5
	v_mul_f32_e32 v8, 0x44000000, v58
	v_mul_f32_e32 v9, 0x44000000, v50
	v_mul_f32_e32 v2, 0x44000000, v2
	v_mul_f32_e32 v4, 0x44000000, v46
	v_cvt_pk_fp8_f32 v134, v8, v9 op_sel:[0,0,1]
	v_mul_f32_e32 v8, 0x44000000, v18
	v_mul_f32_e32 v9, 0x44000000, v14
	v_cvt_pk_fp8_f32 v137, v2, v4 op_sel:[0,0,1]
	v_mul_f32_e32 v2, 0x44000000, v63
	v_mul_f32_e32 v5, 0x44000000, v55
	v_mov_b32_e32 v4, v131
	v_cvt_pk_fp8_f32 v136, v8, v9 op_sel:[0,0,1]
	v_cvt_pk_fp8_f32 v4, v2, v5
	v_mul_f32_e32 v2, 0x44000000, v43
	v_mul_f32_e32 v9, 0x44000000, v39
	v_mov_b32_e32 v5, v131
	v_cvt_pk_fp8_f32 v5, v2, v9
	v_mul_f32_e32 v6, 0x44000000, v59
	v_mul_f32_e32 v8, 0x44000000, v51
	v_cvt_pk_fp8_f32 v4, v6, v8 op_sel:[0,0,1]
	v_mul_f32_e32 v2, 0x44000000, v35
	v_mul_f32_e32 v6, 0x44000000, v31
	v_cvt_pk_fp8_f32 v5, v2, v6 op_sel:[0,0,1]
	v_mul_f32_e32 v2, 0x44000000, v27
	v_mul_f32_e32 v8, 0x44000000, v23
	v_mov_b32_e32 v6, v131
	v_cvt_pk_fp8_f32 v6, v2, v8
	v_mul_f32_e32 v2, 0x44000000, v11
	v_mul_f32_e32 v8, 0x44000000, v7
	v_mov_b32_e32 v7, v131
	v_cvt_pk_fp8_f32 v7, v2, v8
	v_mul_f32_e32 v9, 0x44000000, v19
	v_mul_f32_e32 v10, 0x44000000, v15
	v_mul_f32_e32 v2, 0x44000000, v3
	v_mul_f32_e32 v3, 0x44000000, v47
	s_add_i32 s0, s0, 16
	v_cvt_pk_fp8_f32 v6, v9, v10 op_sel:[0,0,1]
	v_cvt_pk_fp8_f32 v7, v2, v3 op_sel:[0,0,1]
	s_min_i32 s0, s0, s2
	v_add_co_u32_e32 v0, vcc, s27, v0
	s_cmp_gt_i32 s0, 0xffff
	s_nop 0
	v_addc_co_u32_e32 v1, vcc, 0, v1, vcc
	s_mov_b64 s[24:25], -1
	global_store_dwordx4 v[0:1], v[134:137], off sc1
	global_store_dwordx4 v[0:1], v[4:7], off offset:2048 sc1
	s_cbranch_scc0 .LBB0_1021
	s_cmp_lt_u32 s0, 0x18000
	s_cbranch_scc0 .LBB0_1018
	s_add_i32 s4, s0, 0xffff0000
	s_lshr_b32 s4, s4, 10
	s_lshl_b64 s[10:11], s[4:5], 22
	s_lshl_b64 s[18:19], s[4:5], 24
	s_add_u32 s18, s70, s18
	s_addc_u32 s19, s71, s19
	s_add_u32 s10, s3, s10
	s_addc_u32 s11, s26, s11
	s_lshl_b32 s4, s0, 1
	s_and_b32 s4, s4, 0x780
	s_lshl_b32 s20, s4, 13
	s_add_u32 s18, s18, s20
	s_addc_u32 s19, s19, 0
	s_lshl_b32 s20, s0, 5
	s_and_b32 s20, s20, 0x7e0
	s_lshl_b32 s22, s20, 2
	s_add_u32 s18, s18, s22
	s_mov_b32 s21, s5
	s_addc_u32 s19, s19, 0
	s_mov_b64 s[24:25], 0
	s_mov_b64 s[22:23], s[4:5]

.LBB0_1064:
	s_not_b32 s12, s34
	s_add_i32 s12, s26, s12
	s_add_i32 s12, s12, 0x14010
	s_cmp_lt_i32 s12, -7
	s_cbranch_scc1 .LBB0_1050
	v_lshlrev_b32_e32 v1, 1, v0
	v_and_b32_e32 v130, -16, v1
	v_lshlrev_b32_e32 v0, 2, v0
	s_ashr_i32 s25, s12, 31
	v_and_b32_e32 v64, 28, v0
	s_lshr_b32 s25, s25, 29
	v_mad_i64_i32 v[0:1], s[26:27], s24, v130, 0
	s_add_i32 s12, s12, s25
	v_lshl_add_u64 v[0:1], v[0:1], 2, s[22:23]
	v_lshlrev_b32_e32 v128, 2, v64
	s_ashr_i32 s35, s12, 3
	s_and_b32 s36, s12, -8
	s_waitcnt vmcnt(4)
	v_lshl_add_u64 v[60:61], v[0:1], 0, v[128:129]
	s_mul_i32 s12, s24, 60
	s_add_i32 s36, s36, s34
	v_lshl_add_u64 v[44:45], v[60:61], 0, s[12:13]
	s_lshl_b32 s12, s24, 2
	s_sub_u32 s22, 0, s12
	s_subb_u32 s23, 0, 0
	v_lshl_add_u64 v[0:1], v[44:45], 0, s[22:23]
	v_lshl_add_u64 v[8:9], v[0:1], 0, s[22:23]
	global_load_dwordx4 v[0:3], v[0:1], off sc1 nt
	s_nop 0
	global_load_dwordx4 v[4:7], v[8:9], off sc1 nt
	v_lshl_add_u64 v[8:9], v[8:9], 0, s[22:23]
	v_lshl_add_u64 v[16:17], v[8:9], 0, s[22:23]
	global_load_dwordx4 v[8:11], v[8:9], off sc1 nt
	s_nop 0
	global_load_dwordx4 v[12:15], v[16:17], off sc1 nt
	v_lshl_add_u64 v[16:17], v[16:17], 0, s[22:23]
	v_lshl_add_u64 v[24:25], v[16:17], 0, s[22:23]
	v_lshl_add_u64 v[28:29], v[24:25], 0, s[22:23]
	v_lshl_add_u64 v[32:33], v[28:29], 0, s[22:23]
	v_lshl_add_u64 v[36:37], v[32:33], 0, s[22:23]
	v_lshl_add_u64 v[40:41], v[36:37], 0, s[22:23]
	v_lshl_add_u64 v[46:47], v[40:41], 0, s[22:23]
	global_load_dwordx4 v[16:19], v[16:17], off sc1 nt
	s_nop 0
	global_load_dwordx4 v[20:23], v[24:25], off sc1 nt
	s_lshl_b64 s[20:21], s[20:21], 11
	global_load_dwordx4 v[24:27], v[28:29], off sc1 nt
	s_add_u32 s12, s16, s20
	global_load_dwordx4 v[28:31], v[32:33], off sc1 nt
	s_addc_u32 s17, s17, s21
	global_load_dwordx4 v[32:35], v[36:37], off sc1 nt
	s_add_u32 s16, s12, s18
	global_load_dwordx4 v[36:39], v[40:41], off sc1 nt
	v_ashrrev_i32_e32 v131, 31, v130
	global_load_dwordx4 v[40:43], v[46:47], off sc1 nt
	v_lshl_add_u64 v[46:47], v[46:47], 0, s[22:23]
	global_load_dwordx4 v[48:51], v[46:47], off sc1 nt
	v_lshl_add_u64 v[46:47], v[46:47], 0, s[22:23]
	global_load_dwordx4 v[56:59], v[46:47], off sc1 nt
	v_lshl_add_u64 v[46:47], v[46:47], 0, s[22:23]
	global_load_dwordx4 v[52:55], v[46:47], off sc1 nt
	s_nop 0
	global_load_dwordx4 v[44:47], v[44:45], off sc1 nt
	s_nop 0
	global_load_dwordx4 v[60:63], v[60:61], off sc1 nt
	s_addc_u32 s17, s17, s19
	v_lshlrev_b32_e32 v132, 11, v64
	v_mov_b32_e32 v133, v129
	s_mov_b32 s37, 0
	v_lshlrev_b32_e32 v128, 2, v64
	s_branch .LBB0_1067
.LBB0_1066:
	s_lshl_b64 s[20:21], s[20:21], 11
	s_add_u32 s12, s18, s20
	s_addc_u32 s19, s19, s21
	s_add_u32 s18, s12, s22
	s_addc_u32 s19, s19, s23
	s_lshl_b64 s[20:21], s[26:27], 11
	s_add_u32 s12, s16, s20
	s_addc_u32 s17, s17, s21
	v_mad_i64_i32 v[0:1], s[20:21], s30, v130, 0
	s_add_u32 s16, s12, s28
	v_lshl_add_u64 v[0:1], v[0:1], 2, s[24:25]
	s_addc_u32 s17, s17, s29
	v_lshl_add_u64 v[0:1], v[0:1], 0, v[128:129]
	s_lshl_b32 s12, s30, 2
	v_lshl_add_u64 v[2:3], v[0:1], 0, s[12:13]
	global_load_dwordx4 v[60:63], v[0:1], off sc1 nt
	global_load_dwordx4 v[52:55], v[2:3], off sc1 nt
	v_lshl_add_u64 v[0:1], v[2:3], 0, s[12:13]
	v_lshl_add_u64 v[2:3], v[0:1], 0, s[12:13]
	global_load_dwordx4 v[56:59], v[0:1], off sc1 nt
	global_load_dwordx4 v[48:51], v[2:3], off sc1 nt
	v_lshl_add_u64 v[0:1], v[2:3], 0, s[12:13]
	v_lshl_add_u64 v[2:3], v[0:1], 0, s[12:13]
	global_load_dwordx4 v[40:43], v[0:1], off sc1 nt
	global_load_dwordx4 v[36:39], v[2:3], off sc1 nt
	v_lshl_add_u64 v[0:1], v[2:3], 0, s[12:13]
	v_lshl_add_u64 v[2:3], v[0:1], 0, s[12:13]
	global_load_dwordx4 v[32:35], v[0:1], off sc1 nt
	global_load_dwordx4 v[28:31], v[2:3], off sc1 nt
	v_lshl_add_u64 v[0:1], v[2:3], 0, s[12:13]
	global_load_dwordx4 v[24:27], v[0:1], off sc1 nt
	v_lshl_add_u64 v[0:1], v[0:1], 0, s[12:13]
	global_load_dwordx4 v[20:23], v[0:1], off sc1 nt
	v_lshl_add_u64 v[0:1], v[0:1], 0, s[12:13]
	global_load_dwordx4 v[16:19], v[0:1], off sc1 nt
	v_lshl_add_u64 v[0:1], v[0:1], 0, s[12:13]
	global_load_dwordx4 v[12:15], v[0:1], off sc1 nt
	v_lshl_add_u64 v[0:1], v[0:1], 0, s[12:13]
	global_load_dwordx4 v[8:11], v[0:1], off sc1 nt
	v_lshl_add_u64 v[0:1], v[0:1], 0, s[12:13]
	v_lshl_add_u64 v[44:45], v[0:1], 0, s[12:13]
	global_load_dwordx4 v[4:7], v[0:1], off sc1 nt
	s_waitcnt vmcnt(33)
	v_mul_f32_e32 v80, 0x44000000, v80
	global_load_dwordx4 v[0:3], v[44:45], off sc1 nt
	v_lshl_add_u64 v[44:45], v[44:45], 0, s[12:13]
	global_load_dwordx4 v[44:47], v[44:45], off sc1 nt
	s_waitcnt vmcnt(34)
	v_mul_f32_e32 v84, 0x44000000, v84
	v_mov_b32_e32 v136, v129
	v_cvt_pk_fp8_f32 v136, v80, v84
	s_waitcnt vmcnt(31)
	v_mul_f32_e32 v80, 0x44000000, v108
	s_waitcnt vmcnt(30)
	v_mul_f32_e32 v84, 0x44000000, v112
	v_mov_b32_e32 v137, v129
	v_cvt_pk_fp8_f32 v137, v80, v84
	s_waitcnt vmcnt(29)
	v_mul_f32_e32 v80, 0x44000000, v88
	s_waitcnt vmcnt(28)
	v_mul_f32_e32 v84, 0x44000000, v92
	s_waitcnt vmcnt(27)
	v_mul_f32_e32 v72, 0x44000000, v72
	v_cvt_pk_fp8_f32 v137, v80, v84 op_sel:[0,0,1]
	s_waitcnt vmcnt(26)
	v_mul_f32_e32 v80, 0x44000000, v96
	v_mov_b32_e32 v138, v129
	v_cvt_pk_fp8_f32 v138, v72, v80
	s_waitcnt vmcnt(23)
	v_mul_f32_e32 v72, 0x44000000, v76
	s_waitcnt vmcnt(22)
	v_mul_f32_e32 v76, 0x44000000, v100
	v_mov_b32_e32 v139, v129
	v_cvt_pk_fp8_f32 v139, v72, v76
	s_waitcnt vmcnt(21)
	v_mul_f32_e32 v64, 0x44000000, v64
	s_waitcnt vmcnt(20)
	v_mul_f32_e32 v68, 0x44000000, v68
	v_mov_b32_e32 v140, v129
	v_cvt_pk_fp8_f32 v139, v64, v68 op_sel:[0,0,1]
	v_mul_f32_e32 v64, 0x44000000, v81
	v_mul_f32_e32 v68, 0x44000000, v85
	v_cvt_pk_fp8_f32 v140, v64, v68
	v_mul_f32_e32 v64, 0x44000000, v109
	v_mul_f32_e32 v68, 0x44000000, v113
	v_mov_b32_e32 v141, v129
	v_cvt_pk_fp8_f32 v141, v64, v68
	v_mul_f32_e32 v64, 0x44000000, v89
	v_mul_f32_e32 v68, 0x44000000, v93
	v_mov_b32_e32 v142, v129
	v_cvt_pk_fp8_f32 v141, v64, v68 op_sel:[0,0,1]
	v_mul_f32_e32 v64, 0x44000000, v73
	v_mul_f32_e32 v68, 0x44000000, v97
	v_cvt_pk_fp8_f32 v142, v64, v68
	v_mul_f32_e32 v64, 0x44000000, v77
	v_mul_f32_e32 v68, 0x44000000, v101
	v_mov_b32_e32 v143, v129
	v_cvt_pk_fp8_f32 v143, v64, v68
	v_mul_f32_e32 v120, 0x44000000, v120
	v_mul_f32_e32 v124, 0x44000000, v124
	v_mul_f32_e32 v84, 0x44000000, v104
	v_mul_f32_e32 v88, 0x44000000, v116
	v_mul_f32_e32 v72, 0x44000000, v121
	v_mul_f32_e32 v76, 0x44000000, v125
	v_cvt_pk_fp8_f32 v136, v120, v124 op_sel:[0,0,1]
	v_cvt_pk_fp8_f32 v138, v84, v88 op_sel:[0,0,1]
	v_cvt_pk_fp8_f32 v140, v72, v76 op_sel:[0,0,1]
	v_mul_f32_e32 v72, 0x44000000, v105
	v_mul_f32_e32 v73, 0x44000000, v117
	v_mul_f32_e32 v64, 0x44000000, v65
	v_mul_f32_e32 v65, 0x44000000, v69
	v_cvt_pk_fp8_f32 v142, v72, v73 op_sel:[0,0,1]
	v_cvt_pk_fp8_f32 v143, v64, v65 op_sel:[0,0,1]
	v_lshl_add_u64 v[64:65], s[18:19], 0, v[132:133]
	v_lshl_add_u64 v[64:65], v[64:65], 0, v[130:131]
	global_store_dwordx4 v[64:65], v[136:139], off sc1
	global_store_dwordx4 v[64:65], v[140:143], off offset:2048 sc1
	v_mul_f32_e32 v68, 0x44000000, v82
	v_mul_f32_e32 v69, 0x44000000, v86
	v_mov_b32_e32 v136, v129
	v_cvt_pk_fp8_f32 v136, v68, v69
	v_mul_f32_e32 v68, 0x44000000, v110
	v_mul_f32_e32 v69, 0x44000000, v114
	v_mov_b32_e32 v137, v129
	v_cvt_pk_fp8_f32 v137, v68, v69
	v_mul_f32_e32 v68, 0x44000000, v90
	v_mul_f32_e32 v69, 0x44000000, v94
	v_mov_b32_e32 v138, v129
	v_cvt_pk_fp8_f32 v137, v68, v69 op_sel:[0,0,1]
	v_mul_f32_e32 v68, 0x44000000, v74
	v_mul_f32_e32 v69, 0x44000000, v98
	v_cvt_pk_fp8_f32 v138, v68, v69
	v_mul_f32_e32 v68, 0x44000000, v78
	v_mul_f32_e32 v69, 0x44000000, v102
	v_mov_b32_e32 v139, v129
	v_cvt_pk_fp8_f32 v139, v68, v69
	v_mul_f32_e32 v72, 0x44000000, v122
	v_mul_f32_e32 v73, 0x44000000, v126
	v_cvt_pk_fp8_f32 v136, v72, v73 op_sel:[0,0,1]
	v_mul_f32_e32 v72, 0x44000000, v106
	v_mul_f32_e32 v73, 0x44000000, v118
	v_mul_f32_e32 v66, 0x44000000, v66
	v_mul_f32_e32 v68, 0x44000000, v70
	v_cvt_pk_fp8_f32 v138, v72, v73 op_sel:[0,0,1]
	v_cvt_pk_fp8_f32 v139, v66, v68 op_sel:[0,0,1]
	v_mul_f32_e32 v66, 0x44000000, v83
	v_mul_f32_e32 v68, 0x44000000, v87
	v_mov_b32_e32 v72, v129
	v_cvt_pk_fp8_f32 v72, v66, v68
	v_mul_f32_e32 v66, 0x44000000, v111
	v_mul_f32_e32 v68, 0x44000000, v115
	v_mov_b32_e32 v73, v129
	v_cvt_pk_fp8_f32 v73, v66, v68
	v_mul_f32_e32 v66, 0x44000000, v91
	v_mul_f32_e32 v68, 0x44000000, v95
	v_mov_b32_e32 v74, v129
	v_cvt_pk_fp8_f32 v73, v66, v68 op_sel:[0,0,1]
	v_mul_f32_e32 v66, 0x44000000, v75
	v_mul_f32_e32 v68, 0x44000000, v99
	v_cvt_pk_fp8_f32 v74, v66, v68
	v_mul_f32_e32 v66, 0x44000000, v79
	v_mul_f32_e32 v68, 0x44000000, v103
	v_mov_b32_e32 v75, v129
	v_cvt_pk_fp8_f32 v75, v66, v68
	v_mul_f32_e32 v69, 0x44000000, v123
	v_mul_f32_e32 v70, 0x44000000, v127
	v_cvt_pk_fp8_f32 v72, v69, v70 op_sel:[0,0,1]
	v_mul_f32_e32 v69, 0x44000000, v107
	v_mul_f32_e32 v70, 0x44000000, v119
	v_mul_f32_e32 v66, 0x44000000, v67
	v_mul_f32_e32 v67, 0x44000000, v71
	v_cvt_pk_fp8_f32 v74, v69, v70 op_sel:[0,0,1]
	v_cvt_pk_fp8_f32 v75, v66, v67 op_sel:[0,0,1]
	v_add_co_u32_e32 v64, vcc, s33, v64
	s_add_i32 s37, s37, 2
	s_nop 0
	v_addc_co_u32_e32 v65, vcc, 0, v65, vcc
	s_cmp_le_i32 s37, s35
	global_store_dwordx4 v[64:65], v[136:139], off sc1
	global_store_dwordx4 v[64:65], v[72:75], off offset:2048 sc1
	s_cbranch_scc0 .LBB0_1050

.LBB0_1075:
	v_mad_i64_i32 v[64:65], s[28:29], s26, v130, 0
	s_add_i32 s12, s34, 16
	v_lshl_add_u64 v[64:65], v[64:65], 2, s[24:25]
	s_min_i32 s34, s12, s36
	v_lshl_add_u64 v[64:65], v[64:65], 0, v[128:129]
	s_lshl_b32 s12, s26, 2
	v_lshl_add_u64 v[66:67], v[64:65], 0, s[12:13]
	global_load_dwordx4 v[80:83], v[64:65], off sc1 nt
	global_load_dwordx4 v[84:87], v[66:67], off sc1 nt
	v_lshl_add_u64 v[64:65], v[66:67], 0, s[12:13]
	v_lshl_add_u64 v[66:67], v[64:65], 0, s[12:13]
	global_load_dwordx4 v[120:123], v[64:65], off sc1 nt
	global_load_dwordx4 v[124:127], v[66:67], off sc1 nt
	v_lshl_add_u64 v[64:65], v[66:67], 0, s[12:13]
	v_lshl_add_u64 v[66:67], v[64:65], 0, s[12:13]
	global_load_dwordx4 v[108:111], v[64:65], off sc1 nt
	global_load_dwordx4 v[112:115], v[66:67], off sc1 nt
	v_lshl_add_u64 v[64:65], v[66:67], 0, s[12:13]
	v_lshl_add_u64 v[66:67], v[64:65], 0, s[12:13]
	global_load_dwordx4 v[88:91], v[64:65], off sc1 nt
	global_load_dwordx4 v[92:95], v[66:67], off sc1 nt
	v_lshl_add_u64 v[64:65], v[66:67], 0, s[12:13]
	global_load_dwordx4 v[72:75], v[64:65], off sc1 nt
	v_lshl_add_u64 v[64:65], v[64:65], 0, s[12:13]
	global_load_dwordx4 v[96:99], v[64:65], off sc1 nt
	v_lshl_add_u64 v[64:65], v[64:65], 0, s[12:13]
	global_load_dwordx4 v[104:107], v[64:65], off sc1 nt
	v_lshl_add_u64 v[64:65], v[64:65], 0, s[12:13]
	global_load_dwordx4 v[116:119], v[64:65], off sc1 nt
	v_lshl_add_u64 v[64:65], v[64:65], 0, s[12:13]
	global_load_dwordx4 v[76:79], v[64:65], off sc1 nt
	v_lshl_add_u64 v[64:65], v[64:65], 0, s[12:13]
	v_lshl_add_u64 v[68:69], v[64:65], 0, s[12:13]
	global_load_dwordx4 v[100:103], v[64:65], off sc1 nt
	s_waitcnt vmcnt(21)
	v_mul_f32_e32 v8, 0x44000000, v8
	global_load_dwordx4 v[64:67], v[68:69], off sc1 nt
	v_lshl_add_u64 v[68:69], v[68:69], 0, s[12:13]
	global_load_dwordx4 v[68:71], v[68:69], off sc1 nt
	s_waitcnt vmcnt(22)
	v_mul_f32_e32 v4, 0x44000000, v4
	v_mov_b32_e32 v139, v129
	v_cvt_pk_fp8_f32 v139, v8, v4
	s_waitcnt vmcnt(21)
	v_mul_f32_e32 v0, 0x44000000, v0
	s_waitcnt vmcnt(17)
	v_mul_f32_e32 v4, 0x44000000, v44
	v_mov_b32_e32 v140, v129
	v_cvt_pk_fp8_f32 v139, v0, v4 op_sel:[0,0,1]
	s_waitcnt vmcnt(16)
	v_mul_f32_e32 v0, 0x44000000, v61
	v_mul_f32_e32 v4, 0x44000000, v53
	v_cvt_pk_fp8_f32 v140, v0, v4
	v_mul_f32_e32 v0, 0x44000000, v41
	v_mul_f32_e32 v4, 0x44000000, v37
	v_mov_b32_e32 v141, v129
	v_cvt_pk_fp8_f32 v141, v0, v4
	v_mul_f32_e32 v24, 0x44000000, v24
	v_mul_f32_e32 v20, 0x44000000, v20
	v_mov_b32_e32 v138, v129
	v_mul_f32_e32 v0, 0x44000000, v33
	v_mul_f32_e32 v4, 0x44000000, v29
	v_mul_f32_e32 v60, 0x44000000, v60
	v_mul_f32_e32 v52, 0x44000000, v52
	v_mov_b32_e32 v136, v129
	v_mul_f32_e32 v40, 0x44000000, v40
	v_mul_f32_e32 v36, 0x44000000, v36
	v_mov_b32_e32 v137, v129
	v_cvt_pk_fp8_f32 v138, v24, v20
	v_cvt_pk_fp8_f32 v141, v0, v4 op_sel:[0,0,1]
	v_mul_f32_e32 v0, 0x44000000, v25
	v_mul_f32_e32 v4, 0x44000000, v21
	v_mov_b32_e32 v142, v129
	v_cvt_pk_fp8_f32 v136, v60, v52
	v_cvt_pk_fp8_f32 v137, v40, v36
	v_cvt_pk_fp8_f32 v142, v0, v4
	v_mul_f32_e32 v0, 0x44000000, v9
	v_mul_f32_e32 v4, 0x44000000, v5
	v_mov_b32_e32 v143, v129
	v_cvt_pk_fp8_f32 v143, v0, v4
	v_mul_f32_e32 v16, 0x44000000, v16
	v_mul_f32_e32 v12, 0x44000000, v12
	v_mul_f32_e32 v56, 0x44000000, v56
	v_mul_f32_e32 v48, 0x44000000, v48
	v_mul_f32_e32 v32, 0x44000000, v32
	v_mul_f32_e32 v28, 0x44000000, v28
	v_cvt_pk_fp8_f32 v138, v16, v12 op_sel:[0,0,1]
	v_mul_f32_e32 v8, 0x44000000, v57
	v_mul_f32_e32 v12, 0x44000000, v49
	v_cvt_pk_fp8_f32 v136, v56, v48 op_sel:[0,0,1]
	v_cvt_pk_fp8_f32 v137, v32, v28 op_sel:[0,0,1]
	v_cvt_pk_fp8_f32 v140, v8, v12 op_sel:[0,0,1]
	v_mul_f32_e32 v8, 0x44000000, v17
	v_mul_f32_e32 v12, 0x44000000, v13
	v_mul_f32_e32 v0, 0x44000000, v1
	v_mul_f32_e32 v1, 0x44000000, v45
	v_cvt_pk_fp8_f32 v142, v8, v12 op_sel:[0,0,1]
	v_cvt_pk_fp8_f32 v143, v0, v1 op_sel:[0,0,1]
	v_lshl_add_u64 v[0:1], s[16:17], 0, v[132:133]
	v_lshl_add_u64 v[0:1], v[0:1], 0, v[130:131]
	global_store_dwordx4 v[0:1], v[136:139], off sc1
	global_store_dwordx4 v[0:1], v[140:143], off offset:2048 sc1
	v_mul_f32_e32 v4, 0x44000000, v62
	v_mul_f32_e32 v5, 0x44000000, v54
	v_mov_b32_e32 v136, v129
	v_cvt_pk_fp8_f32 v136, v4, v5
	v_mul_f32_e32 v4, 0x44000000, v42
	v_mul_f32_e32 v5, 0x44000000, v38
	v_mov_b32_e32 v137, v129
	v_cvt_pk_fp8_f32 v137, v4, v5
	v_mul_f32_e32 v4, 0x44000000, v34
	v_mul_f32_e32 v5, 0x44000000, v30
	v_mov_b32_e32 v138, v129
	v_cvt_pk_fp8_f32 v137, v4, v5 op_sel:[0,0,1]
	v_mul_f32_e32 v4, 0x44000000, v26
	v_mul_f32_e32 v5, 0x44000000, v22
	v_cvt_pk_fp8_f32 v138, v4, v5
	v_mul_f32_e32 v4, 0x44000000, v10
	v_mul_f32_e32 v5, 0x44000000, v6
	v_mov_b32_e32 v139, v129
	v_cvt_pk_fp8_f32 v139, v4, v5
	v_mul_f32_e32 v8, 0x44000000, v58
	v_mul_f32_e32 v9, 0x44000000, v50
	v_mul_f32_e32 v2, 0x44000000, v2
	v_mul_f32_e32 v4, 0x44000000, v46
	v_cvt_pk_fp8_f32 v136, v8, v9 op_sel:[0,0,1]
	v_mul_f32_e32 v8, 0x44000000, v18
	v_mul_f32_e32 v9, 0x44000000, v14
	v_cvt_pk_fp8_f32 v139, v2, v4 op_sel:[0,0,1]
	v_mul_f32_e32 v2, 0x44000000, v63
	v_mul_f32_e32 v5, 0x44000000, v55
	v_mov_b32_e32 v4, v129
	v_cvt_pk_fp8_f32 v138, v8, v9 op_sel:[0,0,1]
	v_cvt_pk_fp8_f32 v4, v2, v5
	v_mul_f32_e32 v2, 0x44000000, v43
	v_mul_f32_e32 v9, 0x44000000, v39
	v_mov_b32_e32 v5, v129
	v_cvt_pk_fp8_f32 v5, v2, v9
	v_mul_f32_e32 v6, 0x44000000, v59
	v_mul_f32_e32 v8, 0x44000000, v51
	v_cvt_pk_fp8_f32 v4, v6, v8 op_sel:[0,0,1]
	v_mul_f32_e32 v2, 0x44000000, v35
	v_mul_f32_e32 v6, 0x44000000, v31
	v_cvt_pk_fp8_f32 v5, v2, v6 op_sel:[0,0,1]
	v_mul_f32_e32 v2, 0x44000000, v27
	v_mul_f32_e32 v8, 0x44000000, v23
	v_mov_b32_e32 v6, v129
	v_cvt_pk_fp8_f32 v6, v2, v8
	v_mul_f32_e32 v2, 0x44000000, v11
	v_mul_f32_e32 v8, 0x44000000, v7
	v_mov_b32_e32 v7, v129
	v_cvt_pk_fp8_f32 v7, v2, v8
	v_mul_f32_e32 v9, 0x44000000, v19
	v_mul_f32_e32 v10, 0x44000000, v15
	v_mul_f32_e32 v2, 0x44000000, v3
	v_mul_f32_e32 v3, 0x44000000, v47
	v_cvt_pk_fp8_f32 v6, v9, v10 op_sel:[0,0,1]
	v_cvt_pk_fp8_f32 v7, v2, v3 op_sel:[0,0,1]
	v_add_co_u32_e32 v0, vcc, s33, v0
	s_cmp_gt_i32 s34, 0xffff
	s_nop 0
	v_addc_co_u32_e32 v1, vcc, 0, v1, vcc
	s_mov_b64 s[30:31], -1
	global_store_dwordx4 v[0:1], v[136:139], off sc1
	global_store_dwordx4 v[0:1], v[4:7], off offset:2048 sc1
	s_cbranch_scc0 .LBB0_1081
	s_cmp_lt_u32 s34, 0x18000
	s_cbranch_scc0 .LBB0_1078
	s_add_i32 s12, s34, 0xffff0000
	s_lshr_b32 s12, s12, 10
	s_lshl_b64 s[16:17], s[12:13], 22
	s_lshl_b64 s[24:25], s[12:13], 24
	s_add_u32 s24, s70, s24
	s_addc_u32 s25, s71, s25
	s_add_u32 s16, s1, s16
	s_addc_u32 s17, s2, s17
	s_lshl_b32 s12, s34, 1
	s_and_b32 s12, s12, 0x780
	s_lshl_b32 s26, s12, 13
	s_add_u32 s24, s24, s26
	s_addc_u32 s25, s25, 0
	s_lshl_b32 s26, s34, 5
	s_and_b32 s26, s26, 0x7e0
	s_lshl_b32 s28, s26, 2
	s_add_u32 s24, s24, s28
	s_mov_b32 s27, s13
	s_addc_u32 s25, s25, 0
	s_mov_b64 s[30:31], 0
	s_mov_b64 s[28:29], s[12:13]
